# retention out pass stage C: state pieces unrolled with a 3-buffer LDS-DMA ring (Q panel 0 held in registers, 2 pieces in flight)
# speedup vs baseline: 1.0124x; 1.0060x over previous
; #define VM_WAIT() asm volatile("s_waitcnt vmcnt(0)" ::: "memory")
; #define FENCE() do { asm volatile("" ::: "memory"); __builtin_amdgcn_sched_barrier(0); } while (0)
; template <int DK, int DV, bool MLSTM>
; __device__ __forceinline__ void out_unit2(LAS unsigned char* lds, LAS unsigned char* ldstab, const OutArgs a, const int wv) {
;     ...
;     const int l = 32 * rb + r32;
;     float a_fl, a_bl;
;     if (MLSTM) { a_fl = a.af[l]; a_bl = a.ab[l]; } else { a_fl = (float)(l + 1) * a.lgf; a_bl = (float)(128 - l) * a.lgb; }
;     VM_WAIT(); __syncthreads();
;     f32x16 p[4];
; #pragma unroll
;     for (int kb = 0; kb < 4; ++kb) p[kb] = (f32x16){};
;     float qnf = 0.f, qnb = 0.f;
; #pragma unroll
;     for (int ks = 0; ks < NKS; ++ks) {
;         const unsigned po = (ks >> 3) * 32768u + ((ks & 1) ? rb1 : rb0) + 512u * ((ks & 7) >> 1);
;         const bf16x8 qf = lds_r128(QP + po + 8192u * rb);
;         bf16x8 kf[4];
; #pragma unroll
;         for (int kb = 0; kb < 4; ++kb) kf[kb] = lds_r128(KP + po + 8192u * kb);
; #pragma unroll
;         for (int kb = 0; kb < 4; ++kb) p[kb] = __builtin_amdgcn_mfma_f32_32x32x16_bf16(kf[kb], qf, p[kb], 0, 0, 0);
;         FENCE();
;     }
.LBB0_1829:
	s_or_b64 exec, exec, s[4:5]
	s_lshl_b32 s4, s6, 10
	s_add_u32 s39, s7, s4
	s_addc_u32 s16, s12, 0
	s_add_u32 s6, s39, 0x1000
	s_addc_u32 s7, s16, 0
	s_lshl_b32 s12, s11, 1
	s_ashr_i32 s13, s12, 31
	s_lshl_b64 s[4:5], s[12:13], 23
	s_add_u32 s4, s51, s4
	s_addc_u32 s5, s52, s5
	s_lshl_b32 s13, s10, 18
	s_add_u32 s4, s4, s13
	s_addc_u32 s5, s5, 0
	s_or_b32 s10, s12, 1
	v_lshlrev_b32_e32 v1, 6, v171
	s_ashr_i32 s11, s10, 31
	v_lshlrev_b32_e32 v0, 8, v171
	v_and_b32_e32 v1, 0x1c0, v1
	s_lshl_b64 s[10:11], s[10:11], 23
	v_and_or_b32 v71, v0, s64, v1
	v_bitop3_b32 v0, v5, v72, 3 bitop3:0x6c
	s_add_u32 s10, s51, s10
	v_lshlrev_b32_e32 v74, 4, v0
	s_addc_u32 s12, s52, s11
	v_or_b32_e32 v173, v74, v71
	s_add_u32 s11, s10, s13
	v_add_u32_e32 v0, s68, v173
	s_addc_u32 s12, s12, 0
	s_and_b32 s10, s38, 3
	s_lshl_b32 s13, s9, 6
	s_waitcnt vmcnt(0)
	s_waitcnt vmcnt(0) lgkmcnt(0)
	s_barrier
	ds_read_b128 v[0:3], v0
	s_and_b32 s41, s13, 0xffffc000
	v_lshlrev_b32_e32 v8, 11, v72
	s_lshl_b32 s13, s10, 13
	v_lshlrev_b32_e32 v9, 4, v171
	s_add_i32 s13, s13, 0
	v_and_or_b32 v12, v9, s66, v8
	v_add_u32_e32 v8, s70, v173
	v_add_u32_e32 v4, s13, v173
	ds_read_b128 v[8:11], v8
	ds_read_b128 v[4:7], v4
	s_waitcnt lgkmcnt(0)
	v_mfma_f32_32x32x16_bf16 v[48:63], v[0:3], v[4:7], 0
	v_lshrrev_b32_e32 v0, 3, v232
	v_bfe_u32 v1, v232, 1, 1
	v_and_or_b32 v0, v0, 2, v1
	v_lshlrev_b32_e32 v0, 4, v0
	v_bitop3_b32 v13, v0, v232, 32 bitop3:0x78
	v_add_u32_e32 v0, s71, v173
	ds_read_b128 v[0:3], v0
	v_mfma_f32_32x32x16_bf16 v[32:47], v[8:11], v[4:7], 0
	v_lshlrev_b32_e32 v8, 3, v171
	v_and_b32_e32 v8, 8, v8
	v_or3_b32 v68, v13, v12, v8
	v_add_u32_e32 v8, s72, v173
	ds_read_b128 v[8:11], v8
	v_and_b32_e32 v233, 31, v232
	s_lshl_b32 s10, s10, 5
	v_or_b32_e32 v66, s10, v233
	s_waitcnt lgkmcnt(1)
	v_mfma_f32_32x32x16_bf16 v[16:31], v[0:3], v[4:7], 0
	v_add_u32_e32 v0, 1, v66
	v_cvt_f32_ubyte0_e32 v67, v0
	v_sub_u32_e32 v0, 0x80, v66
	v_cvt_f32_ubyte0_e32 v70, v0
	s_mov_b32 s15, 4
	v_or_b32_e32 v175, s41, v68
	s_waitcnt lgkmcnt(0)
	v_mfma_f32_32x32x16_bf16 v[0:15], v[8:11], v[4:7], 0
	s_movk_i32 s14, 0x80
	v_mul_f32_e32 v69, v64, v67
	v_bitop3_b32 v177, v74, 32, v71 bitop3:0x36
	v_add_u32_e32 v71, s68, v177
	ds_read_b128 v[74:77], v71
	v_add_u32_e32 v71, s13, v177
	ds_read_b128 v[78:81], v71
	v_add_u32_e32 v71, s70, v177
	s_waitcnt lgkmcnt(0)
	v_mfma_f32_32x32x16_bf16 v[48:63], v[74:77], v[78:81], v[48:63]
	ds_read_b128 v[74:77], v71
	v_add_u32_e32 v71, s71, v177
	s_waitcnt lgkmcnt(0)
	v_mfma_f32_32x32x16_bf16 v[32:47], v[74:77], v[78:81], v[32:47]
	ds_read_b128 v[74:77], v71
	v_add_u32_e32 v71, s72, v177
	s_waitcnt lgkmcnt(0)
	v_mfma_f32_32x32x16_bf16 v[16:31], v[74:77], v[78:81], v[16:31]
	ds_read_b128 v[74:77], v71
	s_waitcnt lgkmcnt(0)
	v_mfma_f32_32x32x16_bf16 v[0:15], v[74:77], v[78:81], v[0:15]
	v_or_b32_e32 v71, 0x200, v173
	v_add_u32_e32 v74, s68, v71
	ds_read_b128 v[74:77], v74
	v_add_u32_e32 v78, s13, v71
	ds_read_b128 v[78:81], v78
	v_add_u32_e32 v82, s70, v71
	s_waitcnt lgkmcnt(0)
	v_mfma_f32_32x32x16_bf16 v[48:63], v[74:77], v[78:81], v[48:63]
	ds_read_b128 v[74:77], v82
	v_add_u32_e32 v82, s71, v71
	v_add_u32_e32 v71, s72, v71
	s_waitcnt lgkmcnt(0)
	v_mfma_f32_32x32x16_bf16 v[32:47], v[74:77], v[78:81], v[32:47]
	ds_read_b128 v[74:77], v82
	s_waitcnt lgkmcnt(0)
	v_mfma_f32_32x32x16_bf16 v[16:31], v[74:77], v[78:81], v[16:31]
	ds_read_b128 v[74:77], v71
	s_waitcnt lgkmcnt(0)
	v_mfma_f32_32x32x16_bf16 v[0:15], v[74:77], v[78:81], v[0:15]
	v_bitop3_b32 v71, v173, s73, 32 bitop3:0xde
	v_add_u32_e32 v74, s68, v71
	ds_read_b128 v[74:77], v74
	v_add_u32_e32 v78, s13, v71
	ds_read_b128 v[78:81], v78
	v_add_u32_e32 v82, s70, v71
	s_waitcnt lgkmcnt(0)
	v_mfma_f32_32x32x16_bf16 v[48:63], v[74:77], v[78:81], v[48:63]
	ds_read_b128 v[74:77], v82
	v_add_u32_e32 v82, s71, v71
	v_add_u32_e32 v71, s72, v71
	s_waitcnt lgkmcnt(0)
	v_mfma_f32_32x32x16_bf16 v[32:47], v[74:77], v[78:81], v[32:47]
	ds_read_b128 v[74:77], v82
	s_waitcnt lgkmcnt(0)
	v_mfma_f32_32x32x16_bf16 v[16:31], v[74:77], v[78:81], v[16:31]
	ds_read_b128 v[74:77], v71
	s_waitcnt lgkmcnt(0)
	v_mfma_f32_32x32x16_bf16 v[0:15], v[74:77], v[78:81], v[0:15]
	v_or_b32_e32 v71, 0x400, v173
	v_add_u32_e32 v74, s68, v71
	ds_read_b128 v[74:77], v74
	v_add_u32_e32 v78, s13, v71
	ds_read_b128 v[78:81], v78
	v_add_u32_e32 v82, s70, v71
	s_waitcnt lgkmcnt(0)
	v_mfma_f32_32x32x16_bf16 v[48:63], v[74:77], v[78:81], v[48:63]
	ds_read_b128 v[74:77], v82
	v_add_u32_e32 v82, s71, v71
	v_add_u32_e32 v71, s72, v71
	s_waitcnt lgkmcnt(0)
	v_mfma_f32_32x32x16_bf16 v[32:47], v[74:77], v[78:81], v[32:47]
	ds_read_b128 v[74:77], v82
	s_waitcnt lgkmcnt(0)
	v_mfma_f32_32x32x16_bf16 v[16:31], v[74:77], v[78:81], v[16:31]
	ds_read_b128 v[74:77], v71
	s_waitcnt lgkmcnt(0)
	v_mfma_f32_32x32x16_bf16 v[0:15], v[74:77], v[78:81], v[0:15]
	v_bitop3_b32 v71, v173, s74, 32 bitop3:0xde
	v_add_u32_e32 v74, s68, v71
	ds_read_b128 v[74:77], v74
	v_add_u32_e32 v78, s13, v71
	ds_read_b128 v[78:81], v78
	v_add_u32_e32 v82, s70, v71
	s_waitcnt lgkmcnt(0)
	v_mfma_f32_32x32x16_bf16 v[48:63], v[74:77], v[78:81], v[48:63]
	ds_read_b128 v[74:77], v82
	v_add_u32_e32 v82, s71, v71
	v_add_u32_e32 v71, s72, v71
	s_waitcnt lgkmcnt(0)
	v_mfma_f32_32x32x16_bf16 v[32:47], v[74:77], v[78:81], v[32:47]
	ds_read_b128 v[74:77], v82
	s_waitcnt lgkmcnt(0)
	v_mfma_f32_32x32x16_bf16 v[16:31], v[74:77], v[78:81], v[16:31]
	ds_read_b128 v[74:77], v71
	s_waitcnt lgkmcnt(0)
	v_mfma_f32_32x32x16_bf16 v[0:15], v[74:77], v[78:81], v[0:15]
	v_or_b32_e32 v71, 0x600, v173
	v_add_u32_e32 v74, s68, v71
	ds_read_b128 v[74:77], v74
	v_add_u32_e32 v78, s13, v71
	ds_read_b128 v[78:81], v78
	v_add_u32_e32 v82, s70, v71
	s_waitcnt lgkmcnt(0)
; #define FENCE() do { asm volatile("" ::: "memory"); __builtin_amdgcn_sched_barrier(0); } while (0)
; template <int DK, int DV, bool MLSTM>
; __device__ __forceinline__ void out_unit2(LAS unsigned char* lds, LAS unsigned char* ldstab, const OutArgs a, const int wv) {
;     ...
; #pragma unroll
;     for (int ks = 0; ks < NKS; ++ks) {
;         const unsigned po = (ks >> 3) * 32768u + ((ks & 1) ? rb1 : rb0) + 512u * ((ks & 7) >> 1);
;         const bf16x8 qf = lds_r128(QP + po + 8192u * rb);
;         bf16x8 kf[4];
; #pragma unroll
;         for (int kb = 0; kb < 4; ++kb) kf[kb] = lds_r128(KP + po + 8192u * kb);
; #pragma unroll
;         for (int kb = 0; kb < 4; ++kb) p[kb] = __builtin_amdgcn_mfma_f32_32x32x16_bf16(kf[kb], qf, p[kb], 0, 0, 0);
;         FENCE();
;     }
	v_mfma_f32_32x32x16_bf16 v[48:63], v[74:77], v[78:81], v[48:63]
	ds_read_b128 v[74:77], v82
	v_add_u32_e32 v82, s71, v71
	v_add_u32_e32 v71, s72, v71
	s_waitcnt lgkmcnt(0)
	v_mfma_f32_32x32x16_bf16 v[32:47], v[74:77], v[78:81], v[32:47]
	ds_read_b128 v[74:77], v82
	s_waitcnt lgkmcnt(0)
	v_mfma_f32_32x32x16_bf16 v[16:31], v[74:77], v[78:81], v[16:31]
	ds_read_b128 v[74:77], v71
	s_waitcnt lgkmcnt(0)
	v_mfma_f32_32x32x16_bf16 v[0:15], v[74:77], v[78:81], v[0:15]
	v_bitop3_b32 v71, v173, s75, 32 bitop3:0xde
	v_add_u32_e32 v74, s68, v71
	ds_read_b128 v[74:77], v74
	v_add_u32_e32 v78, s13, v71
	ds_read_b128 v[78:81], v78
	v_add_u32_e32 v82, s70, v71
	s_waitcnt lgkmcnt(0)
	v_mfma_f32_32x32x16_bf16 v[48:63], v[74:77], v[78:81], v[48:63]
	ds_read_b128 v[74:77], v82
	v_add_u32_e32 v82, s71, v71
	v_add_u32_e32 v71, s72, v71
	s_waitcnt lgkmcnt(0)
	v_mfma_f32_32x32x16_bf16 v[32:47], v[74:77], v[78:81], v[32:47]
	ds_read_b128 v[74:77], v82
	s_waitcnt lgkmcnt(0)
	v_mfma_f32_32x32x16_bf16 v[16:31], v[74:77], v[78:81], v[16:31]
	ds_read_b128 v[74:77], v71
	s_waitcnt lgkmcnt(0)
	v_mfma_f32_32x32x16_bf16 v[0:15], v[74:77], v[78:81], v[0:15]
	v_or_b32_e32 v71, 0x8000, v173
	v_add_u32_e32 v74, s68, v71
	ds_read_b128 v[74:77], v74
	v_add_u32_e32 v78, s13, v71
	ds_read_b128 v[78:81], v78
	v_add_u32_e32 v82, s70, v71
	s_waitcnt lgkmcnt(0)
	v_mfma_f32_32x32x16_bf16 v[48:63], v[74:77], v[78:81], v[48:63]
	ds_read_b128 v[74:77], v82
	v_add_u32_e32 v82, s71, v71
	v_add_u32_e32 v71, s72, v71
	s_waitcnt lgkmcnt(0)
	v_mfma_f32_32x32x16_bf16 v[32:47], v[74:77], v[78:81], v[32:47]
	ds_read_b128 v[74:77], v82
	s_waitcnt lgkmcnt(0)
	v_mfma_f32_32x32x16_bf16 v[16:31], v[74:77], v[78:81], v[16:31]
	ds_read_b128 v[74:77], v71
	s_waitcnt lgkmcnt(0)
	v_mfma_f32_32x32x16_bf16 v[0:15], v[74:77], v[78:81], v[0:15]
	v_bitop3_b32 v71, v173, s76, 32 bitop3:0xde
	v_add_u32_e32 v74, s68, v71
	ds_read_b128 v[74:77], v74
	v_add_u32_e32 v78, s13, v71
	ds_read_b128 v[78:81], v78
	v_add_u32_e32 v82, s70, v71
	s_waitcnt lgkmcnt(0)
	v_mfma_f32_32x32x16_bf16 v[48:63], v[74:77], v[78:81], v[48:63]
	ds_read_b128 v[74:77], v82
	v_add_u32_e32 v82, s71, v71
	v_add_u32_e32 v71, s72, v71
	s_waitcnt lgkmcnt(0)
	v_mfma_f32_32x32x16_bf16 v[32:47], v[74:77], v[78:81], v[32:47]
	ds_read_b128 v[74:77], v82
	s_waitcnt lgkmcnt(0)
	v_mfma_f32_32x32x16_bf16 v[16:31], v[74:77], v[78:81], v[16:31]
	ds_read_b128 v[74:77], v71
	s_waitcnt lgkmcnt(0)
	v_mfma_f32_32x32x16_bf16 v[0:15], v[74:77], v[78:81], v[0:15]
	v_or_b32_e32 v71, 0x8200, v173
	v_add_u32_e32 v74, s68, v71
	ds_read_b128 v[74:77], v74
	v_add_u32_e32 v78, s13, v71
	ds_read_b128 v[78:81], v78
	v_add_u32_e32 v82, s70, v71
	s_waitcnt lgkmcnt(0)
	v_mfma_f32_32x32x16_bf16 v[48:63], v[74:77], v[78:81], v[48:63]
	ds_read_b128 v[74:77], v82
	v_add_u32_e32 v82, s71, v71
	v_add_u32_e32 v71, s72, v71
	s_waitcnt lgkmcnt(0)
	v_mfma_f32_32x32x16_bf16 v[32:47], v[74:77], v[78:81], v[32:47]
	ds_read_b128 v[74:77], v82
	s_waitcnt lgkmcnt(0)
	v_mfma_f32_32x32x16_bf16 v[16:31], v[74:77], v[78:81], v[16:31]
	ds_read_b128 v[74:77], v71
	s_waitcnt lgkmcnt(0)
	v_mfma_f32_32x32x16_bf16 v[0:15], v[74:77], v[78:81], v[0:15]
	v_bitop3_b32 v71, v173, s77, 32 bitop3:0xde
	v_add_u32_e32 v74, s68, v71
	ds_read_b128 v[74:77], v74
	v_add_u32_e32 v78, s13, v71
	ds_read_b128 v[78:81], v78
	v_add_u32_e32 v82, s70, v71
	s_waitcnt lgkmcnt(0)
	v_mfma_f32_32x32x16_bf16 v[48:63], v[74:77], v[78:81], v[48:63]
	ds_read_b128 v[74:77], v82
	v_add_u32_e32 v82, s71, v71
	v_add_u32_e32 v71, s72, v71
	s_waitcnt lgkmcnt(0)
	v_mfma_f32_32x32x16_bf16 v[32:47], v[74:77], v[78:81], v[32:47]
	ds_read_b128 v[74:77], v82
	s_waitcnt lgkmcnt(0)
	v_mfma_f32_32x32x16_bf16 v[16:31], v[74:77], v[78:81], v[16:31]
	ds_read_b128 v[74:77], v71
	s_waitcnt lgkmcnt(0)
	v_mfma_f32_32x32x16_bf16 v[0:15], v[74:77], v[78:81], v[0:15]
	v_or_b32_e32 v71, 0x8400, v173
	v_add_u32_e32 v74, s68, v71
	ds_read_b128 v[74:77], v74
	v_add_u32_e32 v78, s13, v71
	ds_read_b128 v[78:81], v78
	v_add_u32_e32 v82, s70, v71
	s_waitcnt lgkmcnt(0)
	v_mfma_f32_32x32x16_bf16 v[48:63], v[74:77], v[78:81], v[48:63]
	ds_read_b128 v[74:77], v82
	v_add_u32_e32 v82, s71, v71
	v_add_u32_e32 v71, s72, v71
	s_waitcnt lgkmcnt(0)
	v_mfma_f32_32x32x16_bf16 v[32:47], v[74:77], v[78:81], v[32:47]
	ds_read_b128 v[74:77], v82
	s_waitcnt lgkmcnt(0)
	v_mfma_f32_32x32x16_bf16 v[16:31], v[74:77], v[78:81], v[16:31]
	ds_read_b128 v[74:77], v71
	s_waitcnt lgkmcnt(0)
	v_mfma_f32_32x32x16_bf16 v[0:15], v[74:77], v[78:81], v[0:15]
	v_bitop3_b32 v71, v173, s78, 32 bitop3:0xde
	v_add_u32_e32 v74, s68, v71
	ds_read_b128 v[74:77], v74
	v_add_u32_e32 v78, s13, v71
	ds_read_b128 v[78:81], v78
	v_add_u32_e32 v82, s70, v71
	s_waitcnt lgkmcnt(0)
	v_mfma_f32_32x32x16_bf16 v[48:63], v[74:77], v[78:81], v[48:63]
	ds_read_b128 v[74:77], v82
	v_add_u32_e32 v82, s71, v71
	v_add_u32_e32 v71, s72, v71
	s_waitcnt lgkmcnt(0)
	v_mfma_f32_32x32x16_bf16 v[32:47], v[74:77], v[78:81], v[32:47]
	ds_read_b128 v[74:77], v82
	s_waitcnt lgkmcnt(0)
	v_mfma_f32_32x32x16_bf16 v[16:31], v[74:77], v[78:81], v[16:31]
	ds_read_b128 v[74:77], v71
	s_waitcnt lgkmcnt(0)
	v_mfma_f32_32x32x16_bf16 v[0:15], v[74:77], v[78:81], v[0:15]
	v_or_b32_e32 v71, 0x8600, v173
	v_add_u32_e32 v74, s68, v71
	ds_read_b128 v[74:77], v74
	v_add_u32_e32 v78, s13, v71
	ds_read_b128 v[78:81], v78
	v_add_u32_e32 v82, s70, v71
	s_waitcnt lgkmcnt(0)
	v_mfma_f32_32x32x16_bf16 v[48:63], v[74:77], v[78:81], v[48:63]
	ds_read_b128 v[74:77], v82
	v_add_u32_e32 v82, s71, v71
	v_add_u32_e32 v71, s72, v71
	s_waitcnt lgkmcnt(0)
	v_mfma_f32_32x32x16_bf16 v[32:47], v[74:77], v[78:81], v[32:47]
	ds_read_b128 v[74:77], v82
	s_waitcnt lgkmcnt(0)
; #define LAS __attribute__((address_space(3)))
; __device__ __forceinline__ int crow(int r, int hi) { return (r & 3) + 8 * (r >> 2) + 4 * hi; }
; __device__ __forceinline__ int crow(int r, int hi) { return (r & 3) + 8 * (r >> 2) + 4 * hi; }
; template <int R, int NP>
; __device__ __forceinline__ void dma_tile(int wid, int lane, unsigned lds_base, const bf16_t* src, int ld) {
;     constexpr int NQ = R * NP / 4, PER = NQ / 8;
;     static_assert(NQ % 8 == 0 && R % 8 == 0, "dma_tile geometry");
;     const int r7 = (lane >> 2) & 7, x = lane & 3, hi = lane >> 5;
; #pragma unroll
;     for (int j = 0; j < PER; ++j) {
;         const int q = wid * PER + j;
;         const int sub = 2 * q + hi, panel = sub / (R / 2), psub = sub % (R / 2), rg = psub >> 2, cblk = psub & 3;
;         const int row = 8 * rg + r7, chlo = x ^ ((row >> 2) & 3);
;         const bf16_t* g = src + (size_t)row * ld + 128 * panel + 32 * cblk + 8 * chlo;
;         __builtin_amdgcn_global_load_lds((const unsigned*)g, (LAS unsigned*)(uintptr_t)(lds_base + q * 1024u), 16, 0, 0);
;     }
; template <int DK, int DV, bool MLSTM>
; __device__ __forceinline__ void out_unit2(LAS unsigned char* lds, LAS unsigned char* ldstab, const OutArgs a, const int wv) {
;     ...
; #pragma unroll
;     for (int kb = 0; kb < 4; ++kb) {
; #pragma unroll
;         for (int r = 0; r < 16; ++r) { const int s = 32 * kb + crow(r, hi);
;             const float xf = a_fl - akf[s], xb = a_bl - akb[s];
;             const float wf = __expf((s <= l2) ? xf : -1.0e30f), wb = __expf((s >= l2) ? xb : -1.0e30f);
;             p[kb][r] *= (wf * rf + wb * rbk); }
	v_mfma_f32_32x32x16_bf16 v[16:31], v[74:77], v[78:81], v[16:31]
	ds_read_b128 v[74:77], v71
	s_waitcnt lgkmcnt(0)
	v_mfma_f32_32x32x16_bf16 v[0:15], v[74:77], v[78:81], v[0:15]
	v_bitop3_b32 v71, v173, s79, 32 bitop3:0xde
	v_add_u32_e32 v74, s68, v71
	ds_read_b128 v[74:77], v74
	v_add_u32_e32 v78, s13, v71
	ds_read_b128 v[78:81], v78
	v_add_u32_e32 v82, s70, v71
	s_waitcnt lgkmcnt(0)
	v_mfma_f32_32x32x16_bf16 v[48:63], v[74:77], v[78:81], v[48:63]
	ds_read_b128 v[74:77], v82
	v_add_u32_e32 v82, s71, v71
	v_add_u32_e32 v71, s72, v71
	s_waitcnt lgkmcnt(0)
	v_mfma_f32_32x32x16_bf16 v[32:47], v[74:77], v[78:81], v[32:47]
	ds_read_b128 v[74:77], v82
	s_waitcnt lgkmcnt(0)
	v_mfma_f32_32x32x16_bf16 v[16:31], v[74:77], v[78:81], v[16:31]
	ds_read_b128 v[74:77], v71
	s_waitcnt lgkmcnt(0)
	v_mfma_f32_32x32x16_bf16 v[0:15], v[74:77], v[78:81], v[0:15]
	v_or_b32_e32 v74, s40, v72
	v_ashrrev_i32_e32 v75, 31, v74
	v_lshrrev_b32_e32 v75, 28, v75
	v_add_u32_e32 v78, v74, v75
	v_and_b32_e32 v75, -16, v78
	v_sub_u32_e32 v79, v74, v75
	v_lshlrev_b32_e32 v78, 3, v78
	v_lshlrev_b32_e32 v74, 1, v79
	v_and_b32_e32 v158, 0xffffff80, v78
	v_and_or_b32 v182, v74, -16, v73
	v_mov_b64_e32 v[74:75], s[6:7]
	v_ashrrev_i32_e32 v159, 31, v158
	v_lshlrev_b32_e32 v78, 5, v79
	v_mad_i64_i32 v[76:77], s[6:7], v182, s57, v[74:75]
	v_lshlrev_b64 v[184:185], 1, v[158:159]
	v_and_b32_e32 v162, 32, v78
	v_lshl_add_u64 v[76:77], v[76:77], 0, v[184:185]
	v_lshlrev_b32_e32 v160, 1, v162
	s_lshl_b32 s6, s38, 12
	s_lshl_b32 s46, s38, 2
	v_lshl_add_u64 v[76:77], v[76:77], 0, v[160:161]
	s_add_i32 s42, s6, s68
	v_lshl_add_u64 v[76:77], v[76:77], 0, v[156:157]
	s_mov_b32 m0, s42
	s_or_b32 s7, s46, 1
	s_barrier
	global_load_lds_dwordx4 v[76:77], off
	v_lshl_or_b32 v76, s7, 1, v72
	v_ashrrev_i32_e32 v77, 31, v76
	v_lshrrev_b32_e32 v77, 28, v77
	v_add_u32_e32 v78, v76, v77
	v_and_b32_e32 v77, -16, v78
	v_sub_u32_e32 v79, v76, v77
	v_lshlrev_b32_e32 v76, 1, v79
	v_and_or_b32 v186, v76, -8, v73
	v_lshlrev_b32_e32 v78, 3, v78
	v_lshrrev_b32_e32 v76, 2, v186
	v_and_b32_e32 v164, 0xffffff80, v78
	v_xor_b32_e32 v80, v76, v232
	v_ashrrev_i32_e32 v165, 31, v164
	v_lshlrev_b32_e32 v78, 5, v79
	v_mad_i64_i32 v[76:77], s[44:45], v186, s57, v[74:75]
	v_lshlrev_b64 v[188:189], 1, v[164:165]
	v_and_b32_e32 v170, 0x60, v78
	v_lshlrev_b32_e32 v78, 3, v80
	v_lshl_add_u64 v[76:77], v[76:77], 0, v[188:189]
	v_lshlrev_b32_e32 v190, 1, v170
	v_mov_b32_e32 v191, v161
	v_and_b32_e32 v172, 24, v78
	s_lshl_b32 s7, s7, 10
	v_lshl_add_u64 v[76:77], v[76:77], 0, v[190:191]
	v_lshlrev_b32_e32 v192, 1, v172
	v_mov_b32_e32 v193, v161
	s_add_i32 s43, s7, s68
	v_lshl_add_u64 v[76:77], v[76:77], 0, v[192:193]
	s_mov_b32 m0, s43
	s_or_b32 s38, s46, 2
	global_load_lds_dwordx4 v[76:77], off
	v_lshl_or_b32 v76, s38, 1, v72
	v_ashrrev_i32_e32 v77, 31, v76
	v_lshrrev_b32_e32 v77, 28, v77
	v_add_u32_e32 v78, v76, v77
	v_and_b32_e32 v77, -16, v78
	v_sub_u32_e32 v79, v76, v77
	v_lshlrev_b32_e32 v76, 1, v79
	v_and_or_b32 v194, v76, -8, v73
	v_lshlrev_b32_e32 v78, 3, v78
	v_lshrrev_b32_e32 v76, 2, v194
	v_and_b32_e32 v166, 0xffffff80, v78
	v_xor_b32_e32 v80, v76, v232
	v_ashrrev_i32_e32 v167, 31, v166
	v_lshlrev_b32_e32 v78, 5, v79
	v_mad_i64_i32 v[76:77], s[44:45], v194, s57, v[74:75]
	v_lshlrev_b64 v[196:197], 1, v[166:167]
	v_and_b32_e32 v174, 0x60, v78
	v_lshlrev_b32_e32 v78, 3, v80
	v_lshl_add_u64 v[76:77], v[76:77], 0, v[196:197]
	v_lshlrev_b32_e32 v198, 1, v174
	v_mov_b32_e32 v199, v161
	v_and_b32_e32 v176, 24, v78
	s_lshl_b32 s38, s38, 10
	v_lshl_add_u64 v[76:77], v[76:77], 0, v[198:199]
	v_lshlrev_b32_e32 v200, 1, v176
	v_mov_b32_e32 v201, v161
	s_add_i32 s44, s38, s68
	v_lshl_add_u64 v[76:77], v[76:77], 0, v[200:201]
	s_mov_b32 m0, s44
	s_or_b32 s40, s46, 3
	global_load_lds_dwordx4 v[76:77], off
	v_lshl_or_b32 v76, s40, 1, v72
	v_ashrrev_i32_e32 v77, 31, v76
	v_lshrrev_b32_e32 v77, 28, v77
	v_add_u32_e32 v77, v76, v77
	v_and_b32_e32 v78, -16, v77
	v_sub_u32_e32 v76, v76, v78
	v_lshlrev_b32_e32 v78, 1, v76
	v_and_or_b32 v202, v78, -8, v73
	v_lshlrev_b32_e32 v77, 3, v77
	v_lshrrev_b32_e32 v73, 2, v202
	v_and_b32_e32 v168, 0xffffff80, v77
	v_xor_b32_e32 v73, v73, v232
	v_ashrrev_i32_e32 v169, 31, v168
	v_lshlrev_b32_e32 v76, 5, v76
	v_mad_i64_i32 v[74:75], s[46:47], v202, s57, v[74:75]
	v_lshlrev_b64 v[204:205], 1, v[168:169]
	v_and_b32_e32 v178, 0x60, v76
	v_lshlrev_b32_e32 v73, 3, v73
	v_lshl_add_u64 v[74:75], v[74:75], 0, v[204:205]
	v_lshlrev_b32_e32 v206, 1, v178
	v_mov_b32_e32 v207, v161
	v_and_b32_e32 v180, 24, v73
	s_lshl_b32 s40, s40, 10
	v_lshl_add_u64 v[74:75], v[74:75], 0, v[206:207]
	v_lshlrev_b32_e32 v208, 1, v180
	v_mov_b32_e32 v209, v161
	s_add_i32 s45, s40, s68
	v_lshl_add_u64 v[74:75], v[74:75], 0, v[208:209]
	s_mov_b32 m0, s45
	s_add_i32 s46, 0, 0x21500
	v_lshlrev_b32_e32 v73, 4, v72
	global_load_lds_dwordx4 v[74:75], off
	v_add_u32_e32 v74, s46, v73
	s_add_i32 s47, 0, 0x21700
	v_add_u32_e32 v73, s47, v73
	ds_read_b128 v[74:77], v74
	ds_read_b128 v[78:81], v73
	v_lshlrev_b32_e32 v234, 2, v72
	v_cmp_le_i32_e32 vcc, v234, v66
	v_or_b32_e32 v84, 8, v234
	s_waitcnt lgkmcnt(0)
; #define FENCE() do { asm volatile("" ::: "memory"); __builtin_amdgcn_sched_barrier(0); } while (0)
; __device__ __forceinline__ int crow(int r, int hi) { return (r & 3) + 8 * (r >> 2) + 4 * hi; }
; __device__ __forceinline__ int crow(int r, int hi) { return (r & 3) + 8 * (r >> 2) + 4 * hi; }
; template <int DK, int DV, bool MLSTM>
; __device__ __forceinline__ void out_unit2(LAS unsigned char* lds, LAS unsigned char* ldstab, const OutArgs a, const int wv) {
;     ...
;     int l2 = l; asm volatile("" : "+v"(l2));
; #pragma unroll
;     for (int kb = 0; kb < 4; ++kb) {
; #pragma unroll
;         for (int r = 0; r < 16; ++r) { const int s = 32 * kb + crow(r, hi);
;             const float xf = a_fl - akf[s], xb = a_bl - akb[s];
;             const float wf = __expf((s <= l2) ? xf : -1.0e30f), wb = __expf((s >= l2) ? xb : -1.0e30f);
;             p[kb][r] *= (wf * rf + wb * rbk); }
;         FENCE(); }
	v_fma_f32 v72, v64, v67, -v74
	v_fma_f32 v73, v65, v70, -v78
	v_mul_f32_e32 v72, 0x3fb8aa3b, v72
	v_fma_f32 v75, v64, v67, -v75
	v_cndmask_b32_e32 v72, v230, v72, vcc
	v_mul_f32_e32 v73, 0x3fb8aa3b, v73
	v_cmp_lt_i32_e32 vcc, v234, v66
	v_or_b32_e32 v74, 1, v234
	v_fma_f32 v78, v65, v70, -v79
	v_mul_f32_e32 v75, 0x3fb8aa3b, v75
	v_cndmask_b32_e32 v73, v73, v230, vcc
	v_cndmask_b32_e32 v75, v230, v75, vcc
	v_mul_f32_e32 v78, 0x3fb8aa3b, v78
	v_cmp_ge_i32_e32 vcc, v74, v66
	v_exp_f32_e32 v72, v72
	v_exp_f32_e32 v73, v73
	v_cndmask_b32_e32 v74, v230, v78, vcc
	v_exp_f32_e32 v75, v75
	v_exp_f32_e32 v74, v74
	v_add_f32_e32 v72, v72, v73
	v_mul_f32_e32 v48, v48, v72
	v_fma_f32 v73, v64, v67, -v76
	v_add_f32_e32 v72, v75, v74
	v_mul_f32_e32 v49, v49, v72
	v_or_b32_e32 v72, 2, v234
	v_mul_f32_e32 v73, 0x3fb8aa3b, v73
	v_cmp_le_i32_e32 vcc, v72, v66
	v_fma_f32 v74, v65, v70, -v80
	v_mul_f32_e32 v71, v65, v70
	v_cndmask_b32_e32 v73, v230, v73, vcc
	v_exp_f32_e32 v80, v73
	v_mul_f32_e32 v73, 0x3fb8aa3b, v74
	v_cmp_ge_i32_e32 vcc, v72, v66
	v_fma_f32 v74, v65, v70, -v81
	v_ashrrev_i32_e32 v183, 31, v182
	v_cndmask_b32_e32 v72, v230, v73, vcc
	v_exp_f32_e32 v82, v72
	v_or_b32_e32 v72, 3, v234
	v_fma_f32 v73, v64, v67, -v77
	v_mul_f32_e32 v73, 0x3fb8aa3b, v73
	v_cmp_le_i32_e32 vcc, v72, v66
	v_add_f32_e32 v80, v80, v82
	v_mul_f32_e32 v50, v50, v80
	v_cndmask_b32_e32 v73, v230, v73, vcc
	v_exp_f32_e32 v81, v73
	v_mul_f32_e32 v73, 0x3fb8aa3b, v74
	v_cmp_ge_i32_e32 vcc, v72, v66
	v_ashrrev_i32_e32 v187, 31, v186
	v_ashrrev_i32_e32 v195, 31, v194
	v_cndmask_b32_e32 v72, v230, v73, vcc
	v_exp_f32_e32 v83, v72
	v_lshlrev_b32_e32 v72, 2, v84
	v_add_u32_e32 v73, s46, v72
	v_add_u32_e32 v76, s47, v72
	ds_read_b128 v[72:75], v73
	ds_read_b128 v[76:79], v76
	v_cmp_le_i32_e32 vcc, v84, v66
	v_add_f32_e32 v80, v81, v83
	v_or_b32_e32 v81, 9, v234
	s_waitcnt lgkmcnt(0)
	v_fma_f32 v72, v64, v67, -v72
	v_fma_f32 v76, v65, v70, -v76
	v_mul_f32_e32 v72, 0x3fb8aa3b, v72
	v_cndmask_b32_e32 v72, v230, v72, vcc
	v_mul_f32_e32 v76, 0x3fb8aa3b, v76
	v_cmp_ge_i32_e32 vcc, v84, v66
	v_fma_f32 v73, v64, v67, -v73
	v_fma_f32 v77, v65, v70, -v77
	v_cndmask_b32_e32 v76, v230, v76, vcc
	v_mul_f32_e32 v73, 0x3fb8aa3b, v73
	v_cmp_le_i32_e32 vcc, v81, v66
	v_mul_f32_e32 v77, 0x3fb8aa3b, v77
	v_exp_f32_e32 v72, v72
	v_cndmask_b32_e32 v73, v230, v73, vcc
	v_cmp_ge_i32_e32 vcc, v81, v66
	v_exp_f32_e32 v76, v76
	v_exp_f32_e32 v73, v73
	v_cndmask_b32_e32 v77, v230, v77, vcc
	v_exp_f32_e32 v77, v77
	v_add_f32_e32 v72, v72, v76
	v_mul_f32_e32 v52, v52, v72
	v_mul_f32_e32 v51, v51, v80
	v_add_f32_e32 v72, v73, v77
	v_mul_f32_e32 v53, v53, v72
	v_or_b32_e32 v72, 10, v234
	v_fma_f32 v73, v64, v67, -v74
	v_mul_f32_e32 v73, 0x3fb8aa3b, v73
	v_cmp_le_i32_e32 vcc, v72, v66
	v_fma_f32 v74, v65, v70, -v78
	v_or_b32_e32 v84, 16, v234
	v_cndmask_b32_e32 v73, v230, v73, vcc
	v_exp_f32_e32 v80, v73
	v_mul_f32_e32 v73, 0x3fb8aa3b, v74
	v_cmp_ge_i32_e32 vcc, v72, v66
	v_fma_f32 v74, v65, v70, -v79
	v_ashrrev_i32_e32 v203, 31, v202
	v_cndmask_b32_e32 v72, v230, v73, vcc
	v_exp_f32_e32 v81, v72
	v_or_b32_e32 v72, 11, v234
	v_fma_f32 v73, v64, v67, -v75
	v_mul_f32_e32 v73, 0x3fb8aa3b, v73
	v_cmp_le_i32_e32 vcc, v72, v66
	v_add_f32_e32 v80, v80, v81
	v_mul_f32_e32 v54, v54, v80
	v_cndmask_b32_e32 v73, v230, v73, vcc
	v_exp_f32_e32 v82, v73
	v_mul_f32_e32 v73, 0x3fb8aa3b, v74
	v_cmp_ge_i32_e32 vcc, v72, v66
	s_nop 1
	v_cndmask_b32_e32 v72, v230, v73, vcc
	v_exp_f32_e32 v83, v72
	v_lshlrev_b32_e32 v72, 2, v84
	v_add_u32_e32 v73, s46, v72
	v_add_u32_e32 v76, s47, v72
	ds_read_b128 v[72:75], v73
	ds_read_b128 v[76:79], v76
	v_cmp_le_i32_e32 vcc, v84, v66
	v_add_f32_e32 v80, v82, v83
	s_waitcnt lgkmcnt(0)
	v_fma_f32 v72, v64, v67, -v72
	v_mul_f32_e32 v72, 0x3fb8aa3b, v72
	v_fma_f32 v76, v65, v70, -v76
	v_cndmask_b32_e32 v72, v230, v72, vcc
	v_exp_f32_e32 v81, v72
	v_mul_f32_e32 v72, 0x3fb8aa3b, v76
	v_cmp_ge_i32_e32 vcc, v84, v66
	v_fma_f32 v73, v64, v67, -v73
	v_fma_f32 v77, v65, v70, -v77
	v_cndmask_b32_e32 v72, v230, v72, vcc
	v_exp_f32_e32 v76, v72
	v_or_b32_e32 v72, 17, v234
	v_mul_f32_e32 v73, 0x3fb8aa3b, v73
	v_cmp_le_i32_e32 vcc, v72, v66
	v_mul_f32_e32 v77, 0x3fb8aa3b, v77
	v_fma_f32 v75, v64, v67, -v75
	v_cndmask_b32_e32 v73, v230, v73, vcc
	v_cmp_ge_i32_e32 vcc, v72, v66
	v_exp_f32_e32 v73, v73
	v_mul_f32_e32 v75, 0x3fb8aa3b, v75
	v_cndmask_b32_e32 v72, v230, v77, vcc
	v_exp_f32_e32 v77, v72
	v_mul_f32_e32 v72, v55, v80
	v_add_f32_e32 v55, v81, v76
	v_mul_f32_e32 v55, v56, v55
	v_add_f32_e32 v56, v73, v77
	v_mul_f32_e32 v56, v57, v56
	v_or_b32_e32 v57, 18, v234
	v_fma_f32 v73, v64, v67, -v74
	v_fma_f32 v74, v65, v70, -v78
	v_mul_f32_e32 v73, 0x3fb8aa3b, v73
	v_cmp_le_i32_e32 vcc, v57, v66
	v_mul_f32_e32 v74, 0x3fb8aa3b, v74
	v_fma_f32 v76, v65, v70, -v79
	v_cndmask_b32_e32 v73, v230, v73, vcc
	v_cmp_ge_i32_e32 vcc, v57, v66
	v_or_b32_e32 v84, 24, v234
	v_exp_f32_e32 v73, v73
	v_cndmask_b32_e32 v57, v230, v74, vcc
	v_or_b32_e32 v74, 19, v234
	v_cmp_le_i32_e32 vcc, v74, v66
	v_exp_f32_e32 v57, v57
	s_nop 0
	v_cndmask_b32_e32 v75, v230, v75, vcc
	v_exp_f32_e32 v82, v75
	v_mul_f32_e32 v75, 0x3fb8aa3b, v76
	v_cmp_ge_i32_e32 vcc, v74, v66
	v_add_f32_e32 v57, v73, v57
	v_mul_f32_e32 v57, v58, v57
	v_cndmask_b32_e32 v74, v230, v75, vcc
	v_exp_f32_e32 v83, v74
	v_lshlrev_b32_e32 v74, 2, v84
	v_add_u32_e32 v75, s46, v74
	v_add_u32_e32 v78, s47, v74
	ds_read_b128 v[74:77], v75
	ds_read_b128 v[78:81], v78
	v_cmp_le_i32_e32 vcc, v84, v66
	v_add_f32_e32 v58, v82, v83
	v_mul_f32_e32 v58, v59, v58
	s_waitcnt lgkmcnt(0)
; #define FENCE() do { asm volatile("" ::: "memory"); __builtin_amdgcn_sched_barrier(0); } while (0)
; __device__ __forceinline__ int crow(int r, int hi) { return (r & 3) + 8 * (r >> 2) + 4 * hi; }
; __device__ __forceinline__ int crow(int r, int hi) { return (r & 3) + 8 * (r >> 2) + 4 * hi; }
; template <int DK, int DV, bool MLSTM>
; __device__ __forceinline__ void out_unit2(LAS unsigned char* lds, LAS unsigned char* ldstab, const OutArgs a, const int wv) {
;     ...
;     int l2 = l; asm volatile("" : "+v"(l2));
; #pragma unroll
;     for (int kb = 0; kb < 4; ++kb) {
; #pragma unroll
;         for (int r = 0; r < 16; ++r) { const int s = 32 * kb + crow(r, hi);
;             const float xf = a_fl - akf[s], xb = a_bl - akb[s];
;             const float wf = __expf((s <= l2) ? xf : -1.0e30f), wb = __expf((s >= l2) ? xb : -1.0e30f);
;             p[kb][r] *= (wf * rf + wb * rbk); }
;         FENCE(); }
	v_fma_f32 v73, v64, v67, -v74
	v_fma_f32 v74, v65, v70, -v78
	v_mul_f32_e32 v73, 0x3fb8aa3b, v73
	v_cndmask_b32_e32 v73, v230, v73, vcc
	v_mul_f32_e32 v74, 0x3fb8aa3b, v74
	v_cmp_ge_i32_e32 vcc, v84, v66
	v_or_b32_e32 v78, 25, v234
	v_fma_f32 v75, v64, v67, -v75
	v_cndmask_b32_e32 v74, v230, v74, vcc
	v_fma_f32 v79, v65, v70, -v79
	v_mul_f32_e32 v75, 0x3fb8aa3b, v75
	v_cmp_le_i32_e32 vcc, v78, v66
	v_mul_f32_e32 v79, 0x3fb8aa3b, v79
	v_exp_f32_e32 v73, v73
	v_cndmask_b32_e32 v75, v230, v75, vcc
	v_cmp_ge_i32_e32 vcc, v78, v66
	v_exp_f32_e32 v74, v74
	v_exp_f32_e32 v75, v75
	v_cndmask_b32_e32 v78, v230, v79, vcc
	v_exp_f32_e32 v78, v78
	v_add_f32_e32 v59, v73, v74
	v_or_b32_e32 v73, 26, v234
	v_fma_f32 v74, v64, v67, -v76
	v_mul_f32_e32 v59, v60, v59
	v_add_f32_e32 v60, v75, v78
	v_fma_f32 v75, v65, v70, -v80
	v_mul_f32_e32 v74, 0x3fb8aa3b, v74
	v_cmp_le_i32_e32 vcc, v73, v66
	v_mul_f32_e32 v75, 0x3fb8aa3b, v75
	v_fma_f32 v76, v64, v67, -v77
	v_cndmask_b32_e32 v74, v230, v74, vcc
	v_cmp_ge_i32_e32 vcc, v73, v66
	v_fma_f32 v77, v65, v70, -v81
	v_mul_f32_e32 v76, 0x3fb8aa3b, v76
	v_cndmask_b32_e32 v73, v230, v75, vcc
	v_or_b32_e32 v75, 27, v234
	v_cmp_le_i32_e32 vcc, v75, v66
	v_mul_f32_e32 v77, 0x3fb8aa3b, v77
	v_exp_f32_e32 v74, v74
	v_cndmask_b32_e32 v76, v230, v76, vcc
	v_cmp_ge_i32_e32 vcc, v75, v66
	v_exp_f32_e32 v73, v73
	v_exp_f32_e32 v76, v76
	v_cndmask_b32_e32 v75, v230, v77, vcc
	v_exp_f32_e32 v75, v75
	v_mul_f32_e32 v60, v61, v60
	v_add_f32_e32 v61, v74, v73
	v_mul_f32_e32 v61, v62, v61
	v_add_f32_e32 v62, v76, v75
	v_mul_f32_e32 v62, v63, v62
	v_or_b32_e32 v63, 32, v234
	v_lshlrev_b32_e32 v73, 2, v63
	v_add_u32_e32 v74, s46, v73
	v_add_u32_e32 v73, s47, v73
	ds_read_b128 v[74:77], v74
	ds_read_b128 v[78:81], v73
	v_cmp_le_i32_e32 vcc, v63, v66
	v_or_b32_e32 v84, 40, v234
	s_waitcnt lgkmcnt(0)
	v_fma_f32 v73, v64, v67, -v74
	v_fma_f32 v74, v65, v70, -v78
	v_mul_f32_e32 v73, 0x3fb8aa3b, v73
	v_cndmask_b32_e32 v73, v230, v73, vcc
	v_mul_f32_e32 v74, 0x3fb8aa3b, v74
	v_cmp_ge_i32_e32 vcc, v63, v66
	v_fma_f32 v75, v64, v67, -v75
	v_fma_f32 v78, v65, v70, -v79
	v_cndmask_b32_e32 v63, v230, v74, vcc
	v_or_b32_e32 v74, 33, v234
	v_mul_f32_e32 v75, 0x3fb8aa3b, v75
	v_cmp_le_i32_e32 vcc, v74, v66
	v_mul_f32_e32 v78, 0x3fb8aa3b, v78
	v_exp_f32_e32 v73, v73
	v_cndmask_b32_e32 v75, v230, v75, vcc
	v_cmp_ge_i32_e32 vcc, v74, v66
	v_exp_f32_e32 v63, v63
	v_exp_f32_e32 v75, v75
	v_cndmask_b32_e32 v74, v230, v78, vcc
	v_exp_f32_e32 v74, v74
	v_add_f32_e32 v63, v73, v63
	v_mul_f32_e32 v32, v32, v63
	v_fma_f32 v73, v64, v67, -v76
	v_add_f32_e32 v63, v75, v74
	v_mul_f32_e32 v33, v33, v63
	v_or_b32_e32 v63, 34, v234
	v_fma_f32 v74, v65, v70, -v80
	v_mul_f32_e32 v73, 0x3fb8aa3b, v73
	v_cmp_le_i32_e32 vcc, v63, v66
	v_mul_f32_e32 v74, 0x3fb8aa3b, v74
	v_fma_f32 v75, v64, v67, -v77
	v_cndmask_b32_e32 v73, v230, v73, vcc
	v_cmp_ge_i32_e32 vcc, v63, v66
	v_mul_f32_e32 v75, 0x3fb8aa3b, v75
	v_fma_f32 v76, v65, v70, -v81
	v_cndmask_b32_e32 v63, v230, v74, vcc
	v_or_b32_e32 v74, 35, v234
	v_cmp_le_i32_e32 vcc, v74, v66
	v_exp_f32_e32 v73, v73
	v_exp_f32_e32 v63, v63
	v_cndmask_b32_e32 v75, v230, v75, vcc
	v_exp_f32_e32 v82, v75
	v_mul_f32_e32 v75, 0x3fb8aa3b, v76
	v_cmp_ge_i32_e32 vcc, v74, v66
	v_add_f32_e32 v63, v73, v63
	v_mul_f32_e32 v34, v34, v63
	v_cndmask_b32_e32 v74, v230, v75, vcc
	v_exp_f32_e32 v83, v74
	v_lshlrev_b32_e32 v74, 2, v84
	v_add_u32_e32 v75, s46, v74
	v_add_u32_e32 v78, s47, v74
	ds_read_b128 v[74:77], v75
	ds_read_b128 v[78:81], v78
	v_cmp_le_i32_e32 vcc, v84, v66
	v_add_f32_e32 v63, v82, v83
	v_mul_f32_e32 v35, v35, v63
	s_waitcnt lgkmcnt(0)
	v_fma_f32 v73, v64, v67, -v74
	v_fma_f32 v74, v65, v70, -v78
	v_mul_f32_e32 v73, 0x3fb8aa3b, v73
	v_cndmask_b32_e32 v73, v230, v73, vcc
	v_mul_f32_e32 v74, 0x3fb8aa3b, v74
	v_cmp_ge_i32_e32 vcc, v84, v66
	v_or_b32_e32 v78, 41, v234
	v_fma_f32 v75, v64, v67, -v75
	v_cndmask_b32_e32 v74, v230, v74, vcc
	v_fma_f32 v79, v65, v70, -v79
	v_mul_f32_e32 v75, 0x3fb8aa3b, v75
	v_cmp_le_i32_e32 vcc, v78, v66
	v_mul_f32_e32 v79, 0x3fb8aa3b, v79
	v_exp_f32_e32 v73, v73
	v_cndmask_b32_e32 v75, v230, v75, vcc
	v_cmp_ge_i32_e32 vcc, v78, v66
	v_exp_f32_e32 v74, v74
	v_exp_f32_e32 v75, v75
	v_cndmask_b32_e32 v78, v230, v79, vcc
	v_exp_f32_e32 v78, v78
	v_add_f32_e32 v63, v73, v74
	v_mul_f32_e32 v36, v36, v63
	v_fma_f32 v73, v64, v67, -v76
	v_add_f32_e32 v63, v75, v78
	v_mul_f32_e32 v37, v37, v63
	v_or_b32_e32 v63, 42, v234
	v_fma_f32 v74, v65, v70, -v80
	v_mul_f32_e32 v73, 0x3fb8aa3b, v73
	v_cmp_le_i32_e32 vcc, v63, v66
	v_mul_f32_e32 v74, 0x3fb8aa3b, v74
	v_fma_f32 v75, v64, v67, -v77
	v_cndmask_b32_e32 v73, v230, v73, vcc
	v_cmp_ge_i32_e32 vcc, v63, v66
	v_mul_f32_e32 v75, 0x3fb8aa3b, v75
	v_fma_f32 v76, v65, v70, -v81
	v_cndmask_b32_e32 v63, v230, v74, vcc
	v_or_b32_e32 v74, 43, v234
	v_cmp_le_i32_e32 vcc, v74, v66
	v_or_b32_e32 v84, 48, v234
	v_exp_f32_e32 v73, v73
	v_cndmask_b32_e32 v75, v230, v75, vcc
	v_exp_f32_e32 v82, v75
	v_mul_f32_e32 v75, 0x3fb8aa3b, v76
	v_cmp_ge_i32_e32 vcc, v74, v66
	v_exp_f32_e32 v63, v63
	s_nop 0
	v_cndmask_b32_e32 v74, v230, v75, vcc
	v_exp_f32_e32 v83, v74
	v_lshlrev_b32_e32 v74, 2, v84
	v_add_u32_e32 v75, s46, v74
	v_add_u32_e32 v78, s47, v74
	ds_read_b128 v[74:77], v75
	ds_read_b128 v[78:81], v78
	v_add_f32_e32 v63, v73, v63
	v_cmp_le_i32_e32 vcc, v84, v66
	v_mul_f32_e32 v38, v38, v63
	s_waitcnt lgkmcnt(0)
; #define FENCE() do { asm volatile("" ::: "memory"); __builtin_amdgcn_sched_barrier(0); } while (0)
; __device__ __forceinline__ int crow(int r, int hi) { return (r & 3) + 8 * (r >> 2) + 4 * hi; }
; __device__ __forceinline__ int crow(int r, int hi) { return (r & 3) + 8 * (r >> 2) + 4 * hi; }
; template <int DK, int DV, bool MLSTM>
; __device__ __forceinline__ void out_unit2(LAS unsigned char* lds, LAS unsigned char* ldstab, const OutArgs a, const int wv) {
;     ...
;     int l2 = l; asm volatile("" : "+v"(l2));
; #pragma unroll
;     for (int kb = 0; kb < 4; ++kb) {
; #pragma unroll
;         for (int r = 0; r < 16; ++r) { const int s = 32 * kb + crow(r, hi);
;             const float xf = a_fl - akf[s], xb = a_bl - akb[s];
;             const float wf = __expf((s <= l2) ? xf : -1.0e30f), wb = __expf((s >= l2) ? xb : -1.0e30f);
;             p[kb][r] *= (wf * rf + wb * rbk); }
;         FENCE(); }
	v_fma_f32 v73, v64, v67, -v74
	v_fma_f32 v74, v65, v70, -v78
	v_mul_f32_e32 v73, 0x3fb8aa3b, v73
	v_cndmask_b32_e32 v73, v230, v73, vcc
	v_mul_f32_e32 v74, 0x3fb8aa3b, v74
	v_cmp_ge_i32_e32 vcc, v84, v66
	v_or_b32_e32 v78, 49, v234
	v_fma_f32 v75, v64, v67, -v75
	v_cndmask_b32_e32 v74, v230, v74, vcc
	v_fma_f32 v79, v65, v70, -v79
	v_mul_f32_e32 v75, 0x3fb8aa3b, v75
	v_cmp_le_i32_e32 vcc, v78, v66
	v_mul_f32_e32 v79, 0x3fb8aa3b, v79
	v_exp_f32_e32 v73, v73
	v_cndmask_b32_e32 v75, v230, v75, vcc
	v_cmp_ge_i32_e32 vcc, v78, v66
	v_exp_f32_e32 v74, v74
	v_exp_f32_e32 v75, v75
	v_cndmask_b32_e32 v78, v230, v79, vcc
	v_exp_f32_e32 v78, v78
	v_add_f32_e32 v63, v82, v83
	v_mul_f32_e32 v63, v39, v63
	v_add_f32_e32 v39, v73, v74
	v_mul_f32_e32 v39, v40, v39
	v_add_f32_e32 v40, v75, v78
	v_mul_f32_e32 v40, v41, v40
	v_or_b32_e32 v41, 50, v234
	v_fma_f32 v73, v64, v67, -v76
	v_fma_f32 v74, v65, v70, -v80
	v_mul_f32_e32 v73, 0x3fb8aa3b, v73
	v_cmp_le_i32_e32 vcc, v41, v66
	v_mul_f32_e32 v74, 0x3fb8aa3b, v74
	v_fma_f32 v75, v64, v67, -v77
	v_cndmask_b32_e32 v73, v230, v73, vcc
	v_cmp_ge_i32_e32 vcc, v41, v66
	v_mul_f32_e32 v75, 0x3fb8aa3b, v75
	v_fma_f32 v76, v65, v70, -v81
	v_cndmask_b32_e32 v41, v230, v74, vcc
	v_or_b32_e32 v74, 51, v234
	v_cmp_le_i32_e32 vcc, v74, v66
	v_or_b32_e32 v84, 56, v234
	v_exp_f32_e32 v73, v73
	v_cndmask_b32_e32 v75, v230, v75, vcc
	v_exp_f32_e32 v82, v75
	v_mul_f32_e32 v75, 0x3fb8aa3b, v76
	v_cmp_ge_i32_e32 vcc, v74, v66
	v_exp_f32_e32 v41, v41
	s_nop 0
	v_cndmask_b32_e32 v74, v230, v75, vcc
	v_exp_f32_e32 v83, v74
	v_lshlrev_b32_e32 v74, 2, v84
	v_add_u32_e32 v75, s46, v74
	v_add_u32_e32 v78, s47, v74
	ds_read_b128 v[74:77], v75
	ds_read_b128 v[78:81], v78
	v_add_f32_e32 v41, v73, v41
	v_cmp_le_i32_e32 vcc, v84, v66
	v_mul_f32_e32 v41, v42, v41
	s_waitcnt lgkmcnt(0)
	v_fma_f32 v73, v64, v67, -v74
	v_fma_f32 v74, v65, v70, -v78
	v_mul_f32_e32 v73, 0x3fb8aa3b, v73
	v_cndmask_b32_e32 v73, v230, v73, vcc
	v_mul_f32_e32 v74, 0x3fb8aa3b, v74
	v_cmp_ge_i32_e32 vcc, v84, v66
	v_or_b32_e32 v78, 57, v234
	v_fma_f32 v75, v64, v67, -v75
	v_cndmask_b32_e32 v74, v230, v74, vcc
	v_fma_f32 v79, v65, v70, -v79
	v_mul_f32_e32 v75, 0x3fb8aa3b, v75
	v_cmp_le_i32_e32 vcc, v78, v66
	v_mul_f32_e32 v79, 0x3fb8aa3b, v79
	v_exp_f32_e32 v73, v73
	v_cndmask_b32_e32 v75, v230, v75, vcc
	v_cmp_ge_i32_e32 vcc, v78, v66
	v_exp_f32_e32 v74, v74
	v_exp_f32_e32 v75, v75
	v_cndmask_b32_e32 v78, v230, v79, vcc
	v_exp_f32_e32 v78, v78
	v_add_f32_e32 v42, v82, v83
	v_mul_f32_e32 v42, v43, v42
	v_add_f32_e32 v43, v73, v74
	v_or_b32_e32 v73, 58, v234
	v_fma_f32 v74, v64, v67, -v76
	v_mul_f32_e32 v43, v44, v43
	v_add_f32_e32 v44, v75, v78
	v_fma_f32 v75, v65, v70, -v80
	v_mul_f32_e32 v74, 0x3fb8aa3b, v74
	v_cmp_le_i32_e32 vcc, v73, v66
	v_mul_f32_e32 v75, 0x3fb8aa3b, v75
	v_fma_f32 v76, v64, v67, -v77
	v_cndmask_b32_e32 v74, v230, v74, vcc
	v_cmp_ge_i32_e32 vcc, v73, v66
	v_fma_f32 v77, v65, v70, -v81
	v_mul_f32_e32 v76, 0x3fb8aa3b, v76
	v_cndmask_b32_e32 v73, v230, v75, vcc
	v_or_b32_e32 v75, 59, v234
	v_cmp_le_i32_e32 vcc, v75, v66
	v_mul_f32_e32 v77, 0x3fb8aa3b, v77
	v_exp_f32_e32 v74, v74
	v_cndmask_b32_e32 v76, v230, v76, vcc
	v_cmp_ge_i32_e32 vcc, v75, v66
	v_exp_f32_e32 v73, v73
	v_exp_f32_e32 v76, v76
	v_cndmask_b32_e32 v75, v230, v77, vcc
	v_exp_f32_e32 v75, v75
	v_mul_f32_e32 v44, v45, v44
	v_add_f32_e32 v45, v74, v73
	v_mul_f32_e32 v45, v46, v45
	v_add_f32_e32 v46, v76, v75
	v_mul_f32_e32 v46, v47, v46
	v_or_b32_e32 v47, 64, v234
	v_lshlrev_b32_e32 v73, 2, v47
	v_add_u32_e32 v74, s46, v73
	v_add_u32_e32 v73, s47, v73
	ds_read_b128 v[74:77], v74
	ds_read_b128 v[78:81], v73
	v_cmp_le_i32_e32 vcc, v47, v66
	v_or_b32_e32 v84, 0x48, v234
	s_waitcnt lgkmcnt(0)
	v_fma_f32 v73, v64, v67, -v74
	v_fma_f32 v74, v65, v70, -v78
	v_mul_f32_e32 v73, 0x3fb8aa3b, v73
	v_cndmask_b32_e32 v73, v230, v73, vcc
	v_mul_f32_e32 v74, 0x3fb8aa3b, v74
	v_cmp_ge_i32_e32 vcc, v47, v66
	v_fma_f32 v75, v64, v67, -v75
	v_fma_f32 v78, v65, v70, -v79
	v_cndmask_b32_e32 v47, v230, v74, vcc
	v_or_b32_e32 v74, 0x41, v234
	v_mul_f32_e32 v75, 0x3fb8aa3b, v75
	v_cmp_le_i32_e32 vcc, v74, v66
	v_mul_f32_e32 v78, 0x3fb8aa3b, v78
	v_exp_f32_e32 v73, v73
	v_cndmask_b32_e32 v75, v230, v75, vcc
	v_cmp_ge_i32_e32 vcc, v74, v66
	v_exp_f32_e32 v47, v47
	v_exp_f32_e32 v75, v75
	v_cndmask_b32_e32 v74, v230, v78, vcc
	v_exp_f32_e32 v74, v74
	v_add_f32_e32 v47, v73, v47
	v_mul_f32_e32 v16, v16, v47
	v_fma_f32 v73, v64, v67, -v76
	v_add_f32_e32 v47, v75, v74
	v_mul_f32_e32 v17, v17, v47
	v_or_b32_e32 v47, 0x42, v234
	v_fma_f32 v74, v65, v70, -v80
	v_mul_f32_e32 v73, 0x3fb8aa3b, v73
	v_cmp_le_i32_e32 vcc, v47, v66
	v_mul_f32_e32 v74, 0x3fb8aa3b, v74
	v_fma_f32 v75, v64, v67, -v77
	v_cndmask_b32_e32 v73, v230, v73, vcc
	v_cmp_ge_i32_e32 vcc, v47, v66
	v_mul_f32_e32 v75, 0x3fb8aa3b, v75
	v_fma_f32 v76, v65, v70, -v81
	v_cndmask_b32_e32 v47, v230, v74, vcc
	v_or_b32_e32 v74, 0x43, v234
	v_cmp_le_i32_e32 vcc, v74, v66
	v_exp_f32_e32 v73, v73
	v_exp_f32_e32 v47, v47
	v_cndmask_b32_e32 v75, v230, v75, vcc
	v_exp_f32_e32 v82, v75
	v_mul_f32_e32 v75, 0x3fb8aa3b, v76
	v_cmp_ge_i32_e32 vcc, v74, v66
	v_add_f32_e32 v47, v73, v47
	v_mul_f32_e32 v47, v18, v47
	v_cndmask_b32_e32 v74, v230, v75, vcc
	v_exp_f32_e32 v83, v74
	v_lshlrev_b32_e32 v74, 2, v84
	v_add_u32_e32 v75, s46, v74
	v_add_u32_e32 v78, s47, v74
	ds_read_b128 v[74:77], v75
	ds_read_b128 v[78:81], v78
	v_cmp_le_i32_e32 vcc, v84, v66
	v_add_f32_e32 v18, v82, v83
	s_waitcnt lgkmcnt(0)
; #define FENCE() do { asm volatile("" ::: "memory"); __builtin_amdgcn_sched_barrier(0); } while (0)
; __device__ __forceinline__ int crow(int r, int hi) { return (r & 3) + 8 * (r >> 2) + 4 * hi; }
; __device__ __forceinline__ int crow(int r, int hi) { return (r & 3) + 8 * (r >> 2) + 4 * hi; }
; template <int DK, int DV, bool MLSTM>
; __device__ __forceinline__ void out_unit2(LAS unsigned char* lds, LAS unsigned char* ldstab, const OutArgs a, const int wv) {
;     ...
;     int l2 = l; asm volatile("" : "+v"(l2));
; #pragma unroll
;     for (int kb = 0; kb < 4; ++kb) {
; #pragma unroll
;         for (int r = 0; r < 16; ++r) { const int s = 32 * kb + crow(r, hi);
;             const float xf = a_fl - akf[s], xb = a_bl - akb[s];
;             const float wf = __expf((s <= l2) ? xf : -1.0e30f), wb = __expf((s >= l2) ? xb : -1.0e30f);
;             p[kb][r] *= (wf * rf + wb * rbk); }
;         FENCE(); }
	v_fma_f32 v73, v64, v67, -v74
	v_fma_f32 v74, v65, v70, -v78
	v_mul_f32_e32 v73, 0x3fb8aa3b, v73
	v_cndmask_b32_e32 v73, v230, v73, vcc
	v_mul_f32_e32 v74, 0x3fb8aa3b, v74
	v_cmp_ge_i32_e32 vcc, v84, v66
	v_or_b32_e32 v78, 0x49, v234
	v_fma_f32 v75, v64, v67, -v75
	v_cndmask_b32_e32 v74, v230, v74, vcc
	v_fma_f32 v79, v65, v70, -v79
	v_mul_f32_e32 v75, 0x3fb8aa3b, v75
	v_cmp_le_i32_e32 vcc, v78, v66
	v_mul_f32_e32 v79, 0x3fb8aa3b, v79
	v_exp_f32_e32 v73, v73
	v_cndmask_b32_e32 v75, v230, v75, vcc
	v_cmp_ge_i32_e32 vcc, v78, v66
	v_exp_f32_e32 v74, v74
	v_exp_f32_e32 v75, v75
	v_cndmask_b32_e32 v78, v230, v79, vcc
	v_exp_f32_e32 v78, v78
	v_mul_f32_e32 v79, v19, v18
	v_add_f32_e32 v18, v73, v74
	v_mul_f32_e32 v73, v20, v18
	v_add_f32_e32 v18, v75, v78
	v_mul_f32_e32 v78, v21, v18
	v_or_b32_e32 v18, 0x4a, v234
	v_fma_f32 v19, v64, v67, -v76
	v_mul_f32_e32 v19, 0x3fb8aa3b, v19
	v_cmp_le_i32_e32 vcc, v18, v66
	v_fma_f32 v20, v65, v70, -v80
	v_or_b32_e32 v84, 0x50, v234
	v_cndmask_b32_e32 v19, v230, v19, vcc
	v_exp_f32_e32 v80, v19
	v_mul_f32_e32 v19, 0x3fb8aa3b, v20
	v_cmp_ge_i32_e32 vcc, v18, v66
	v_fma_f32 v20, v65, v70, -v81
	s_nop 0
	v_cndmask_b32_e32 v18, v230, v19, vcc
	v_exp_f32_e32 v82, v18
	v_or_b32_e32 v18, 0x4b, v234
	v_fma_f32 v19, v64, v67, -v77
	v_mul_f32_e32 v19, 0x3fb8aa3b, v19
	v_cmp_le_i32_e32 vcc, v18, v66
	v_add_f32_e32 v80, v80, v82
	v_mul_f32_e32 v80, v22, v80
	v_cndmask_b32_e32 v19, v230, v19, vcc
	v_exp_f32_e32 v81, v19
	v_mul_f32_e32 v19, 0x3fb8aa3b, v20
	v_cmp_ge_i32_e32 vcc, v18, v66
	s_nop 1
	v_cndmask_b32_e32 v18, v230, v19, vcc
	v_exp_f32_e32 v83, v18
	v_lshlrev_b32_e32 v18, 2, v84
	v_add_u32_e32 v19, s46, v18
	v_add_u32_e32 v74, s47, v18
	ds_read_b128 v[18:21], v19
	ds_read_b128 v[74:77], v74
	v_cmp_le_i32_e32 vcc, v84, v66
	v_add_f32_e32 v22, v81, v83
	v_or_b32_e32 v81, 0x51, v234
	s_waitcnt lgkmcnt(0)
	v_fma_f32 v18, v64, v67, -v18
	v_fma_f32 v74, v65, v70, -v74
	v_mul_f32_e32 v18, 0x3fb8aa3b, v18
	v_cndmask_b32_e32 v18, v230, v18, vcc
	v_mul_f32_e32 v74, 0x3fb8aa3b, v74
	v_cmp_ge_i32_e32 vcc, v84, v66
	v_fma_f32 v19, v64, v67, -v19
	v_fma_f32 v75, v65, v70, -v75
	v_cndmask_b32_e32 v74, v230, v74, vcc
	v_mul_f32_e32 v19, 0x3fb8aa3b, v19
	v_cmp_le_i32_e32 vcc, v81, v66
	v_mul_f32_e32 v75, 0x3fb8aa3b, v75
	v_exp_f32_e32 v18, v18
	v_cndmask_b32_e32 v19, v230, v19, vcc
	v_cmp_ge_i32_e32 vcc, v81, v66
	v_exp_f32_e32 v74, v74
	v_exp_f32_e32 v19, v19
	v_cndmask_b32_e32 v75, v230, v75, vcc
	v_exp_f32_e32 v75, v75
	v_add_f32_e32 v18, v18, v74
	v_mul_f32_e32 v74, v24, v18
	v_or_b32_e32 v84, 0x58, v234
	v_add_f32_e32 v18, v19, v75
	v_mul_f32_e32 v75, v25, v18
	v_or_b32_e32 v18, 0x52, v234
	v_fma_f32 v19, v64, v67, -v20
	v_mul_f32_e32 v19, 0x3fb8aa3b, v19
	v_cmp_le_i32_e32 vcc, v18, v66
	v_fma_f32 v20, v65, v70, -v76
	v_mul_f32_e32 v81, v23, v22
	v_cndmask_b32_e32 v19, v230, v19, vcc
	v_exp_f32_e32 v76, v19
	v_mul_f32_e32 v19, 0x3fb8aa3b, v20
	v_cmp_ge_i32_e32 vcc, v18, v66
	v_fma_f32 v20, v65, v70, -v77
	s_nop 0
	v_cndmask_b32_e32 v18, v230, v19, vcc
	v_exp_f32_e32 v82, v18
	v_or_b32_e32 v18, 0x53, v234
	v_fma_f32 v19, v64, v67, -v21
	v_mul_f32_e32 v19, 0x3fb8aa3b, v19
	v_cmp_le_i32_e32 vcc, v18, v66
	v_add_f32_e32 v76, v76, v82
	v_mul_f32_e32 v26, v26, v76
	v_cndmask_b32_e32 v19, v230, v19, vcc
	v_exp_f32_e32 v77, v19
	v_mul_f32_e32 v19, 0x3fb8aa3b, v20
	v_cmp_ge_i32_e32 vcc, v18, v66
	s_nop 1
	v_cndmask_b32_e32 v18, v230, v19, vcc
	v_exp_f32_e32 v83, v18
	v_lshlrev_b32_e32 v18, 2, v84
	v_add_u32_e32 v19, s46, v18
	v_add_u32_e32 v22, s47, v18
	ds_read_b128 v[18:21], v19
	ds_read_b128 v[22:25], v22
	v_cmp_le_i32_e32 vcc, v84, v66
	v_add_f32_e32 v76, v77, v83
	v_or_b32_e32 v77, 0x59, v234
	s_waitcnt lgkmcnt(0)
	v_fma_f32 v18, v64, v67, -v18
	v_fma_f32 v22, v65, v70, -v22
	v_mul_f32_e32 v18, 0x3fb8aa3b, v18
	v_cndmask_b32_e32 v18, v230, v18, vcc
	v_mul_f32_e32 v22, 0x3fb8aa3b, v22
	v_cmp_ge_i32_e32 vcc, v84, v66
	v_fma_f32 v19, v64, v67, -v19
	v_fma_f32 v23, v65, v70, -v23
	v_cndmask_b32_e32 v22, v230, v22, vcc
	v_mul_f32_e32 v19, 0x3fb8aa3b, v19
	v_cmp_le_i32_e32 vcc, v77, v66
	v_mul_f32_e32 v23, 0x3fb8aa3b, v23
	v_exp_f32_e32 v18, v18
	v_cndmask_b32_e32 v19, v230, v19, vcc
	v_cmp_ge_i32_e32 vcc, v77, v66
	v_exp_f32_e32 v22, v22
	v_exp_f32_e32 v19, v19
	v_cndmask_b32_e32 v23, v230, v23, vcc
	v_exp_f32_e32 v23, v23
	v_add_f32_e32 v18, v18, v22
	v_mul_f32_e32 v28, v28, v18
	v_fma_f32 v20, v64, v67, -v20
	v_add_f32_e32 v18, v19, v23
	v_or_b32_e32 v19, 0x5a, v234
	v_fma_f32 v22, v65, v70, -v24
	v_mul_f32_e32 v20, 0x3fb8aa3b, v20
	v_cmp_le_i32_e32 vcc, v19, v66
	v_mul_f32_e32 v22, 0x3fb8aa3b, v22
	v_fma_f32 v21, v64, v67, -v21
	v_cndmask_b32_e32 v20, v230, v20, vcc
	v_cmp_ge_i32_e32 vcc, v19, v66
	v_fma_f32 v23, v65, v70, -v25
	v_mul_f32_e32 v21, 0x3fb8aa3b, v21
	v_cndmask_b32_e32 v19, v230, v22, vcc
	v_or_b32_e32 v22, 0x5b, v234
	v_cmp_le_i32_e32 vcc, v22, v66
	v_mul_f32_e32 v23, 0x3fb8aa3b, v23
	v_exp_f32_e32 v20, v20
	v_cndmask_b32_e32 v21, v230, v21, vcc
	v_cmp_ge_i32_e32 vcc, v22, v66
	v_exp_f32_e32 v19, v19
	v_exp_f32_e32 v21, v21
	v_cndmask_b32_e32 v22, v230, v23, vcc
	v_exp_f32_e32 v22, v22
	v_mul_f32_e32 v29, v29, v18
	v_add_f32_e32 v18, v20, v19
	v_mul_f32_e32 v30, v30, v18
	v_add_f32_e32 v18, v21, v22
	v_mul_f32_e32 v27, v27, v76
	v_mul_f32_e32 v31, v31, v18
	v_or_b32_e32 v76, 0x60, v234
	v_lshlrev_b32_e32 v18, 2, v76
	v_add_u32_e32 v19, s46, v18
	v_add_u32_e32 v22, s47, v18
	ds_read_b128 v[18:21], v19
	ds_read_b128 v[22:25], v22
	v_cmp_le_i32_e32 vcc, v76, v66
	v_or_b32_e32 v84, 0x68, v234
	s_waitcnt lgkmcnt(0)
; #define FENCE() do { asm volatile("" ::: "memory"); __builtin_amdgcn_sched_barrier(0); } while (0)
; __device__ __forceinline__ int crow(int r, int hi) { return (r & 3) + 8 * (r >> 2) + 4 * hi; }
; __device__ __forceinline__ int crow(int r, int hi) { return (r & 3) + 8 * (r >> 2) + 4 * hi; }
; template <int DK, int DV, bool MLSTM>
; __device__ __forceinline__ void out_unit2(LAS unsigned char* lds, LAS unsigned char* ldstab, const OutArgs a, const int wv) {
;     ...
;     int l2 = l; asm volatile("" : "+v"(l2));
; #pragma unroll
;     for (int kb = 0; kb < 4; ++kb) {
; #pragma unroll
;         for (int r = 0; r < 16; ++r) { const int s = 32 * kb + crow(r, hi);
;             const float xf = a_fl - akf[s], xb = a_bl - akb[s];
;             const float wf = __expf((s <= l2) ? xf : -1.0e30f), wb = __expf((s >= l2) ? xb : -1.0e30f);
;             p[kb][r] *= (wf * rf + wb * rbk); }
;         FENCE(); }
	v_fma_f32 v18, v64, v67, -v18
	v_fma_f32 v22, v65, v70, -v22
	v_mul_f32_e32 v18, 0x3fb8aa3b, v18
	v_cndmask_b32_e32 v18, v230, v18, vcc
	v_mul_f32_e32 v22, 0x3fb8aa3b, v22
	v_cmp_ge_i32_e32 vcc, v76, v66
	v_or_b32_e32 v76, 0x61, v234
	v_fma_f32 v19, v64, v67, -v19
	v_cndmask_b32_e32 v22, v230, v22, vcc
	v_fma_f32 v23, v65, v70, -v23
	v_mul_f32_e32 v19, 0x3fb8aa3b, v19
	v_cmp_le_i32_e32 vcc, v76, v66
	v_mul_f32_e32 v23, 0x3fb8aa3b, v23
	v_exp_f32_e32 v18, v18
	v_cndmask_b32_e32 v19, v230, v19, vcc
	v_cmp_ge_i32_e32 vcc, v76, v66
	v_exp_f32_e32 v22, v22
	v_exp_f32_e32 v19, v19
	v_cndmask_b32_e32 v23, v230, v23, vcc
	v_exp_f32_e32 v23, v23
	v_add_f32_e32 v18, v18, v22
	v_mul_f32_e32 v76, v0, v18
	v_fma_f32 v18, v65, v70, -v24
	v_add_f32_e32 v0, v19, v23
	v_mul_f32_e32 v77, v1, v0
	v_or_b32_e32 v0, 0x62, v234
	v_fma_f32 v1, v64, v67, -v20
	v_mul_f32_e32 v1, 0x3fb8aa3b, v1
	v_cmp_le_i32_e32 vcc, v0, v66
	v_mul_f32_e32 v18, 0x3fb8aa3b, v18
	v_fma_f32 v19, v64, v67, -v21
	v_cndmask_b32_e32 v1, v230, v1, vcc
	v_cmp_ge_i32_e32 vcc, v0, v66
	v_mul_f32_e32 v19, 0x3fb8aa3b, v19
	v_fma_f32 v20, v65, v70, -v25
	v_cndmask_b32_e32 v0, v230, v18, vcc
	v_or_b32_e32 v18, 0x63, v234
	v_cmp_le_i32_e32 vcc, v18, v66
	v_exp_f32_e32 v1, v1
	v_exp_f32_e32 v0, v0
	v_cndmask_b32_e32 v19, v230, v19, vcc
	v_exp_f32_e32 v82, v19
	v_mul_f32_e32 v19, 0x3fb8aa3b, v20
	v_cmp_ge_i32_e32 vcc, v18, v66
	v_add_f32_e32 v0, v1, v0
	v_mul_f32_e32 v85, v2, v0
	v_cndmask_b32_e32 v18, v230, v19, vcc
	v_exp_f32_e32 v83, v18
	v_lshlrev_b32_e32 v18, 2, v84
	v_add_u32_e32 v19, s46, v18
	v_add_u32_e32 v22, s47, v18
	ds_read_b128 v[18:21], v19
	ds_read_b128 v[22:25], v22
	v_cmp_le_i32_e32 vcc, v84, v66
	v_add_f32_e32 v0, v82, v83
	v_or_b32_e32 v83, 0x70, v234
	s_waitcnt lgkmcnt(0)
	v_fma_f32 v1, v64, v67, -v18
	v_fma_f32 v2, v65, v70, -v22
	v_mul_f32_e32 v1, 0x3fb8aa3b, v1
	v_cndmask_b32_e32 v1, v230, v1, vcc
	v_mul_f32_e32 v2, 0x3fb8aa3b, v2
	v_cmp_ge_i32_e32 vcc, v84, v66
	v_or_b32_e32 v18, 0x69, v234
	v_fma_f32 v19, v64, v67, -v19
	v_cndmask_b32_e32 v2, v230, v2, vcc
	v_fma_f32 v22, v65, v70, -v23
	v_mul_f32_e32 v19, 0x3fb8aa3b, v19
	v_cmp_le_i32_e32 vcc, v18, v66
	v_mul_f32_e32 v22, 0x3fb8aa3b, v22
	v_exp_f32_e32 v1, v1
	v_cndmask_b32_e32 v19, v230, v19, vcc
	v_cmp_ge_i32_e32 vcc, v18, v66
	v_exp_f32_e32 v2, v2
	v_exp_f32_e32 v19, v19
	v_cndmask_b32_e32 v18, v230, v22, vcc
	v_exp_f32_e32 v18, v18
	v_mul_f32_e32 v22, v3, v0
	v_add_f32_e32 v0, v1, v2
	v_mul_f32_e32 v23, v4, v0
	v_add_f32_e32 v0, v19, v18
	v_mul_f32_e32 v82, v5, v0
	v_or_b32_e32 v0, 0x6a, v234
	v_fma_f32 v1, v64, v67, -v20
	v_mul_f32_e32 v1, 0x3fb8aa3b, v1
	v_cmp_le_i32_e32 vcc, v0, v66
	v_fma_f32 v2, v65, v70, -v24
	s_nop 0
	v_cndmask_b32_e32 v1, v230, v1, vcc
	v_exp_f32_e32 v4, v1
	v_mul_f32_e32 v1, 0x3fb8aa3b, v2
	v_cmp_ge_i32_e32 vcc, v0, v66
	v_fma_f32 v2, v65, v70, -v25
	s_nop 0
	v_cndmask_b32_e32 v0, v230, v1, vcc
	v_exp_f32_e32 v5, v0
	v_or_b32_e32 v0, 0x6b, v234
	v_fma_f32 v1, v64, v67, -v21
	v_mul_f32_e32 v1, 0x3fb8aa3b, v1
	v_cmp_le_i32_e32 vcc, v0, v66
	v_add_f32_e32 v4, v4, v5
	v_mul_f32_e32 v84, v6, v4
	v_cndmask_b32_e32 v1, v230, v1, vcc
	v_exp_f32_e32 v24, v1
	v_mul_f32_e32 v1, 0x3fb8aa3b, v2
	v_cmp_ge_i32_e32 vcc, v0, v66
	v_or_b32_e32 v6, 0x71, v234
	s_nop 0
	v_cndmask_b32_e32 v0, v230, v1, vcc
	v_exp_f32_e32 v25, v0
	v_lshlrev_b32_e32 v0, 2, v83
	v_add_u32_e32 v1, s46, v0
	v_add_u32_e32 v18, s47, v0
	ds_read_b128 v[0:3], v1
	ds_read_b128 v[18:21], v18
	v_cmp_le_i32_e32 vcc, v83, v66
	v_add_f32_e32 v4, v24, v25
	v_or_b32_e32 v25, 0x78, v234
	s_waitcnt lgkmcnt(0)
	v_fma_f32 v0, v64, v67, -v0
	v_fma_f32 v5, v65, v70, -v18
	v_mul_f32_e32 v0, 0x3fb8aa3b, v0
	v_cndmask_b32_e32 v0, v230, v0, vcc
	v_mul_f32_e32 v5, 0x3fb8aa3b, v5
	v_cmp_ge_i32_e32 vcc, v83, v66
	v_fma_f32 v1, v64, v67, -v1
	v_fma_f32 v18, v65, v70, -v19
	v_cndmask_b32_e32 v5, v230, v5, vcc
	v_mul_f32_e32 v1, 0x3fb8aa3b, v1
	v_cmp_le_i32_e32 vcc, v6, v66
	v_mul_f32_e32 v18, 0x3fb8aa3b, v18
	v_exp_f32_e32 v0, v0
	v_cndmask_b32_e32 v1, v230, v1, vcc
	v_cmp_ge_i32_e32 vcc, v6, v66
	v_exp_f32_e32 v5, v5
	v_exp_f32_e32 v1, v1
	v_cndmask_b32_e32 v6, v230, v18, vcc
	v_exp_f32_e32 v6, v6
	v_add_f32_e32 v0, v0, v5
	v_mul_f32_e32 v8, v8, v0
	v_mul_f32_e32 v18, v7, v4
	v_add_f32_e32 v0, v1, v6
	v_mul_f32_e32 v9, v9, v0
	v_or_b32_e32 v0, 0x72, v234
	v_fma_f32 v1, v64, v67, -v2
	v_mul_f32_e32 v1, 0x3fb8aa3b, v1
	v_cmp_le_i32_e32 vcc, v0, v66
	v_fma_f32 v2, v65, v70, -v20
	s_nop 0
	v_cndmask_b32_e32 v1, v230, v1, vcc
	v_exp_f32_e32 v19, v1
	v_mul_f32_e32 v1, 0x3fb8aa3b, v2
	v_cmp_ge_i32_e32 vcc, v0, v66
	v_fma_f32 v2, v65, v70, -v21
	s_nop 0
	v_cndmask_b32_e32 v0, v230, v1, vcc
	v_exp_f32_e32 v20, v0
	v_or_b32_e32 v0, 0x73, v234
	v_fma_f32 v1, v64, v67, -v3
	v_mul_f32_e32 v1, 0x3fb8aa3b, v1
	v_cmp_le_i32_e32 vcc, v0, v66
	v_add_f32_e32 v19, v19, v20
	v_or_b32_e32 v20, 0x79, v234
	v_cndmask_b32_e32 v1, v230, v1, vcc
	v_exp_f32_e32 v21, v1
	v_mul_f32_e32 v1, 0x3fb8aa3b, v2
	v_cmp_ge_i32_e32 vcc, v0, v66
	v_mul_f32_e32 v10, v10, v19
	s_nop 0
	v_cndmask_b32_e32 v0, v230, v1, vcc
	v_exp_f32_e32 v24, v0
	v_lshlrev_b32_e32 v0, 2, v25
	v_add_u32_e32 v1, s46, v0
	v_add_u32_e32 v4, s47, v0
	ds_read_b128 v[0:3], v1
	ds_read_b128 v[4:7], v4
	v_cmp_le_i32_e32 vcc, v25, v66
	v_add_f32_e32 v19, v21, v24
	s_waitcnt lgkmcnt(0)
; #define VM_WAIT() asm volatile("s_waitcnt vmcnt(0)" ::: "memory")
; #define FENCE() do { asm volatile("" ::: "memory"); __builtin_amdgcn_sched_barrier(0); } while (0)
; __device__ __forceinline__ int crow(int r, int hi) { return (r & 3) + 8 * (r >> 2) + 4 * hi; }
; __device__ __forceinline__ int crow(int r, int hi) { return (r & 3) + 8 * (r >> 2) + 4 * hi; }
; template <int DK, int DV, bool MLSTM>
; __device__ __forceinline__ void out_unit2(LAS unsigned char* lds, LAS unsigned char* ldstab, const OutArgs a, const int wv) {
;     ...
;     int l2 = l; asm volatile("" : "+v"(l2));
; #pragma unroll
;     for (int kb = 0; kb < 4; ++kb) {
; #pragma unroll
;         for (int r = 0; r < 16; ++r) { const int s = 32 * kb + crow(r, hi);
;             const float xf = a_fl - akf[s], xb = a_bl - akb[s];
;             const float wf = __expf((s <= l2) ? xf : -1.0e30f), wb = __expf((s >= l2) ? xb : -1.0e30f);
;             p[kb][r] *= (wf * rf + wb * rbk); }
;         FENCE(); }
;     const float qsf = __expf(a_fl) * rf, qsb = __expf(a_bl) * rbk;
;     bf16x8 pa[8];
;     ...
; #pragma unroll
;     for (int kb = 0; kb < 4; ++kb) { LA_PK4(p[kb], 0, pa[2 * kb]); LA_PK4(p[kb], 8, pa[2 * kb + 1]); }
;     ...
;     f32x16 o[NB];
; #pragma unroll
;     for (int nb = 0; nb < NB; ++nb) o[nb] = (f32x16){};
;     ...
; #pragma unroll
;     for (int pc = 0; pc < 4; ++pc) {
;         VM_WAIT(); __syncthreads();
;         OUT_DMA(pc + 1);
;         const bf16x8 af0 = pa[2 * pc], af1 = pa[2 * pc + 1];
;         OUT_MMA(pc & 1);
	v_fma_f32 v0, v64, v67, -v0
	v_fma_f32 v4, v65, v70, -v4
	v_mul_f32_e32 v0, 0x3fb8aa3b, v0
	v_cndmask_b32_e32 v0, v230, v0, vcc
	v_mul_f32_e32 v4, 0x3fb8aa3b, v4
	v_cmp_ge_i32_e32 vcc, v25, v66
	v_fma_f32 v1, v64, v67, -v1
	v_fma_f32 v5, v65, v70, -v5
	v_cndmask_b32_e32 v4, v230, v4, vcc
	v_mul_f32_e32 v1, 0x3fb8aa3b, v1
	v_cmp_le_i32_e32 vcc, v20, v66
	v_mul_f32_e32 v5, 0x3fb8aa3b, v5
	v_exp_f32_e32 v0, v0
	v_cndmask_b32_e32 v1, v230, v1, vcc
	v_cmp_ge_i32_e32 vcc, v20, v66
	v_exp_f32_e32 v4, v4
	v_exp_f32_e32 v1, v1
	v_cndmask_b32_e32 v5, v230, v5, vcc
	v_exp_f32_e32 v5, v5
	v_add_f32_e32 v0, v0, v4
	v_or_b32_e32 v4, 0x7a, v234
	v_fma_f32 v2, v64, v67, -v2
	v_add_f32_e32 v1, v1, v5
	v_fma_f32 v5, v65, v70, -v6
	v_mul_f32_e32 v2, 0x3fb8aa3b, v2
	v_cmp_le_i32_e32 vcc, v4, v66
	v_mul_f32_e32 v5, 0x3fb8aa3b, v5
	v_fma_f32 v3, v64, v67, -v3
	v_cndmask_b32_e32 v2, v230, v2, vcc
	v_cmp_ge_i32_e32 vcc, v4, v66
	v_fma_f32 v6, v65, v70, -v7
	v_mul_f32_e32 v3, 0x3fb8aa3b, v3
	v_cndmask_b32_e32 v4, v230, v5, vcc
	v_or_b32_e32 v5, 0x7b, v234
	v_cmp_le_i32_e32 vcc, v5, v66
	v_mul_f32_e32 v6, 0x3fb8aa3b, v6
	v_exp_f32_e32 v2, v2
	v_cndmask_b32_e32 v3, v230, v3, vcc
	v_cmp_ge_i32_e32 vcc, v5, v66
	v_exp_f32_e32 v4, v4
	v_exp_f32_e32 v3, v3
	v_cndmask_b32_e32 v5, v230, v6, vcc
	v_exp_f32_e32 v5, v5
	v_add_f32_e32 v2, v2, v4
	v_mul_f32_e32 v11, v11, v19
	v_mul_f32_e32 v0, v12, v0
	v_add_f32_e32 v3, v3, v5
	v_mul_f32_e32 v1, v13, v1
	v_mul_f32_e32 v2, v14, v2
	v_mul_f32_e32 v3, v15, v3
	s_add_u32 s46, s39, 0x61000
	s_addc_u32 s47, s16, 0
	v_cvt_pk_bf16_f32 v64, v48, v49
	v_cvt_pk_bf16_f32 v65, v50, v51
	v_cvt_pk_bf16_f32 v66, v52, v53
	v_cvt_pk_bf16_f32 v67, v54, v72
	v_cvt_pk_bf16_f32 v152, v55, v56
	v_cvt_pk_bf16_f32 v153, v57, v58
	v_cvt_pk_bf16_f32 v154, v59, v60
	v_cvt_pk_bf16_f32 v155, v61, v62
	v_cvt_pk_bf16_f32 v148, v32, v33
	v_cvt_pk_bf16_f32 v149, v34, v35
	v_cvt_pk_bf16_f32 v150, v36, v37
	v_cvt_pk_bf16_f32 v151, v38, v63
	v_cvt_pk_bf16_f32 v144, v39, v40
	v_cvt_pk_bf16_f32 v145, v41, v42
	v_cvt_pk_bf16_f32 v146, v43, v44
	v_cvt_pk_bf16_f32 v147, v45, v46
	v_cvt_pk_bf16_f32 v140, v16, v17
	v_cvt_pk_bf16_f32 v141, v47, v79
	v_cvt_pk_bf16_f32 v142, v73, v78
	v_cvt_pk_bf16_f32 v143, v80, v81
	v_cvt_pk_bf16_f32 v136, v74, v75
	v_cvt_pk_bf16_f32 v137, v26, v27
	v_cvt_pk_bf16_f32 v138, v28, v29
	v_cvt_pk_bf16_f32 v139, v30, v31
	v_cvt_pk_bf16_f32 v132, v76, v77
	v_cvt_pk_bf16_f32 v133, v85, v22
	v_cvt_pk_bf16_f32 v134, v23, v82
	v_cvt_pk_bf16_f32 v135, v84, v18
	v_cvt_pk_bf16_f32 v128, v8, v9
	v_cvt_pk_bf16_f32 v129, v10, v11
	v_cvt_pk_bf16_f32 v130, v0, v1
	v_mov_b64_e32 v[0:1], s[46:47]
	v_cvt_pk_bf16_f32 v131, v2, v3
	v_mad_i64_i32 v[2:3], s[46:47], v182, s57, v[0:1]
	v_lshl_add_u64 v[2:3], v[2:3], 0, v[184:185]
	v_lshl_add_u64 v[2:3], v[2:3], 0, v[160:161]
	s_add_i32 s94, s6, s80
	v_lshl_add_u64 v[2:3], v[2:3], 0, v[156:157]
	s_mov_b32 m0, s94
	s_waitcnt vmcnt(0)
	s_waitcnt vmcnt(0)
	s_barrier
	global_load_lds_dwordx4 v[2:3], off
	v_mad_i64_i32 v[2:3], s[46:47], v186, s57, v[0:1]
	v_lshl_add_u64 v[2:3], v[2:3], 0, v[188:189]
	v_lshl_add_u64 v[2:3], v[2:3], 0, v[190:191]
	s_add_i32 s46, s7, s80
	v_lshl_add_u64 v[2:3], v[2:3], 0, v[192:193]
	s_mov_b32 m0, s46
	s_add_i32 s47, s38, s80
	global_load_lds_dwordx4 v[2:3], off
	v_mad_i64_i32 v[2:3], s[96:97], v194, s57, v[0:1]
	v_lshl_add_u64 v[2:3], v[2:3], 0, v[196:197]
	v_mad_i64_i32 v[0:1], s[96:97], v202, s57, v[0:1]
	v_lshl_add_u64 v[2:3], v[2:3], 0, v[198:199]
	v_lshl_add_u64 v[0:1], v[0:1], 0, v[204:205]
	v_lshl_add_u64 v[2:3], v[2:3], 0, v[200:201]
	s_mov_b32 m0, s47
	v_lshl_add_u64 v[0:1], v[0:1], 0, v[206:207]
	s_add_i32 s93, s40, s80
	global_load_lds_dwordx4 v[2:3], off
	v_lshl_add_u64 v[0:1], v[0:1], 0, v[208:209]
	s_mov_b32 m0, s93
	v_lshl_add_u64 v[2:3], s[4:5], 0, v[188:189]
	global_load_lds_dwordx4 v[0:1], off
	v_mul_f32_e32 v0, 0x3fb8aa3b, v69
	v_exp_f32_e32 v179, v0
	v_lshl_add_u64 v[0:1], s[4:5], 0, v[184:185]
	v_lshl_add_u64 v[0:1], v[0:1], 0, v[160:161]
	v_lshl_add_u64 v[0:1], v[0:1], 0, v[156:157]
	v_lshl_add_u64 v[2:3], v[2:3], 0, v[190:191]
	v_lshl_add_u64 v[4:5], s[4:5], 0, v[196:197]
	v_lshlrev_b64 v[210:211], 10, v[182:183]
	v_lshl_add_u64 v[2:3], v[2:3], 0, v[192:193]
	v_lshl_add_u64 v[4:5], v[4:5], 0, v[198:199]
	v_lshl_add_u64 v[6:7], s[4:5], 0, v[204:205]
	v_lshl_add_u64 v[222:223], v[0:1], 0, v[210:211]
	v_lshlrev_b64 v[212:213], 10, v[186:187]
	v_lshlrev_b64 v[214:215], 10, v[194:195]
	v_bitop3_b32 v183, v68, 16, s41 bitop3:0x36
	v_add_u32_e32 v195, s68, v175
	ds_read_b64_tr_b16 v[0:1], v195 offset:0
	v_lshl_add_u64 v[4:5], v[4:5], 0, v[200:201]
	v_lshl_add_u64 v[6:7], v[6:7], 0, v[206:207]
	v_lshl_add_u64 v[224:225], v[2:3], 0, v[212:213]
	v_lshlrev_b64 v[216:217], 10, v[202:203]
	v_add_u32_e32 v203, s81, v183
	ds_read_b64_tr_b16 v[2:3], v203 offset:0
	v_lshl_add_u64 v[6:7], v[6:7], 0, v[208:209]
	v_lshl_add_u64 v[218:219], v[4:5], 0, v[214:215]
	ds_read_b64_tr_b16 v[4:5], v195 offset:0x200
	v_lshl_add_u64 v[220:221], v[6:7], 0, v[216:217]
	ds_read_b64_tr_b16 v[6:7], v203 offset:0x200
	ds_read_b64_tr_b16 v[32:33], v195 offset:0x400
	ds_read_b64_tr_b16 v[34:35], v203 offset:0x400
	ds_read_b64_tr_b16 v[48:49], v195 offset:0x600
	ds_read_b64_tr_b16 v[50:51], v203 offset:0x600
	s_waitcnt lgkmcnt(0)
; #define VM_WAIT() asm volatile("s_waitcnt vmcnt(0)" ::: "memory")
; template <int DK, int DV, bool MLSTM>
; __device__ __forceinline__ void out_unit2(LAS unsigned char* lds, LAS unsigned char* ldstab, const OutArgs a, const int wv) {
;     ...
; #pragma unroll
;     for (int kb = 0; kb < 4; ++kb) { LA_PK4(p[kb], 0, pa[2 * kb]); LA_PK4(p[kb], 8, pa[2 * kb + 1]); }
;     ...
;     f32x16 o[NB];
; #pragma unroll
;     for (int nb = 0; nb < NB; ++nb) o[nb] = (f32x16){};
;     ...
; #pragma unroll
;     for (int pc = 0; pc < 4; ++pc) {
;         VM_WAIT(); __syncthreads();
;         OUT_DMA(pc + 1);
;         const bf16x8 af0 = pa[2 * pc], af1 = pa[2 * pc + 1];
;         OUT_MMA(pc & 1);
	v_permlane32_swap_b32_e32 v64, v66
	v_permlane32_swap_b32_e32 v65, v67
	v_permlane32_swap_b32_e32 v144, v146
	v_permlane32_swap_b32_e32 v140, v142
	v_permlane32_swap_b32_e32 v136, v138
	v_permlane32_swap_b32_e32 v132, v134
	v_add_u32_e32 v181, 0x100, v183
	v_mul_f32_e32 v235, 0x3fb8aa3b, v71
	v_permlane32_swap_b32_e32 v152, v154
	v_permlane32_swap_b32_e32 v153, v155
	v_permlane32_swap_b32_e32 v148, v150
	v_permlane32_swap_b32_e32 v149, v151
	v_permlane32_swap_b32_e32 v145, v147
	v_permlane32_swap_b32_e32 v141, v143
	v_permlane32_swap_b32_e32 v137, v139
	v_permlane32_swap_b32_e32 v133, v135
	v_permlane32_swap_b32_e32 v128, v130
	v_permlane32_swap_b32_e32 v129, v131
	ds_read_b64_tr_b16 v[68:69], v195 offset:0x1000
	ds_read_b64_tr_b16 v[70:71], v203 offset:0x1000
	ds_read_b64_tr_b16 v[72:73], v195 offset:0x1200
	v_mfma_f32_32x32x16_bf16 v[16:31], v[64:67], v[0:3], 0
	ds_read_b64_tr_b16 v[74:75], v203 offset:0x1200
	ds_read_b64_tr_b16 v[76:77], v195 offset:0x1400
	ds_read_b64_tr_b16 v[78:79], v203 offset:0x1400
	ds_read_b64_tr_b16 v[80:81], v195 offset:0x1600
	ds_read_b64_tr_b16 v[82:83], v203 offset:0x1600
	s_waitcnt lgkmcnt(0)
	v_mfma_f32_32x32x16_bf16 v[0:15], v[64:67], v[4:7], 0
	v_mfma_f32_32x32x16_bf16 v[32:47], v[64:67], v[32:35], 0
	v_mfma_f32_32x32x16_bf16 v[48:63], v[64:67], v[48:51], 0
	v_mfma_f32_32x32x16_bf16 v[16:31], v[152:155], v[68:71], v[16:31]
	v_add_u32_e32 v252, s70, v175
	ds_read_b64_tr_b16 v[68:69], v252 offset:0
	v_add_u32_e32 v253, s82, v183
	ds_read_b64_tr_b16 v[70:71], v253 offset:0
	v_mfma_f32_32x32x16_bf16 v[0:15], v[152:155], v[72:75], v[0:15]
	ds_read_b64_tr_b16 v[72:73], v252 offset:0x200
	ds_read_b64_tr_b16 v[74:75], v253 offset:0x200
	v_mfma_f32_32x32x16_bf16 v[32:47], v[152:155], v[76:79], v[32:47]
	ds_read_b64_tr_b16 v[76:77], v252 offset:0x400
	ds_read_b64_tr_b16 v[78:79], v253 offset:0x400
	ds_read_b64_tr_b16 v[236:237], v252 offset:0x600
	ds_read_b64_tr_b16 v[238:239], v253 offset:0x600
	s_waitcnt lgkmcnt(0)
	v_mfma_f32_32x32x16_bf16 v[48:63], v[152:155], v[80:83], v[48:63]
	v_mfma_f32_32x32x16_bf16 v[96:111], v[64:67], v[68:71], 0
	v_mfma_f32_32x32x16_bf16 v[112:127], v[64:67], v[72:75], 0
	v_mfma_f32_32x32x16_bf16 v[80:95], v[64:67], v[76:79], 0
	v_mfma_f32_32x32x16_bf16 v[64:79], v[64:67], v[236:239], 0
	ds_read_b64_tr_b16 v[236:237], v252 offset:0x1000
	ds_read_b64_tr_b16 v[238:239], v253 offset:0x1000
	ds_read_b64_tr_b16 v[240:241], v252 offset:0x1200
	ds_read_b64_tr_b16 v[242:243], v253 offset:0x1200
	ds_read_b64_tr_b16 v[244:245], v252 offset:0x1400
	ds_read_b64_tr_b16 v[246:247], v253 offset:0x1400
	ds_read_b64_tr_b16 v[248:249], v252 offset:0x1600
	ds_read_b64_tr_b16 v[250:251], v253 offset:0x1600
	s_waitcnt lgkmcnt(0)
	s_add_u32 s96, s39, 0xc1000
	s_addc_u32 s97, s16, 0
	v_mfma_f32_32x32x16_bf16 v[96:111], v[152:155], v[236:239], v[96:111]
	v_mov_b64_e32 v[236:237], s[96:97]
	v_mad_i64_i32 v[238:239], s[96:97], v182, s57, v[236:237]
	v_lshl_add_u64 v[238:239], v[238:239], 0, v[184:185]
	v_lshl_add_u64 v[238:239], v[238:239], 0, v[160:161]
	s_mov_b32 m0, s42
	v_lshl_add_u64 v[238:239], v[238:239], 0, v[156:157]
	s_waitcnt vmcnt(0)
	s_waitcnt vmcnt(0) lgkmcnt(0)
	s_barrier
	global_load_lds_dwordx4 v[238:239], off
	v_mad_i64_i32 v[238:239], s[96:97], v186, s57, v[236:237]
	v_lshl_add_u64 v[238:239], v[238:239], 0, v[188:189]
	v_lshl_add_u64 v[238:239], v[238:239], 0, v[190:191]
	v_lshl_add_u64 v[238:239], v[238:239], 0, v[192:193]
	s_mov_b32 m0, s43
	v_mfma_f32_32x32x16_bf16 v[112:127], v[152:155], v[240:243], v[112:127]
	global_load_lds_dwordx4 v[238:239], off
	v_mad_i64_i32 v[238:239], s[96:97], v194, s57, v[236:237]
	v_lshl_add_u64 v[238:239], v[238:239], 0, v[196:197]
	v_mad_i64_i32 v[236:237], s[96:97], v202, s57, v[236:237]
	v_lshl_add_u64 v[238:239], v[238:239], 0, v[198:199]
	v_lshl_add_u64 v[236:237], v[236:237], 0, v[204:205]
	v_lshl_add_u64 v[238:239], v[238:239], 0, v[200:201]
	s_mov_b32 m0, s44
	v_lshl_add_u64 v[236:237], v[236:237], 0, v[206:207]
	global_load_lds_dwordx4 v[238:239], off
	v_lshl_add_u64 v[236:237], v[236:237], 0, v[208:209]
	s_mov_b32 m0, s45
	v_mfma_f32_32x32x16_bf16 v[80:95], v[152:155], v[244:247], v[80:95]
	global_load_lds_dwordx4 v[236:237], off
	v_add_u32_e32 v254, s80, v175
	v_add_u32_e32 v255, s83, v183
	v_mfma_f32_32x32x16_bf16 v[64:79], v[152:155], v[248:251], v[64:79]
	ds_read_b64_tr_b16 v[152:153], v254 offset:0
	ds_read_b64_tr_b16 v[154:155], v255 offset:0
	ds_read_b64_tr_b16 v[236:237], v254 offset:0x200
	ds_read_b64_tr_b16 v[238:239], v255 offset:0x200
	ds_read_b64_tr_b16 v[240:241], v254 offset:0x400
	ds_read_b64_tr_b16 v[242:243], v255 offset:0x400
	ds_read_b64_tr_b16 v[244:245], v254 offset:0x600
	ds_read_b64_tr_b16 v[246:247], v255 offset:0x600
	s_waitcnt lgkmcnt(0)
	s_nop 0
	v_mfma_f32_32x32x16_bf16 v[16:31], v[148:151], v[152:155], v[16:31]
	ds_read_b64_tr_b16 v[152:153], v254 offset:0x1000
	ds_read_b64_tr_b16 v[154:155], v255 offset:0x1000
	v_mfma_f32_32x32x16_bf16 v[0:15], v[148:151], v[236:239], v[0:15]
	ds_read_b64_tr_b16 v[236:237], v254 offset:0x1200
	ds_read_b64_tr_b16 v[238:239], v255 offset:0x1200
	v_mfma_f32_32x32x16_bf16 v[32:47], v[148:151], v[240:243], v[32:47]
	ds_read_b64_tr_b16 v[240:241], v254 offset:0x1400
	ds_read_b64_tr_b16 v[242:243], v255 offset:0x1400
	ds_read_b64_tr_b16 v[248:249], v254 offset:0x1600
	ds_read_b64_tr_b16 v[250:251], v255 offset:0x1600
	s_waitcnt lgkmcnt(0)
; #define VM_WAIT() asm volatile("s_waitcnt vmcnt(0)" ::: "memory")
; template <int DK, int DV, bool MLSTM>
; __device__ __forceinline__ void out_unit2(LAS unsigned char* lds, LAS unsigned char* ldstab, const OutArgs a, const int wv) {
;     ...
; #pragma unroll
;     for (int pc = 0; pc < 4; ++pc) {
;         VM_WAIT(); __syncthreads();
;         OUT_DMA(pc + 1);
;         const bf16x8 af0 = pa[2 * pc], af1 = pa[2 * pc + 1];
;         OUT_MMA(pc & 1);
	v_mfma_f32_32x32x16_bf16 v[48:63], v[148:151], v[244:247], v[48:63]
	v_mfma_f32_32x32x16_bf16 v[16:31], v[144:147], v[152:155], v[16:31]
	v_add_u32_e32 v226, s84, v175
	ds_read_b64_tr_b16 v[152:153], v226 offset:0
	v_add_u32_e32 v227, s85, v183
	ds_read_b64_tr_b16 v[154:155], v227 offset:0
	v_mfma_f32_32x32x16_bf16 v[0:15], v[144:147], v[236:239], v[0:15]
	ds_read_b64_tr_b16 v[236:237], v226 offset:0x200
	ds_read_b64_tr_b16 v[238:239], v227 offset:0x200
	v_mfma_f32_32x32x16_bf16 v[32:47], v[144:147], v[240:243], v[32:47]
	ds_read_b64_tr_b16 v[240:241], v226 offset:0x400
	ds_read_b64_tr_b16 v[242:243], v227 offset:0x400
	ds_read_b64_tr_b16 v[244:245], v226 offset:0x600
	ds_read_b64_tr_b16 v[246:247], v227 offset:0x600
	s_waitcnt lgkmcnt(0)
	v_mfma_f32_32x32x16_bf16 v[48:63], v[144:147], v[248:251], v[48:63]
	v_mfma_f32_32x32x16_bf16 v[96:111], v[148:151], v[152:155], v[96:111]
	ds_read_b64_tr_b16 v[152:153], v226 offset:0x1000
	ds_read_b64_tr_b16 v[154:155], v227 offset:0x1000
	v_mfma_f32_32x32x16_bf16 v[112:127], v[148:151], v[236:239], v[112:127]
	ds_read_b64_tr_b16 v[236:237], v226 offset:0x1200
	ds_read_b64_tr_b16 v[238:239], v227 offset:0x1200
	v_mfma_f32_32x32x16_bf16 v[80:95], v[148:151], v[240:243], v[80:95]
	ds_read_b64_tr_b16 v[240:241], v226 offset:0x1400
	ds_read_b64_tr_b16 v[242:243], v227 offset:0x1400
	ds_read_b64_tr_b16 v[248:249], v226 offset:0x1600
	ds_read_b64_tr_b16 v[250:251], v227 offset:0x1600
	s_waitcnt lgkmcnt(0)
	v_mfma_f32_32x32x16_bf16 v[64:79], v[148:151], v[244:247], v[64:79]
	s_mov_b32 m0, s94
	s_add_u32 s94, s39, 0x121000
	s_addc_u32 s95, s16, 0
	v_mov_b64_e32 v[148:149], s[94:95]
	v_mad_i64_i32 v[150:151], s[94:95], v182, s57, v[148:149]
	v_lshl_add_u64 v[150:151], v[150:151], 0, v[184:185]
	v_lshl_add_u64 v[150:151], v[150:151], 0, v[160:161]
	v_lshl_add_u64 v[150:151], v[150:151], 0, v[156:157]
	s_waitcnt vmcnt(0)
	s_waitcnt vmcnt(0) lgkmcnt(0)
	s_barrier
	global_load_lds_dwordx4 v[150:151], off
	v_mad_i64_i32 v[150:151], s[94:95], v186, s57, v[148:149]
	v_lshl_add_u64 v[150:151], v[150:151], 0, v[188:189]
	v_lshl_add_u64 v[150:151], v[150:151], 0, v[190:191]
	v_lshl_add_u64 v[150:151], v[150:151], 0, v[192:193]
	s_mov_b32 m0, s46
	v_mfma_f32_32x32x16_bf16 v[96:111], v[144:147], v[152:155], v[96:111]
	global_load_lds_dwordx4 v[150:151], off
	v_mad_i64_i32 v[150:151], s[94:95], v194, s57, v[148:149]
	v_lshl_add_u64 v[150:151], v[150:151], 0, v[196:197]
	s_mov_b32 m0, s47
	v_mad_i64_i32 v[148:149], s[46:47], v202, s57, v[148:149]
	v_lshl_add_u64 v[150:151], v[150:151], 0, v[198:199]
	v_lshl_add_u64 v[148:149], v[148:149], 0, v[204:205]
	v_lshl_add_u64 v[150:151], v[150:151], 0, v[200:201]
	v_lshl_add_u64 v[148:149], v[148:149], 0, v[206:207]
	global_load_lds_dwordx4 v[150:151], off
	v_lshl_add_u64 v[148:149], v[148:149], 0, v[208:209]
	s_mov_b32 m0, s93
	v_mfma_f32_32x32x16_bf16 v[112:127], v[144:147], v[236:239], v[112:127]
	global_load_lds_dwordx4 v[148:149], off
	v_mfma_f32_32x32x16_bf16 v[80:95], v[144:147], v[240:243], v[80:95]
	v_mfma_f32_32x32x16_bf16 v[64:79], v[144:147], v[248:251], v[64:79]
	ds_read_b64_tr_b16 v[144:145], v195 offset:0
	ds_read_b64_tr_b16 v[146:147], v203 offset:0
	ds_read_b64_tr_b16 v[148:149], v195 offset:0x200
	ds_read_b64_tr_b16 v[150:151], v203 offset:0x200
	ds_read_b64_tr_b16 v[152:153], v195 offset:0x400
	ds_read_b64_tr_b16 v[154:155], v203 offset:0x400
	ds_read_b64_tr_b16 v[182:183], v195 offset:0x600
	ds_read_b64_tr_b16 v[184:185], v203 offset:0x600
	s_waitcnt lgkmcnt(0)
	s_nop 0
	v_mfma_f32_32x32x16_bf16 v[16:31], v[140:143], v[144:147], v[16:31]
	ds_read_b64_tr_b16 v[144:145], v195 offset:0x1000
	ds_read_b64_tr_b16 v[146:147], v203 offset:0x1000
	v_mfma_f32_32x32x16_bf16 v[0:15], v[140:143], v[148:151], v[0:15]
	ds_read_b64_tr_b16 v[148:149], v195 offset:0x1200
	ds_read_b64_tr_b16 v[150:151], v203 offset:0x1200
	v_mfma_f32_32x32x16_bf16 v[32:47], v[140:143], v[152:155], v[32:47]
	ds_read_b64_tr_b16 v[152:153], v195 offset:0x1400
	ds_read_b64_tr_b16 v[154:155], v203 offset:0x1400
	ds_read_b64_tr_b16 v[186:187], v195 offset:0x1600
	ds_read_b64_tr_b16 v[188:189], v203 offset:0x1600
	s_waitcnt lgkmcnt(0)
	v_mfma_f32_32x32x16_bf16 v[48:63], v[140:143], v[182:185], v[48:63]
	v_mfma_f32_32x32x16_bf16 v[16:31], v[136:139], v[144:147], v[16:31]
	ds_read_b64_tr_b16 v[144:145], v252 offset:0
	ds_read_b64_tr_b16 v[146:147], v253 offset:0
	v_mfma_f32_32x32x16_bf16 v[0:15], v[136:139], v[148:151], v[0:15]
	ds_read_b64_tr_b16 v[148:149], v252 offset:0x200
	ds_read_b64_tr_b16 v[150:151], v253 offset:0x200
	v_mfma_f32_32x32x16_bf16 v[32:47], v[136:139], v[152:155], v[32:47]
	ds_read_b64_tr_b16 v[152:153], v252 offset:0x400
	ds_read_b64_tr_b16 v[154:155], v253 offset:0x400
	ds_read_b64_tr_b16 v[182:183], v252 offset:0x600
	ds_read_b64_tr_b16 v[184:185], v253 offset:0x600
	s_waitcnt lgkmcnt(0)
	v_mfma_f32_32x32x16_bf16 v[48:63], v[136:139], v[186:189], v[48:63]
	v_mfma_f32_32x32x16_bf16 v[96:111], v[140:143], v[144:147], v[96:111]
	ds_read_b64_tr_b16 v[144:145], v252 offset:0x1000
	ds_read_b64_tr_b16 v[146:147], v253 offset:0x1000
	v_mfma_f32_32x32x16_bf16 v[112:127], v[140:143], v[148:151], v[112:127]
	ds_read_b64_tr_b16 v[148:149], v252 offset:0x1200
	ds_read_b64_tr_b16 v[150:151], v253 offset:0x1200
	v_mfma_f32_32x32x16_bf16 v[80:95], v[140:143], v[152:155], v[80:95]
	ds_read_b64_tr_b16 v[152:153], v252 offset:0x1400
	ds_read_b64_tr_b16 v[154:155], v253 offset:0x1400
	ds_read_b64_tr_b16 v[186:187], v252 offset:0x1600
	ds_read_b64_tr_b16 v[188:189], v253 offset:0x1600
	s_waitcnt lgkmcnt(0)
	v_mfma_f32_32x32x16_bf16 v[64:79], v[140:143], v[182:185], v[64:79]
	s_mov_b32 m0, s42
	s_waitcnt vmcnt(0)
	s_waitcnt vmcnt(0) lgkmcnt(0)
	s_barrier
; #define VM_WAIT() asm volatile("s_waitcnt vmcnt(0)" ::: "memory")
; template <int DK, int DV, bool MLSTM>
; __device__ __forceinline__ void out_unit2(LAS unsigned char* lds, LAS unsigned char* ldstab, const OutArgs a, const int wv) {
;     ...
; #pragma unroll
;     for (int pc = 0; pc < 4; ++pc) {
;         VM_WAIT(); __syncthreads();
;         OUT_DMA(pc + 1);
;         const bf16x8 af0 = pa[2 * pc], af1 = pa[2 * pc + 1];
;         OUT_MMA(pc & 1);
;     }
; #pragma unroll 1
;     for (int pc = 4; pc < 4 + 2 * NCP; ++pc) {
;         VM_WAIT(); __syncthreads();
;         if (pc + 1 < 4 + 2 * NCP) OUT_DMA(pc + 1);
;         const int cq = pc - 4, dirb = cq >= NCP, cp = dirb ? cq - NCP : cq;
;         const float qs = dirb ? qsb : qsf;
;         const unsigned qa = QP + (cp >> 2) * 32768u + 512u * (cp & 3) + 8192u * rb;
;         const bf16x8 af0 = scale_frag(lds_r128(qa + rb0), qs), af1 = scale_frag(lds_r128(qa + rb1), qs);
	global_load_lds_dwordx4 v[222:223], off
	s_mov_b32 m0, s43
	v_mfma_f32_32x32x16_bf16 v[96:111], v[136:139], v[144:147], v[96:111]
	global_load_lds_dwordx4 v[224:225], off
	s_mov_b32 m0, s44
	s_nop 0
	global_load_lds_dwordx4 v[218:219], off
	s_mov_b32 m0, s45
	v_mfma_f32_32x32x16_bf16 v[112:127], v[136:139], v[148:151], v[112:127]
	global_load_lds_dwordx4 v[220:221], off
	ds_read_b64_tr_b16 v[140:141], v254 offset:0
	ds_read_b64_tr_b16 v[142:143], v255 offset:0
	ds_read_b64_tr_b16 v[144:145], v254 offset:0x200
	ds_read_b64_tr_b16 v[146:147], v255 offset:0x200
	ds_read_b64_tr_b16 v[148:149], v254 offset:0x400
	v_mfma_f32_32x32x16_bf16 v[80:95], v[136:139], v[152:155], v[80:95]
	ds_read_b64_tr_b16 v[150:151], v255 offset:0x400
	ds_read_b64_tr_b16 v[152:153], v254 offset:0x600
	ds_read_b64_tr_b16 v[154:155], v255 offset:0x600
	s_waitcnt lgkmcnt(0)
	v_mfma_f32_32x32x16_bf16 v[64:79], v[136:139], v[186:189], v[64:79]
	ds_read_b64_tr_b16 v[136:137], v254 offset:0x1000
	ds_read_b64_tr_b16 v[138:139], v255 offset:0x1000
	v_mfma_f32_32x32x16_bf16 v[16:31], v[132:135], v[140:143], v[16:31]
	ds_read_b64_tr_b16 v[140:141], v254 offset:0x1200
	ds_read_b64_tr_b16 v[142:143], v255 offset:0x1200
	v_mfma_f32_32x32x16_bf16 v[0:15], v[132:135], v[144:147], v[0:15]
	ds_read_b64_tr_b16 v[144:145], v254 offset:0x1400
	ds_read_b64_tr_b16 v[146:147], v255 offset:0x1400
	v_mfma_f32_32x32x16_bf16 v[32:47], v[132:135], v[148:151], v[32:47]
	ds_read_b64_tr_b16 v[148:149], v254 offset:0x1600
	ds_read_b64_tr_b16 v[150:151], v255 offset:0x1600
	s_waitcnt lgkmcnt(0)
	v_mfma_f32_32x32x16_bf16 v[48:63], v[132:135], v[152:155], v[48:63]
	v_mfma_f32_32x32x16_bf16 v[16:31], v[128:131], v[136:139], v[16:31]
	ds_read_b64_tr_b16 v[136:137], v226 offset:0
	ds_read_b64_tr_b16 v[138:139], v227 offset:0
	v_mfma_f32_32x32x16_bf16 v[0:15], v[128:131], v[140:143], v[0:15]
	ds_read_b64_tr_b16 v[140:141], v226 offset:0x200
	ds_read_b64_tr_b16 v[142:143], v227 offset:0x200
	v_mfma_f32_32x32x16_bf16 v[32:47], v[128:131], v[144:147], v[32:47]
	ds_read_b64_tr_b16 v[144:145], v226 offset:0x400
	ds_read_b64_tr_b16 v[146:147], v227 offset:0x400
	ds_read_b64_tr_b16 v[152:153], v226 offset:0x600
	ds_read_b64_tr_b16 v[154:155], v227 offset:0x600
	s_waitcnt lgkmcnt(0)
	v_mfma_f32_32x32x16_bf16 v[48:63], v[128:131], v[148:151], v[48:63]
	v_mfma_f32_32x32x16_bf16 v[96:111], v[132:135], v[136:139], v[96:111]
	ds_read_b64_tr_b16 v[136:137], v226 offset:0x1000
	ds_read_b64_tr_b16 v[138:139], v227 offset:0x1000
	v_mfma_f32_32x32x16_bf16 v[112:127], v[132:135], v[140:143], v[112:127]
	ds_read_b64_tr_b16 v[140:141], v226 offset:0x1200
	ds_read_b64_tr_b16 v[142:143], v227 offset:0x1200
	v_mfma_f32_32x32x16_bf16 v[80:95], v[132:135], v[144:147], v[80:95]
	ds_read_b64_tr_b16 v[146:147], v226 offset:0x1400
	ds_read_b64_tr_b16 v[148:149], v227 offset:0x1400
	ds_read_b64_tr_b16 v[182:183], v226 offset:0x1600
	ds_read_b64_tr_b16 v[184:185], v227 offset:0x1600
	s_waitcnt lgkmcnt(0)
	v_mfma_f32_32x32x16_bf16 v[64:79], v[132:135], v[152:155], v[64:79]
	v_mfma_f32_32x32x16_bf16 v[96:111], v[128:131], v[136:139], v[96:111]
	v_add_u32_e32 v226, s13, v173
	v_add_u32_e32 v227, s13, v177
	ds_read_b128 v[236:239], v226 offset:0
	ds_read_b128 v[240:243], v227 offset:0
	ds_read_b128 v[244:247], v226 offset:512
	ds_read_b128 v[248:251], v227 offset:512
	ds_read_b128 v[252:255], v226 offset:1024
	ds_read_b128 v[218:221], v227 offset:1024
	ds_read_b128 v[222:225], v226 offset:1536
	ds_read_b128 v[206:209], v227 offset:1536
	v_exp_f32_e32 v144, v235
	s_mov_b32 s39, 0x28000
	s_movk_i32 s41, 0x800
	v_lshlrev_b32_e32 v160, 1, v162
	v_lshlrev_b32_e32 v132, 1, v170
	v_lshlrev_b32_e32 v134, 1, v172
	v_lshlrev_b32_e32 v136, 1, v174
	v_mfma_f32_32x32x16_bf16 v[112:127], v[128:131], v[140:143], v[112:127]
	v_lshlrev_b32_e32 v138, 1, v176
	v_lshlrev_b32_e32 v140, 1, v178
	v_lshlrev_b32_e32 v142, 1, v180
	v_mfma_f32_32x32x16_bf16 v[80:95], v[128:131], v[146:149], v[80:95]
	v_mfma_f32_32x32x16_bf16 v[64:79], v[128:131], v[182:185], v[64:79]
	v_lshl_add_u64 v[198:199], v[158:159], 1, v[210:211]
	v_lshl_add_u64 v[198:199], v[198:199], 0, v[160:161]
	v_mov_b32_e32 v157, v161
	v_lshl_add_u64 v[198:199], v[198:199], 0, v[156:157]
	v_mov_b32_e32 v133, v161
	v_mov_b32_e32 v135, v161
	v_lshl_add_u64 v[200:201], v[164:165], 1, v[212:213]
	v_lshl_add_u64 v[200:201], v[200:201], 0, v[132:133]
	v_lshl_add_u64 v[200:201], v[200:201], 0, v[134:135]
	v_mov_b32_e32 v137, v161
	v_mov_b32_e32 v139, v161
	v_lshl_add_u64 v[202:203], v[166:167], 1, v[214:215]
	v_lshl_add_u64 v[202:203], v[202:203], 0, v[136:137]
	v_lshl_add_u64 v[202:203], v[202:203], 0, v[138:139]
	v_mov_b32_e32 v141, v161
	v_mov_b32_e32 v143, v161
	v_lshl_add_u64 v[204:205], v[168:169], 1, v[216:217]
	v_lshl_add_u64 v[204:205], v[204:205], 0, v[140:141]
	v_lshl_add_u64 v[204:205], v[204:205], 0, v[142:143]
	s_waitcnt vmcnt(0) lgkmcnt(0)
	s_barrier
; #define VM_WAIT() asm volatile("s_waitcnt vmcnt(0)" ::: "memory")
; template <int DK, int DV, bool MLSTM>
; __device__ __forceinline__ void out_unit2(LAS unsigned char* lds, LAS unsigned char* ldstab, const OutArgs a, const int wv) {
;     ...
; #pragma unroll
;     for (int pc = 0; pc < 4; ++pc) {
;         VM_WAIT(); __syncthreads();
;         OUT_DMA(pc + 1);
;         const bf16x8 af0 = pa[2 * pc], af1 = pa[2 * pc + 1];
;         OUT_MMA(pc & 1);
;     }
; #pragma unroll 1
;     for (int pc = 4; pc < 4 + 2 * NCP; ++pc) {
;         VM_WAIT(); __syncthreads();
;         if (pc + 1 < 4 + 2 * NCP) OUT_DMA(pc + 1);
;         const int cq = pc - 4, dirb = cq >= NCP, cp = dirb ? cq - NCP : cq;
;         const float qs = dirb ? qsb : qsf;
;         const unsigned qa = QP + (cp >> 2) * 32768u + 512u * (cp & 3) + 8192u * rb;
;         const bf16x8 af0 = scale_frag(lds_r128(qa + rb0), qs), af1 = scale_frag(lds_r128(qa + rb1), qs);
	s_add_u32 s42, s4, 0x8000
	s_addc_u32 s43, s5, 0
	v_lshl_add_u64 v[128:129], s[42:43], 0, v[198:199]
	v_lshl_add_u64 v[130:131], s[42:43], 0, v[200:201]
	v_lshl_add_u64 v[146:147], s[42:43], 0, v[202:203]
	v_lshl_add_u64 v[148:149], s[42:43], 0, v[204:205]
	s_add_i32 m0, s6, 0x18000
	s_nop 0
	global_load_lds_dwordx4 v[128:129], off
	s_add_i32 m0, s7, 0x18000
	s_nop 0
	global_load_lds_dwordx4 v[130:131], off
	s_add_i32 m0, s38, 0x18000
	s_nop 0
	global_load_lds_dwordx4 v[146:147], off
	s_add_i32 m0, s40, 0x18000
	s_nop 0
	global_load_lds_dwordx4 v[148:149], off
	s_add_u32 s42, s4, 0x10000
	s_addc_u32 s43, s5, 0
	v_lshl_add_u64 v[128:129], s[42:43], 0, v[198:199]
	v_lshl_add_u64 v[130:131], s[42:43], 0, v[200:201]
	v_lshl_add_u64 v[146:147], s[42:43], 0, v[202:203]
	v_lshl_add_u64 v[148:149], s[42:43], 0, v[204:205]
	s_mov_b32 m0, s6
	s_nop 0
	global_load_lds_dwordx4 v[128:129], off
	s_mov_b32 m0, s7
	s_nop 0
	global_load_lds_dwordx4 v[130:131], off
	s_mov_b32 m0, s38
	s_nop 0
	global_load_lds_dwordx4 v[146:147], off
	s_mov_b32 m0, s40
	s_nop 0
	global_load_lds_dwordx4 v[148:149], off
	v_lshlrev_b32_e32 v135, 16, v236
	v_and_b32_e32 v137, 0xffff0000, v236
	v_mul_f32_e32 v135, v179, v135
	v_mul_f32_e32 v137, v179, v137
	v_cvt_pk_bf16_f32 v128, v135, v137
	v_lshlrev_b32_e32 v135, 16, v237
	v_and_b32_e32 v137, 0xffff0000, v237
	v_mul_f32_e32 v135, v179, v135
	v_mul_f32_e32 v137, v179, v137
	v_cvt_pk_bf16_f32 v129, v135, v137
	v_lshlrev_b32_e32 v135, 16, v238
	v_and_b32_e32 v137, 0xffff0000, v238
	v_mul_f32_e32 v135, v179, v135
	v_mul_f32_e32 v137, v179, v137
	v_cvt_pk_bf16_f32 v130, v135, v137
	v_lshlrev_b32_e32 v135, 16, v239
	v_and_b32_e32 v137, 0xffff0000, v239
	v_mul_f32_e32 v135, v179, v135
	v_mul_f32_e32 v137, v179, v137
	v_cvt_pk_bf16_f32 v131, v135, v137
	v_lshlrev_b32_e32 v135, 16, v240
	v_and_b32_e32 v137, 0xffff0000, v240
	v_mul_f32_e32 v135, v179, v135
	v_mul_f32_e32 v137, v179, v137
	v_cvt_pk_bf16_f32 v146, v135, v137
	v_lshlrev_b32_e32 v135, 16, v241
	v_and_b32_e32 v137, 0xffff0000, v241
	v_mul_f32_e32 v135, v179, v135
	v_mul_f32_e32 v137, v179, v137
	v_cvt_pk_bf16_f32 v147, v135, v137
	v_lshlrev_b32_e32 v135, 16, v242
	v_and_b32_e32 v137, 0xffff0000, v242
	v_mul_f32_e32 v135, v179, v135
	v_mul_f32_e32 v137, v179, v137
	v_cvt_pk_bf16_f32 v148, v135, v137
	v_lshlrev_b32_e32 v135, 16, v243
	v_and_b32_e32 v137, 0xffff0000, v243
	v_mul_f32_e32 v135, v179, v135
	v_mul_f32_e32 v137, v179, v137
	v_cvt_pk_bf16_f32 v149, v135, v137
	v_add_u32_e32 v133, 0x10000, v175
	ds_read_b64_tr_b16 v[150:151], v133 offset:0
	v_add_u32_e32 v135, 0x10000, v181
	ds_read_b64_tr_b16 v[152:153], v135 offset:0
	ds_read_b64_tr_b16 v[182:183], v133 offset:0x200
	ds_read_b64_tr_b16 v[184:185], v135 offset:0x200
	ds_read_b64_tr_b16 v[186:187], v133 offset:0x400
	ds_read_b64_tr_b16 v[188:189], v135 offset:0x400
	ds_read_b64_tr_b16 v[190:191], v133 offset:0x600
	ds_read_b64_tr_b16 v[192:193], v135 offset:0x600
	s_waitcnt lgkmcnt(0)
	s_nop 0
	v_mfma_f32_32x32x16_bf16 v[16:31], v[128:131], v[150:153], v[16:31]
	ds_read_b64_tr_b16 v[150:151], v133 offset:0x1000
	ds_read_b64_tr_b16 v[152:153], v135 offset:0x1000
	v_mfma_f32_32x32x16_bf16 v[0:15], v[128:131], v[182:185], v[0:15]
	ds_read_b64_tr_b16 v[182:183], v133 offset:0x1200
	ds_read_b64_tr_b16 v[184:185], v135 offset:0x1200
	v_mfma_f32_32x32x16_bf16 v[32:47], v[128:131], v[186:189], v[32:47]
	ds_read_b64_tr_b16 v[186:187], v133 offset:0x1400
	ds_read_b64_tr_b16 v[188:189], v135 offset:0x1400
	ds_read_b64_tr_b16 v[194:195], v133 offset:0x1600
	ds_read_b64_tr_b16 v[196:197], v135 offset:0x1600
	s_waitcnt lgkmcnt(0)
	v_mfma_f32_32x32x16_bf16 v[48:63], v[128:131], v[190:193], v[48:63]
	v_mfma_f32_32x32x16_bf16 v[16:31], v[146:149], v[150:153], v[16:31]
	v_add_u32_e32 v133, 0x2000, v133
	ds_read_b64_tr_b16 v[150:151], v133 offset:0
	v_add_u32_e32 v135, 0x2000, v135
	ds_read_b64_tr_b16 v[152:153], v135 offset:0
	v_mfma_f32_32x32x16_bf16 v[0:15], v[146:149], v[182:185], v[0:15]
	ds_read_b64_tr_b16 v[182:183], v133 offset:0x200
	ds_read_b64_tr_b16 v[184:185], v135 offset:0x200
	v_mfma_f32_32x32x16_bf16 v[32:47], v[146:149], v[186:189], v[32:47]
	ds_read_b64_tr_b16 v[186:187], v133 offset:0x400
	ds_read_b64_tr_b16 v[188:189], v135 offset:0x400
	ds_read_b64_tr_b16 v[190:191], v133 offset:0x600
	ds_read_b64_tr_b16 v[192:193], v135 offset:0x600
	s_waitcnt lgkmcnt(0)
	v_mfma_f32_32x32x16_bf16 v[48:63], v[146:149], v[194:197], v[48:63]
	v_mfma_f32_32x32x16_bf16 v[96:111], v[128:131], v[150:153], v[96:111]
	ds_read_b64_tr_b16 v[150:151], v133 offset:0x1000
	ds_read_b64_tr_b16 v[152:153], v135 offset:0x1000
	v_mfma_f32_32x32x16_bf16 v[112:127], v[128:131], v[182:185], v[112:127]
	ds_read_b64_tr_b16 v[182:183], v133 offset:0x1200
	ds_read_b64_tr_b16 v[184:185], v135 offset:0x1200
	v_mfma_f32_32x32x16_bf16 v[80:95], v[128:131], v[186:189], v[80:95]
	ds_read_b64_tr_b16 v[186:187], v133 offset:0x1400
	ds_read_b64_tr_b16 v[188:189], v135 offset:0x1400
	ds_read_b64_tr_b16 v[194:195], v133 offset:0x1600
	ds_read_b64_tr_b16 v[196:197], v135 offset:0x1600
	s_waitcnt lgkmcnt(0)
	v_mfma_f32_32x32x16_bf16 v[64:79], v[128:131], v[190:193], v[64:79]
	v_mfma_f32_32x32x16_bf16 v[96:111], v[146:149], v[150:153], v[96:111]
	v_mfma_f32_32x32x16_bf16 v[112:127], v[146:149], v[182:185], v[112:127]
	v_mfma_f32_32x32x16_bf16 v[80:95], v[146:149], v[186:189], v[80:95]
	v_mfma_f32_32x32x16_bf16 v[64:79], v[146:149], v[194:197], v[64:79]
	s_waitcnt vmcnt(4) lgkmcnt(0)
	s_barrier
; #define VM_WAIT() asm volatile("s_waitcnt vmcnt(0)" ::: "memory")
; template <int DK, int DV, bool MLSTM>
; __device__ __forceinline__ void out_unit2(LAS unsigned char* lds, LAS unsigned char* ldstab, const OutArgs a, const int wv) {
;     ...
; #pragma unroll
;     for (int pc = 0; pc < 4; ++pc) {
;         VM_WAIT(); __syncthreads();
;         OUT_DMA(pc + 1);
;         const bf16x8 af0 = pa[2 * pc], af1 = pa[2 * pc + 1];
;         OUT_MMA(pc & 1);
;     }
; #pragma unroll 1
;     for (int pc = 4; pc < 4 + 2 * NCP; ++pc) {
;         VM_WAIT(); __syncthreads();
;         if (pc + 1 < 4 + 2 * NCP) OUT_DMA(pc + 1);
;         const int cq = pc - 4, dirb = cq >= NCP, cp = dirb ? cq - NCP : cq;
;         const float qs = dirb ? qsb : qsf;
;         const unsigned qa = QP + (cp >> 2) * 32768u + 512u * (cp & 3) + 8192u * rb;
;         const bf16x8 af0 = scale_frag(lds_r128(qa + rb0), qs), af1 = scale_frag(lds_r128(qa + rb1), qs);
	s_add_u32 s42, s4, 0x18000
	s_addc_u32 s43, s5, 0
	v_lshl_add_u64 v[128:129], s[42:43], 0, v[198:199]
	v_lshl_add_u64 v[130:131], s[42:43], 0, v[200:201]
	v_lshl_add_u64 v[146:147], s[42:43], 0, v[202:203]
	v_lshl_add_u64 v[148:149], s[42:43], 0, v[204:205]
	s_add_i32 m0, s6, 0x10000
	s_nop 0
	global_load_lds_dwordx4 v[128:129], off
	s_add_i32 m0, s7, 0x10000
	s_nop 0
	global_load_lds_dwordx4 v[130:131], off
	s_add_i32 m0, s38, 0x10000
	s_nop 0
	global_load_lds_dwordx4 v[146:147], off
	s_add_i32 m0, s40, 0x10000
	s_nop 0
	global_load_lds_dwordx4 v[148:149], off
	v_lshlrev_b32_e32 v135, 16, v244
	v_and_b32_e32 v137, 0xffff0000, v244
	v_mul_f32_e32 v135, v179, v135
	v_mul_f32_e32 v137, v179, v137
	v_cvt_pk_bf16_f32 v128, v135, v137
	v_lshlrev_b32_e32 v135, 16, v245
	v_and_b32_e32 v137, 0xffff0000, v245
	v_mul_f32_e32 v135, v179, v135
	v_mul_f32_e32 v137, v179, v137
	v_cvt_pk_bf16_f32 v129, v135, v137
	v_lshlrev_b32_e32 v135, 16, v246
	v_and_b32_e32 v137, 0xffff0000, v246
	v_mul_f32_e32 v135, v179, v135
	v_mul_f32_e32 v137, v179, v137
	v_cvt_pk_bf16_f32 v130, v135, v137
	v_lshlrev_b32_e32 v135, 16, v247
	v_and_b32_e32 v137, 0xffff0000, v247
	v_mul_f32_e32 v135, v179, v135
	v_mul_f32_e32 v137, v179, v137
	v_cvt_pk_bf16_f32 v131, v135, v137
	v_lshlrev_b32_e32 v135, 16, v248
	v_and_b32_e32 v137, 0xffff0000, v248
	v_mul_f32_e32 v135, v179, v135
	v_mul_f32_e32 v137, v179, v137
	v_cvt_pk_bf16_f32 v146, v135, v137
	v_lshlrev_b32_e32 v135, 16, v249
	v_and_b32_e32 v137, 0xffff0000, v249
	v_mul_f32_e32 v135, v179, v135
	v_mul_f32_e32 v137, v179, v137
	v_cvt_pk_bf16_f32 v147, v135, v137
	v_lshlrev_b32_e32 v135, 16, v250
	v_and_b32_e32 v137, 0xffff0000, v250
	v_mul_f32_e32 v135, v179, v135
	v_mul_f32_e32 v137, v179, v137
	v_cvt_pk_bf16_f32 v148, v135, v137
	v_lshlrev_b32_e32 v135, 16, v251
	v_and_b32_e32 v137, 0xffff0000, v251
	v_mul_f32_e32 v135, v179, v135
	v_mul_f32_e32 v137, v179, v137
	v_cvt_pk_bf16_f32 v149, v135, v137
	v_add_u32_e32 v133, 0x18000, v175
	ds_read_b64_tr_b16 v[150:151], v133 offset:0
	v_add_u32_e32 v135, 0x18000, v181
	ds_read_b64_tr_b16 v[152:153], v135 offset:0
	ds_read_b64_tr_b16 v[182:183], v133 offset:0x200
	ds_read_b64_tr_b16 v[184:185], v135 offset:0x200
	ds_read_b64_tr_b16 v[186:187], v133 offset:0x400
	ds_read_b64_tr_b16 v[188:189], v135 offset:0x400
	ds_read_b64_tr_b16 v[190:191], v133 offset:0x600
	ds_read_b64_tr_b16 v[192:193], v135 offset:0x600
	s_waitcnt lgkmcnt(0)
	s_nop 0
	v_mfma_f32_32x32x16_bf16 v[16:31], v[128:131], v[150:153], v[16:31]
	ds_read_b64_tr_b16 v[150:151], v133 offset:0x1000
	ds_read_b64_tr_b16 v[152:153], v135 offset:0x1000
	v_mfma_f32_32x32x16_bf16 v[0:15], v[128:131], v[182:185], v[0:15]
	ds_read_b64_tr_b16 v[182:183], v133 offset:0x1200
	ds_read_b64_tr_b16 v[184:185], v135 offset:0x1200
	v_mfma_f32_32x32x16_bf16 v[32:47], v[128:131], v[186:189], v[32:47]
	ds_read_b64_tr_b16 v[186:187], v133 offset:0x1400
	ds_read_b64_tr_b16 v[188:189], v135 offset:0x1400
	ds_read_b64_tr_b16 v[194:195], v133 offset:0x1600
	ds_read_b64_tr_b16 v[196:197], v135 offset:0x1600
	s_waitcnt lgkmcnt(0)
	v_mfma_f32_32x32x16_bf16 v[48:63], v[128:131], v[190:193], v[48:63]
	v_mfma_f32_32x32x16_bf16 v[16:31], v[146:149], v[150:153], v[16:31]
	v_add_u32_e32 v133, 0x2000, v133
	ds_read_b64_tr_b16 v[150:151], v133 offset:0
	v_add_u32_e32 v135, 0x2000, v135
	ds_read_b64_tr_b16 v[152:153], v135 offset:0
	v_mfma_f32_32x32x16_bf16 v[0:15], v[146:149], v[182:185], v[0:15]
	ds_read_b64_tr_b16 v[182:183], v133 offset:0x200
	ds_read_b64_tr_b16 v[184:185], v135 offset:0x200
	v_mfma_f32_32x32x16_bf16 v[32:47], v[146:149], v[186:189], v[32:47]
	ds_read_b64_tr_b16 v[186:187], v133 offset:0x400
	ds_read_b64_tr_b16 v[188:189], v135 offset:0x400
	ds_read_b64_tr_b16 v[190:191], v133 offset:0x600
	ds_read_b64_tr_b16 v[192:193], v135 offset:0x600
	s_waitcnt lgkmcnt(0)
	v_mfma_f32_32x32x16_bf16 v[48:63], v[146:149], v[194:197], v[48:63]
	v_mfma_f32_32x32x16_bf16 v[96:111], v[128:131], v[150:153], v[96:111]
	ds_read_b64_tr_b16 v[150:151], v133 offset:0x1000
	ds_read_b64_tr_b16 v[152:153], v135 offset:0x1000
	v_mfma_f32_32x32x16_bf16 v[112:127], v[128:131], v[182:185], v[112:127]
	ds_read_b64_tr_b16 v[182:183], v133 offset:0x1200
	ds_read_b64_tr_b16 v[184:185], v135 offset:0x1200
	v_mfma_f32_32x32x16_bf16 v[80:95], v[128:131], v[186:189], v[80:95]
	ds_read_b64_tr_b16 v[186:187], v133 offset:0x1400
	ds_read_b64_tr_b16 v[188:189], v135 offset:0x1400
	ds_read_b64_tr_b16 v[194:195], v133 offset:0x1600
	ds_read_b64_tr_b16 v[196:197], v135 offset:0x1600
	s_waitcnt lgkmcnt(0)
	v_mfma_f32_32x32x16_bf16 v[64:79], v[128:131], v[190:193], v[64:79]
	v_mfma_f32_32x32x16_bf16 v[96:111], v[146:149], v[150:153], v[96:111]
	v_mfma_f32_32x32x16_bf16 v[112:127], v[146:149], v[182:185], v[112:127]
	v_mfma_f32_32x32x16_bf16 v[80:95], v[146:149], v[186:189], v[80:95]
	v_mfma_f32_32x32x16_bf16 v[64:79], v[146:149], v[194:197], v[64:79]
	s_waitcnt vmcnt(4) lgkmcnt(0)
	s_barrier
; #define VM_WAIT() asm volatile("s_waitcnt vmcnt(0)" ::: "memory")
; template <int DK, int DV, bool MLSTM>
; __device__ __forceinline__ void out_unit2(LAS unsigned char* lds, LAS unsigned char* ldstab, const OutArgs a, const int wv) {
;     ...
; #pragma unroll
;     for (int pc = 0; pc < 4; ++pc) {
;         VM_WAIT(); __syncthreads();
;         OUT_DMA(pc + 1);
;         const bf16x8 af0 = pa[2 * pc], af1 = pa[2 * pc + 1];
;         OUT_MMA(pc & 1);
;     }
; #pragma unroll 1
;     for (int pc = 4; pc < 4 + 2 * NCP; ++pc) {
;         VM_WAIT(); __syncthreads();
;         if (pc + 1 < 4 + 2 * NCP) OUT_DMA(pc + 1);
;         const int cq = pc - 4, dirb = cq >= NCP, cp = dirb ? cq - NCP : cq;
;         const float qs = dirb ? qsb : qsf;
;         const unsigned qa = QP + (cp >> 2) * 32768u + 512u * (cp & 3) + 8192u * rb;
;         const bf16x8 af0 = scale_frag(lds_r128(qa + rb0), qs), af1 = scale_frag(lds_r128(qa + rb1), qs);
	s_add_u32 s42, s4, 0x20000
	s_addc_u32 s43, s5, 0
	v_lshl_add_u64 v[128:129], s[42:43], 0, v[198:199]
	v_lshl_add_u64 v[130:131], s[42:43], 0, v[200:201]
	v_lshl_add_u64 v[146:147], s[42:43], 0, v[202:203]
	v_lshl_add_u64 v[148:149], s[42:43], 0, v[204:205]
	s_add_i32 m0, s6, 0x18000
	s_nop 0
	global_load_lds_dwordx4 v[128:129], off
	s_add_i32 m0, s7, 0x18000
	s_nop 0
	global_load_lds_dwordx4 v[130:131], off
	s_add_i32 m0, s38, 0x18000
	s_nop 0
	global_load_lds_dwordx4 v[146:147], off
	s_add_i32 m0, s40, 0x18000
	s_nop 0
	global_load_lds_dwordx4 v[148:149], off
	v_lshlrev_b32_e32 v135, 16, v252
	v_and_b32_e32 v137, 0xffff0000, v252
	v_mul_f32_e32 v135, v179, v135
	v_mul_f32_e32 v137, v179, v137
	v_cvt_pk_bf16_f32 v128, v135, v137
	v_lshlrev_b32_e32 v135, 16, v253
	v_and_b32_e32 v137, 0xffff0000, v253
	v_mul_f32_e32 v135, v179, v135
	v_mul_f32_e32 v137, v179, v137
	v_cvt_pk_bf16_f32 v129, v135, v137
	v_lshlrev_b32_e32 v135, 16, v254
	v_and_b32_e32 v137, 0xffff0000, v254
	v_mul_f32_e32 v135, v179, v135
	v_mul_f32_e32 v137, v179, v137
	v_cvt_pk_bf16_f32 v130, v135, v137
	v_lshlrev_b32_e32 v135, 16, v255
	v_and_b32_e32 v137, 0xffff0000, v255
	v_mul_f32_e32 v135, v179, v135
	v_mul_f32_e32 v137, v179, v137
	v_cvt_pk_bf16_f32 v131, v135, v137
	v_lshlrev_b32_e32 v135, 16, v218
	v_and_b32_e32 v137, 0xffff0000, v218
	v_mul_f32_e32 v135, v179, v135
	v_mul_f32_e32 v137, v179, v137
	v_cvt_pk_bf16_f32 v146, v135, v137
	v_lshlrev_b32_e32 v135, 16, v219
	v_and_b32_e32 v137, 0xffff0000, v219
	v_mul_f32_e32 v135, v179, v135
	v_mul_f32_e32 v137, v179, v137
	v_cvt_pk_bf16_f32 v147, v135, v137
	v_lshlrev_b32_e32 v135, 16, v220
	v_and_b32_e32 v137, 0xffff0000, v220
	v_mul_f32_e32 v135, v179, v135
	v_mul_f32_e32 v137, v179, v137
	v_cvt_pk_bf16_f32 v148, v135, v137
	v_lshlrev_b32_e32 v135, 16, v221
	v_and_b32_e32 v137, 0xffff0000, v221
	v_mul_f32_e32 v135, v179, v135
	v_mul_f32_e32 v137, v179, v137
	v_cvt_pk_bf16_f32 v149, v135, v137
	v_mov_b32_e32 v133, v175
	ds_read_b64_tr_b16 v[150:151], v133 offset:0
	v_mov_b32_e32 v135, v181
	ds_read_b64_tr_b16 v[152:153], v135 offset:0
	ds_read_b64_tr_b16 v[182:183], v133 offset:0x200
	ds_read_b64_tr_b16 v[184:185], v135 offset:0x200
	ds_read_b64_tr_b16 v[186:187], v133 offset:0x400
	ds_read_b64_tr_b16 v[188:189], v135 offset:0x400
	ds_read_b64_tr_b16 v[190:191], v133 offset:0x600
	ds_read_b64_tr_b16 v[192:193], v135 offset:0x600
	s_waitcnt lgkmcnt(0)
	s_nop 0
	v_mfma_f32_32x32x16_bf16 v[16:31], v[128:131], v[150:153], v[16:31]
	ds_read_b64_tr_b16 v[150:151], v133 offset:0x1000
	ds_read_b64_tr_b16 v[152:153], v135 offset:0x1000
	v_mfma_f32_32x32x16_bf16 v[0:15], v[128:131], v[182:185], v[0:15]
	ds_read_b64_tr_b16 v[182:183], v133 offset:0x1200
	ds_read_b64_tr_b16 v[184:185], v135 offset:0x1200
	v_mfma_f32_32x32x16_bf16 v[32:47], v[128:131], v[186:189], v[32:47]
	ds_read_b64_tr_b16 v[186:187], v133 offset:0x1400
	ds_read_b64_tr_b16 v[188:189], v135 offset:0x1400
	ds_read_b64_tr_b16 v[194:195], v133 offset:0x1600
	ds_read_b64_tr_b16 v[196:197], v135 offset:0x1600
	s_waitcnt lgkmcnt(0)
	v_mfma_f32_32x32x16_bf16 v[48:63], v[128:131], v[190:193], v[48:63]
	v_mfma_f32_32x32x16_bf16 v[16:31], v[146:149], v[150:153], v[16:31]
	v_add_u32_e32 v133, 0x2000, v133
	ds_read_b64_tr_b16 v[150:151], v133 offset:0
	v_add_u32_e32 v135, 0x2000, v135
	ds_read_b64_tr_b16 v[152:153], v135 offset:0
	v_mfma_f32_32x32x16_bf16 v[0:15], v[146:149], v[182:185], v[0:15]
	ds_read_b64_tr_b16 v[182:183], v133 offset:0x200
	ds_read_b64_tr_b16 v[184:185], v135 offset:0x200
	v_mfma_f32_32x32x16_bf16 v[32:47], v[146:149], v[186:189], v[32:47]
	ds_read_b64_tr_b16 v[186:187], v133 offset:0x400
	ds_read_b64_tr_b16 v[188:189], v135 offset:0x400
	ds_read_b64_tr_b16 v[190:191], v133 offset:0x600
	ds_read_b64_tr_b16 v[192:193], v135 offset:0x600
	s_waitcnt lgkmcnt(0)
	v_mfma_f32_32x32x16_bf16 v[48:63], v[146:149], v[194:197], v[48:63]
	v_mfma_f32_32x32x16_bf16 v[96:111], v[128:131], v[150:153], v[96:111]
	ds_read_b64_tr_b16 v[150:151], v133 offset:0x1000
	ds_read_b64_tr_b16 v[152:153], v135 offset:0x1000
	v_mfma_f32_32x32x16_bf16 v[112:127], v[128:131], v[182:185], v[112:127]
	ds_read_b64_tr_b16 v[182:183], v133 offset:0x1200
	ds_read_b64_tr_b16 v[184:185], v135 offset:0x1200
	v_mfma_f32_32x32x16_bf16 v[80:95], v[128:131], v[186:189], v[80:95]
	ds_read_b64_tr_b16 v[186:187], v133 offset:0x1400
	ds_read_b64_tr_b16 v[188:189], v135 offset:0x1400
	ds_read_b64_tr_b16 v[194:195], v133 offset:0x1600
	ds_read_b64_tr_b16 v[196:197], v135 offset:0x1600
	s_waitcnt lgkmcnt(0)
	v_mfma_f32_32x32x16_bf16 v[64:79], v[128:131], v[190:193], v[64:79]
	v_mfma_f32_32x32x16_bf16 v[96:111], v[146:149], v[150:153], v[96:111]
	v_mfma_f32_32x32x16_bf16 v[112:127], v[146:149], v[182:185], v[112:127]
	v_mfma_f32_32x32x16_bf16 v[80:95], v[146:149], v[186:189], v[80:95]
	v_mfma_f32_32x32x16_bf16 v[64:79], v[146:149], v[194:197], v[64:79]
	s_waitcnt vmcnt(4) lgkmcnt(0)
	s_barrier
; #define VM_WAIT() asm volatile("s_waitcnt vmcnt(0)" ::: "memory")
; template <int DK, int DV, bool MLSTM>
; __device__ __forceinline__ void out_unit2(LAS unsigned char* lds, LAS unsigned char* ldstab, const OutArgs a, const int wv) {
;     ...
; #pragma unroll
;     for (int pc = 0; pc < 4; ++pc) {
;         VM_WAIT(); __syncthreads();
;         OUT_DMA(pc + 1);
;         const bf16x8 af0 = pa[2 * pc], af1 = pa[2 * pc + 1];
;         OUT_MMA(pc & 1);
;     }
; #pragma unroll 1
;     for (int pc = 4; pc < 4 + 2 * NCP; ++pc) {
;         VM_WAIT(); __syncthreads();
;         if (pc + 1 < 4 + 2 * NCP) OUT_DMA(pc + 1);
;         const int cq = pc - 4, dirb = cq >= NCP, cp = dirb ? cq - NCP : cq;
;         const float qs = dirb ? qsb : qsf;
;         const unsigned qa = QP + (cp >> 2) * 32768u + 512u * (cp & 3) + 8192u * rb;
;         const bf16x8 af0 = scale_frag(lds_r128(qa + rb0), qs), af1 = scale_frag(lds_r128(qa + rb1), qs);
	s_add_u32 s42, s4, 0x28000
	s_addc_u32 s43, s5, 0
	v_lshl_add_u64 v[128:129], s[42:43], 0, v[198:199]
	v_lshl_add_u64 v[130:131], s[42:43], 0, v[200:201]
	v_lshl_add_u64 v[146:147], s[42:43], 0, v[202:203]
	v_lshl_add_u64 v[148:149], s[42:43], 0, v[204:205]
	s_mov_b32 m0, s6
	s_nop 0
	global_load_lds_dwordx4 v[128:129], off
	s_mov_b32 m0, s7
	s_nop 0
	global_load_lds_dwordx4 v[130:131], off
	s_mov_b32 m0, s38
	s_nop 0
	global_load_lds_dwordx4 v[146:147], off
	s_mov_b32 m0, s40
	s_nop 0
	global_load_lds_dwordx4 v[148:149], off
	v_lshlrev_b32_e32 v135, 16, v222
	v_and_b32_e32 v137, 0xffff0000, v222
	v_mul_f32_e32 v135, v179, v135
	v_mul_f32_e32 v137, v179, v137
	v_cvt_pk_bf16_f32 v128, v135, v137
	v_lshlrev_b32_e32 v135, 16, v223
	v_and_b32_e32 v137, 0xffff0000, v223
	v_mul_f32_e32 v135, v179, v135
	v_mul_f32_e32 v137, v179, v137
	v_cvt_pk_bf16_f32 v129, v135, v137
	v_lshlrev_b32_e32 v135, 16, v224
	v_and_b32_e32 v137, 0xffff0000, v224
	v_mul_f32_e32 v135, v179, v135
	v_mul_f32_e32 v137, v179, v137
	v_cvt_pk_bf16_f32 v130, v135, v137
	v_lshlrev_b32_e32 v135, 16, v225
	v_and_b32_e32 v137, 0xffff0000, v225
	v_mul_f32_e32 v135, v179, v135
	v_mul_f32_e32 v137, v179, v137
	v_cvt_pk_bf16_f32 v131, v135, v137
	v_lshlrev_b32_e32 v135, 16, v206
	v_and_b32_e32 v137, 0xffff0000, v206
	v_mul_f32_e32 v135, v179, v135
	v_mul_f32_e32 v137, v179, v137
	v_cvt_pk_bf16_f32 v146, v135, v137
	v_lshlrev_b32_e32 v135, 16, v207
	v_and_b32_e32 v137, 0xffff0000, v207
	v_mul_f32_e32 v135, v179, v135
	v_mul_f32_e32 v137, v179, v137
	v_cvt_pk_bf16_f32 v147, v135, v137
	v_lshlrev_b32_e32 v135, 16, v208
	v_and_b32_e32 v137, 0xffff0000, v208
	v_mul_f32_e32 v135, v179, v135
	v_mul_f32_e32 v137, v179, v137
	v_cvt_pk_bf16_f32 v148, v135, v137
	v_lshlrev_b32_e32 v135, 16, v209
	v_and_b32_e32 v137, 0xffff0000, v209
	v_mul_f32_e32 v135, v179, v135
	v_mul_f32_e32 v137, v179, v137
	v_cvt_pk_bf16_f32 v149, v135, v137
	v_add_u32_e32 v133, 0x10000, v175
	ds_read_b64_tr_b16 v[150:151], v133 offset:0
	v_add_u32_e32 v135, 0x10000, v181
	ds_read_b64_tr_b16 v[152:153], v135 offset:0
	ds_read_b64_tr_b16 v[182:183], v133 offset:0x200
	ds_read_b64_tr_b16 v[184:185], v135 offset:0x200
	ds_read_b64_tr_b16 v[186:187], v133 offset:0x400
	ds_read_b64_tr_b16 v[188:189], v135 offset:0x400
	ds_read_b64_tr_b16 v[190:191], v133 offset:0x600
	ds_read_b64_tr_b16 v[192:193], v135 offset:0x600
	s_waitcnt lgkmcnt(0)
	s_nop 0
	v_mfma_f32_32x32x16_bf16 v[16:31], v[128:131], v[150:153], v[16:31]
	ds_read_b64_tr_b16 v[150:151], v133 offset:0x1000
	ds_read_b64_tr_b16 v[152:153], v135 offset:0x1000
	v_mfma_f32_32x32x16_bf16 v[0:15], v[128:131], v[182:185], v[0:15]
	ds_read_b64_tr_b16 v[182:183], v133 offset:0x1200
	ds_read_b64_tr_b16 v[184:185], v135 offset:0x1200
	v_mfma_f32_32x32x16_bf16 v[32:47], v[128:131], v[186:189], v[32:47]
	ds_read_b64_tr_b16 v[186:187], v133 offset:0x1400
	ds_read_b64_tr_b16 v[188:189], v135 offset:0x1400
	ds_read_b64_tr_b16 v[194:195], v133 offset:0x1600
	ds_read_b64_tr_b16 v[196:197], v135 offset:0x1600
	s_waitcnt lgkmcnt(0)
	v_mfma_f32_32x32x16_bf16 v[48:63], v[128:131], v[190:193], v[48:63]
	v_mfma_f32_32x32x16_bf16 v[16:31], v[146:149], v[150:153], v[16:31]
	v_add_u32_e32 v133, 0x2000, v133
	ds_read_b64_tr_b16 v[150:151], v133 offset:0
	v_add_u32_e32 v135, 0x2000, v135
	ds_read_b64_tr_b16 v[152:153], v135 offset:0
	v_mfma_f32_32x32x16_bf16 v[0:15], v[146:149], v[182:185], v[0:15]
	ds_read_b64_tr_b16 v[182:183], v133 offset:0x200
	ds_read_b64_tr_b16 v[184:185], v135 offset:0x200
	v_mfma_f32_32x32x16_bf16 v[32:47], v[146:149], v[186:189], v[32:47]
	ds_read_b64_tr_b16 v[186:187], v133 offset:0x400
	ds_read_b64_tr_b16 v[188:189], v135 offset:0x400
	ds_read_b64_tr_b16 v[190:191], v133 offset:0x600
	ds_read_b64_tr_b16 v[192:193], v135 offset:0x600
	s_waitcnt lgkmcnt(0)
	v_mfma_f32_32x32x16_bf16 v[48:63], v[146:149], v[194:197], v[48:63]
	v_mfma_f32_32x32x16_bf16 v[96:111], v[128:131], v[150:153], v[96:111]
	ds_read_b64_tr_b16 v[150:151], v133 offset:0x1000
	ds_read_b64_tr_b16 v[152:153], v135 offset:0x1000
	v_mfma_f32_32x32x16_bf16 v[112:127], v[128:131], v[182:185], v[112:127]
	ds_read_b64_tr_b16 v[182:183], v133 offset:0x1200
	ds_read_b64_tr_b16 v[184:185], v135 offset:0x1200
	v_mfma_f32_32x32x16_bf16 v[80:95], v[128:131], v[186:189], v[80:95]
	ds_read_b64_tr_b16 v[186:187], v133 offset:0x1400
	ds_read_b64_tr_b16 v[188:189], v135 offset:0x1400
	ds_read_b64_tr_b16 v[194:195], v133 offset:0x1600
	ds_read_b64_tr_b16 v[196:197], v135 offset:0x1600
	s_waitcnt lgkmcnt(0)
	v_mfma_f32_32x32x16_bf16 v[64:79], v[128:131], v[190:193], v[64:79]
	v_mfma_f32_32x32x16_bf16 v[96:111], v[146:149], v[150:153], v[96:111]
	v_mfma_f32_32x32x16_bf16 v[112:127], v[146:149], v[182:185], v[112:127]
	v_mfma_f32_32x32x16_bf16 v[80:95], v[146:149], v[186:189], v[80:95]
	v_mfma_f32_32x32x16_bf16 v[64:79], v[146:149], v[194:197], v[64:79]
	s_waitcnt vmcnt(4) lgkmcnt(0)
	s_barrier
; #define VM_WAIT() asm volatile("s_waitcnt vmcnt(0)" ::: "memory")
; template <int DK, int DV, bool MLSTM>
; __device__ __forceinline__ void out_unit2(LAS unsigned char* lds, LAS unsigned char* ldstab, const OutArgs a, const int wv) {
;     ...
; #pragma unroll
;     for (int pc = 0; pc < 4; ++pc) {
;         VM_WAIT(); __syncthreads();
;         OUT_DMA(pc + 1);
;         const bf16x8 af0 = pa[2 * pc], af1 = pa[2 * pc + 1];
;         OUT_MMA(pc & 1);
;     }
; #pragma unroll 1
;     for (int pc = 4; pc < 4 + 2 * NCP; ++pc) {
;         VM_WAIT(); __syncthreads();
;         if (pc + 1 < 4 + 2 * NCP) OUT_DMA(pc + 1);
;         const int cq = pc - 4, dirb = cq >= NCP, cp = dirb ? cq - NCP : cq;
;         const float qs = dirb ? qsb : qsf;
;         const unsigned qa = QP + (cp >> 2) * 32768u + 512u * (cp & 3) + 8192u * rb;
;         const bf16x8 af0 = scale_frag(lds_r128(qa + rb0), qs), af1 = scale_frag(lds_r128(qa + rb1), qs);
	s_add_u32 s42, s4, 0x30000
	s_addc_u32 s43, s5, 0
	v_lshl_add_u64 v[128:129], s[42:43], 0, v[198:199]
	v_lshl_add_u64 v[130:131], s[42:43], 0, v[200:201]
	v_lshl_add_u64 v[146:147], s[42:43], 0, v[202:203]
	v_lshl_add_u64 v[148:149], s[42:43], 0, v[204:205]
	s_add_i32 m0, s6, 0x10000
	s_nop 0
	global_load_lds_dwordx4 v[128:129], off
	s_add_i32 m0, s7, 0x10000
	s_nop 0
	global_load_lds_dwordx4 v[130:131], off
	s_add_i32 m0, s38, 0x10000
	s_nop 0
	global_load_lds_dwordx4 v[146:147], off
	s_add_i32 m0, s40, 0x10000
	s_nop 0
	global_load_lds_dwordx4 v[148:149], off
	v_add_u32_e32 v133, s13, v173
	v_add_u32_e32 v135, s13, v177
	ds_read_b128 v[128:131], v133 offset:32768
	ds_read_b128 v[146:149], v135 offset:32768
	s_waitcnt lgkmcnt(0)
	v_lshlrev_b32_e32 v135, 16, v128
	v_and_b32_e32 v137, 0xffff0000, v128
	v_mul_f32_e32 v135, v179, v135
	v_mul_f32_e32 v137, v179, v137
	v_cvt_pk_bf16_f32 v128, v135, v137
	v_lshlrev_b32_e32 v135, 16, v129
	v_and_b32_e32 v137, 0xffff0000, v129
	v_mul_f32_e32 v135, v179, v135
	v_mul_f32_e32 v137, v179, v137
	v_cvt_pk_bf16_f32 v129, v135, v137
	v_lshlrev_b32_e32 v135, 16, v130
	v_and_b32_e32 v137, 0xffff0000, v130
	v_mul_f32_e32 v135, v179, v135
	v_mul_f32_e32 v137, v179, v137
	v_cvt_pk_bf16_f32 v130, v135, v137
	v_lshlrev_b32_e32 v135, 16, v131
	v_and_b32_e32 v137, 0xffff0000, v131
	v_mul_f32_e32 v135, v179, v135
	v_mul_f32_e32 v137, v179, v137
	v_cvt_pk_bf16_f32 v131, v135, v137
	v_lshlrev_b32_e32 v135, 16, v146
	v_and_b32_e32 v137, 0xffff0000, v146
	v_mul_f32_e32 v135, v179, v135
	v_mul_f32_e32 v137, v179, v137
	v_cvt_pk_bf16_f32 v146, v135, v137
	v_lshlrev_b32_e32 v135, 16, v147
	v_and_b32_e32 v137, 0xffff0000, v147
	v_mul_f32_e32 v135, v179, v135
	v_mul_f32_e32 v137, v179, v137
	v_cvt_pk_bf16_f32 v147, v135, v137
	v_lshlrev_b32_e32 v135, 16, v148
	v_and_b32_e32 v137, 0xffff0000, v148
	v_mul_f32_e32 v135, v179, v135
	v_mul_f32_e32 v137, v179, v137
	v_cvt_pk_bf16_f32 v148, v135, v137
	v_lshlrev_b32_e32 v135, 16, v149
	v_and_b32_e32 v137, 0xffff0000, v149
	v_mul_f32_e32 v135, v179, v135
	v_mul_f32_e32 v137, v179, v137
	v_cvt_pk_bf16_f32 v149, v135, v137
	v_add_u32_e32 v133, 0x18000, v175
	ds_read_b64_tr_b16 v[150:151], v133 offset:0
	v_add_u32_e32 v135, 0x18000, v181
	ds_read_b64_tr_b16 v[152:153], v135 offset:0
	ds_read_b64_tr_b16 v[182:183], v133 offset:0x200
	ds_read_b64_tr_b16 v[184:185], v135 offset:0x200
	ds_read_b64_tr_b16 v[186:187], v133 offset:0x400
	ds_read_b64_tr_b16 v[188:189], v135 offset:0x400
	ds_read_b64_tr_b16 v[190:191], v133 offset:0x600
	ds_read_b64_tr_b16 v[192:193], v135 offset:0x600
	s_waitcnt lgkmcnt(0)
	s_nop 0
	v_mfma_f32_32x32x16_bf16 v[16:31], v[128:131], v[150:153], v[16:31]
	ds_read_b64_tr_b16 v[150:151], v133 offset:0x1000
	ds_read_b64_tr_b16 v[152:153], v135 offset:0x1000
	v_mfma_f32_32x32x16_bf16 v[0:15], v[128:131], v[182:185], v[0:15]
	ds_read_b64_tr_b16 v[182:183], v133 offset:0x1200
	ds_read_b64_tr_b16 v[184:185], v135 offset:0x1200
	v_mfma_f32_32x32x16_bf16 v[32:47], v[128:131], v[186:189], v[32:47]
	ds_read_b64_tr_b16 v[186:187], v133 offset:0x1400
	ds_read_b64_tr_b16 v[188:189], v135 offset:0x1400
	ds_read_b64_tr_b16 v[194:195], v133 offset:0x1600
	ds_read_b64_tr_b16 v[196:197], v135 offset:0x1600
	s_waitcnt lgkmcnt(0)
	v_mfma_f32_32x32x16_bf16 v[48:63], v[128:131], v[190:193], v[48:63]
	v_mfma_f32_32x32x16_bf16 v[16:31], v[146:149], v[150:153], v[16:31]
	v_add_u32_e32 v133, 0x2000, v133
	ds_read_b64_tr_b16 v[150:151], v133 offset:0
	v_add_u32_e32 v135, 0x2000, v135
	ds_read_b64_tr_b16 v[152:153], v135 offset:0
	v_mfma_f32_32x32x16_bf16 v[0:15], v[146:149], v[182:185], v[0:15]
	ds_read_b64_tr_b16 v[182:183], v133 offset:0x200
	ds_read_b64_tr_b16 v[184:185], v135 offset:0x200
	v_mfma_f32_32x32x16_bf16 v[32:47], v[146:149], v[186:189], v[32:47]
	ds_read_b64_tr_b16 v[186:187], v133 offset:0x400
	ds_read_b64_tr_b16 v[188:189], v135 offset:0x400
	ds_read_b64_tr_b16 v[190:191], v133 offset:0x600
	ds_read_b64_tr_b16 v[192:193], v135 offset:0x600
	s_waitcnt lgkmcnt(0)
	v_mfma_f32_32x32x16_bf16 v[48:63], v[146:149], v[194:197], v[48:63]
	v_mfma_f32_32x32x16_bf16 v[96:111], v[128:131], v[150:153], v[96:111]
	ds_read_b64_tr_b16 v[150:151], v133 offset:0x1000
	ds_read_b64_tr_b16 v[152:153], v135 offset:0x1000
	v_mfma_f32_32x32x16_bf16 v[112:127], v[128:131], v[182:185], v[112:127]
	ds_read_b64_tr_b16 v[182:183], v133 offset:0x1200
	ds_read_b64_tr_b16 v[184:185], v135 offset:0x1200
	v_mfma_f32_32x32x16_bf16 v[80:95], v[128:131], v[186:189], v[80:95]
	ds_read_b64_tr_b16 v[186:187], v133 offset:0x1400
	ds_read_b64_tr_b16 v[188:189], v135 offset:0x1400
	ds_read_b64_tr_b16 v[194:195], v133 offset:0x1600
	ds_read_b64_tr_b16 v[196:197], v135 offset:0x1600
	s_waitcnt lgkmcnt(0)
	v_mfma_f32_32x32x16_bf16 v[64:79], v[128:131], v[190:193], v[64:79]
	v_mfma_f32_32x32x16_bf16 v[96:111], v[146:149], v[150:153], v[96:111]
	v_mfma_f32_32x32x16_bf16 v[112:127], v[146:149], v[182:185], v[112:127]
	v_mfma_f32_32x32x16_bf16 v[80:95], v[146:149], v[186:189], v[80:95]
	v_mfma_f32_32x32x16_bf16 v[64:79], v[146:149], v[194:197], v[64:79]
	s_waitcnt vmcnt(4) lgkmcnt(0)
	s_barrier
; #define VM_WAIT() asm volatile("s_waitcnt vmcnt(0)" ::: "memory")
; template <int DK, int DV, bool MLSTM>
; __device__ __forceinline__ void out_unit2(LAS unsigned char* lds, LAS unsigned char* ldstab, const OutArgs a, const int wv) {
;     ...
; #pragma unroll
;     for (int pc = 0; pc < 4; ++pc) {
;         VM_WAIT(); __syncthreads();
;         OUT_DMA(pc + 1);
;         const bf16x8 af0 = pa[2 * pc], af1 = pa[2 * pc + 1];
;         OUT_MMA(pc & 1);
;     }
; #pragma unroll 1
;     for (int pc = 4; pc < 4 + 2 * NCP; ++pc) {
;         VM_WAIT(); __syncthreads();
;         if (pc + 1 < 4 + 2 * NCP) OUT_DMA(pc + 1);
;         const int cq = pc - 4, dirb = cq >= NCP, cp = dirb ? cq - NCP : cq;
;         const float qs = dirb ? qsb : qsf;
;         const unsigned qa = QP + (cp >> 2) * 32768u + 512u * (cp & 3) + 8192u * rb;
;         const bf16x8 af0 = scale_frag(lds_r128(qa + rb0), qs), af1 = scale_frag(lds_r128(qa + rb1), qs);
	s_add_u32 s42, s4, 0x38000
	s_addc_u32 s43, s5, 0
	v_lshl_add_u64 v[128:129], s[42:43], 0, v[198:199]
	v_lshl_add_u64 v[130:131], s[42:43], 0, v[200:201]
	v_lshl_add_u64 v[146:147], s[42:43], 0, v[202:203]
	v_lshl_add_u64 v[148:149], s[42:43], 0, v[204:205]
	s_add_i32 m0, s6, 0x18000
	s_nop 0
	global_load_lds_dwordx4 v[128:129], off
	s_add_i32 m0, s7, 0x18000
	s_nop 0
	global_load_lds_dwordx4 v[130:131], off
	s_add_i32 m0, s38, 0x18000
	s_nop 0
	global_load_lds_dwordx4 v[146:147], off
	s_add_i32 m0, s40, 0x18000
	s_nop 0
	global_load_lds_dwordx4 v[148:149], off
	v_add_u32_e32 v133, s13, v173
	v_add_u32_e32 v135, s13, v177
	ds_read_b128 v[128:131], v133 offset:33280
	ds_read_b128 v[146:149], v135 offset:33280
	s_waitcnt lgkmcnt(0)
	v_lshlrev_b32_e32 v135, 16, v128
	v_and_b32_e32 v137, 0xffff0000, v128
	v_mul_f32_e32 v135, v179, v135
	v_mul_f32_e32 v137, v179, v137
	v_cvt_pk_bf16_f32 v128, v135, v137
	v_lshlrev_b32_e32 v135, 16, v129
	v_and_b32_e32 v137, 0xffff0000, v129
	v_mul_f32_e32 v135, v179, v135
	v_mul_f32_e32 v137, v179, v137
	v_cvt_pk_bf16_f32 v129, v135, v137
	v_lshlrev_b32_e32 v135, 16, v130
	v_and_b32_e32 v137, 0xffff0000, v130
	v_mul_f32_e32 v135, v179, v135
	v_mul_f32_e32 v137, v179, v137
	v_cvt_pk_bf16_f32 v130, v135, v137
	v_lshlrev_b32_e32 v135, 16, v131
	v_and_b32_e32 v137, 0xffff0000, v131
	v_mul_f32_e32 v135, v179, v135
	v_mul_f32_e32 v137, v179, v137
	v_cvt_pk_bf16_f32 v131, v135, v137
	v_lshlrev_b32_e32 v135, 16, v146
	v_and_b32_e32 v137, 0xffff0000, v146
	v_mul_f32_e32 v135, v179, v135
	v_mul_f32_e32 v137, v179, v137
	v_cvt_pk_bf16_f32 v146, v135, v137
	v_lshlrev_b32_e32 v135, 16, v147
	v_and_b32_e32 v137, 0xffff0000, v147
	v_mul_f32_e32 v135, v179, v135
	v_mul_f32_e32 v137, v179, v137
	v_cvt_pk_bf16_f32 v147, v135, v137
	v_lshlrev_b32_e32 v135, 16, v148
	v_and_b32_e32 v137, 0xffff0000, v148
	v_mul_f32_e32 v135, v179, v135
	v_mul_f32_e32 v137, v179, v137
	v_cvt_pk_bf16_f32 v148, v135, v137
	v_lshlrev_b32_e32 v135, 16, v149
	v_and_b32_e32 v137, 0xffff0000, v149
	v_mul_f32_e32 v135, v179, v135
	v_mul_f32_e32 v137, v179, v137
	v_cvt_pk_bf16_f32 v149, v135, v137
	v_mov_b32_e32 v133, v175
	ds_read_b64_tr_b16 v[150:151], v133 offset:0
	v_mov_b32_e32 v135, v181
	ds_read_b64_tr_b16 v[152:153], v135 offset:0
	ds_read_b64_tr_b16 v[182:183], v133 offset:0x200
	ds_read_b64_tr_b16 v[184:185], v135 offset:0x200
	ds_read_b64_tr_b16 v[186:187], v133 offset:0x400
	ds_read_b64_tr_b16 v[188:189], v135 offset:0x400
	ds_read_b64_tr_b16 v[190:191], v133 offset:0x600
	ds_read_b64_tr_b16 v[192:193], v135 offset:0x600
	s_waitcnt lgkmcnt(0)
	s_nop 0
	v_mfma_f32_32x32x16_bf16 v[16:31], v[128:131], v[150:153], v[16:31]
	ds_read_b64_tr_b16 v[150:151], v133 offset:0x1000
	ds_read_b64_tr_b16 v[152:153], v135 offset:0x1000
	v_mfma_f32_32x32x16_bf16 v[0:15], v[128:131], v[182:185], v[0:15]
	ds_read_b64_tr_b16 v[182:183], v133 offset:0x1200
	ds_read_b64_tr_b16 v[184:185], v135 offset:0x1200
	v_mfma_f32_32x32x16_bf16 v[32:47], v[128:131], v[186:189], v[32:47]
	ds_read_b64_tr_b16 v[186:187], v133 offset:0x1400
	ds_read_b64_tr_b16 v[188:189], v135 offset:0x1400
	ds_read_b64_tr_b16 v[194:195], v133 offset:0x1600
	ds_read_b64_tr_b16 v[196:197], v135 offset:0x1600
	s_waitcnt lgkmcnt(0)
	v_mfma_f32_32x32x16_bf16 v[48:63], v[128:131], v[190:193], v[48:63]
	v_mfma_f32_32x32x16_bf16 v[16:31], v[146:149], v[150:153], v[16:31]
	v_add_u32_e32 v133, 0x2000, v133
	ds_read_b64_tr_b16 v[150:151], v133 offset:0
	v_add_u32_e32 v135, 0x2000, v135
	ds_read_b64_tr_b16 v[152:153], v135 offset:0
	v_mfma_f32_32x32x16_bf16 v[0:15], v[146:149], v[182:185], v[0:15]
	ds_read_b64_tr_b16 v[182:183], v133 offset:0x200
	ds_read_b64_tr_b16 v[184:185], v135 offset:0x200
	v_mfma_f32_32x32x16_bf16 v[32:47], v[146:149], v[186:189], v[32:47]
	ds_read_b64_tr_b16 v[186:187], v133 offset:0x400
	ds_read_b64_tr_b16 v[188:189], v135 offset:0x400
	ds_read_b64_tr_b16 v[190:191], v133 offset:0x600
	ds_read_b64_tr_b16 v[192:193], v135 offset:0x600
	s_waitcnt lgkmcnt(0)
	v_mfma_f32_32x32x16_bf16 v[48:63], v[146:149], v[194:197], v[48:63]
	v_mfma_f32_32x32x16_bf16 v[96:111], v[128:131], v[150:153], v[96:111]
	ds_read_b64_tr_b16 v[150:151], v133 offset:0x1000
	ds_read_b64_tr_b16 v[152:153], v135 offset:0x1000
	v_mfma_f32_32x32x16_bf16 v[112:127], v[128:131], v[182:185], v[112:127]
	ds_read_b64_tr_b16 v[182:183], v133 offset:0x1200
	ds_read_b64_tr_b16 v[184:185], v135 offset:0x1200
	v_mfma_f32_32x32x16_bf16 v[80:95], v[128:131], v[186:189], v[80:95]
	ds_read_b64_tr_b16 v[186:187], v133 offset:0x1400
	ds_read_b64_tr_b16 v[188:189], v135 offset:0x1400
	ds_read_b64_tr_b16 v[194:195], v133 offset:0x1600
	ds_read_b64_tr_b16 v[196:197], v135 offset:0x1600
	s_waitcnt lgkmcnt(0)
	v_mfma_f32_32x32x16_bf16 v[64:79], v[128:131], v[190:193], v[64:79]
	v_mfma_f32_32x32x16_bf16 v[96:111], v[146:149], v[150:153], v[96:111]
	v_mfma_f32_32x32x16_bf16 v[112:127], v[146:149], v[182:185], v[112:127]
	v_mfma_f32_32x32x16_bf16 v[80:95], v[146:149], v[186:189], v[80:95]
	v_mfma_f32_32x32x16_bf16 v[64:79], v[146:149], v[194:197], v[64:79]
	s_waitcnt vmcnt(4) lgkmcnt(0)
	s_barrier
; #define VM_WAIT() asm volatile("s_waitcnt vmcnt(0)" ::: "memory")
; template <int DK, int DV, bool MLSTM>
; __device__ __forceinline__ void out_unit2(LAS unsigned char* lds, LAS unsigned char* ldstab, const OutArgs a, const int wv) {
;     ...
; #pragma unroll
;     for (int pc = 0; pc < 4; ++pc) {
;         VM_WAIT(); __syncthreads();
;         OUT_DMA(pc + 1);
;         const bf16x8 af0 = pa[2 * pc], af1 = pa[2 * pc + 1];
;         OUT_MMA(pc & 1);
;     }
; #pragma unroll 1
;     for (int pc = 4; pc < 4 + 2 * NCP; ++pc) {
;         VM_WAIT(); __syncthreads();
;         if (pc + 1 < 4 + 2 * NCP) OUT_DMA(pc + 1);
;         const int cq = pc - 4, dirb = cq >= NCP, cp = dirb ? cq - NCP : cq;
;         const float qs = dirb ? qsb : qsf;
;         const unsigned qa = QP + (cp >> 2) * 32768u + 512u * (cp & 3) + 8192u * rb;
;         const bf16x8 af0 = scale_frag(lds_r128(qa + rb0), qs), af1 = scale_frag(lds_r128(qa + rb1), qs);
	s_add_u32 s42, s11, 0x0
	s_addc_u32 s43, s12, 0
	v_lshl_add_u64 v[128:129], s[42:43], 0, v[198:199]
	v_lshl_add_u64 v[130:131], s[42:43], 0, v[200:201]
	v_lshl_add_u64 v[146:147], s[42:43], 0, v[202:203]
	v_lshl_add_u64 v[148:149], s[42:43], 0, v[204:205]
	s_mov_b32 m0, s6
	s_nop 0
	global_load_lds_dwordx4 v[128:129], off
	s_mov_b32 m0, s7
	s_nop 0
	global_load_lds_dwordx4 v[130:131], off
	s_mov_b32 m0, s38
	s_nop 0
	global_load_lds_dwordx4 v[146:147], off
	s_mov_b32 m0, s40
	s_nop 0
	global_load_lds_dwordx4 v[148:149], off
	v_add_u32_e32 v133, s13, v173
	v_add_u32_e32 v135, s13, v177
	ds_read_b128 v[128:131], v133 offset:33792
	ds_read_b128 v[146:149], v135 offset:33792
	s_waitcnt lgkmcnt(0)
	v_lshlrev_b32_e32 v135, 16, v128
	v_and_b32_e32 v137, 0xffff0000, v128
	v_mul_f32_e32 v135, v179, v135
	v_mul_f32_e32 v137, v179, v137
	v_cvt_pk_bf16_f32 v128, v135, v137
	v_lshlrev_b32_e32 v135, 16, v129
	v_and_b32_e32 v137, 0xffff0000, v129
	v_mul_f32_e32 v135, v179, v135
	v_mul_f32_e32 v137, v179, v137
	v_cvt_pk_bf16_f32 v129, v135, v137
	v_lshlrev_b32_e32 v135, 16, v130
	v_and_b32_e32 v137, 0xffff0000, v130
	v_mul_f32_e32 v135, v179, v135
	v_mul_f32_e32 v137, v179, v137
	v_cvt_pk_bf16_f32 v130, v135, v137
	v_lshlrev_b32_e32 v135, 16, v131
	v_and_b32_e32 v137, 0xffff0000, v131
	v_mul_f32_e32 v135, v179, v135
	v_mul_f32_e32 v137, v179, v137
	v_cvt_pk_bf16_f32 v131, v135, v137
	v_lshlrev_b32_e32 v135, 16, v146
	v_and_b32_e32 v137, 0xffff0000, v146
	v_mul_f32_e32 v135, v179, v135
	v_mul_f32_e32 v137, v179, v137
	v_cvt_pk_bf16_f32 v146, v135, v137
	v_lshlrev_b32_e32 v135, 16, v147
	v_and_b32_e32 v137, 0xffff0000, v147
	v_mul_f32_e32 v135, v179, v135
	v_mul_f32_e32 v137, v179, v137
	v_cvt_pk_bf16_f32 v147, v135, v137
	v_lshlrev_b32_e32 v135, 16, v148
	v_and_b32_e32 v137, 0xffff0000, v148
	v_mul_f32_e32 v135, v179, v135
	v_mul_f32_e32 v137, v179, v137
	v_cvt_pk_bf16_f32 v148, v135, v137
	v_lshlrev_b32_e32 v135, 16, v149
	v_and_b32_e32 v137, 0xffff0000, v149
	v_mul_f32_e32 v135, v179, v135
	v_mul_f32_e32 v137, v179, v137
	v_cvt_pk_bf16_f32 v149, v135, v137
	v_add_u32_e32 v133, 0x10000, v175
	ds_read_b64_tr_b16 v[150:151], v133 offset:0
	v_add_u32_e32 v135, 0x10000, v181
	ds_read_b64_tr_b16 v[152:153], v135 offset:0
	ds_read_b64_tr_b16 v[182:183], v133 offset:0x200
	ds_read_b64_tr_b16 v[184:185], v135 offset:0x200
	ds_read_b64_tr_b16 v[186:187], v133 offset:0x400
	ds_read_b64_tr_b16 v[188:189], v135 offset:0x400
	ds_read_b64_tr_b16 v[190:191], v133 offset:0x600
	ds_read_b64_tr_b16 v[192:193], v135 offset:0x600
	s_waitcnt lgkmcnt(0)
	s_nop 0
	v_mfma_f32_32x32x16_bf16 v[16:31], v[128:131], v[150:153], v[16:31]
	ds_read_b64_tr_b16 v[150:151], v133 offset:0x1000
	ds_read_b64_tr_b16 v[152:153], v135 offset:0x1000
	v_mfma_f32_32x32x16_bf16 v[0:15], v[128:131], v[182:185], v[0:15]
	ds_read_b64_tr_b16 v[182:183], v133 offset:0x1200
	ds_read_b64_tr_b16 v[184:185], v135 offset:0x1200
	v_mfma_f32_32x32x16_bf16 v[32:47], v[128:131], v[186:189], v[32:47]
	ds_read_b64_tr_b16 v[186:187], v133 offset:0x1400
	ds_read_b64_tr_b16 v[188:189], v135 offset:0x1400
	ds_read_b64_tr_b16 v[194:195], v133 offset:0x1600
	ds_read_b64_tr_b16 v[196:197], v135 offset:0x1600
	s_waitcnt lgkmcnt(0)
	v_mfma_f32_32x32x16_bf16 v[48:63], v[128:131], v[190:193], v[48:63]
	v_mfma_f32_32x32x16_bf16 v[16:31], v[146:149], v[150:153], v[16:31]
	v_add_u32_e32 v133, 0x2000, v133
	ds_read_b64_tr_b16 v[150:151], v133 offset:0
	v_add_u32_e32 v135, 0x2000, v135
	ds_read_b64_tr_b16 v[152:153], v135 offset:0
	v_mfma_f32_32x32x16_bf16 v[0:15], v[146:149], v[182:185], v[0:15]
	ds_read_b64_tr_b16 v[182:183], v133 offset:0x200
	ds_read_b64_tr_b16 v[184:185], v135 offset:0x200
	v_mfma_f32_32x32x16_bf16 v[32:47], v[146:149], v[186:189], v[32:47]
	ds_read_b64_tr_b16 v[186:187], v133 offset:0x400
	ds_read_b64_tr_b16 v[188:189], v135 offset:0x400
	ds_read_b64_tr_b16 v[190:191], v133 offset:0x600
	ds_read_b64_tr_b16 v[192:193], v135 offset:0x600
	s_waitcnt lgkmcnt(0)
	v_mfma_f32_32x32x16_bf16 v[48:63], v[146:149], v[194:197], v[48:63]
	v_mfma_f32_32x32x16_bf16 v[96:111], v[128:131], v[150:153], v[96:111]
	ds_read_b64_tr_b16 v[150:151], v133 offset:0x1000
	ds_read_b64_tr_b16 v[152:153], v135 offset:0x1000
	v_mfma_f32_32x32x16_bf16 v[112:127], v[128:131], v[182:185], v[112:127]
	ds_read_b64_tr_b16 v[182:183], v133 offset:0x1200
	ds_read_b64_tr_b16 v[184:185], v135 offset:0x1200
	v_mfma_f32_32x32x16_bf16 v[80:95], v[128:131], v[186:189], v[80:95]
	ds_read_b64_tr_b16 v[186:187], v133 offset:0x1400
	ds_read_b64_tr_b16 v[188:189], v135 offset:0x1400
	ds_read_b64_tr_b16 v[194:195], v133 offset:0x1600
	ds_read_b64_tr_b16 v[196:197], v135 offset:0x1600
	s_waitcnt lgkmcnt(0)
	v_mfma_f32_32x32x16_bf16 v[64:79], v[128:131], v[190:193], v[64:79]
	v_mfma_f32_32x32x16_bf16 v[96:111], v[146:149], v[150:153], v[96:111]
	v_mfma_f32_32x32x16_bf16 v[112:127], v[146:149], v[182:185], v[112:127]
	v_mfma_f32_32x32x16_bf16 v[80:95], v[146:149], v[186:189], v[80:95]
	v_mfma_f32_32x32x16_bf16 v[64:79], v[146:149], v[194:197], v[64:79]
	s_waitcnt vmcnt(4) lgkmcnt(0)
	s_barrier
; #define VM_WAIT() asm volatile("s_waitcnt vmcnt(0)" ::: "memory")
; template <int DK, int DV, bool MLSTM>
; __device__ __forceinline__ void out_unit2(LAS unsigned char* lds, LAS unsigned char* ldstab, const OutArgs a, const int wv) {
;     ...
; #pragma unroll
;     for (int pc = 0; pc < 4; ++pc) {
;         VM_WAIT(); __syncthreads();
;         OUT_DMA(pc + 1);
;         const bf16x8 af0 = pa[2 * pc], af1 = pa[2 * pc + 1];
;         OUT_MMA(pc & 1);
;     }
; #pragma unroll 1
;     for (int pc = 4; pc < 4 + 2 * NCP; ++pc) {
;         VM_WAIT(); __syncthreads();
;         if (pc + 1 < 4 + 2 * NCP) OUT_DMA(pc + 1);
;         const int cq = pc - 4, dirb = cq >= NCP, cp = dirb ? cq - NCP : cq;
;         const float qs = dirb ? qsb : qsf;
;         const unsigned qa = QP + (cp >> 2) * 32768u + 512u * (cp & 3) + 8192u * rb;
;         const bf16x8 af0 = scale_frag(lds_r128(qa + rb0), qs), af1 = scale_frag(lds_r128(qa + rb1), qs);
	s_add_u32 s42, s11, 0x8000
	s_addc_u32 s43, s12, 0
	v_lshl_add_u64 v[128:129], s[42:43], 0, v[198:199]
	v_lshl_add_u64 v[130:131], s[42:43], 0, v[200:201]
	v_lshl_add_u64 v[146:147], s[42:43], 0, v[202:203]
	v_lshl_add_u64 v[148:149], s[42:43], 0, v[204:205]
	s_add_i32 m0, s6, 0x10000
	s_nop 0
	global_load_lds_dwordx4 v[128:129], off
	s_add_i32 m0, s7, 0x10000
	s_nop 0
	global_load_lds_dwordx4 v[130:131], off
	s_add_i32 m0, s38, 0x10000
	s_nop 0
	global_load_lds_dwordx4 v[146:147], off
	s_add_i32 m0, s40, 0x10000
	s_nop 0
	global_load_lds_dwordx4 v[148:149], off
	v_add_u32_e32 v133, s13, v173
	v_add_u32_e32 v135, s13, v177
	ds_read_b128 v[128:131], v133 offset:34304
	ds_read_b128 v[146:149], v135 offset:34304
	s_waitcnt lgkmcnt(0)
	v_lshlrev_b32_e32 v135, 16, v128
	v_and_b32_e32 v137, 0xffff0000, v128
	v_mul_f32_e32 v135, v179, v135
	v_mul_f32_e32 v137, v179, v137
	v_cvt_pk_bf16_f32 v128, v135, v137
	v_lshlrev_b32_e32 v135, 16, v129
	v_and_b32_e32 v137, 0xffff0000, v129
	v_mul_f32_e32 v135, v179, v135
	v_mul_f32_e32 v137, v179, v137
	v_cvt_pk_bf16_f32 v129, v135, v137
	v_lshlrev_b32_e32 v135, 16, v130
	v_and_b32_e32 v137, 0xffff0000, v130
	v_mul_f32_e32 v135, v179, v135
	v_mul_f32_e32 v137, v179, v137
	v_cvt_pk_bf16_f32 v130, v135, v137
	v_lshlrev_b32_e32 v135, 16, v131
	v_and_b32_e32 v137, 0xffff0000, v131
	v_mul_f32_e32 v135, v179, v135
	v_mul_f32_e32 v137, v179, v137
	v_cvt_pk_bf16_f32 v131, v135, v137
	v_lshlrev_b32_e32 v135, 16, v146
	v_and_b32_e32 v137, 0xffff0000, v146
	v_mul_f32_e32 v135, v179, v135
	v_mul_f32_e32 v137, v179, v137
	v_cvt_pk_bf16_f32 v146, v135, v137
	v_lshlrev_b32_e32 v135, 16, v147
	v_and_b32_e32 v137, 0xffff0000, v147
	v_mul_f32_e32 v135, v179, v135
	v_mul_f32_e32 v137, v179, v137
	v_cvt_pk_bf16_f32 v147, v135, v137
	v_lshlrev_b32_e32 v135, 16, v148
	v_and_b32_e32 v137, 0xffff0000, v148
	v_mul_f32_e32 v135, v179, v135
	v_mul_f32_e32 v137, v179, v137
	v_cvt_pk_bf16_f32 v148, v135, v137
	v_lshlrev_b32_e32 v135, 16, v149
	v_and_b32_e32 v137, 0xffff0000, v149
	v_mul_f32_e32 v135, v179, v135
	v_mul_f32_e32 v137, v179, v137
	v_cvt_pk_bf16_f32 v149, v135, v137
	v_add_u32_e32 v133, 0x18000, v175
	ds_read_b64_tr_b16 v[150:151], v133 offset:0
	v_add_u32_e32 v135, 0x18000, v181
	ds_read_b64_tr_b16 v[152:153], v135 offset:0
	ds_read_b64_tr_b16 v[182:183], v133 offset:0x200
	ds_read_b64_tr_b16 v[184:185], v135 offset:0x200
	ds_read_b64_tr_b16 v[186:187], v133 offset:0x400
	ds_read_b64_tr_b16 v[188:189], v135 offset:0x400
	ds_read_b64_tr_b16 v[190:191], v133 offset:0x600
	ds_read_b64_tr_b16 v[192:193], v135 offset:0x600
	s_waitcnt lgkmcnt(0)
	s_nop 0
	v_mfma_f32_32x32x16_bf16 v[16:31], v[128:131], v[150:153], v[16:31]
	ds_read_b64_tr_b16 v[150:151], v133 offset:0x1000
	ds_read_b64_tr_b16 v[152:153], v135 offset:0x1000
	v_mfma_f32_32x32x16_bf16 v[0:15], v[128:131], v[182:185], v[0:15]
	ds_read_b64_tr_b16 v[182:183], v133 offset:0x1200
	ds_read_b64_tr_b16 v[184:185], v135 offset:0x1200
	v_mfma_f32_32x32x16_bf16 v[32:47], v[128:131], v[186:189], v[32:47]
	ds_read_b64_tr_b16 v[186:187], v133 offset:0x1400
	ds_read_b64_tr_b16 v[188:189], v135 offset:0x1400
	ds_read_b64_tr_b16 v[194:195], v133 offset:0x1600
	ds_read_b64_tr_b16 v[196:197], v135 offset:0x1600
	s_waitcnt lgkmcnt(0)
	v_mfma_f32_32x32x16_bf16 v[48:63], v[128:131], v[190:193], v[48:63]
	v_mfma_f32_32x32x16_bf16 v[16:31], v[146:149], v[150:153], v[16:31]
	v_add_u32_e32 v133, 0x2000, v133
	ds_read_b64_tr_b16 v[150:151], v133 offset:0
	v_add_u32_e32 v135, 0x2000, v135
	ds_read_b64_tr_b16 v[152:153], v135 offset:0
	v_mfma_f32_32x32x16_bf16 v[0:15], v[146:149], v[182:185], v[0:15]
	ds_read_b64_tr_b16 v[182:183], v133 offset:0x200
	ds_read_b64_tr_b16 v[184:185], v135 offset:0x200
	v_mfma_f32_32x32x16_bf16 v[32:47], v[146:149], v[186:189], v[32:47]
	ds_read_b64_tr_b16 v[186:187], v133 offset:0x400
	ds_read_b64_tr_b16 v[188:189], v135 offset:0x400
	ds_read_b64_tr_b16 v[190:191], v133 offset:0x600
	ds_read_b64_tr_b16 v[192:193], v135 offset:0x600
	s_waitcnt lgkmcnt(0)
	v_mfma_f32_32x32x16_bf16 v[48:63], v[146:149], v[194:197], v[48:63]
	v_mfma_f32_32x32x16_bf16 v[96:111], v[128:131], v[150:153], v[96:111]
	ds_read_b64_tr_b16 v[150:151], v133 offset:0x1000
	ds_read_b64_tr_b16 v[152:153], v135 offset:0x1000
	v_mfma_f32_32x32x16_bf16 v[112:127], v[128:131], v[182:185], v[112:127]
	ds_read_b64_tr_b16 v[182:183], v133 offset:0x1200
	ds_read_b64_tr_b16 v[184:185], v135 offset:0x1200
	v_mfma_f32_32x32x16_bf16 v[80:95], v[128:131], v[186:189], v[80:95]
	ds_read_b64_tr_b16 v[186:187], v133 offset:0x1400
	ds_read_b64_tr_b16 v[188:189], v135 offset:0x1400
	ds_read_b64_tr_b16 v[194:195], v133 offset:0x1600
	ds_read_b64_tr_b16 v[196:197], v135 offset:0x1600
	s_waitcnt lgkmcnt(0)
	v_mfma_f32_32x32x16_bf16 v[64:79], v[128:131], v[190:193], v[64:79]
	v_mfma_f32_32x32x16_bf16 v[96:111], v[146:149], v[150:153], v[96:111]
	v_mfma_f32_32x32x16_bf16 v[112:127], v[146:149], v[182:185], v[112:127]
	v_mfma_f32_32x32x16_bf16 v[80:95], v[146:149], v[186:189], v[80:95]
	v_mfma_f32_32x32x16_bf16 v[64:79], v[146:149], v[194:197], v[64:79]
	s_waitcnt vmcnt(4) lgkmcnt(0)
	s_barrier
; #define VM_WAIT() asm volatile("s_waitcnt vmcnt(0)" ::: "memory")
; template <int DK, int DV, bool MLSTM>
; __device__ __forceinline__ void out_unit2(LAS unsigned char* lds, LAS unsigned char* ldstab, const OutArgs a, const int wv) {
;     ...
; #pragma unroll
;     for (int pc = 0; pc < 4; ++pc) {
;         VM_WAIT(); __syncthreads();
;         OUT_DMA(pc + 1);
;         const bf16x8 af0 = pa[2 * pc], af1 = pa[2 * pc + 1];
;         OUT_MMA(pc & 1);
;     }
; #pragma unroll 1
;     for (int pc = 4; pc < 4 + 2 * NCP; ++pc) {
;         VM_WAIT(); __syncthreads();
;         if (pc + 1 < 4 + 2 * NCP) OUT_DMA(pc + 1);
;         const int cq = pc - 4, dirb = cq >= NCP, cp = dirb ? cq - NCP : cq;
;         const float qs = dirb ? qsb : qsf;
;         const unsigned qa = QP + (cp >> 2) * 32768u + 512u * (cp & 3) + 8192u * rb;
;         const bf16x8 af0 = scale_frag(lds_r128(qa + rb0), qs), af1 = scale_frag(lds_r128(qa + rb1), qs);
	s_add_u32 s42, s11, 0x10000
	s_addc_u32 s43, s12, 0
	v_lshl_add_u64 v[128:129], s[42:43], 0, v[198:199]
	v_lshl_add_u64 v[130:131], s[42:43], 0, v[200:201]
	v_lshl_add_u64 v[146:147], s[42:43], 0, v[202:203]
	v_lshl_add_u64 v[148:149], s[42:43], 0, v[204:205]
	s_add_i32 m0, s6, 0x18000
	s_nop 0
	global_load_lds_dwordx4 v[128:129], off
	s_add_i32 m0, s7, 0x18000
	s_nop 0
	global_load_lds_dwordx4 v[130:131], off
	s_add_i32 m0, s38, 0x18000
	s_nop 0
	global_load_lds_dwordx4 v[146:147], off
	s_add_i32 m0, s40, 0x18000
	s_nop 0
	global_load_lds_dwordx4 v[148:149], off
	v_lshlrev_b32_e32 v135, 16, v236
	v_and_b32_e32 v137, 0xffff0000, v236
	v_mul_f32_e32 v135, v144, v135
	v_mul_f32_e32 v137, v144, v137
	v_cvt_pk_bf16_f32 v128, v135, v137
	v_lshlrev_b32_e32 v135, 16, v237
	v_and_b32_e32 v137, 0xffff0000, v237
	v_mul_f32_e32 v135, v144, v135
	v_mul_f32_e32 v137, v144, v137
	v_cvt_pk_bf16_f32 v129, v135, v137
	v_lshlrev_b32_e32 v135, 16, v238
	v_and_b32_e32 v137, 0xffff0000, v238
	v_mul_f32_e32 v135, v144, v135
	v_mul_f32_e32 v137, v144, v137
	v_cvt_pk_bf16_f32 v130, v135, v137
	v_lshlrev_b32_e32 v135, 16, v239
	v_and_b32_e32 v137, 0xffff0000, v239
	v_mul_f32_e32 v135, v144, v135
	v_mul_f32_e32 v137, v144, v137
	v_cvt_pk_bf16_f32 v131, v135, v137
	v_lshlrev_b32_e32 v135, 16, v240
	v_and_b32_e32 v137, 0xffff0000, v240
	v_mul_f32_e32 v135, v144, v135
	v_mul_f32_e32 v137, v144, v137
	v_cvt_pk_bf16_f32 v146, v135, v137
	v_lshlrev_b32_e32 v135, 16, v241
	v_and_b32_e32 v137, 0xffff0000, v241
	v_mul_f32_e32 v135, v144, v135
	v_mul_f32_e32 v137, v144, v137
	v_cvt_pk_bf16_f32 v147, v135, v137
	v_lshlrev_b32_e32 v135, 16, v242
	v_and_b32_e32 v137, 0xffff0000, v242
	v_mul_f32_e32 v135, v144, v135
	v_mul_f32_e32 v137, v144, v137
	v_cvt_pk_bf16_f32 v148, v135, v137
	v_lshlrev_b32_e32 v135, 16, v243
	v_and_b32_e32 v137, 0xffff0000, v243
	v_mul_f32_e32 v135, v144, v135
	v_mul_f32_e32 v137, v144, v137
	v_cvt_pk_bf16_f32 v149, v135, v137
	v_mov_b32_e32 v133, v175
	ds_read_b64_tr_b16 v[150:151], v133 offset:0
	v_mov_b32_e32 v135, v181
	ds_read_b64_tr_b16 v[152:153], v135 offset:0
	ds_read_b64_tr_b16 v[182:183], v133 offset:0x200
	ds_read_b64_tr_b16 v[184:185], v135 offset:0x200
	ds_read_b64_tr_b16 v[186:187], v133 offset:0x400
	ds_read_b64_tr_b16 v[188:189], v135 offset:0x400
	ds_read_b64_tr_b16 v[190:191], v133 offset:0x600
	ds_read_b64_tr_b16 v[192:193], v135 offset:0x600
	s_waitcnt lgkmcnt(0)
	s_nop 0
	v_mfma_f32_32x32x16_bf16 v[16:31], v[128:131], v[150:153], v[16:31]
	ds_read_b64_tr_b16 v[150:151], v133 offset:0x1000
	ds_read_b64_tr_b16 v[152:153], v135 offset:0x1000
	v_mfma_f32_32x32x16_bf16 v[0:15], v[128:131], v[182:185], v[0:15]
	ds_read_b64_tr_b16 v[182:183], v133 offset:0x1200
	ds_read_b64_tr_b16 v[184:185], v135 offset:0x1200
	v_mfma_f32_32x32x16_bf16 v[32:47], v[128:131], v[186:189], v[32:47]
	ds_read_b64_tr_b16 v[186:187], v133 offset:0x1400
	ds_read_b64_tr_b16 v[188:189], v135 offset:0x1400
	ds_read_b64_tr_b16 v[194:195], v133 offset:0x1600
	ds_read_b64_tr_b16 v[196:197], v135 offset:0x1600
	s_waitcnt lgkmcnt(0)
	v_mfma_f32_32x32x16_bf16 v[48:63], v[128:131], v[190:193], v[48:63]
	v_mfma_f32_32x32x16_bf16 v[16:31], v[146:149], v[150:153], v[16:31]
	v_add_u32_e32 v133, 0x2000, v133
	ds_read_b64_tr_b16 v[150:151], v133 offset:0
	v_add_u32_e32 v135, 0x2000, v135
	ds_read_b64_tr_b16 v[152:153], v135 offset:0
	v_mfma_f32_32x32x16_bf16 v[0:15], v[146:149], v[182:185], v[0:15]
	ds_read_b64_tr_b16 v[182:183], v133 offset:0x200
	ds_read_b64_tr_b16 v[184:185], v135 offset:0x200
	v_mfma_f32_32x32x16_bf16 v[32:47], v[146:149], v[186:189], v[32:47]
	ds_read_b64_tr_b16 v[186:187], v133 offset:0x400
	ds_read_b64_tr_b16 v[188:189], v135 offset:0x400
	ds_read_b64_tr_b16 v[190:191], v133 offset:0x600
	ds_read_b64_tr_b16 v[192:193], v135 offset:0x600
	s_waitcnt lgkmcnt(0)
	v_mfma_f32_32x32x16_bf16 v[48:63], v[146:149], v[194:197], v[48:63]
	v_mfma_f32_32x32x16_bf16 v[96:111], v[128:131], v[150:153], v[96:111]
	ds_read_b64_tr_b16 v[150:151], v133 offset:0x1000
	ds_read_b64_tr_b16 v[152:153], v135 offset:0x1000
	v_mfma_f32_32x32x16_bf16 v[112:127], v[128:131], v[182:185], v[112:127]
	ds_read_b64_tr_b16 v[182:183], v133 offset:0x1200
	ds_read_b64_tr_b16 v[184:185], v135 offset:0x1200
	v_mfma_f32_32x32x16_bf16 v[80:95], v[128:131], v[186:189], v[80:95]
	ds_read_b64_tr_b16 v[186:187], v133 offset:0x1400
	ds_read_b64_tr_b16 v[188:189], v135 offset:0x1400
	ds_read_b64_tr_b16 v[194:195], v133 offset:0x1600
	ds_read_b64_tr_b16 v[196:197], v135 offset:0x1600
	s_waitcnt lgkmcnt(0)
	v_mfma_f32_32x32x16_bf16 v[64:79], v[128:131], v[190:193], v[64:79]
	v_mfma_f32_32x32x16_bf16 v[96:111], v[146:149], v[150:153], v[96:111]
	v_mfma_f32_32x32x16_bf16 v[112:127], v[146:149], v[182:185], v[112:127]
	v_mfma_f32_32x32x16_bf16 v[80:95], v[146:149], v[186:189], v[80:95]
	v_mfma_f32_32x32x16_bf16 v[64:79], v[146:149], v[194:197], v[64:79]
	s_waitcnt vmcnt(4) lgkmcnt(0)
	s_barrier
; #define VM_WAIT() asm volatile("s_waitcnt vmcnt(0)" ::: "memory")
; template <int DK, int DV, bool MLSTM>
; __device__ __forceinline__ void out_unit2(LAS unsigned char* lds, LAS unsigned char* ldstab, const OutArgs a, const int wv) {
;     ...
; #pragma unroll
;     for (int pc = 0; pc < 4; ++pc) {
;         VM_WAIT(); __syncthreads();
;         OUT_DMA(pc + 1);
;         const bf16x8 af0 = pa[2 * pc], af1 = pa[2 * pc + 1];
;         OUT_MMA(pc & 1);
;     }
; #pragma unroll 1
;     for (int pc = 4; pc < 4 + 2 * NCP; ++pc) {
;         VM_WAIT(); __syncthreads();
;         if (pc + 1 < 4 + 2 * NCP) OUT_DMA(pc + 1);
;         const int cq = pc - 4, dirb = cq >= NCP, cp = dirb ? cq - NCP : cq;
;         const float qs = dirb ? qsb : qsf;
;         const unsigned qa = QP + (cp >> 2) * 32768u + 512u * (cp & 3) + 8192u * rb;
;         const bf16x8 af0 = scale_frag(lds_r128(qa + rb0), qs), af1 = scale_frag(lds_r128(qa + rb1), qs);
	s_add_u32 s42, s11, 0x18000
	s_addc_u32 s43, s12, 0
	v_lshl_add_u64 v[128:129], s[42:43], 0, v[198:199]
	v_lshl_add_u64 v[130:131], s[42:43], 0, v[200:201]
	v_lshl_add_u64 v[146:147], s[42:43], 0, v[202:203]
	v_lshl_add_u64 v[148:149], s[42:43], 0, v[204:205]
	s_mov_b32 m0, s6
	s_nop 0
	global_load_lds_dwordx4 v[128:129], off
	s_mov_b32 m0, s7
	s_nop 0
	global_load_lds_dwordx4 v[130:131], off
	s_mov_b32 m0, s38
	s_nop 0
	global_load_lds_dwordx4 v[146:147], off
	s_mov_b32 m0, s40
	s_nop 0
	global_load_lds_dwordx4 v[148:149], off
	v_lshlrev_b32_e32 v135, 16, v244
	v_and_b32_e32 v137, 0xffff0000, v244
	v_mul_f32_e32 v135, v144, v135
	v_mul_f32_e32 v137, v144, v137
	v_cvt_pk_bf16_f32 v128, v135, v137
	v_lshlrev_b32_e32 v135, 16, v245
	v_and_b32_e32 v137, 0xffff0000, v245
	v_mul_f32_e32 v135, v144, v135
	v_mul_f32_e32 v137, v144, v137
	v_cvt_pk_bf16_f32 v129, v135, v137
	v_lshlrev_b32_e32 v135, 16, v246
	v_and_b32_e32 v137, 0xffff0000, v246
	v_mul_f32_e32 v135, v144, v135
	v_mul_f32_e32 v137, v144, v137
	v_cvt_pk_bf16_f32 v130, v135, v137
	v_lshlrev_b32_e32 v135, 16, v247
	v_and_b32_e32 v137, 0xffff0000, v247
	v_mul_f32_e32 v135, v144, v135
	v_mul_f32_e32 v137, v144, v137
	v_cvt_pk_bf16_f32 v131, v135, v137
	v_lshlrev_b32_e32 v135, 16, v248
	v_and_b32_e32 v137, 0xffff0000, v248
	v_mul_f32_e32 v135, v144, v135
	v_mul_f32_e32 v137, v144, v137
	v_cvt_pk_bf16_f32 v146, v135, v137
	v_lshlrev_b32_e32 v135, 16, v249
	v_and_b32_e32 v137, 0xffff0000, v249
	v_mul_f32_e32 v135, v144, v135
	v_mul_f32_e32 v137, v144, v137
	v_cvt_pk_bf16_f32 v147, v135, v137
	v_lshlrev_b32_e32 v135, 16, v250
	v_and_b32_e32 v137, 0xffff0000, v250
	v_mul_f32_e32 v135, v144, v135
	v_mul_f32_e32 v137, v144, v137
	v_cvt_pk_bf16_f32 v148, v135, v137
	v_lshlrev_b32_e32 v135, 16, v251
	v_and_b32_e32 v137, 0xffff0000, v251
	v_mul_f32_e32 v135, v144, v135
	v_mul_f32_e32 v137, v144, v137
	v_cvt_pk_bf16_f32 v149, v135, v137
	v_add_u32_e32 v133, 0x10000, v175
	ds_read_b64_tr_b16 v[150:151], v133 offset:0
	v_add_u32_e32 v135, 0x10000, v181
	ds_read_b64_tr_b16 v[152:153], v135 offset:0
	ds_read_b64_tr_b16 v[182:183], v133 offset:0x200
	ds_read_b64_tr_b16 v[184:185], v135 offset:0x200
	ds_read_b64_tr_b16 v[186:187], v133 offset:0x400
	ds_read_b64_tr_b16 v[188:189], v135 offset:0x400
	ds_read_b64_tr_b16 v[190:191], v133 offset:0x600
	ds_read_b64_tr_b16 v[192:193], v135 offset:0x600
	s_waitcnt lgkmcnt(0)
	s_nop 0
	v_mfma_f32_32x32x16_bf16 v[16:31], v[128:131], v[150:153], v[16:31]
	ds_read_b64_tr_b16 v[150:151], v133 offset:0x1000
	ds_read_b64_tr_b16 v[152:153], v135 offset:0x1000
	v_mfma_f32_32x32x16_bf16 v[0:15], v[128:131], v[182:185], v[0:15]
	ds_read_b64_tr_b16 v[182:183], v133 offset:0x1200
	ds_read_b64_tr_b16 v[184:185], v135 offset:0x1200
	v_mfma_f32_32x32x16_bf16 v[32:47], v[128:131], v[186:189], v[32:47]
	ds_read_b64_tr_b16 v[186:187], v133 offset:0x1400
	ds_read_b64_tr_b16 v[188:189], v135 offset:0x1400
	ds_read_b64_tr_b16 v[194:195], v133 offset:0x1600
	ds_read_b64_tr_b16 v[196:197], v135 offset:0x1600
	s_waitcnt lgkmcnt(0)
	v_mfma_f32_32x32x16_bf16 v[48:63], v[128:131], v[190:193], v[48:63]
	v_mfma_f32_32x32x16_bf16 v[16:31], v[146:149], v[150:153], v[16:31]
	v_add_u32_e32 v133, 0x2000, v133
	ds_read_b64_tr_b16 v[150:151], v133 offset:0
	v_add_u32_e32 v135, 0x2000, v135
	ds_read_b64_tr_b16 v[152:153], v135 offset:0
	v_mfma_f32_32x32x16_bf16 v[0:15], v[146:149], v[182:185], v[0:15]
	ds_read_b64_tr_b16 v[182:183], v133 offset:0x200
	ds_read_b64_tr_b16 v[184:185], v135 offset:0x200
	v_mfma_f32_32x32x16_bf16 v[32:47], v[146:149], v[186:189], v[32:47]
	ds_read_b64_tr_b16 v[186:187], v133 offset:0x400
	ds_read_b64_tr_b16 v[188:189], v135 offset:0x400
	ds_read_b64_tr_b16 v[190:191], v133 offset:0x600
	ds_read_b64_tr_b16 v[192:193], v135 offset:0x600
	s_waitcnt lgkmcnt(0)
	v_mfma_f32_32x32x16_bf16 v[48:63], v[146:149], v[194:197], v[48:63]
	v_mfma_f32_32x32x16_bf16 v[96:111], v[128:131], v[150:153], v[96:111]
	ds_read_b64_tr_b16 v[150:151], v133 offset:0x1000
	ds_read_b64_tr_b16 v[152:153], v135 offset:0x1000
	v_mfma_f32_32x32x16_bf16 v[112:127], v[128:131], v[182:185], v[112:127]
	ds_read_b64_tr_b16 v[182:183], v133 offset:0x1200
	ds_read_b64_tr_b16 v[184:185], v135 offset:0x1200
	v_mfma_f32_32x32x16_bf16 v[80:95], v[128:131], v[186:189], v[80:95]
	ds_read_b64_tr_b16 v[186:187], v133 offset:0x1400
	ds_read_b64_tr_b16 v[188:189], v135 offset:0x1400
	ds_read_b64_tr_b16 v[194:195], v133 offset:0x1600
	ds_read_b64_tr_b16 v[196:197], v135 offset:0x1600
	s_waitcnt lgkmcnt(0)
	v_mfma_f32_32x32x16_bf16 v[64:79], v[128:131], v[190:193], v[64:79]
	v_mfma_f32_32x32x16_bf16 v[96:111], v[146:149], v[150:153], v[96:111]
	v_mfma_f32_32x32x16_bf16 v[112:127], v[146:149], v[182:185], v[112:127]
	v_mfma_f32_32x32x16_bf16 v[80:95], v[146:149], v[186:189], v[80:95]
	v_mfma_f32_32x32x16_bf16 v[64:79], v[146:149], v[194:197], v[64:79]
	s_waitcnt vmcnt(4) lgkmcnt(0)
	s_barrier
; #define VM_WAIT() asm volatile("s_waitcnt vmcnt(0)" ::: "memory")
; template <int DK, int DV, bool MLSTM>
; __device__ __forceinline__ void out_unit2(LAS unsigned char* lds, LAS unsigned char* ldstab, const OutArgs a, const int wv) {
;     ...
; #pragma unroll
;     for (int pc = 0; pc < 4; ++pc) {
;         VM_WAIT(); __syncthreads();
;         OUT_DMA(pc + 1);
;         const bf16x8 af0 = pa[2 * pc], af1 = pa[2 * pc + 1];
;         OUT_MMA(pc & 1);
;     }
; #pragma unroll 1
;     for (int pc = 4; pc < 4 + 2 * NCP; ++pc) {
;         VM_WAIT(); __syncthreads();
;         if (pc + 1 < 4 + 2 * NCP) OUT_DMA(pc + 1);
;         const int cq = pc - 4, dirb = cq >= NCP, cp = dirb ? cq - NCP : cq;
;         const float qs = dirb ? qsb : qsf;
;         const unsigned qa = QP + (cp >> 2) * 32768u + 512u * (cp & 3) + 8192u * rb;
;         const bf16x8 af0 = scale_frag(lds_r128(qa + rb0), qs), af1 = scale_frag(lds_r128(qa + rb1), qs);
	s_add_u32 s42, s11, 0x20000
	s_addc_u32 s43, s12, 0
	v_lshl_add_u64 v[128:129], s[42:43], 0, v[198:199]
	v_lshl_add_u64 v[130:131], s[42:43], 0, v[200:201]
	v_lshl_add_u64 v[146:147], s[42:43], 0, v[202:203]
	v_lshl_add_u64 v[148:149], s[42:43], 0, v[204:205]
	s_add_i32 m0, s6, 0x10000
	s_nop 0
	global_load_lds_dwordx4 v[128:129], off
	s_add_i32 m0, s7, 0x10000
	s_nop 0
	global_load_lds_dwordx4 v[130:131], off
	s_add_i32 m0, s38, 0x10000
	s_nop 0
	global_load_lds_dwordx4 v[146:147], off
	s_add_i32 m0, s40, 0x10000
	s_nop 0
	global_load_lds_dwordx4 v[148:149], off
	v_lshlrev_b32_e32 v135, 16, v252
	v_and_b32_e32 v137, 0xffff0000, v252
	v_mul_f32_e32 v135, v144, v135
	v_mul_f32_e32 v137, v144, v137
	v_cvt_pk_bf16_f32 v128, v135, v137
	v_lshlrev_b32_e32 v135, 16, v253
	v_and_b32_e32 v137, 0xffff0000, v253
	v_mul_f32_e32 v135, v144, v135
	v_mul_f32_e32 v137, v144, v137
	v_cvt_pk_bf16_f32 v129, v135, v137
	v_lshlrev_b32_e32 v135, 16, v254
	v_and_b32_e32 v137, 0xffff0000, v254
	v_mul_f32_e32 v135, v144, v135
	v_mul_f32_e32 v137, v144, v137
	v_cvt_pk_bf16_f32 v130, v135, v137
	v_lshlrev_b32_e32 v135, 16, v255
	v_and_b32_e32 v137, 0xffff0000, v255
	v_mul_f32_e32 v135, v144, v135
	v_mul_f32_e32 v137, v144, v137
	v_cvt_pk_bf16_f32 v131, v135, v137
	v_lshlrev_b32_e32 v135, 16, v218
	v_and_b32_e32 v137, 0xffff0000, v218
	v_mul_f32_e32 v135, v144, v135
	v_mul_f32_e32 v137, v144, v137
	v_cvt_pk_bf16_f32 v146, v135, v137
	v_lshlrev_b32_e32 v135, 16, v219
	v_and_b32_e32 v137, 0xffff0000, v219
	v_mul_f32_e32 v135, v144, v135
	v_mul_f32_e32 v137, v144, v137
	v_cvt_pk_bf16_f32 v147, v135, v137
	v_lshlrev_b32_e32 v135, 16, v220
	v_and_b32_e32 v137, 0xffff0000, v220
	v_mul_f32_e32 v135, v144, v135
	v_mul_f32_e32 v137, v144, v137
	v_cvt_pk_bf16_f32 v148, v135, v137
	v_lshlrev_b32_e32 v135, 16, v221
	v_and_b32_e32 v137, 0xffff0000, v221
	v_mul_f32_e32 v135, v144, v135
	v_mul_f32_e32 v137, v144, v137
	v_cvt_pk_bf16_f32 v149, v135, v137
	v_add_u32_e32 v133, 0x18000, v175
	ds_read_b64_tr_b16 v[150:151], v133 offset:0
	v_add_u32_e32 v135, 0x18000, v181
	ds_read_b64_tr_b16 v[152:153], v135 offset:0
	ds_read_b64_tr_b16 v[182:183], v133 offset:0x200
	ds_read_b64_tr_b16 v[184:185], v135 offset:0x200
	ds_read_b64_tr_b16 v[186:187], v133 offset:0x400
	ds_read_b64_tr_b16 v[188:189], v135 offset:0x400
	ds_read_b64_tr_b16 v[190:191], v133 offset:0x600
	ds_read_b64_tr_b16 v[192:193], v135 offset:0x600
	s_waitcnt lgkmcnt(0)
	s_nop 0
	v_mfma_f32_32x32x16_bf16 v[16:31], v[128:131], v[150:153], v[16:31]
	ds_read_b64_tr_b16 v[150:151], v133 offset:0x1000
	ds_read_b64_tr_b16 v[152:153], v135 offset:0x1000
	v_mfma_f32_32x32x16_bf16 v[0:15], v[128:131], v[182:185], v[0:15]
	ds_read_b64_tr_b16 v[182:183], v133 offset:0x1200
	ds_read_b64_tr_b16 v[184:185], v135 offset:0x1200
	v_mfma_f32_32x32x16_bf16 v[32:47], v[128:131], v[186:189], v[32:47]
	ds_read_b64_tr_b16 v[186:187], v133 offset:0x1400
	ds_read_b64_tr_b16 v[188:189], v135 offset:0x1400
	ds_read_b64_tr_b16 v[194:195], v133 offset:0x1600
	ds_read_b64_tr_b16 v[196:197], v135 offset:0x1600
	s_waitcnt lgkmcnt(0)
	v_mfma_f32_32x32x16_bf16 v[48:63], v[128:131], v[190:193], v[48:63]
	v_mfma_f32_32x32x16_bf16 v[16:31], v[146:149], v[150:153], v[16:31]
	v_add_u32_e32 v133, 0x2000, v133
	ds_read_b64_tr_b16 v[150:151], v133 offset:0
	v_add_u32_e32 v135, 0x2000, v135
	ds_read_b64_tr_b16 v[152:153], v135 offset:0
	v_mfma_f32_32x32x16_bf16 v[0:15], v[146:149], v[182:185], v[0:15]
	ds_read_b64_tr_b16 v[182:183], v133 offset:0x200
	ds_read_b64_tr_b16 v[184:185], v135 offset:0x200
	v_mfma_f32_32x32x16_bf16 v[32:47], v[146:149], v[186:189], v[32:47]
	ds_read_b64_tr_b16 v[186:187], v133 offset:0x400
	ds_read_b64_tr_b16 v[188:189], v135 offset:0x400
	ds_read_b64_tr_b16 v[190:191], v133 offset:0x600
	ds_read_b64_tr_b16 v[192:193], v135 offset:0x600
	s_waitcnt lgkmcnt(0)
	v_mfma_f32_32x32x16_bf16 v[48:63], v[146:149], v[194:197], v[48:63]
	v_mfma_f32_32x32x16_bf16 v[96:111], v[128:131], v[150:153], v[96:111]
	ds_read_b64_tr_b16 v[150:151], v133 offset:0x1000
	ds_read_b64_tr_b16 v[152:153], v135 offset:0x1000
	v_mfma_f32_32x32x16_bf16 v[112:127], v[128:131], v[182:185], v[112:127]
	ds_read_b64_tr_b16 v[182:183], v133 offset:0x1200
	ds_read_b64_tr_b16 v[184:185], v135 offset:0x1200
	v_mfma_f32_32x32x16_bf16 v[80:95], v[128:131], v[186:189], v[80:95]
	ds_read_b64_tr_b16 v[186:187], v133 offset:0x1400
	ds_read_b64_tr_b16 v[188:189], v135 offset:0x1400
	ds_read_b64_tr_b16 v[194:195], v133 offset:0x1600
	ds_read_b64_tr_b16 v[196:197], v135 offset:0x1600
	s_waitcnt lgkmcnt(0)
	v_mfma_f32_32x32x16_bf16 v[64:79], v[128:131], v[190:193], v[64:79]
	v_mfma_f32_32x32x16_bf16 v[96:111], v[146:149], v[150:153], v[96:111]
	v_mfma_f32_32x32x16_bf16 v[112:127], v[146:149], v[182:185], v[112:127]
	v_mfma_f32_32x32x16_bf16 v[80:95], v[146:149], v[186:189], v[80:95]
	v_mfma_f32_32x32x16_bf16 v[64:79], v[146:149], v[194:197], v[64:79]
	s_waitcnt vmcnt(4) lgkmcnt(0)
	s_barrier
; #define VM_WAIT() asm volatile("s_waitcnt vmcnt(0)" ::: "memory")
; template <int DK, int DV, bool MLSTM>
; __device__ __forceinline__ void out_unit2(LAS unsigned char* lds, LAS unsigned char* ldstab, const OutArgs a, const int wv) {
;     ...
; #pragma unroll
;     for (int pc = 0; pc < 4; ++pc) {
;         VM_WAIT(); __syncthreads();
;         OUT_DMA(pc + 1);
;         const bf16x8 af0 = pa[2 * pc], af1 = pa[2 * pc + 1];
;         OUT_MMA(pc & 1);
;     }
; #pragma unroll 1
;     for (int pc = 4; pc < 4 + 2 * NCP; ++pc) {
;         VM_WAIT(); __syncthreads();
;         if (pc + 1 < 4 + 2 * NCP) OUT_DMA(pc + 1);
;         const int cq = pc - 4, dirb = cq >= NCP, cp = dirb ? cq - NCP : cq;
;         const float qs = dirb ? qsb : qsf;
;         const unsigned qa = QP + (cp >> 2) * 32768u + 512u * (cp & 3) + 8192u * rb;
;         const bf16x8 af0 = scale_frag(lds_r128(qa + rb0), qs), af1 = scale_frag(lds_r128(qa + rb1), qs);
	s_add_u32 s42, s11, 0x28000
	s_addc_u32 s43, s12, 0
	v_lshl_add_u64 v[128:129], s[42:43], 0, v[198:199]
	v_lshl_add_u64 v[130:131], s[42:43], 0, v[200:201]
	v_lshl_add_u64 v[146:147], s[42:43], 0, v[202:203]
	v_lshl_add_u64 v[148:149], s[42:43], 0, v[204:205]
	s_add_i32 m0, s6, 0x18000
	s_nop 0
	global_load_lds_dwordx4 v[128:129], off
	s_add_i32 m0, s7, 0x18000
	s_nop 0
	global_load_lds_dwordx4 v[130:131], off
	s_add_i32 m0, s38, 0x18000
	s_nop 0
	global_load_lds_dwordx4 v[146:147], off
	s_add_i32 m0, s40, 0x18000
	s_nop 0
	global_load_lds_dwordx4 v[148:149], off
	v_lshlrev_b32_e32 v135, 16, v222
	v_and_b32_e32 v137, 0xffff0000, v222
	v_mul_f32_e32 v135, v144, v135
	v_mul_f32_e32 v137, v144, v137
	v_cvt_pk_bf16_f32 v128, v135, v137
	v_lshlrev_b32_e32 v135, 16, v223
	v_and_b32_e32 v137, 0xffff0000, v223
	v_mul_f32_e32 v135, v144, v135
	v_mul_f32_e32 v137, v144, v137
	v_cvt_pk_bf16_f32 v129, v135, v137
	v_lshlrev_b32_e32 v135, 16, v224
	v_and_b32_e32 v137, 0xffff0000, v224
	v_mul_f32_e32 v135, v144, v135
	v_mul_f32_e32 v137, v144, v137
	v_cvt_pk_bf16_f32 v130, v135, v137
	v_lshlrev_b32_e32 v135, 16, v225
	v_and_b32_e32 v137, 0xffff0000, v225
	v_mul_f32_e32 v135, v144, v135
	v_mul_f32_e32 v137, v144, v137
	v_cvt_pk_bf16_f32 v131, v135, v137
	v_lshlrev_b32_e32 v135, 16, v206
	v_and_b32_e32 v137, 0xffff0000, v206
	v_mul_f32_e32 v135, v144, v135
	v_mul_f32_e32 v137, v144, v137
	v_cvt_pk_bf16_f32 v146, v135, v137
	v_lshlrev_b32_e32 v135, 16, v207
	v_and_b32_e32 v137, 0xffff0000, v207
	v_mul_f32_e32 v135, v144, v135
	v_mul_f32_e32 v137, v144, v137
	v_cvt_pk_bf16_f32 v147, v135, v137
	v_lshlrev_b32_e32 v135, 16, v208
	v_and_b32_e32 v137, 0xffff0000, v208
	v_mul_f32_e32 v135, v144, v135
	v_mul_f32_e32 v137, v144, v137
	v_cvt_pk_bf16_f32 v148, v135, v137
	v_lshlrev_b32_e32 v135, 16, v209
	v_and_b32_e32 v137, 0xffff0000, v209
	v_mul_f32_e32 v135, v144, v135
	v_mul_f32_e32 v137, v144, v137
	v_cvt_pk_bf16_f32 v149, v135, v137
	v_mov_b32_e32 v133, v175
	ds_read_b64_tr_b16 v[150:151], v133 offset:0
	v_mov_b32_e32 v135, v181
	ds_read_b64_tr_b16 v[152:153], v135 offset:0
	ds_read_b64_tr_b16 v[182:183], v133 offset:0x200
	ds_read_b64_tr_b16 v[184:185], v135 offset:0x200
	ds_read_b64_tr_b16 v[186:187], v133 offset:0x400
	ds_read_b64_tr_b16 v[188:189], v135 offset:0x400
	ds_read_b64_tr_b16 v[190:191], v133 offset:0x600
	ds_read_b64_tr_b16 v[192:193], v135 offset:0x600
	s_waitcnt lgkmcnt(0)
	s_nop 0
	v_mfma_f32_32x32x16_bf16 v[16:31], v[128:131], v[150:153], v[16:31]
	ds_read_b64_tr_b16 v[150:151], v133 offset:0x1000
	ds_read_b64_tr_b16 v[152:153], v135 offset:0x1000
	v_mfma_f32_32x32x16_bf16 v[0:15], v[128:131], v[182:185], v[0:15]
	ds_read_b64_tr_b16 v[182:183], v133 offset:0x1200
	ds_read_b64_tr_b16 v[184:185], v135 offset:0x1200
	v_mfma_f32_32x32x16_bf16 v[32:47], v[128:131], v[186:189], v[32:47]
	ds_read_b64_tr_b16 v[186:187], v133 offset:0x1400
	ds_read_b64_tr_b16 v[188:189], v135 offset:0x1400
	ds_read_b64_tr_b16 v[194:195], v133 offset:0x1600
	ds_read_b64_tr_b16 v[196:197], v135 offset:0x1600
	s_waitcnt lgkmcnt(0)
	v_mfma_f32_32x32x16_bf16 v[48:63], v[128:131], v[190:193], v[48:63]
	v_mfma_f32_32x32x16_bf16 v[16:31], v[146:149], v[150:153], v[16:31]
	v_add_u32_e32 v133, 0x2000, v133
	ds_read_b64_tr_b16 v[150:151], v133 offset:0
	v_add_u32_e32 v135, 0x2000, v135
	ds_read_b64_tr_b16 v[152:153], v135 offset:0
	v_mfma_f32_32x32x16_bf16 v[0:15], v[146:149], v[182:185], v[0:15]
	ds_read_b64_tr_b16 v[182:183], v133 offset:0x200
	ds_read_b64_tr_b16 v[184:185], v135 offset:0x200
	v_mfma_f32_32x32x16_bf16 v[32:47], v[146:149], v[186:189], v[32:47]
	ds_read_b64_tr_b16 v[186:187], v133 offset:0x400
	ds_read_b64_tr_b16 v[188:189], v135 offset:0x400
	ds_read_b64_tr_b16 v[190:191], v133 offset:0x600
	ds_read_b64_tr_b16 v[192:193], v135 offset:0x600
	s_waitcnt lgkmcnt(0)
	v_mfma_f32_32x32x16_bf16 v[48:63], v[146:149], v[194:197], v[48:63]
	v_mfma_f32_32x32x16_bf16 v[96:111], v[128:131], v[150:153], v[96:111]
	ds_read_b64_tr_b16 v[150:151], v133 offset:0x1000
	ds_read_b64_tr_b16 v[152:153], v135 offset:0x1000
	v_mfma_f32_32x32x16_bf16 v[112:127], v[128:131], v[182:185], v[112:127]
	ds_read_b64_tr_b16 v[182:183], v133 offset:0x1200
	ds_read_b64_tr_b16 v[184:185], v135 offset:0x1200
	v_mfma_f32_32x32x16_bf16 v[80:95], v[128:131], v[186:189], v[80:95]
	ds_read_b64_tr_b16 v[186:187], v133 offset:0x1400
	ds_read_b64_tr_b16 v[188:189], v135 offset:0x1400
	ds_read_b64_tr_b16 v[194:195], v133 offset:0x1600
	ds_read_b64_tr_b16 v[196:197], v135 offset:0x1600
	s_waitcnt lgkmcnt(0)
	v_mfma_f32_32x32x16_bf16 v[64:79], v[128:131], v[190:193], v[64:79]
	v_mfma_f32_32x32x16_bf16 v[96:111], v[146:149], v[150:153], v[96:111]
	v_mfma_f32_32x32x16_bf16 v[112:127], v[146:149], v[182:185], v[112:127]
	v_mfma_f32_32x32x16_bf16 v[80:95], v[146:149], v[186:189], v[80:95]
	v_mfma_f32_32x32x16_bf16 v[64:79], v[146:149], v[194:197], v[64:79]
	s_waitcnt vmcnt(4) lgkmcnt(0)
	s_barrier
; #define VM_WAIT() asm volatile("s_waitcnt vmcnt(0)" ::: "memory")
; template <int DK, int DV, bool MLSTM>
; __device__ __forceinline__ void out_unit2(LAS unsigned char* lds, LAS unsigned char* ldstab, const OutArgs a, const int wv) {
;     ...
; #pragma unroll
;     for (int pc = 0; pc < 4; ++pc) {
;         VM_WAIT(); __syncthreads();
;         OUT_DMA(pc + 1);
;         const bf16x8 af0 = pa[2 * pc], af1 = pa[2 * pc + 1];
;         OUT_MMA(pc & 1);
;     }
; #pragma unroll 1
;     for (int pc = 4; pc < 4 + 2 * NCP; ++pc) {
;         VM_WAIT(); __syncthreads();
;         if (pc + 1 < 4 + 2 * NCP) OUT_DMA(pc + 1);
;         const int cq = pc - 4, dirb = cq >= NCP, cp = dirb ? cq - NCP : cq;
;         const float qs = dirb ? qsb : qsf;
;         const unsigned qa = QP + (cp >> 2) * 32768u + 512u * (cp & 3) + 8192u * rb;
;         const bf16x8 af0 = scale_frag(lds_r128(qa + rb0), qs), af1 = scale_frag(lds_r128(qa + rb1), qs);
	s_add_u32 s42, s11, 0x30000
	s_addc_u32 s43, s12, 0
	v_lshl_add_u64 v[128:129], s[42:43], 0, v[198:199]
	v_lshl_add_u64 v[130:131], s[42:43], 0, v[200:201]
	v_lshl_add_u64 v[146:147], s[42:43], 0, v[202:203]
	v_lshl_add_u64 v[148:149], s[42:43], 0, v[204:205]
	s_mov_b32 m0, s6
	s_nop 0
	global_load_lds_dwordx4 v[128:129], off
	s_mov_b32 m0, s7
	s_nop 0
	global_load_lds_dwordx4 v[130:131], off
	s_mov_b32 m0, s38
	s_nop 0
	global_load_lds_dwordx4 v[146:147], off
	s_mov_b32 m0, s40
	s_nop 0
	global_load_lds_dwordx4 v[148:149], off
	v_add_u32_e32 v133, s13, v173
	v_add_u32_e32 v135, s13, v177
	ds_read_b128 v[128:131], v133 offset:32768
	ds_read_b128 v[146:149], v135 offset:32768
	s_waitcnt lgkmcnt(0)
	v_lshlrev_b32_e32 v135, 16, v128
	v_and_b32_e32 v137, 0xffff0000, v128
	v_mul_f32_e32 v135, v144, v135
	v_mul_f32_e32 v137, v144, v137
	v_cvt_pk_bf16_f32 v128, v135, v137
	v_lshlrev_b32_e32 v135, 16, v129
	v_and_b32_e32 v137, 0xffff0000, v129
	v_mul_f32_e32 v135, v144, v135
	v_mul_f32_e32 v137, v144, v137
	v_cvt_pk_bf16_f32 v129, v135, v137
	v_lshlrev_b32_e32 v135, 16, v130
	v_and_b32_e32 v137, 0xffff0000, v130
	v_mul_f32_e32 v135, v144, v135
	v_mul_f32_e32 v137, v144, v137
	v_cvt_pk_bf16_f32 v130, v135, v137
	v_lshlrev_b32_e32 v135, 16, v131
	v_and_b32_e32 v137, 0xffff0000, v131
	v_mul_f32_e32 v135, v144, v135
	v_mul_f32_e32 v137, v144, v137
	v_cvt_pk_bf16_f32 v131, v135, v137
	v_lshlrev_b32_e32 v135, 16, v146
	v_and_b32_e32 v137, 0xffff0000, v146
	v_mul_f32_e32 v135, v144, v135
	v_mul_f32_e32 v137, v144, v137
	v_cvt_pk_bf16_f32 v146, v135, v137
	v_lshlrev_b32_e32 v135, 16, v147
	v_and_b32_e32 v137, 0xffff0000, v147
	v_mul_f32_e32 v135, v144, v135
	v_mul_f32_e32 v137, v144, v137
	v_cvt_pk_bf16_f32 v147, v135, v137
	v_lshlrev_b32_e32 v135, 16, v148
	v_and_b32_e32 v137, 0xffff0000, v148
	v_mul_f32_e32 v135, v144, v135
	v_mul_f32_e32 v137, v144, v137
	v_cvt_pk_bf16_f32 v148, v135, v137
	v_lshlrev_b32_e32 v135, 16, v149
	v_and_b32_e32 v137, 0xffff0000, v149
	v_mul_f32_e32 v135, v144, v135
	v_mul_f32_e32 v137, v144, v137
	v_cvt_pk_bf16_f32 v149, v135, v137
	v_add_u32_e32 v133, 0x10000, v175
	ds_read_b64_tr_b16 v[150:151], v133 offset:0
	v_add_u32_e32 v135, 0x10000, v181
	ds_read_b64_tr_b16 v[152:153], v135 offset:0
	ds_read_b64_tr_b16 v[182:183], v133 offset:0x200
	ds_read_b64_tr_b16 v[184:185], v135 offset:0x200
	ds_read_b64_tr_b16 v[186:187], v133 offset:0x400
	ds_read_b64_tr_b16 v[188:189], v135 offset:0x400
	ds_read_b64_tr_b16 v[190:191], v133 offset:0x600
	ds_read_b64_tr_b16 v[192:193], v135 offset:0x600
	s_waitcnt lgkmcnt(0)
	s_nop 0
	v_mfma_f32_32x32x16_bf16 v[16:31], v[128:131], v[150:153], v[16:31]
	ds_read_b64_tr_b16 v[150:151], v133 offset:0x1000
	ds_read_b64_tr_b16 v[152:153], v135 offset:0x1000
	v_mfma_f32_32x32x16_bf16 v[0:15], v[128:131], v[182:185], v[0:15]
	ds_read_b64_tr_b16 v[182:183], v133 offset:0x1200
	ds_read_b64_tr_b16 v[184:185], v135 offset:0x1200
	v_mfma_f32_32x32x16_bf16 v[32:47], v[128:131], v[186:189], v[32:47]
	ds_read_b64_tr_b16 v[186:187], v133 offset:0x1400
	ds_read_b64_tr_b16 v[188:189], v135 offset:0x1400
	ds_read_b64_tr_b16 v[194:195], v133 offset:0x1600
	ds_read_b64_tr_b16 v[196:197], v135 offset:0x1600
	s_waitcnt lgkmcnt(0)
	v_mfma_f32_32x32x16_bf16 v[48:63], v[128:131], v[190:193], v[48:63]
	v_mfma_f32_32x32x16_bf16 v[16:31], v[146:149], v[150:153], v[16:31]
	v_add_u32_e32 v133, 0x2000, v133
	ds_read_b64_tr_b16 v[150:151], v133 offset:0
	v_add_u32_e32 v135, 0x2000, v135
	ds_read_b64_tr_b16 v[152:153], v135 offset:0
	v_mfma_f32_32x32x16_bf16 v[0:15], v[146:149], v[182:185], v[0:15]
	ds_read_b64_tr_b16 v[182:183], v133 offset:0x200
	ds_read_b64_tr_b16 v[184:185], v135 offset:0x200
	v_mfma_f32_32x32x16_bf16 v[32:47], v[146:149], v[186:189], v[32:47]
	ds_read_b64_tr_b16 v[186:187], v133 offset:0x400
	ds_read_b64_tr_b16 v[188:189], v135 offset:0x400
	ds_read_b64_tr_b16 v[190:191], v133 offset:0x600
	ds_read_b64_tr_b16 v[192:193], v135 offset:0x600
	s_waitcnt lgkmcnt(0)
	v_mfma_f32_32x32x16_bf16 v[48:63], v[146:149], v[194:197], v[48:63]
	v_mfma_f32_32x32x16_bf16 v[96:111], v[128:131], v[150:153], v[96:111]
	ds_read_b64_tr_b16 v[150:151], v133 offset:0x1000
	ds_read_b64_tr_b16 v[152:153], v135 offset:0x1000
	v_mfma_f32_32x32x16_bf16 v[112:127], v[128:131], v[182:185], v[112:127]
	ds_read_b64_tr_b16 v[182:183], v133 offset:0x1200
	ds_read_b64_tr_b16 v[184:185], v135 offset:0x1200
	v_mfma_f32_32x32x16_bf16 v[80:95], v[128:131], v[186:189], v[80:95]
	ds_read_b64_tr_b16 v[186:187], v133 offset:0x1400
	ds_read_b64_tr_b16 v[188:189], v135 offset:0x1400
	ds_read_b64_tr_b16 v[194:195], v133 offset:0x1600
	ds_read_b64_tr_b16 v[196:197], v135 offset:0x1600
	s_waitcnt lgkmcnt(0)
	v_mfma_f32_32x32x16_bf16 v[64:79], v[128:131], v[190:193], v[64:79]
	v_mfma_f32_32x32x16_bf16 v[96:111], v[146:149], v[150:153], v[96:111]
	v_mfma_f32_32x32x16_bf16 v[112:127], v[146:149], v[182:185], v[112:127]
	v_mfma_f32_32x32x16_bf16 v[80:95], v[146:149], v[186:189], v[80:95]
	v_mfma_f32_32x32x16_bf16 v[64:79], v[146:149], v[194:197], v[64:79]
	s_waitcnt vmcnt(4) lgkmcnt(0)
	s_barrier
; #define VM_WAIT() asm volatile("s_waitcnt vmcnt(0)" ::: "memory")
; template <int DK, int DV, bool MLSTM>
; __device__ __forceinline__ void out_unit2(LAS unsigned char* lds, LAS unsigned char* ldstab, const OutArgs a, const int wv) {
;     ...
; #pragma unroll
;     for (int pc = 0; pc < 4; ++pc) {
;         VM_WAIT(); __syncthreads();
;         OUT_DMA(pc + 1);
;         const bf16x8 af0 = pa[2 * pc], af1 = pa[2 * pc + 1];
;         OUT_MMA(pc & 1);
;     }
; #pragma unroll 1
;     for (int pc = 4; pc < 4 + 2 * NCP; ++pc) {
;         VM_WAIT(); __syncthreads();
;         if (pc + 1 < 4 + 2 * NCP) OUT_DMA(pc + 1);
;         const int cq = pc - 4, dirb = cq >= NCP, cp = dirb ? cq - NCP : cq;
;         const float qs = dirb ? qsb : qsf;
;         const unsigned qa = QP + (cp >> 2) * 32768u + 512u * (cp & 3) + 8192u * rb;
;         const bf16x8 af0 = scale_frag(lds_r128(qa + rb0), qs), af1 = scale_frag(lds_r128(qa + rb1), qs);
	s_add_u32 s42, s11, 0x38000
	s_addc_u32 s43, s12, 0
	v_lshl_add_u64 v[128:129], s[42:43], 0, v[198:199]
	v_lshl_add_u64 v[130:131], s[42:43], 0, v[200:201]
	v_lshl_add_u64 v[146:147], s[42:43], 0, v[202:203]
	v_lshl_add_u64 v[148:149], s[42:43], 0, v[204:205]
	s_add_i32 m0, s6, 0x10000
	s_nop 0
	global_load_lds_dwordx4 v[128:129], off
	s_add_i32 m0, s7, 0x10000
	s_nop 0
	global_load_lds_dwordx4 v[130:131], off
	s_add_i32 m0, s38, 0x10000
	s_nop 0
	global_load_lds_dwordx4 v[146:147], off
	s_add_i32 m0, s40, 0x10000
	s_nop 0
	global_load_lds_dwordx4 v[148:149], off
	v_add_u32_e32 v133, s13, v173
	v_add_u32_e32 v135, s13, v177
	ds_read_b128 v[128:131], v133 offset:33280
	ds_read_b128 v[146:149], v135 offset:33280
	s_waitcnt lgkmcnt(0)
	v_lshlrev_b32_e32 v135, 16, v128
	v_and_b32_e32 v137, 0xffff0000, v128
	v_mul_f32_e32 v135, v144, v135
	v_mul_f32_e32 v137, v144, v137
	v_cvt_pk_bf16_f32 v128, v135, v137
	v_lshlrev_b32_e32 v135, 16, v129
	v_and_b32_e32 v137, 0xffff0000, v129
	v_mul_f32_e32 v135, v144, v135
	v_mul_f32_e32 v137, v144, v137
	v_cvt_pk_bf16_f32 v129, v135, v137
	v_lshlrev_b32_e32 v135, 16, v130
	v_and_b32_e32 v137, 0xffff0000, v130
	v_mul_f32_e32 v135, v144, v135
	v_mul_f32_e32 v137, v144, v137
	v_cvt_pk_bf16_f32 v130, v135, v137
	v_lshlrev_b32_e32 v135, 16, v131
	v_and_b32_e32 v137, 0xffff0000, v131
	v_mul_f32_e32 v135, v144, v135
	v_mul_f32_e32 v137, v144, v137
	v_cvt_pk_bf16_f32 v131, v135, v137
	v_lshlrev_b32_e32 v135, 16, v146
	v_and_b32_e32 v137, 0xffff0000, v146
	v_mul_f32_e32 v135, v144, v135
	v_mul_f32_e32 v137, v144, v137
	v_cvt_pk_bf16_f32 v146, v135, v137
	v_lshlrev_b32_e32 v135, 16, v147
	v_and_b32_e32 v137, 0xffff0000, v147
	v_mul_f32_e32 v135, v144, v135
	v_mul_f32_e32 v137, v144, v137
	v_cvt_pk_bf16_f32 v147, v135, v137
	v_lshlrev_b32_e32 v135, 16, v148
	v_and_b32_e32 v137, 0xffff0000, v148
	v_mul_f32_e32 v135, v144, v135
	v_mul_f32_e32 v137, v144, v137
	v_cvt_pk_bf16_f32 v148, v135, v137
	v_lshlrev_b32_e32 v135, 16, v149
	v_and_b32_e32 v137, 0xffff0000, v149
	v_mul_f32_e32 v135, v144, v135
	v_mul_f32_e32 v137, v144, v137
	v_cvt_pk_bf16_f32 v149, v135, v137
	v_add_u32_e32 v133, 0x18000, v175
	ds_read_b64_tr_b16 v[150:151], v133 offset:0
	v_add_u32_e32 v135, 0x18000, v181
	ds_read_b64_tr_b16 v[152:153], v135 offset:0
	ds_read_b64_tr_b16 v[182:183], v133 offset:0x200
	ds_read_b64_tr_b16 v[184:185], v135 offset:0x200
	ds_read_b64_tr_b16 v[186:187], v133 offset:0x400
	ds_read_b64_tr_b16 v[188:189], v135 offset:0x400
	ds_read_b64_tr_b16 v[190:191], v133 offset:0x600
	ds_read_b64_tr_b16 v[192:193], v135 offset:0x600
	s_waitcnt lgkmcnt(0)
	s_nop 0
	v_mfma_f32_32x32x16_bf16 v[16:31], v[128:131], v[150:153], v[16:31]
	ds_read_b64_tr_b16 v[150:151], v133 offset:0x1000
	ds_read_b64_tr_b16 v[152:153], v135 offset:0x1000
	v_mfma_f32_32x32x16_bf16 v[0:15], v[128:131], v[182:185], v[0:15]
	ds_read_b64_tr_b16 v[182:183], v133 offset:0x1200
	ds_read_b64_tr_b16 v[184:185], v135 offset:0x1200
	v_mfma_f32_32x32x16_bf16 v[32:47], v[128:131], v[186:189], v[32:47]
	ds_read_b64_tr_b16 v[186:187], v133 offset:0x1400
	ds_read_b64_tr_b16 v[188:189], v135 offset:0x1400
	ds_read_b64_tr_b16 v[194:195], v133 offset:0x1600
	ds_read_b64_tr_b16 v[196:197], v135 offset:0x1600
	s_waitcnt lgkmcnt(0)
	v_mfma_f32_32x32x16_bf16 v[48:63], v[128:131], v[190:193], v[48:63]
	v_mfma_f32_32x32x16_bf16 v[16:31], v[146:149], v[150:153], v[16:31]
	v_add_u32_e32 v133, 0x2000, v133
	ds_read_b64_tr_b16 v[150:151], v133 offset:0
	v_add_u32_e32 v135, 0x2000, v135
	ds_read_b64_tr_b16 v[152:153], v135 offset:0
	v_mfma_f32_32x32x16_bf16 v[0:15], v[146:149], v[182:185], v[0:15]
	ds_read_b64_tr_b16 v[182:183], v133 offset:0x200
	ds_read_b64_tr_b16 v[184:185], v135 offset:0x200
	v_mfma_f32_32x32x16_bf16 v[32:47], v[146:149], v[186:189], v[32:47]
	ds_read_b64_tr_b16 v[186:187], v133 offset:0x400
	ds_read_b64_tr_b16 v[188:189], v135 offset:0x400
	ds_read_b64_tr_b16 v[190:191], v133 offset:0x600
	ds_read_b64_tr_b16 v[192:193], v135 offset:0x600
	s_waitcnt lgkmcnt(0)
	v_mfma_f32_32x32x16_bf16 v[48:63], v[146:149], v[194:197], v[48:63]
	v_mfma_f32_32x32x16_bf16 v[96:111], v[128:131], v[150:153], v[96:111]
	ds_read_b64_tr_b16 v[150:151], v133 offset:0x1000
	ds_read_b64_tr_b16 v[152:153], v135 offset:0x1000
	v_mfma_f32_32x32x16_bf16 v[112:127], v[128:131], v[182:185], v[112:127]
	ds_read_b64_tr_b16 v[182:183], v133 offset:0x1200
	ds_read_b64_tr_b16 v[184:185], v135 offset:0x1200
	v_mfma_f32_32x32x16_bf16 v[80:95], v[128:131], v[186:189], v[80:95]
	ds_read_b64_tr_b16 v[186:187], v133 offset:0x1400
	ds_read_b64_tr_b16 v[188:189], v135 offset:0x1400
	ds_read_b64_tr_b16 v[194:195], v133 offset:0x1600
	ds_read_b64_tr_b16 v[196:197], v135 offset:0x1600
	s_waitcnt lgkmcnt(0)
	v_mfma_f32_32x32x16_bf16 v[64:79], v[128:131], v[190:193], v[64:79]
	v_mfma_f32_32x32x16_bf16 v[96:111], v[146:149], v[150:153], v[96:111]
	v_mfma_f32_32x32x16_bf16 v[112:127], v[146:149], v[182:185], v[112:127]
	v_mfma_f32_32x32x16_bf16 v[80:95], v[146:149], v[186:189], v[80:95]
	v_mfma_f32_32x32x16_bf16 v[64:79], v[146:149], v[194:197], v[64:79]
	s_waitcnt vmcnt(4) lgkmcnt(0)
	s_barrier
; #define VM_WAIT() asm volatile("s_waitcnt vmcnt(0)" ::: "memory")
; template <int DK, int DV, bool MLSTM>
; __device__ __forceinline__ void out_unit2(LAS unsigned char* lds, LAS unsigned char* ldstab, const OutArgs a, const int wv) {
;     ...
;     for (int pc = 4; pc < 4 + 2 * NCP; ++pc) {
;         VM_WAIT(); __syncthreads();
;         if (pc + 1 < 4 + 2 * NCP) OUT_DMA(pc + 1);
;         const int cq = pc - 4, dirb = cq >= NCP, cp = dirb ? cq - NCP : cq;
;         const float qs = dirb ? qsb : qsf;
;         const unsigned qa = QP + (cp >> 2) * 32768u + 512u * (cp & 3) + 8192u * rb;
;         const bf16x8 af0 = scale_frag(lds_r128(qa + rb0), qs), af1 = scale_frag(lds_r128(qa + rb1), qs);
;         OUT_MMA(pc & 1);
	v_add_u32_e32 v133, s13, v173
	v_add_u32_e32 v135, s13, v177
	ds_read_b128 v[128:131], v133 offset:33792
	ds_read_b128 v[146:149], v135 offset:33792
	s_waitcnt lgkmcnt(0)
	v_lshlrev_b32_e32 v135, 16, v128
	v_and_b32_e32 v137, 0xffff0000, v128
	v_mul_f32_e32 v135, v144, v135
	v_mul_f32_e32 v137, v144, v137
	v_cvt_pk_bf16_f32 v128, v135, v137
	v_lshlrev_b32_e32 v135, 16, v129
	v_and_b32_e32 v137, 0xffff0000, v129
	v_mul_f32_e32 v135, v144, v135
	v_mul_f32_e32 v137, v144, v137
	v_cvt_pk_bf16_f32 v129, v135, v137
	v_lshlrev_b32_e32 v135, 16, v130
	v_and_b32_e32 v137, 0xffff0000, v130
	v_mul_f32_e32 v135, v144, v135
	v_mul_f32_e32 v137, v144, v137
	v_cvt_pk_bf16_f32 v130, v135, v137
	v_lshlrev_b32_e32 v135, 16, v131
	v_and_b32_e32 v137, 0xffff0000, v131
	v_mul_f32_e32 v135, v144, v135
	v_mul_f32_e32 v137, v144, v137
	v_cvt_pk_bf16_f32 v131, v135, v137
	v_lshlrev_b32_e32 v135, 16, v146
	v_and_b32_e32 v137, 0xffff0000, v146
	v_mul_f32_e32 v135, v144, v135
	v_mul_f32_e32 v137, v144, v137
	v_cvt_pk_bf16_f32 v146, v135, v137
	v_lshlrev_b32_e32 v135, 16, v147
	v_and_b32_e32 v137, 0xffff0000, v147
	v_mul_f32_e32 v135, v144, v135
	v_mul_f32_e32 v137, v144, v137
	v_cvt_pk_bf16_f32 v147, v135, v137
	v_lshlrev_b32_e32 v135, 16, v148
	v_and_b32_e32 v137, 0xffff0000, v148
	v_mul_f32_e32 v135, v144, v135
	v_mul_f32_e32 v137, v144, v137
	v_cvt_pk_bf16_f32 v148, v135, v137
	v_lshlrev_b32_e32 v135, 16, v149
	v_and_b32_e32 v137, 0xffff0000, v149
	v_mul_f32_e32 v135, v144, v135
	v_mul_f32_e32 v137, v144, v137
	v_cvt_pk_bf16_f32 v149, v135, v137
	v_mov_b32_e32 v133, v175
	ds_read_b64_tr_b16 v[150:151], v133 offset:0
	v_mov_b32_e32 v135, v181
	ds_read_b64_tr_b16 v[152:153], v135 offset:0
	ds_read_b64_tr_b16 v[182:183], v133 offset:0x200
	ds_read_b64_tr_b16 v[184:185], v135 offset:0x200
	ds_read_b64_tr_b16 v[186:187], v133 offset:0x400
	ds_read_b64_tr_b16 v[188:189], v135 offset:0x400
	ds_read_b64_tr_b16 v[190:191], v133 offset:0x600
	ds_read_b64_tr_b16 v[192:193], v135 offset:0x600
	s_waitcnt lgkmcnt(0)
	s_nop 0
	v_mfma_f32_32x32x16_bf16 v[16:31], v[128:131], v[150:153], v[16:31]
	ds_read_b64_tr_b16 v[150:151], v133 offset:0x1000
	ds_read_b64_tr_b16 v[152:153], v135 offset:0x1000
	v_mfma_f32_32x32x16_bf16 v[0:15], v[128:131], v[182:185], v[0:15]
	ds_read_b64_tr_b16 v[182:183], v133 offset:0x1200
	ds_read_b64_tr_b16 v[184:185], v135 offset:0x1200
	v_mfma_f32_32x32x16_bf16 v[32:47], v[128:131], v[186:189], v[32:47]
	ds_read_b64_tr_b16 v[186:187], v133 offset:0x1400
	ds_read_b64_tr_b16 v[188:189], v135 offset:0x1400
	ds_read_b64_tr_b16 v[194:195], v133 offset:0x1600
	ds_read_b64_tr_b16 v[196:197], v135 offset:0x1600
	s_waitcnt lgkmcnt(0)
	v_mfma_f32_32x32x16_bf16 v[48:63], v[128:131], v[190:193], v[48:63]
	v_mfma_f32_32x32x16_bf16 v[16:31], v[146:149], v[150:153], v[16:31]
	v_add_u32_e32 v133, 0x2000, v133
	ds_read_b64_tr_b16 v[150:151], v133 offset:0
	v_add_u32_e32 v135, 0x2000, v135
	ds_read_b64_tr_b16 v[152:153], v135 offset:0
	v_mfma_f32_32x32x16_bf16 v[0:15], v[146:149], v[182:185], v[0:15]
	ds_read_b64_tr_b16 v[182:183], v133 offset:0x200
	ds_read_b64_tr_b16 v[184:185], v135 offset:0x200
	v_mfma_f32_32x32x16_bf16 v[32:47], v[146:149], v[186:189], v[32:47]
	ds_read_b64_tr_b16 v[186:187], v133 offset:0x400
	ds_read_b64_tr_b16 v[188:189], v135 offset:0x400
	ds_read_b64_tr_b16 v[190:191], v133 offset:0x600
	ds_read_b64_tr_b16 v[192:193], v135 offset:0x600
	s_waitcnt lgkmcnt(0)
	v_mfma_f32_32x32x16_bf16 v[48:63], v[146:149], v[194:197], v[48:63]
	v_mfma_f32_32x32x16_bf16 v[96:111], v[128:131], v[150:153], v[96:111]
	ds_read_b64_tr_b16 v[150:151], v133 offset:0x1000
	ds_read_b64_tr_b16 v[152:153], v135 offset:0x1000
	v_mfma_f32_32x32x16_bf16 v[112:127], v[128:131], v[182:185], v[112:127]
	ds_read_b64_tr_b16 v[182:183], v133 offset:0x1200
	ds_read_b64_tr_b16 v[184:185], v135 offset:0x1200
	v_mfma_f32_32x32x16_bf16 v[80:95], v[128:131], v[186:189], v[80:95]
	ds_read_b64_tr_b16 v[186:187], v133 offset:0x1400
	ds_read_b64_tr_b16 v[188:189], v135 offset:0x1400
	ds_read_b64_tr_b16 v[194:195], v133 offset:0x1600
	ds_read_b64_tr_b16 v[196:197], v135 offset:0x1600
	s_waitcnt lgkmcnt(0)
	v_mfma_f32_32x32x16_bf16 v[64:79], v[128:131], v[190:193], v[64:79]
	v_mfma_f32_32x32x16_bf16 v[96:111], v[146:149], v[150:153], v[96:111]
	v_mfma_f32_32x32x16_bf16 v[112:127], v[146:149], v[182:185], v[112:127]
	v_mfma_f32_32x32x16_bf16 v[80:95], v[146:149], v[186:189], v[80:95]
	v_mfma_f32_32x32x16_bf16 v[64:79], v[146:149], v[194:197], v[64:79]
	s_waitcnt vmcnt(0) lgkmcnt(0)
	s_barrier
; #define VM_WAIT() asm volatile("s_waitcnt vmcnt(0)" ::: "memory")
; template <int DK, int DV, bool MLSTM>
; __device__ __forceinline__ void out_unit2(LAS unsigned char* lds, LAS unsigned char* ldstab, const OutArgs a, const int wv) {
;     ...
;     for (int pc = 4; pc < 4 + 2 * NCP; ++pc) {
;         VM_WAIT(); __syncthreads();
;         if (pc + 1 < 4 + 2 * NCP) OUT_DMA(pc + 1);
;         const int cq = pc - 4, dirb = cq >= NCP, cp = dirb ? cq - NCP : cq;
;         const float qs = dirb ? qsb : qsf;
;         const unsigned qa = QP + (cp >> 2) * 32768u + 512u * (cp & 3) + 8192u * rb;
;         const bf16x8 af0 = scale_frag(lds_r128(qa + rb0), qs), af1 = scale_frag(lds_r128(qa + rb1), qs);
;         OUT_MMA(pc & 1);
	v_add_u32_e32 v133, s13, v173
	v_add_u32_e32 v135, s13, v177
	ds_read_b128 v[128:131], v133 offset:34304
	ds_read_b128 v[146:149], v135 offset:34304
	s_waitcnt lgkmcnt(0)
	v_lshlrev_b32_e32 v135, 16, v128
	v_and_b32_e32 v137, 0xffff0000, v128
	v_mul_f32_e32 v135, v144, v135
	v_mul_f32_e32 v137, v144, v137
	v_cvt_pk_bf16_f32 v128, v135, v137
	v_lshlrev_b32_e32 v135, 16, v129
	v_and_b32_e32 v137, 0xffff0000, v129
	v_mul_f32_e32 v135, v144, v135
	v_mul_f32_e32 v137, v144, v137
	v_cvt_pk_bf16_f32 v129, v135, v137
	v_lshlrev_b32_e32 v135, 16, v130
	v_and_b32_e32 v137, 0xffff0000, v130
	v_mul_f32_e32 v135, v144, v135
	v_mul_f32_e32 v137, v144, v137
	v_cvt_pk_bf16_f32 v130, v135, v137
	v_lshlrev_b32_e32 v135, 16, v131
	v_and_b32_e32 v137, 0xffff0000, v131
	v_mul_f32_e32 v135, v144, v135
	v_mul_f32_e32 v137, v144, v137
	v_cvt_pk_bf16_f32 v131, v135, v137
	v_lshlrev_b32_e32 v135, 16, v146
	v_and_b32_e32 v137, 0xffff0000, v146
	v_mul_f32_e32 v135, v144, v135
	v_mul_f32_e32 v137, v144, v137
	v_cvt_pk_bf16_f32 v146, v135, v137
	v_lshlrev_b32_e32 v135, 16, v147
	v_and_b32_e32 v137, 0xffff0000, v147
	v_mul_f32_e32 v135, v144, v135
	v_mul_f32_e32 v137, v144, v137
	v_cvt_pk_bf16_f32 v147, v135, v137
	v_lshlrev_b32_e32 v135, 16, v148
	v_and_b32_e32 v137, 0xffff0000, v148
	v_mul_f32_e32 v135, v144, v135
	v_mul_f32_e32 v137, v144, v137
	v_cvt_pk_bf16_f32 v148, v135, v137
	v_lshlrev_b32_e32 v135, 16, v149
	v_and_b32_e32 v137, 0xffff0000, v149
	v_mul_f32_e32 v135, v144, v135
	v_mul_f32_e32 v137, v144, v137
	v_cvt_pk_bf16_f32 v149, v135, v137
	v_add_u32_e32 v133, 0x10000, v175
	ds_read_b64_tr_b16 v[150:151], v133 offset:0
	v_add_u32_e32 v135, 0x10000, v181
	ds_read_b64_tr_b16 v[152:153], v135 offset:0
	ds_read_b64_tr_b16 v[182:183], v133 offset:0x200
	ds_read_b64_tr_b16 v[184:185], v135 offset:0x200
	ds_read_b64_tr_b16 v[186:187], v133 offset:0x400
	ds_read_b64_tr_b16 v[188:189], v135 offset:0x400
	ds_read_b64_tr_b16 v[190:191], v133 offset:0x600
	ds_read_b64_tr_b16 v[192:193], v135 offset:0x600
	s_waitcnt lgkmcnt(0)
	s_nop 0
	v_mfma_f32_32x32x16_bf16 v[16:31], v[128:131], v[150:153], v[16:31]
	ds_read_b64_tr_b16 v[150:151], v133 offset:0x1000
	ds_read_b64_tr_b16 v[152:153], v135 offset:0x1000
	v_mfma_f32_32x32x16_bf16 v[0:15], v[128:131], v[182:185], v[0:15]
	ds_read_b64_tr_b16 v[182:183], v133 offset:0x1200
	ds_read_b64_tr_b16 v[184:185], v135 offset:0x1200
	v_mfma_f32_32x32x16_bf16 v[32:47], v[128:131], v[186:189], v[32:47]
	ds_read_b64_tr_b16 v[186:187], v133 offset:0x1400
	ds_read_b64_tr_b16 v[188:189], v135 offset:0x1400
	ds_read_b64_tr_b16 v[194:195], v133 offset:0x1600
	ds_read_b64_tr_b16 v[196:197], v135 offset:0x1600
	s_waitcnt lgkmcnt(0)
	v_mfma_f32_32x32x16_bf16 v[48:63], v[128:131], v[190:193], v[48:63]
	v_mfma_f32_32x32x16_bf16 v[16:31], v[146:149], v[150:153], v[16:31]
	v_add_u32_e32 v133, 0x2000, v133
	ds_read_b64_tr_b16 v[150:151], v133 offset:0
	v_add_u32_e32 v135, 0x2000, v135
	ds_read_b64_tr_b16 v[152:153], v135 offset:0
	v_mfma_f32_32x32x16_bf16 v[0:15], v[146:149], v[182:185], v[0:15]
	ds_read_b64_tr_b16 v[182:183], v133 offset:0x200
	ds_read_b64_tr_b16 v[184:185], v135 offset:0x200
	v_mfma_f32_32x32x16_bf16 v[32:47], v[146:149], v[186:189], v[32:47]
	ds_read_b64_tr_b16 v[186:187], v133 offset:0x400
	ds_read_b64_tr_b16 v[188:189], v135 offset:0x400
	ds_read_b64_tr_b16 v[190:191], v133 offset:0x600
	ds_read_b64_tr_b16 v[192:193], v135 offset:0x600
	s_waitcnt lgkmcnt(0)
	v_mfma_f32_32x32x16_bf16 v[48:63], v[146:149], v[194:197], v[48:63]
	v_mfma_f32_32x32x16_bf16 v[96:111], v[128:131], v[150:153], v[96:111]
	ds_read_b64_tr_b16 v[150:151], v133 offset:0x1000
	ds_read_b64_tr_b16 v[152:153], v135 offset:0x1000
	v_mfma_f32_32x32x16_bf16 v[112:127], v[128:131], v[182:185], v[112:127]
	ds_read_b64_tr_b16 v[182:183], v133 offset:0x1200
	ds_read_b64_tr_b16 v[184:185], v135 offset:0x1200
	v_mfma_f32_32x32x16_bf16 v[80:95], v[128:131], v[186:189], v[80:95]
	ds_read_b64_tr_b16 v[186:187], v133 offset:0x1400
	ds_read_b64_tr_b16 v[188:189], v135 offset:0x1400
	ds_read_b64_tr_b16 v[194:195], v133 offset:0x1600
	ds_read_b64_tr_b16 v[196:197], v135 offset:0x1600
	s_waitcnt lgkmcnt(0)
	v_mfma_f32_32x32x16_bf16 v[64:79], v[128:131], v[190:193], v[64:79]
	v_mfma_f32_32x32x16_bf16 v[96:111], v[146:149], v[150:153], v[96:111]
	v_mfma_f32_32x32x16_bf16 v[112:127], v[146:149], v[182:185], v[112:127]
	v_mfma_f32_32x32x16_bf16 v[80:95], v[146:149], v[186:189], v[80:95]
	v_mfma_f32_32x32x16_bf16 v[64:79], v[146:149], v[194:197], v[64:79]

; #define VM_WAIT() asm volatile("s_waitcnt vmcnt(0)" ::: "memory")
; #define FENCE() do { asm volatile("" ::: "memory"); __builtin_amdgcn_sched_barrier(0); } while (0)
; template <int DK, int DV, bool MLSTM>
; __device__ __forceinline__ void out_unit2(LAS unsigned char* lds, LAS unsigned char* ldstab, const OutArgs a, const int wv) {
;     ...
;     const int l = 32 * rb + r32;
;     float a_fl, a_bl;
;     if (MLSTM) { a_fl = a.af[l]; a_bl = a.ab[l]; } else { a_fl = (float)(l + 1) * a.lgf; a_bl = (float)(128 - l) * a.lgb; }
;     VM_WAIT(); __syncthreads();
;     f32x16 p[4];
; #pragma unroll
;     for (int kb = 0; kb < 4; ++kb) p[kb] = (f32x16){};
;     float qnf = 0.f, qnb = 0.f;
; #pragma unroll
;     for (int ks = 0; ks < NKS; ++ks) {
;         const unsigned po = (ks >> 3) * 32768u + ((ks & 1) ? rb1 : rb0) + 512u * ((ks & 7) >> 1);
;         const bf16x8 qf = lds_r128(QP + po + 8192u * rb);
;         bf16x8 kf[4];
; #pragma unroll
;         for (int kb = 0; kb < 4; ++kb) kf[kb] = lds_r128(KP + po + 8192u * kb);
; #pragma unroll
;         for (int kb = 0; kb < 4; ++kb) p[kb] = __builtin_amdgcn_mfma_f32_32x32x16_bf16(kf[kb], qf, p[kb], 0, 0, 0);
;         FENCE();
;     }
.LBB0_4304:
	s_or_b64 exec, exec, s[4:5]
	s_lshl_b32 s4, s6, 10
	s_add_u32 s37, s7, s4
	s_addc_u32 s16, s12, 0
	s_add_u32 s6, s37, 0x1000
	s_addc_u32 s7, s16, 0
	s_lshl_b32 s12, s11, 1
	s_ashr_i32 s13, s12, 31
	s_lshl_b64 s[4:5], s[12:13], 23
	s_add_u32 s4, s49, s4
	s_addc_u32 s5, s50, s5
	s_lshl_b32 s13, s10, 18
	s_add_u32 s4, s4, s13
	s_addc_u32 s5, s5, 0
	s_or_b32 s10, s12, 1
	v_lshlrev_b32_e32 v1, 6, v171
	s_ashr_i32 s11, s10, 31
	v_lshlrev_b32_e32 v0, 8, v171
	v_and_b32_e32 v1, 0x1c0, v1
	s_lshl_b64 s[10:11], s[10:11], 23
	v_and_or_b32 v71, v0, s64, v1
	v_bitop3_b32 v0, v5, v72, 3 bitop3:0x6c
	s_add_u32 s10, s49, s10
	v_lshlrev_b32_e32 v74, 4, v0
	s_addc_u32 s12, s50, s11
	v_or_b32_e32 v173, v74, v71
	s_add_u32 s11, s10, s13
	v_add_u32_e32 v0, s68, v173
	s_addc_u32 s12, s12, 0
	s_and_b32 s10, s36, 3
	s_lshl_b32 s13, s9, 6
	s_waitcnt vmcnt(0)
	s_waitcnt vmcnt(0) lgkmcnt(0)
	s_barrier
	ds_read_b128 v[0:3], v0
	s_and_b32 s39, s13, 0xffffc000
	v_lshlrev_b32_e32 v8, 11, v72
	s_lshl_b32 s13, s10, 13
	v_lshlrev_b32_e32 v9, 4, v171
	s_add_i32 s13, s13, 0
	v_and_or_b32 v12, v9, s66, v8
	v_add_u32_e32 v8, s70, v173
	v_add_u32_e32 v4, s13, v173
	ds_read_b128 v[8:11], v8
	ds_read_b128 v[4:7], v4
	s_waitcnt lgkmcnt(0)
	v_mfma_f32_32x32x16_bf16 v[48:63], v[0:3], v[4:7], 0
	v_lshrrev_b32_e32 v0, 3, v232
	v_bfe_u32 v1, v232, 1, 1
	v_and_or_b32 v0, v0, 2, v1
	v_lshlrev_b32_e32 v0, 4, v0
	v_bitop3_b32 v13, v0, v232, 32 bitop3:0x78
	v_add_u32_e32 v0, s71, v173
	ds_read_b128 v[0:3], v0
	v_mfma_f32_32x32x16_bf16 v[32:47], v[8:11], v[4:7], 0
	v_lshlrev_b32_e32 v8, 3, v171
	v_and_b32_e32 v8, 8, v8
	v_or3_b32 v68, v13, v12, v8
	v_add_u32_e32 v8, s72, v173
	ds_read_b128 v[8:11], v8
	v_and_b32_e32 v233, 31, v232
	s_lshl_b32 s10, s10, 5
	v_or_b32_e32 v66, s10, v233
	s_waitcnt lgkmcnt(1)
	v_mfma_f32_32x32x16_bf16 v[16:31], v[0:3], v[4:7], 0
	v_add_u32_e32 v0, 1, v66
	v_cvt_f32_ubyte0_e32 v67, v0
	v_sub_u32_e32 v0, 0x80, v66
	v_cvt_f32_ubyte0_e32 v70, v0
	s_mov_b32 s15, 4
	v_or_b32_e32 v175, s39, v68
	s_waitcnt lgkmcnt(0)
	v_mfma_f32_32x32x16_bf16 v[0:15], v[8:11], v[4:7], 0
	s_movk_i32 s14, 0x80
	v_mul_f32_e32 v69, v64, v67
	v_bitop3_b32 v177, v74, 32, v71 bitop3:0x36
	v_add_u32_e32 v71, s68, v177
	ds_read_b128 v[74:77], v71
	v_add_u32_e32 v71, s13, v177
	ds_read_b128 v[78:81], v71
	v_add_u32_e32 v71, s70, v177
	s_waitcnt lgkmcnt(0)
	v_mfma_f32_32x32x16_bf16 v[48:63], v[74:77], v[78:81], v[48:63]
	ds_read_b128 v[74:77], v71
	v_add_u32_e32 v71, s71, v177
	s_waitcnt lgkmcnt(0)
	v_mfma_f32_32x32x16_bf16 v[32:47], v[74:77], v[78:81], v[32:47]
	ds_read_b128 v[74:77], v71
	v_add_u32_e32 v71, s72, v177
	s_waitcnt lgkmcnt(0)
	v_mfma_f32_32x32x16_bf16 v[16:31], v[74:77], v[78:81], v[16:31]
	ds_read_b128 v[74:77], v71
	s_waitcnt lgkmcnt(0)
	v_mfma_f32_32x32x16_bf16 v[0:15], v[74:77], v[78:81], v[0:15]
	v_or_b32_e32 v71, 0x200, v173
	v_add_u32_e32 v74, s68, v71
	ds_read_b128 v[74:77], v74
	v_add_u32_e32 v78, s13, v71
	ds_read_b128 v[78:81], v78
	v_add_u32_e32 v82, s70, v71
	s_waitcnt lgkmcnt(0)
	v_mfma_f32_32x32x16_bf16 v[48:63], v[74:77], v[78:81], v[48:63]
	ds_read_b128 v[74:77], v82
	v_add_u32_e32 v82, s71, v71
	v_add_u32_e32 v71, s72, v71
	s_waitcnt lgkmcnt(0)
	v_mfma_f32_32x32x16_bf16 v[32:47], v[74:77], v[78:81], v[32:47]
	ds_read_b128 v[74:77], v82
	s_waitcnt lgkmcnt(0)
	v_mfma_f32_32x32x16_bf16 v[16:31], v[74:77], v[78:81], v[16:31]
	ds_read_b128 v[74:77], v71
	s_waitcnt lgkmcnt(0)
	v_mfma_f32_32x32x16_bf16 v[0:15], v[74:77], v[78:81], v[0:15]
	v_bitop3_b32 v71, v173, s73, 32 bitop3:0xde
	v_add_u32_e32 v74, s68, v71
	ds_read_b128 v[74:77], v74
	v_add_u32_e32 v78, s13, v71
	ds_read_b128 v[78:81], v78
	v_add_u32_e32 v82, s70, v71
	s_waitcnt lgkmcnt(0)
	v_mfma_f32_32x32x16_bf16 v[48:63], v[74:77], v[78:81], v[48:63]
	ds_read_b128 v[74:77], v82
	v_add_u32_e32 v82, s71, v71
	v_add_u32_e32 v71, s72, v71
	s_waitcnt lgkmcnt(0)
	v_mfma_f32_32x32x16_bf16 v[32:47], v[74:77], v[78:81], v[32:47]
	ds_read_b128 v[74:77], v82
	s_waitcnt lgkmcnt(0)
	v_mfma_f32_32x32x16_bf16 v[16:31], v[74:77], v[78:81], v[16:31]
	ds_read_b128 v[74:77], v71
	s_waitcnt lgkmcnt(0)
	v_mfma_f32_32x32x16_bf16 v[0:15], v[74:77], v[78:81], v[0:15]
	v_or_b32_e32 v71, 0x400, v173
	v_add_u32_e32 v74, s68, v71
	ds_read_b128 v[74:77], v74
	v_add_u32_e32 v78, s13, v71
	ds_read_b128 v[78:81], v78
	v_add_u32_e32 v82, s70, v71
	s_waitcnt lgkmcnt(0)
	v_mfma_f32_32x32x16_bf16 v[48:63], v[74:77], v[78:81], v[48:63]
	ds_read_b128 v[74:77], v82
	v_add_u32_e32 v82, s71, v71
	v_add_u32_e32 v71, s72, v71
	s_waitcnt lgkmcnt(0)
	v_mfma_f32_32x32x16_bf16 v[32:47], v[74:77], v[78:81], v[32:47]
	ds_read_b128 v[74:77], v82
	s_waitcnt lgkmcnt(0)
	v_mfma_f32_32x32x16_bf16 v[16:31], v[74:77], v[78:81], v[16:31]
	ds_read_b128 v[74:77], v71
	s_waitcnt lgkmcnt(0)
	v_mfma_f32_32x32x16_bf16 v[0:15], v[74:77], v[78:81], v[0:15]
	v_bitop3_b32 v71, v173, s74, 32 bitop3:0xde
	v_add_u32_e32 v74, s68, v71
	ds_read_b128 v[74:77], v74
	v_add_u32_e32 v78, s13, v71
	ds_read_b128 v[78:81], v78
	v_add_u32_e32 v82, s70, v71
	s_waitcnt lgkmcnt(0)
	v_mfma_f32_32x32x16_bf16 v[48:63], v[74:77], v[78:81], v[48:63]
	ds_read_b128 v[74:77], v82
	v_add_u32_e32 v82, s71, v71
	v_add_u32_e32 v71, s72, v71
	s_waitcnt lgkmcnt(0)
	v_mfma_f32_32x32x16_bf16 v[32:47], v[74:77], v[78:81], v[32:47]
	ds_read_b128 v[74:77], v82
	s_waitcnt lgkmcnt(0)
	v_mfma_f32_32x32x16_bf16 v[16:31], v[74:77], v[78:81], v[16:31]
	ds_read_b128 v[74:77], v71
	s_waitcnt lgkmcnt(0)
	v_mfma_f32_32x32x16_bf16 v[0:15], v[74:77], v[78:81], v[0:15]
	v_or_b32_e32 v71, 0x600, v173
	v_add_u32_e32 v74, s68, v71
	ds_read_b128 v[74:77], v74
	v_add_u32_e32 v78, s13, v71
	ds_read_b128 v[78:81], v78
	v_add_u32_e32 v82, s70, v71
	s_waitcnt lgkmcnt(0)
; #define FENCE() do { asm volatile("" ::: "memory"); __builtin_amdgcn_sched_barrier(0); } while (0)
; template <int DK, int DV, bool MLSTM>
; __device__ __forceinline__ void out_unit2(LAS unsigned char* lds, LAS unsigned char* ldstab, const OutArgs a, const int wv) {
;     ...
; #pragma unroll
;     for (int ks = 0; ks < NKS; ++ks) {
;         const unsigned po = (ks >> 3) * 32768u + ((ks & 1) ? rb1 : rb0) + 512u * ((ks & 7) >> 1);
;         const bf16x8 qf = lds_r128(QP + po + 8192u * rb);
;         bf16x8 kf[4];
; #pragma unroll
;         for (int kb = 0; kb < 4; ++kb) kf[kb] = lds_r128(KP + po + 8192u * kb);
; #pragma unroll
;         for (int kb = 0; kb < 4; ++kb) p[kb] = __builtin_amdgcn_mfma_f32_32x32x16_bf16(kf[kb], qf, p[kb], 0, 0, 0);
;         FENCE();
;     }
	v_mfma_f32_32x32x16_bf16 v[48:63], v[74:77], v[78:81], v[48:63]
	ds_read_b128 v[74:77], v82
	v_add_u32_e32 v82, s71, v71
	v_add_u32_e32 v71, s72, v71
	s_waitcnt lgkmcnt(0)
	v_mfma_f32_32x32x16_bf16 v[32:47], v[74:77], v[78:81], v[32:47]
	ds_read_b128 v[74:77], v82
	s_waitcnt lgkmcnt(0)
	v_mfma_f32_32x32x16_bf16 v[16:31], v[74:77], v[78:81], v[16:31]
	ds_read_b128 v[74:77], v71
	s_waitcnt lgkmcnt(0)
	v_mfma_f32_32x32x16_bf16 v[0:15], v[74:77], v[78:81], v[0:15]
	v_bitop3_b32 v71, v173, s75, 32 bitop3:0xde
	v_add_u32_e32 v74, s68, v71
	ds_read_b128 v[74:77], v74
	v_add_u32_e32 v78, s13, v71
	ds_read_b128 v[78:81], v78
	v_add_u32_e32 v82, s70, v71
	s_waitcnt lgkmcnt(0)
	v_mfma_f32_32x32x16_bf16 v[48:63], v[74:77], v[78:81], v[48:63]
	ds_read_b128 v[74:77], v82
	v_add_u32_e32 v82, s71, v71
	v_add_u32_e32 v71, s72, v71
	s_waitcnt lgkmcnt(0)
	v_mfma_f32_32x32x16_bf16 v[32:47], v[74:77], v[78:81], v[32:47]
	ds_read_b128 v[74:77], v82
	s_waitcnt lgkmcnt(0)
	v_mfma_f32_32x32x16_bf16 v[16:31], v[74:77], v[78:81], v[16:31]
	ds_read_b128 v[74:77], v71
	s_waitcnt lgkmcnt(0)
	v_mfma_f32_32x32x16_bf16 v[0:15], v[74:77], v[78:81], v[0:15]
	v_or_b32_e32 v71, 0x8000, v173
	v_add_u32_e32 v74, s68, v71
	ds_read_b128 v[74:77], v74
	v_add_u32_e32 v78, s13, v71
	ds_read_b128 v[78:81], v78
	v_add_u32_e32 v82, s70, v71
	s_waitcnt lgkmcnt(0)
	v_mfma_f32_32x32x16_bf16 v[48:63], v[74:77], v[78:81], v[48:63]
	ds_read_b128 v[74:77], v82
	v_add_u32_e32 v82, s71, v71
	v_add_u32_e32 v71, s72, v71
	s_waitcnt lgkmcnt(0)
	v_mfma_f32_32x32x16_bf16 v[32:47], v[74:77], v[78:81], v[32:47]
	ds_read_b128 v[74:77], v82
	s_waitcnt lgkmcnt(0)
	v_mfma_f32_32x32x16_bf16 v[16:31], v[74:77], v[78:81], v[16:31]
	ds_read_b128 v[74:77], v71
	s_waitcnt lgkmcnt(0)
	v_mfma_f32_32x32x16_bf16 v[0:15], v[74:77], v[78:81], v[0:15]
	v_bitop3_b32 v71, v173, s76, 32 bitop3:0xde
	v_add_u32_e32 v74, s68, v71
	ds_read_b128 v[74:77], v74
	v_add_u32_e32 v78, s13, v71
	ds_read_b128 v[78:81], v78
	v_add_u32_e32 v82, s70, v71
	s_waitcnt lgkmcnt(0)
	v_mfma_f32_32x32x16_bf16 v[48:63], v[74:77], v[78:81], v[48:63]
	ds_read_b128 v[74:77], v82
	v_add_u32_e32 v82, s71, v71
	v_add_u32_e32 v71, s72, v71
	s_waitcnt lgkmcnt(0)
	v_mfma_f32_32x32x16_bf16 v[32:47], v[74:77], v[78:81], v[32:47]
	ds_read_b128 v[74:77], v82
	s_waitcnt lgkmcnt(0)
	v_mfma_f32_32x32x16_bf16 v[16:31], v[74:77], v[78:81], v[16:31]
	ds_read_b128 v[74:77], v71
	s_waitcnt lgkmcnt(0)
	v_mfma_f32_32x32x16_bf16 v[0:15], v[74:77], v[78:81], v[0:15]
	v_or_b32_e32 v71, 0x8200, v173
	v_add_u32_e32 v74, s68, v71
	ds_read_b128 v[74:77], v74
	v_add_u32_e32 v78, s13, v71
	ds_read_b128 v[78:81], v78
	v_add_u32_e32 v82, s70, v71
	s_waitcnt lgkmcnt(0)
	v_mfma_f32_32x32x16_bf16 v[48:63], v[74:77], v[78:81], v[48:63]
	ds_read_b128 v[74:77], v82
	v_add_u32_e32 v82, s71, v71
	v_add_u32_e32 v71, s72, v71
	s_waitcnt lgkmcnt(0)
	v_mfma_f32_32x32x16_bf16 v[32:47], v[74:77], v[78:81], v[32:47]
	ds_read_b128 v[74:77], v82
	s_waitcnt lgkmcnt(0)
	v_mfma_f32_32x32x16_bf16 v[16:31], v[74:77], v[78:81], v[16:31]
	ds_read_b128 v[74:77], v71
	s_waitcnt lgkmcnt(0)
	v_mfma_f32_32x32x16_bf16 v[0:15], v[74:77], v[78:81], v[0:15]
	v_bitop3_b32 v71, v173, s77, 32 bitop3:0xde
	v_add_u32_e32 v74, s68, v71
	ds_read_b128 v[74:77], v74
	v_add_u32_e32 v78, s13, v71
	ds_read_b128 v[78:81], v78
	v_add_u32_e32 v82, s70, v71
	s_waitcnt lgkmcnt(0)
	v_mfma_f32_32x32x16_bf16 v[48:63], v[74:77], v[78:81], v[48:63]
	ds_read_b128 v[74:77], v82
	v_add_u32_e32 v82, s71, v71
	v_add_u32_e32 v71, s72, v71
	s_waitcnt lgkmcnt(0)
	v_mfma_f32_32x32x16_bf16 v[32:47], v[74:77], v[78:81], v[32:47]
	ds_read_b128 v[74:77], v82
	s_waitcnt lgkmcnt(0)
	v_mfma_f32_32x32x16_bf16 v[16:31], v[74:77], v[78:81], v[16:31]
	ds_read_b128 v[74:77], v71
	s_waitcnt lgkmcnt(0)
	v_mfma_f32_32x32x16_bf16 v[0:15], v[74:77], v[78:81], v[0:15]
	v_or_b32_e32 v71, 0x8400, v173
	v_add_u32_e32 v74, s68, v71
	ds_read_b128 v[74:77], v74
	v_add_u32_e32 v78, s13, v71
	ds_read_b128 v[78:81], v78
	v_add_u32_e32 v82, s70, v71
	s_waitcnt lgkmcnt(0)
	v_mfma_f32_32x32x16_bf16 v[48:63], v[74:77], v[78:81], v[48:63]
	ds_read_b128 v[74:77], v82
	v_add_u32_e32 v82, s71, v71
	v_add_u32_e32 v71, s72, v71
	s_waitcnt lgkmcnt(0)
	v_mfma_f32_32x32x16_bf16 v[32:47], v[74:77], v[78:81], v[32:47]
	ds_read_b128 v[74:77], v82
	s_waitcnt lgkmcnt(0)
	v_mfma_f32_32x32x16_bf16 v[16:31], v[74:77], v[78:81], v[16:31]
	ds_read_b128 v[74:77], v71
	s_waitcnt lgkmcnt(0)
	v_mfma_f32_32x32x16_bf16 v[0:15], v[74:77], v[78:81], v[0:15]
	v_bitop3_b32 v71, v173, s78, 32 bitop3:0xde
	v_add_u32_e32 v74, s68, v71
	ds_read_b128 v[74:77], v74
	v_add_u32_e32 v78, s13, v71
	ds_read_b128 v[78:81], v78
	v_add_u32_e32 v82, s70, v71
	s_waitcnt lgkmcnt(0)
	v_mfma_f32_32x32x16_bf16 v[48:63], v[74:77], v[78:81], v[48:63]
	ds_read_b128 v[74:77], v82
	v_add_u32_e32 v82, s71, v71
	v_add_u32_e32 v71, s72, v71
	s_waitcnt lgkmcnt(0)
	v_mfma_f32_32x32x16_bf16 v[32:47], v[74:77], v[78:81], v[32:47]
	ds_read_b128 v[74:77], v82
	s_waitcnt lgkmcnt(0)
	v_mfma_f32_32x32x16_bf16 v[16:31], v[74:77], v[78:81], v[16:31]
	ds_read_b128 v[74:77], v71
	s_waitcnt lgkmcnt(0)
	v_mfma_f32_32x32x16_bf16 v[0:15], v[74:77], v[78:81], v[0:15]
	v_or_b32_e32 v71, 0x8600, v173
	v_add_u32_e32 v74, s68, v71
	ds_read_b128 v[74:77], v74
	v_add_u32_e32 v78, s13, v71
	ds_read_b128 v[78:81], v78
	v_add_u32_e32 v82, s70, v71
	s_waitcnt lgkmcnt(0)
	v_mfma_f32_32x32x16_bf16 v[48:63], v[74:77], v[78:81], v[48:63]
	ds_read_b128 v[74:77], v82
	v_add_u32_e32 v82, s71, v71
	v_add_u32_e32 v71, s72, v71
	s_waitcnt lgkmcnt(0)
	v_mfma_f32_32x32x16_bf16 v[32:47], v[74:77], v[78:81], v[32:47]
	ds_read_b128 v[74:77], v82
	s_waitcnt lgkmcnt(0)
; #define LAS __attribute__((address_space(3)))
; #define FENCE() do { asm volatile("" ::: "memory"); __builtin_amdgcn_sched_barrier(0); } while (0)
; template <int R, int NP>
; __device__ __forceinline__ void dma_tile(int wid, int lane, unsigned lds_base, const bf16_t* src, int ld) {
;     constexpr int NQ = R * NP / 4, PER = NQ / 8;
;     static_assert(NQ % 8 == 0 && R % 8 == 0, "dma_tile geometry");
;     const int r7 = (lane >> 2) & 7, x = lane & 3, hi = lane >> 5;
; #pragma unroll
;     for (int j = 0; j < PER; ++j) {
;         const int q = wid * PER + j;
;         const int sub = 2 * q + hi, panel = sub / (R / 2), psub = sub % (R / 2), rg = psub >> 2, cblk = psub & 3;
;         const int row = 8 * rg + r7, chlo = x ^ ((row >> 2) & 3);
;         const bf16_t* g = src + (size_t)row * ld + 128 * panel + 32 * cblk + 8 * chlo;
;         __builtin_amdgcn_global_load_lds((const unsigned*)g, (LAS unsigned*)(uintptr_t)(lds_base + q * 1024u), 16, 0, 0);
;     }
; template <int DK, int DV, bool MLSTM>
; __device__ __forceinline__ void out_unit2(LAS unsigned char* lds, LAS unsigned char* ldstab, const OutArgs a, const int wv) {
;     ...
;         for (int kb = 0; kb < 4; ++kb) p[kb] = __builtin_amdgcn_mfma_f32_32x32x16_bf16(kf[kb], qf, p[kb], 0, 0, 0);
;         FENCE();
;     }
;     ...
;     __syncthreads();
;     dma_tile<32, NPV>(wid, lane, SB, a.V, a.ldv);
	v_mfma_f32_32x32x16_bf16 v[16:31], v[74:77], v[78:81], v[16:31]
	ds_read_b128 v[74:77], v71
	s_waitcnt lgkmcnt(0)
	v_mfma_f32_32x32x16_bf16 v[0:15], v[74:77], v[78:81], v[0:15]
	v_bitop3_b32 v71, v173, s79, 32 bitop3:0xde
	v_add_u32_e32 v74, s68, v71
	ds_read_b128 v[74:77], v74
	v_add_u32_e32 v78, s13, v71
	ds_read_b128 v[78:81], v78
	v_add_u32_e32 v82, s70, v71
	s_waitcnt lgkmcnt(0)
	v_mfma_f32_32x32x16_bf16 v[48:63], v[74:77], v[78:81], v[48:63]
	ds_read_b128 v[74:77], v82
	v_add_u32_e32 v82, s71, v71
	v_add_u32_e32 v71, s72, v71
	s_waitcnt lgkmcnt(0)
	v_mfma_f32_32x32x16_bf16 v[32:47], v[74:77], v[78:81], v[32:47]
	ds_read_b128 v[74:77], v82
	s_waitcnt lgkmcnt(0)
	v_mfma_f32_32x32x16_bf16 v[16:31], v[74:77], v[78:81], v[16:31]
	ds_read_b128 v[74:77], v71
	s_waitcnt lgkmcnt(0)
	v_mfma_f32_32x32x16_bf16 v[0:15], v[74:77], v[78:81], v[0:15]
	v_or_b32_e32 v74, s38, v72
	v_ashrrev_i32_e32 v75, 31, v74
	v_lshrrev_b32_e32 v75, 28, v75
	v_add_u32_e32 v78, v74, v75
	v_and_b32_e32 v75, -16, v78
	v_sub_u32_e32 v79, v74, v75
	v_lshlrev_b32_e32 v78, 3, v78
	v_lshlrev_b32_e32 v74, 1, v79
	v_and_b32_e32 v158, 0xffffff80, v78
	v_and_or_b32 v182, v74, -16, v73
	v_mov_b64_e32 v[74:75], s[6:7]
	v_ashrrev_i32_e32 v159, 31, v158
	v_lshlrev_b32_e32 v78, 5, v79
	v_mad_i64_i32 v[76:77], s[6:7], v182, s57, v[74:75]
	v_lshlrev_b64 v[184:185], 1, v[158:159]
	v_and_b32_e32 v162, 32, v78
	v_lshl_add_u64 v[76:77], v[76:77], 0, v[184:185]
	v_lshlrev_b32_e32 v160, 1, v162
	s_lshl_b32 s6, s36, 12
	s_lshl_b32 s44, s36, 2
	v_lshl_add_u64 v[76:77], v[76:77], 0, v[160:161]
	s_add_i32 s40, s6, s68
	v_lshl_add_u64 v[76:77], v[76:77], 0, v[156:157]
	s_mov_b32 m0, s40
	s_or_b32 s7, s44, 1
	s_barrier
	global_load_lds_dwordx4 v[76:77], off
	v_lshl_or_b32 v76, s7, 1, v72
	v_ashrrev_i32_e32 v77, 31, v76
	v_lshrrev_b32_e32 v77, 28, v77
	v_add_u32_e32 v78, v76, v77
	v_and_b32_e32 v77, -16, v78
	v_sub_u32_e32 v79, v76, v77
	v_lshlrev_b32_e32 v76, 1, v79
	v_and_or_b32 v186, v76, -8, v73
	v_lshlrev_b32_e32 v78, 3, v78
	v_lshrrev_b32_e32 v76, 2, v186
	v_and_b32_e32 v164, 0xffffff80, v78
	v_xor_b32_e32 v80, v76, v232
	v_ashrrev_i32_e32 v165, 31, v164
	v_lshlrev_b32_e32 v78, 5, v79
	v_mad_i64_i32 v[76:77], s[42:43], v186, s57, v[74:75]
	v_lshlrev_b64 v[188:189], 1, v[164:165]
	v_and_b32_e32 v170, 0x60, v78
	v_lshlrev_b32_e32 v78, 3, v80
	v_lshl_add_u64 v[76:77], v[76:77], 0, v[188:189]
	v_lshlrev_b32_e32 v190, 1, v170
	v_mov_b32_e32 v191, v161
	v_and_b32_e32 v172, 24, v78
	s_lshl_b32 s7, s7, 10
	v_lshl_add_u64 v[76:77], v[76:77], 0, v[190:191]
	v_lshlrev_b32_e32 v192, 1, v172
	v_mov_b32_e32 v193, v161
	s_add_i32 s41, s7, s68
	v_lshl_add_u64 v[76:77], v[76:77], 0, v[192:193]
	s_mov_b32 m0, s41
	s_or_b32 s36, s44, 2
	global_load_lds_dwordx4 v[76:77], off
	v_lshl_or_b32 v76, s36, 1, v72
	v_ashrrev_i32_e32 v77, 31, v76
	v_lshrrev_b32_e32 v77, 28, v77
	v_add_u32_e32 v78, v76, v77
	v_and_b32_e32 v77, -16, v78
	v_sub_u32_e32 v79, v76, v77
	v_lshlrev_b32_e32 v76, 1, v79
	v_and_or_b32 v194, v76, -8, v73
	v_lshlrev_b32_e32 v78, 3, v78
	v_lshrrev_b32_e32 v76, 2, v194
	v_and_b32_e32 v166, 0xffffff80, v78
	v_xor_b32_e32 v80, v76, v232
	v_ashrrev_i32_e32 v167, 31, v166
	v_lshlrev_b32_e32 v78, 5, v79
	v_mad_i64_i32 v[76:77], s[42:43], v194, s57, v[74:75]
	v_lshlrev_b64 v[196:197], 1, v[166:167]
	v_and_b32_e32 v174, 0x60, v78
	v_lshlrev_b32_e32 v78, 3, v80
	v_lshl_add_u64 v[76:77], v[76:77], 0, v[196:197]
	v_lshlrev_b32_e32 v198, 1, v174
	v_mov_b32_e32 v199, v161
	v_and_b32_e32 v176, 24, v78
	s_lshl_b32 s36, s36, 10
	v_lshl_add_u64 v[76:77], v[76:77], 0, v[198:199]
	v_lshlrev_b32_e32 v200, 1, v176
	v_mov_b32_e32 v201, v161
	s_add_i32 s42, s36, s68
	v_lshl_add_u64 v[76:77], v[76:77], 0, v[200:201]
	s_mov_b32 m0, s42
	s_or_b32 s38, s44, 3
	global_load_lds_dwordx4 v[76:77], off
	v_lshl_or_b32 v76, s38, 1, v72
	v_ashrrev_i32_e32 v77, 31, v76
	v_lshrrev_b32_e32 v77, 28, v77
	v_add_u32_e32 v77, v76, v77
	v_and_b32_e32 v78, -16, v77
	v_sub_u32_e32 v76, v76, v78
	v_lshlrev_b32_e32 v78, 1, v76
	v_and_or_b32 v202, v78, -8, v73
	v_lshlrev_b32_e32 v77, 3, v77
	v_lshrrev_b32_e32 v73, 2, v202
	v_and_b32_e32 v168, 0xffffff80, v77
	v_xor_b32_e32 v73, v73, v232
	v_ashrrev_i32_e32 v169, 31, v168
	v_lshlrev_b32_e32 v76, 5, v76
	v_mad_i64_i32 v[74:75], s[44:45], v202, s57, v[74:75]
	v_lshlrev_b64 v[204:205], 1, v[168:169]
	v_and_b32_e32 v178, 0x60, v76
	v_lshlrev_b32_e32 v73, 3, v73
	v_lshl_add_u64 v[74:75], v[74:75], 0, v[204:205]
	v_lshlrev_b32_e32 v206, 1, v178
	v_mov_b32_e32 v207, v161
	v_and_b32_e32 v180, 24, v73
	s_lshl_b32 s38, s38, 10
	v_lshl_add_u64 v[74:75], v[74:75], 0, v[206:207]
	v_lshlrev_b32_e32 v208, 1, v180
	v_mov_b32_e32 v209, v161
	s_add_i32 s43, s38, s68
	v_lshl_add_u64 v[74:75], v[74:75], 0, v[208:209]
	s_mov_b32 m0, s43
	s_add_i32 s44, 0, 0x21500
	v_lshlrev_b32_e32 v73, 4, v72
	global_load_lds_dwordx4 v[74:75], off
	v_add_u32_e32 v74, s44, v73
	s_add_i32 s45, 0, 0x21700
	v_add_u32_e32 v73, s45, v73
	ds_read_b128 v[74:77], v74
	ds_read_b128 v[78:81], v73
	v_lshlrev_b32_e32 v234, 2, v72
	v_cmp_le_i32_e32 vcc, v234, v66
	v_or_b32_e32 v84, 8, v234
	s_waitcnt lgkmcnt(0)
; #define FENCE() do { asm volatile("" ::: "memory"); __builtin_amdgcn_sched_barrier(0); } while (0)
; __device__ __forceinline__ int crow(int r, int hi) { return (r & 3) + 8 * (r >> 2) + 4 * hi; }
; __device__ __forceinline__ int crow(int r, int hi) { return (r & 3) + 8 * (r >> 2) + 4 * hi; }
; template <int DK, int DV, bool MLSTM>
; __device__ __forceinline__ void out_unit2(LAS unsigned char* lds, LAS unsigned char* ldstab, const OutArgs a, const int wv) {
;     ...
; #pragma unroll
;     for (int kb = 0; kb < 4; ++kb) {
; #pragma unroll
;         for (int r = 0; r < 16; ++r) { const int s = 32 * kb + crow(r, hi);
;             const float xf = a_fl - akf[s], xb = a_bl - akb[s];
;             const float wf = __expf((s <= l2) ? xf : -1.0e30f), wb = __expf((s >= l2) ? xb : -1.0e30f);
;             p[kb][r] *= (wf * rf + wb * rbk); }
;         FENCE(); }
	v_fma_f32 v72, v64, v67, -v74
	v_fma_f32 v73, v65, v70, -v78
	v_mul_f32_e32 v72, 0x3fb8aa3b, v72
	v_fma_f32 v75, v64, v67, -v75
	v_cndmask_b32_e32 v72, v230, v72, vcc
	v_mul_f32_e32 v73, 0x3fb8aa3b, v73
	v_cmp_lt_i32_e32 vcc, v234, v66
	v_or_b32_e32 v74, 1, v234
	v_fma_f32 v78, v65, v70, -v79
	v_mul_f32_e32 v75, 0x3fb8aa3b, v75
	v_cndmask_b32_e32 v73, v73, v230, vcc
	v_cndmask_b32_e32 v75, v230, v75, vcc
	v_mul_f32_e32 v78, 0x3fb8aa3b, v78
	v_cmp_ge_i32_e32 vcc, v74, v66
	v_exp_f32_e32 v72, v72
	v_exp_f32_e32 v73, v73
	v_cndmask_b32_e32 v74, v230, v78, vcc
	v_exp_f32_e32 v75, v75
	v_exp_f32_e32 v74, v74
	v_add_f32_e32 v72, v72, v73
	v_mul_f32_e32 v48, v48, v72
	v_fma_f32 v73, v64, v67, -v76
	v_add_f32_e32 v72, v75, v74
	v_mul_f32_e32 v49, v49, v72
	v_or_b32_e32 v72, 2, v234
	v_mul_f32_e32 v73, 0x3fb8aa3b, v73
	v_cmp_le_i32_e32 vcc, v72, v66
	v_fma_f32 v74, v65, v70, -v80
	v_mul_f32_e32 v71, v65, v70
	v_cndmask_b32_e32 v73, v230, v73, vcc
	v_exp_f32_e32 v80, v73
	v_mul_f32_e32 v73, 0x3fb8aa3b, v74
	v_cmp_ge_i32_e32 vcc, v72, v66
	v_fma_f32 v74, v65, v70, -v81
	v_ashrrev_i32_e32 v183, 31, v182
	v_cndmask_b32_e32 v72, v230, v73, vcc
	v_exp_f32_e32 v82, v72
	v_or_b32_e32 v72, 3, v234
	v_fma_f32 v73, v64, v67, -v77
	v_mul_f32_e32 v73, 0x3fb8aa3b, v73
	v_cmp_le_i32_e32 vcc, v72, v66
	v_add_f32_e32 v80, v80, v82
	v_mul_f32_e32 v50, v50, v80
	v_cndmask_b32_e32 v73, v230, v73, vcc
	v_exp_f32_e32 v81, v73
	v_mul_f32_e32 v73, 0x3fb8aa3b, v74
	v_cmp_ge_i32_e32 vcc, v72, v66
	v_ashrrev_i32_e32 v187, 31, v186
	v_ashrrev_i32_e32 v195, 31, v194
	v_cndmask_b32_e32 v72, v230, v73, vcc
	v_exp_f32_e32 v83, v72
	v_lshlrev_b32_e32 v72, 2, v84
	v_add_u32_e32 v73, s44, v72
	v_add_u32_e32 v76, s45, v72
	ds_read_b128 v[72:75], v73
	ds_read_b128 v[76:79], v76
	v_cmp_le_i32_e32 vcc, v84, v66
	v_add_f32_e32 v80, v81, v83
	v_or_b32_e32 v81, 9, v234
	s_waitcnt lgkmcnt(0)
	v_fma_f32 v72, v64, v67, -v72
	v_fma_f32 v76, v65, v70, -v76
	v_mul_f32_e32 v72, 0x3fb8aa3b, v72
	v_cndmask_b32_e32 v72, v230, v72, vcc
	v_mul_f32_e32 v76, 0x3fb8aa3b, v76
	v_cmp_ge_i32_e32 vcc, v84, v66
	v_fma_f32 v73, v64, v67, -v73
	v_fma_f32 v77, v65, v70, -v77
	v_cndmask_b32_e32 v76, v230, v76, vcc
	v_mul_f32_e32 v73, 0x3fb8aa3b, v73
	v_cmp_le_i32_e32 vcc, v81, v66
	v_mul_f32_e32 v77, 0x3fb8aa3b, v77
	v_exp_f32_e32 v72, v72
	v_cndmask_b32_e32 v73, v230, v73, vcc
	v_cmp_ge_i32_e32 vcc, v81, v66
	v_exp_f32_e32 v76, v76
	v_exp_f32_e32 v73, v73
	v_cndmask_b32_e32 v77, v230, v77, vcc
	v_exp_f32_e32 v77, v77
	v_add_f32_e32 v72, v72, v76
	v_mul_f32_e32 v52, v52, v72
	v_mul_f32_e32 v51, v51, v80
	v_add_f32_e32 v72, v73, v77
	v_mul_f32_e32 v53, v53, v72
	v_or_b32_e32 v72, 10, v234
	v_fma_f32 v73, v64, v67, -v74
	v_mul_f32_e32 v73, 0x3fb8aa3b, v73
	v_cmp_le_i32_e32 vcc, v72, v66
	v_fma_f32 v74, v65, v70, -v78
	v_or_b32_e32 v84, 16, v234
	v_cndmask_b32_e32 v73, v230, v73, vcc
	v_exp_f32_e32 v80, v73
	v_mul_f32_e32 v73, 0x3fb8aa3b, v74
	v_cmp_ge_i32_e32 vcc, v72, v66
	v_fma_f32 v74, v65, v70, -v79
	v_ashrrev_i32_e32 v203, 31, v202
	v_cndmask_b32_e32 v72, v230, v73, vcc
	v_exp_f32_e32 v81, v72
	v_or_b32_e32 v72, 11, v234
	v_fma_f32 v73, v64, v67, -v75
	v_mul_f32_e32 v73, 0x3fb8aa3b, v73
	v_cmp_le_i32_e32 vcc, v72, v66
	v_add_f32_e32 v80, v80, v81
	v_mul_f32_e32 v54, v54, v80
	v_cndmask_b32_e32 v73, v230, v73, vcc
	v_exp_f32_e32 v82, v73
	v_mul_f32_e32 v73, 0x3fb8aa3b, v74
	v_cmp_ge_i32_e32 vcc, v72, v66
	s_nop 1
	v_cndmask_b32_e32 v72, v230, v73, vcc
	v_exp_f32_e32 v83, v72
	v_lshlrev_b32_e32 v72, 2, v84
	v_add_u32_e32 v73, s44, v72
	v_add_u32_e32 v76, s45, v72
	ds_read_b128 v[72:75], v73
	ds_read_b128 v[76:79], v76
	v_cmp_le_i32_e32 vcc, v84, v66
	v_add_f32_e32 v80, v82, v83
	s_waitcnt lgkmcnt(0)
	v_fma_f32 v72, v64, v67, -v72
	v_mul_f32_e32 v72, 0x3fb8aa3b, v72
	v_fma_f32 v76, v65, v70, -v76
	v_cndmask_b32_e32 v72, v230, v72, vcc
	v_exp_f32_e32 v81, v72
	v_mul_f32_e32 v72, 0x3fb8aa3b, v76
	v_cmp_ge_i32_e32 vcc, v84, v66
	v_fma_f32 v73, v64, v67, -v73
	v_fma_f32 v77, v65, v70, -v77
	v_cndmask_b32_e32 v72, v230, v72, vcc
	v_exp_f32_e32 v76, v72
	v_or_b32_e32 v72, 17, v234
	v_mul_f32_e32 v73, 0x3fb8aa3b, v73
	v_cmp_le_i32_e32 vcc, v72, v66
	v_mul_f32_e32 v77, 0x3fb8aa3b, v77
	v_fma_f32 v75, v64, v67, -v75
	v_cndmask_b32_e32 v73, v230, v73, vcc
	v_cmp_ge_i32_e32 vcc, v72, v66
	v_exp_f32_e32 v73, v73
	v_mul_f32_e32 v75, 0x3fb8aa3b, v75
	v_cndmask_b32_e32 v72, v230, v77, vcc
	v_exp_f32_e32 v77, v72
	v_mul_f32_e32 v72, v55, v80
	v_add_f32_e32 v55, v81, v76
	v_mul_f32_e32 v55, v56, v55
	v_add_f32_e32 v56, v73, v77
	v_mul_f32_e32 v56, v57, v56
	v_or_b32_e32 v57, 18, v234
	v_fma_f32 v73, v64, v67, -v74
	v_fma_f32 v74, v65, v70, -v78
	v_mul_f32_e32 v73, 0x3fb8aa3b, v73
	v_cmp_le_i32_e32 vcc, v57, v66
	v_mul_f32_e32 v74, 0x3fb8aa3b, v74
	v_fma_f32 v76, v65, v70, -v79
	v_cndmask_b32_e32 v73, v230, v73, vcc
	v_cmp_ge_i32_e32 vcc, v57, v66
	v_or_b32_e32 v84, 24, v234
	v_exp_f32_e32 v73, v73
	v_cndmask_b32_e32 v57, v230, v74, vcc
	v_or_b32_e32 v74, 19, v234
	v_cmp_le_i32_e32 vcc, v74, v66
	v_exp_f32_e32 v57, v57
	s_nop 0
	v_cndmask_b32_e32 v75, v230, v75, vcc
	v_exp_f32_e32 v82, v75
	v_mul_f32_e32 v75, 0x3fb8aa3b, v76
	v_cmp_ge_i32_e32 vcc, v74, v66
	v_add_f32_e32 v57, v73, v57
	v_mul_f32_e32 v57, v58, v57
	v_cndmask_b32_e32 v74, v230, v75, vcc
	v_exp_f32_e32 v83, v74
	v_lshlrev_b32_e32 v74, 2, v84
	v_add_u32_e32 v75, s44, v74
	v_add_u32_e32 v78, s45, v74
	ds_read_b128 v[74:77], v75
	ds_read_b128 v[78:81], v78
	v_cmp_le_i32_e32 vcc, v84, v66
	v_add_f32_e32 v58, v82, v83
	v_mul_f32_e32 v58, v59, v58
	s_waitcnt lgkmcnt(0)
; #define FENCE() do { asm volatile("" ::: "memory"); __builtin_amdgcn_sched_barrier(0); } while (0)
; __device__ __forceinline__ int crow(int r, int hi) { return (r & 3) + 8 * (r >> 2) + 4 * hi; }
; __device__ __forceinline__ int crow(int r, int hi) { return (r & 3) + 8 * (r >> 2) + 4 * hi; }
; template <int DK, int DV, bool MLSTM>
; __device__ __forceinline__ void out_unit2(LAS unsigned char* lds, LAS unsigned char* ldstab, const OutArgs a, const int wv) {
;     ...
; #pragma unroll
;     for (int kb = 0; kb < 4; ++kb) {
; #pragma unroll
;         for (int r = 0; r < 16; ++r) { const int s = 32 * kb + crow(r, hi);
;             const float xf = a_fl - akf[s], xb = a_bl - akb[s];
;             const float wf = __expf((s <= l2) ? xf : -1.0e30f), wb = __expf((s >= l2) ? xb : -1.0e30f);
;             p[kb][r] *= (wf * rf + wb * rbk); }
;         FENCE(); }
	v_fma_f32 v73, v64, v67, -v74
	v_fma_f32 v74, v65, v70, -v78
	v_mul_f32_e32 v73, 0x3fb8aa3b, v73
	v_cndmask_b32_e32 v73, v230, v73, vcc
	v_mul_f32_e32 v74, 0x3fb8aa3b, v74
	v_cmp_ge_i32_e32 vcc, v84, v66
	v_or_b32_e32 v78, 25, v234
	v_fma_f32 v75, v64, v67, -v75
	v_cndmask_b32_e32 v74, v230, v74, vcc
	v_fma_f32 v79, v65, v70, -v79
	v_mul_f32_e32 v75, 0x3fb8aa3b, v75
	v_cmp_le_i32_e32 vcc, v78, v66
	v_mul_f32_e32 v79, 0x3fb8aa3b, v79
	v_exp_f32_e32 v73, v73
	v_cndmask_b32_e32 v75, v230, v75, vcc
	v_cmp_ge_i32_e32 vcc, v78, v66
	v_exp_f32_e32 v74, v74
	v_exp_f32_e32 v75, v75
	v_cndmask_b32_e32 v78, v230, v79, vcc
	v_exp_f32_e32 v78, v78
	v_add_f32_e32 v59, v73, v74
	v_or_b32_e32 v73, 26, v234
	v_fma_f32 v74, v64, v67, -v76
	v_mul_f32_e32 v59, v60, v59
	v_add_f32_e32 v60, v75, v78
	v_fma_f32 v75, v65, v70, -v80
	v_mul_f32_e32 v74, 0x3fb8aa3b, v74
	v_cmp_le_i32_e32 vcc, v73, v66
	v_mul_f32_e32 v75, 0x3fb8aa3b, v75
	v_fma_f32 v76, v64, v67, -v77
	v_cndmask_b32_e32 v74, v230, v74, vcc
	v_cmp_ge_i32_e32 vcc, v73, v66
	v_fma_f32 v77, v65, v70, -v81
	v_mul_f32_e32 v76, 0x3fb8aa3b, v76
	v_cndmask_b32_e32 v73, v230, v75, vcc
	v_or_b32_e32 v75, 27, v234
	v_cmp_le_i32_e32 vcc, v75, v66
	v_mul_f32_e32 v77, 0x3fb8aa3b, v77
	v_exp_f32_e32 v74, v74
	v_cndmask_b32_e32 v76, v230, v76, vcc
	v_cmp_ge_i32_e32 vcc, v75, v66
	v_exp_f32_e32 v73, v73
	v_exp_f32_e32 v76, v76
	v_cndmask_b32_e32 v75, v230, v77, vcc
	v_exp_f32_e32 v75, v75
	v_mul_f32_e32 v60, v61, v60
	v_add_f32_e32 v61, v74, v73
	v_mul_f32_e32 v61, v62, v61
	v_add_f32_e32 v62, v76, v75
	v_mul_f32_e32 v62, v63, v62
	v_or_b32_e32 v63, 32, v234
	v_lshlrev_b32_e32 v73, 2, v63
	v_add_u32_e32 v74, s44, v73
	v_add_u32_e32 v73, s45, v73
	ds_read_b128 v[74:77], v74
	ds_read_b128 v[78:81], v73
	v_cmp_le_i32_e32 vcc, v63, v66
	v_or_b32_e32 v84, 40, v234
	s_waitcnt lgkmcnt(0)
	v_fma_f32 v73, v64, v67, -v74
	v_fma_f32 v74, v65, v70, -v78
	v_mul_f32_e32 v73, 0x3fb8aa3b, v73
	v_cndmask_b32_e32 v73, v230, v73, vcc
	v_mul_f32_e32 v74, 0x3fb8aa3b, v74
	v_cmp_ge_i32_e32 vcc, v63, v66
	v_fma_f32 v75, v64, v67, -v75
	v_fma_f32 v78, v65, v70, -v79
	v_cndmask_b32_e32 v63, v230, v74, vcc
	v_or_b32_e32 v74, 33, v234
	v_mul_f32_e32 v75, 0x3fb8aa3b, v75
	v_cmp_le_i32_e32 vcc, v74, v66
	v_mul_f32_e32 v78, 0x3fb8aa3b, v78
	v_exp_f32_e32 v73, v73
	v_cndmask_b32_e32 v75, v230, v75, vcc
	v_cmp_ge_i32_e32 vcc, v74, v66
	v_exp_f32_e32 v63, v63
	v_exp_f32_e32 v75, v75
	v_cndmask_b32_e32 v74, v230, v78, vcc
	v_exp_f32_e32 v74, v74
	v_add_f32_e32 v63, v73, v63
	v_mul_f32_e32 v32, v32, v63
	v_fma_f32 v73, v64, v67, -v76
	v_add_f32_e32 v63, v75, v74
	v_mul_f32_e32 v33, v33, v63
	v_or_b32_e32 v63, 34, v234
	v_fma_f32 v74, v65, v70, -v80
	v_mul_f32_e32 v73, 0x3fb8aa3b, v73
	v_cmp_le_i32_e32 vcc, v63, v66
	v_mul_f32_e32 v74, 0x3fb8aa3b, v74
	v_fma_f32 v75, v64, v67, -v77
	v_cndmask_b32_e32 v73, v230, v73, vcc
	v_cmp_ge_i32_e32 vcc, v63, v66
	v_mul_f32_e32 v75, 0x3fb8aa3b, v75
	v_fma_f32 v76, v65, v70, -v81
	v_cndmask_b32_e32 v63, v230, v74, vcc
	v_or_b32_e32 v74, 35, v234
	v_cmp_le_i32_e32 vcc, v74, v66
	v_exp_f32_e32 v73, v73
	v_exp_f32_e32 v63, v63
	v_cndmask_b32_e32 v75, v230, v75, vcc
	v_exp_f32_e32 v82, v75
	v_mul_f32_e32 v75, 0x3fb8aa3b, v76
	v_cmp_ge_i32_e32 vcc, v74, v66
	v_add_f32_e32 v63, v73, v63
	v_mul_f32_e32 v34, v34, v63
	v_cndmask_b32_e32 v74, v230, v75, vcc
	v_exp_f32_e32 v83, v74
	v_lshlrev_b32_e32 v74, 2, v84
	v_add_u32_e32 v75, s44, v74
	v_add_u32_e32 v78, s45, v74
	ds_read_b128 v[74:77], v75
	ds_read_b128 v[78:81], v78
	v_cmp_le_i32_e32 vcc, v84, v66
	v_add_f32_e32 v63, v82, v83
	v_mul_f32_e32 v35, v35, v63
	s_waitcnt lgkmcnt(0)
	v_fma_f32 v73, v64, v67, -v74
	v_fma_f32 v74, v65, v70, -v78
	v_mul_f32_e32 v73, 0x3fb8aa3b, v73
	v_cndmask_b32_e32 v73, v230, v73, vcc
	v_mul_f32_e32 v74, 0x3fb8aa3b, v74
	v_cmp_ge_i32_e32 vcc, v84, v66
	v_or_b32_e32 v78, 41, v234
	v_fma_f32 v75, v64, v67, -v75
	v_cndmask_b32_e32 v74, v230, v74, vcc
	v_fma_f32 v79, v65, v70, -v79
	v_mul_f32_e32 v75, 0x3fb8aa3b, v75
	v_cmp_le_i32_e32 vcc, v78, v66
	v_mul_f32_e32 v79, 0x3fb8aa3b, v79
	v_exp_f32_e32 v73, v73
	v_cndmask_b32_e32 v75, v230, v75, vcc
	v_cmp_ge_i32_e32 vcc, v78, v66
	v_exp_f32_e32 v74, v74
	v_exp_f32_e32 v75, v75
	v_cndmask_b32_e32 v78, v230, v79, vcc
	v_exp_f32_e32 v78, v78
	v_add_f32_e32 v63, v73, v74
	v_mul_f32_e32 v36, v36, v63
	v_fma_f32 v73, v64, v67, -v76
	v_add_f32_e32 v63, v75, v78
	v_mul_f32_e32 v37, v37, v63
	v_or_b32_e32 v63, 42, v234
	v_fma_f32 v74, v65, v70, -v80
	v_mul_f32_e32 v73, 0x3fb8aa3b, v73
	v_cmp_le_i32_e32 vcc, v63, v66
	v_mul_f32_e32 v74, 0x3fb8aa3b, v74
	v_fma_f32 v75, v64, v67, -v77
	v_cndmask_b32_e32 v73, v230, v73, vcc
	v_cmp_ge_i32_e32 vcc, v63, v66
	v_mul_f32_e32 v75, 0x3fb8aa3b, v75
	v_fma_f32 v76, v65, v70, -v81
	v_cndmask_b32_e32 v63, v230, v74, vcc
	v_or_b32_e32 v74, 43, v234
	v_cmp_le_i32_e32 vcc, v74, v66
	v_or_b32_e32 v84, 48, v234
	v_exp_f32_e32 v73, v73
	v_cndmask_b32_e32 v75, v230, v75, vcc
	v_exp_f32_e32 v82, v75
	v_mul_f32_e32 v75, 0x3fb8aa3b, v76
	v_cmp_ge_i32_e32 vcc, v74, v66
	v_exp_f32_e32 v63, v63
	s_nop 0
	v_cndmask_b32_e32 v74, v230, v75, vcc
	v_exp_f32_e32 v83, v74
	v_lshlrev_b32_e32 v74, 2, v84
	v_add_u32_e32 v75, s44, v74
	v_add_u32_e32 v78, s45, v74
	ds_read_b128 v[74:77], v75
	ds_read_b128 v[78:81], v78
	v_add_f32_e32 v63, v73, v63
	v_cmp_le_i32_e32 vcc, v84, v66
	v_mul_f32_e32 v38, v38, v63
	s_waitcnt lgkmcnt(0)
; #define FENCE() do { asm volatile("" ::: "memory"); __builtin_amdgcn_sched_barrier(0); } while (0)
; __device__ __forceinline__ int crow(int r, int hi) { return (r & 3) + 8 * (r >> 2) + 4 * hi; }
; __device__ __forceinline__ int crow(int r, int hi) { return (r & 3) + 8 * (r >> 2) + 4 * hi; }
; template <int DK, int DV, bool MLSTM>
; __device__ __forceinline__ void out_unit2(LAS unsigned char* lds, LAS unsigned char* ldstab, const OutArgs a, const int wv) {
;     ...
; #pragma unroll
;     for (int kb = 0; kb < 4; ++kb) {
; #pragma unroll
;         for (int r = 0; r < 16; ++r) { const int s = 32 * kb + crow(r, hi);
;             const float xf = a_fl - akf[s], xb = a_bl - akb[s];
;             const float wf = __expf((s <= l2) ? xf : -1.0e30f), wb = __expf((s >= l2) ? xb : -1.0e30f);
;             p[kb][r] *= (wf * rf + wb * rbk); }
;         FENCE(); }
	v_fma_f32 v73, v64, v67, -v74
	v_fma_f32 v74, v65, v70, -v78
	v_mul_f32_e32 v73, 0x3fb8aa3b, v73
	v_cndmask_b32_e32 v73, v230, v73, vcc
	v_mul_f32_e32 v74, 0x3fb8aa3b, v74
	v_cmp_ge_i32_e32 vcc, v84, v66
	v_or_b32_e32 v78, 49, v234
	v_fma_f32 v75, v64, v67, -v75
	v_cndmask_b32_e32 v74, v230, v74, vcc
	v_fma_f32 v79, v65, v70, -v79
	v_mul_f32_e32 v75, 0x3fb8aa3b, v75
	v_cmp_le_i32_e32 vcc, v78, v66
	v_mul_f32_e32 v79, 0x3fb8aa3b, v79
	v_exp_f32_e32 v73, v73
	v_cndmask_b32_e32 v75, v230, v75, vcc
	v_cmp_ge_i32_e32 vcc, v78, v66
	v_exp_f32_e32 v74, v74
	v_exp_f32_e32 v75, v75
	v_cndmask_b32_e32 v78, v230, v79, vcc
	v_exp_f32_e32 v78, v78
	v_add_f32_e32 v63, v82, v83
	v_mul_f32_e32 v63, v39, v63
	v_add_f32_e32 v39, v73, v74
	v_mul_f32_e32 v39, v40, v39
	v_add_f32_e32 v40, v75, v78
	v_mul_f32_e32 v40, v41, v40
	v_or_b32_e32 v41, 50, v234
	v_fma_f32 v73, v64, v67, -v76
	v_fma_f32 v74, v65, v70, -v80
	v_mul_f32_e32 v73, 0x3fb8aa3b, v73
	v_cmp_le_i32_e32 vcc, v41, v66
	v_mul_f32_e32 v74, 0x3fb8aa3b, v74
	v_fma_f32 v75, v64, v67, -v77
	v_cndmask_b32_e32 v73, v230, v73, vcc
	v_cmp_ge_i32_e32 vcc, v41, v66
	v_mul_f32_e32 v75, 0x3fb8aa3b, v75
	v_fma_f32 v76, v65, v70, -v81
	v_cndmask_b32_e32 v41, v230, v74, vcc
	v_or_b32_e32 v74, 51, v234
	v_cmp_le_i32_e32 vcc, v74, v66
	v_or_b32_e32 v84, 56, v234
	v_exp_f32_e32 v73, v73
	v_cndmask_b32_e32 v75, v230, v75, vcc
	v_exp_f32_e32 v82, v75
	v_mul_f32_e32 v75, 0x3fb8aa3b, v76
	v_cmp_ge_i32_e32 vcc, v74, v66
	v_exp_f32_e32 v41, v41
	s_nop 0
	v_cndmask_b32_e32 v74, v230, v75, vcc
	v_exp_f32_e32 v83, v74
	v_lshlrev_b32_e32 v74, 2, v84
	v_add_u32_e32 v75, s44, v74
	v_add_u32_e32 v78, s45, v74
	ds_read_b128 v[74:77], v75
	ds_read_b128 v[78:81], v78
	v_add_f32_e32 v41, v73, v41
	v_cmp_le_i32_e32 vcc, v84, v66
	v_mul_f32_e32 v41, v42, v41
	s_waitcnt lgkmcnt(0)
	v_fma_f32 v73, v64, v67, -v74
	v_fma_f32 v74, v65, v70, -v78
	v_mul_f32_e32 v73, 0x3fb8aa3b, v73
	v_cndmask_b32_e32 v73, v230, v73, vcc
	v_mul_f32_e32 v74, 0x3fb8aa3b, v74
	v_cmp_ge_i32_e32 vcc, v84, v66
	v_or_b32_e32 v78, 57, v234
	v_fma_f32 v75, v64, v67, -v75
	v_cndmask_b32_e32 v74, v230, v74, vcc
	v_fma_f32 v79, v65, v70, -v79
	v_mul_f32_e32 v75, 0x3fb8aa3b, v75
	v_cmp_le_i32_e32 vcc, v78, v66
	v_mul_f32_e32 v79, 0x3fb8aa3b, v79
	v_exp_f32_e32 v73, v73
	v_cndmask_b32_e32 v75, v230, v75, vcc
	v_cmp_ge_i32_e32 vcc, v78, v66
	v_exp_f32_e32 v74, v74
	v_exp_f32_e32 v75, v75
	v_cndmask_b32_e32 v78, v230, v79, vcc
	v_exp_f32_e32 v78, v78
	v_add_f32_e32 v42, v82, v83
	v_mul_f32_e32 v42, v43, v42
	v_add_f32_e32 v43, v73, v74
	v_or_b32_e32 v73, 58, v234
	v_fma_f32 v74, v64, v67, -v76
	v_mul_f32_e32 v43, v44, v43
	v_add_f32_e32 v44, v75, v78
	v_fma_f32 v75, v65, v70, -v80
	v_mul_f32_e32 v74, 0x3fb8aa3b, v74
	v_cmp_le_i32_e32 vcc, v73, v66
	v_mul_f32_e32 v75, 0x3fb8aa3b, v75
	v_fma_f32 v76, v64, v67, -v77
	v_cndmask_b32_e32 v74, v230, v74, vcc
	v_cmp_ge_i32_e32 vcc, v73, v66
	v_fma_f32 v77, v65, v70, -v81
	v_mul_f32_e32 v76, 0x3fb8aa3b, v76
	v_cndmask_b32_e32 v73, v230, v75, vcc
	v_or_b32_e32 v75, 59, v234
	v_cmp_le_i32_e32 vcc, v75, v66
	v_mul_f32_e32 v77, 0x3fb8aa3b, v77
	v_exp_f32_e32 v74, v74
	v_cndmask_b32_e32 v76, v230, v76, vcc
	v_cmp_ge_i32_e32 vcc, v75, v66
	v_exp_f32_e32 v73, v73
	v_exp_f32_e32 v76, v76
	v_cndmask_b32_e32 v75, v230, v77, vcc
	v_exp_f32_e32 v75, v75
	v_mul_f32_e32 v44, v45, v44
	v_add_f32_e32 v45, v74, v73
	v_mul_f32_e32 v45, v46, v45
	v_add_f32_e32 v46, v76, v75
	v_mul_f32_e32 v46, v47, v46
	v_or_b32_e32 v47, 64, v234
	v_lshlrev_b32_e32 v73, 2, v47
	v_add_u32_e32 v74, s44, v73
	v_add_u32_e32 v73, s45, v73
	ds_read_b128 v[74:77], v74
	ds_read_b128 v[78:81], v73
	v_cmp_le_i32_e32 vcc, v47, v66
	v_or_b32_e32 v84, 0x48, v234
	s_waitcnt lgkmcnt(0)
	v_fma_f32 v73, v64, v67, -v74
	v_fma_f32 v74, v65, v70, -v78
	v_mul_f32_e32 v73, 0x3fb8aa3b, v73
	v_cndmask_b32_e32 v73, v230, v73, vcc
	v_mul_f32_e32 v74, 0x3fb8aa3b, v74
	v_cmp_ge_i32_e32 vcc, v47, v66
	v_fma_f32 v75, v64, v67, -v75
	v_fma_f32 v78, v65, v70, -v79
	v_cndmask_b32_e32 v47, v230, v74, vcc
	v_or_b32_e32 v74, 0x41, v234
	v_mul_f32_e32 v75, 0x3fb8aa3b, v75
	v_cmp_le_i32_e32 vcc, v74, v66
	v_mul_f32_e32 v78, 0x3fb8aa3b, v78
	v_exp_f32_e32 v73, v73
	v_cndmask_b32_e32 v75, v230, v75, vcc
	v_cmp_ge_i32_e32 vcc, v74, v66
	v_exp_f32_e32 v47, v47
	v_exp_f32_e32 v75, v75
	v_cndmask_b32_e32 v74, v230, v78, vcc
	v_exp_f32_e32 v74, v74
	v_add_f32_e32 v47, v73, v47
	v_mul_f32_e32 v16, v16, v47
	v_fma_f32 v73, v64, v67, -v76
	v_add_f32_e32 v47, v75, v74
	v_mul_f32_e32 v17, v17, v47
	v_or_b32_e32 v47, 0x42, v234
	v_fma_f32 v74, v65, v70, -v80
	v_mul_f32_e32 v73, 0x3fb8aa3b, v73
	v_cmp_le_i32_e32 vcc, v47, v66
	v_mul_f32_e32 v74, 0x3fb8aa3b, v74
	v_fma_f32 v75, v64, v67, -v77
	v_cndmask_b32_e32 v73, v230, v73, vcc
	v_cmp_ge_i32_e32 vcc, v47, v66
	v_mul_f32_e32 v75, 0x3fb8aa3b, v75
	v_fma_f32 v76, v65, v70, -v81
	v_cndmask_b32_e32 v47, v230, v74, vcc
	v_or_b32_e32 v74, 0x43, v234
	v_cmp_le_i32_e32 vcc, v74, v66
	v_exp_f32_e32 v73, v73
	v_exp_f32_e32 v47, v47
	v_cndmask_b32_e32 v75, v230, v75, vcc
	v_exp_f32_e32 v82, v75
	v_mul_f32_e32 v75, 0x3fb8aa3b, v76
	v_cmp_ge_i32_e32 vcc, v74, v66
	v_add_f32_e32 v47, v73, v47
	v_mul_f32_e32 v47, v18, v47
	v_cndmask_b32_e32 v74, v230, v75, vcc
	v_exp_f32_e32 v83, v74
	v_lshlrev_b32_e32 v74, 2, v84
	v_add_u32_e32 v75, s44, v74
	v_add_u32_e32 v78, s45, v74
	ds_read_b128 v[74:77], v75
	ds_read_b128 v[78:81], v78
	v_cmp_le_i32_e32 vcc, v84, v66
	v_add_f32_e32 v18, v82, v83
	s_waitcnt lgkmcnt(0)
; #define FENCE() do { asm volatile("" ::: "memory"); __builtin_amdgcn_sched_barrier(0); } while (0)
; __device__ __forceinline__ int crow(int r, int hi) { return (r & 3) + 8 * (r >> 2) + 4 * hi; }
; __device__ __forceinline__ int crow(int r, int hi) { return (r & 3) + 8 * (r >> 2) + 4 * hi; }
; template <int DK, int DV, bool MLSTM>
; __device__ __forceinline__ void out_unit2(LAS unsigned char* lds, LAS unsigned char* ldstab, const OutArgs a, const int wv) {
;     ...
; #pragma unroll
;     for (int kb = 0; kb < 4; ++kb) {
; #pragma unroll
;         for (int r = 0; r < 16; ++r) { const int s = 32 * kb + crow(r, hi);
;             const float xf = a_fl - akf[s], xb = a_bl - akb[s];
;             const float wf = __expf((s <= l2) ? xf : -1.0e30f), wb = __expf((s >= l2) ? xb : -1.0e30f);
;             p[kb][r] *= (wf * rf + wb * rbk); }
;         FENCE(); }
	v_fma_f32 v73, v64, v67, -v74
	v_fma_f32 v74, v65, v70, -v78
	v_mul_f32_e32 v73, 0x3fb8aa3b, v73
	v_cndmask_b32_e32 v73, v230, v73, vcc
	v_mul_f32_e32 v74, 0x3fb8aa3b, v74
	v_cmp_ge_i32_e32 vcc, v84, v66
	v_or_b32_e32 v78, 0x49, v234
	v_fma_f32 v75, v64, v67, -v75
	v_cndmask_b32_e32 v74, v230, v74, vcc
	v_fma_f32 v79, v65, v70, -v79
	v_mul_f32_e32 v75, 0x3fb8aa3b, v75
	v_cmp_le_i32_e32 vcc, v78, v66
	v_mul_f32_e32 v79, 0x3fb8aa3b, v79
	v_exp_f32_e32 v73, v73
	v_cndmask_b32_e32 v75, v230, v75, vcc
	v_cmp_ge_i32_e32 vcc, v78, v66
	v_exp_f32_e32 v74, v74
	v_exp_f32_e32 v75, v75
	v_cndmask_b32_e32 v78, v230, v79, vcc
	v_exp_f32_e32 v78, v78
	v_mul_f32_e32 v79, v19, v18
	v_add_f32_e32 v18, v73, v74
	v_mul_f32_e32 v73, v20, v18
	v_add_f32_e32 v18, v75, v78
	v_mul_f32_e32 v78, v21, v18
	v_or_b32_e32 v18, 0x4a, v234
	v_fma_f32 v19, v64, v67, -v76
	v_mul_f32_e32 v19, 0x3fb8aa3b, v19
	v_cmp_le_i32_e32 vcc, v18, v66
	v_fma_f32 v20, v65, v70, -v80
	v_or_b32_e32 v84, 0x50, v234
	v_cndmask_b32_e32 v19, v230, v19, vcc
	v_exp_f32_e32 v80, v19
	v_mul_f32_e32 v19, 0x3fb8aa3b, v20
	v_cmp_ge_i32_e32 vcc, v18, v66
	v_fma_f32 v20, v65, v70, -v81
	s_nop 0
	v_cndmask_b32_e32 v18, v230, v19, vcc
	v_exp_f32_e32 v82, v18
	v_or_b32_e32 v18, 0x4b, v234
	v_fma_f32 v19, v64, v67, -v77
	v_mul_f32_e32 v19, 0x3fb8aa3b, v19
	v_cmp_le_i32_e32 vcc, v18, v66
	v_add_f32_e32 v80, v80, v82
	v_mul_f32_e32 v80, v22, v80
	v_cndmask_b32_e32 v19, v230, v19, vcc
	v_exp_f32_e32 v81, v19
	v_mul_f32_e32 v19, 0x3fb8aa3b, v20
	v_cmp_ge_i32_e32 vcc, v18, v66
	s_nop 1
	v_cndmask_b32_e32 v18, v230, v19, vcc
	v_exp_f32_e32 v83, v18
	v_lshlrev_b32_e32 v18, 2, v84
	v_add_u32_e32 v19, s44, v18
	v_add_u32_e32 v74, s45, v18
	ds_read_b128 v[18:21], v19
	ds_read_b128 v[74:77], v74
	v_cmp_le_i32_e32 vcc, v84, v66
	v_add_f32_e32 v22, v81, v83
	v_or_b32_e32 v81, 0x51, v234
	s_waitcnt lgkmcnt(0)
	v_fma_f32 v18, v64, v67, -v18
	v_fma_f32 v74, v65, v70, -v74
	v_mul_f32_e32 v18, 0x3fb8aa3b, v18
	v_cndmask_b32_e32 v18, v230, v18, vcc
	v_mul_f32_e32 v74, 0x3fb8aa3b, v74
	v_cmp_ge_i32_e32 vcc, v84, v66
	v_fma_f32 v19, v64, v67, -v19
	v_fma_f32 v75, v65, v70, -v75
	v_cndmask_b32_e32 v74, v230, v74, vcc
	v_mul_f32_e32 v19, 0x3fb8aa3b, v19
	v_cmp_le_i32_e32 vcc, v81, v66
	v_mul_f32_e32 v75, 0x3fb8aa3b, v75
	v_exp_f32_e32 v18, v18
	v_cndmask_b32_e32 v19, v230, v19, vcc
	v_cmp_ge_i32_e32 vcc, v81, v66
	v_exp_f32_e32 v74, v74
	v_exp_f32_e32 v19, v19
	v_cndmask_b32_e32 v75, v230, v75, vcc
	v_exp_f32_e32 v75, v75
	v_add_f32_e32 v18, v18, v74
	v_mul_f32_e32 v74, v24, v18
	v_or_b32_e32 v84, 0x58, v234
	v_add_f32_e32 v18, v19, v75
	v_mul_f32_e32 v75, v25, v18
	v_or_b32_e32 v18, 0x52, v234
	v_fma_f32 v19, v64, v67, -v20
	v_mul_f32_e32 v19, 0x3fb8aa3b, v19
	v_cmp_le_i32_e32 vcc, v18, v66
	v_fma_f32 v20, v65, v70, -v76
	v_mul_f32_e32 v81, v23, v22
	v_cndmask_b32_e32 v19, v230, v19, vcc
	v_exp_f32_e32 v76, v19
	v_mul_f32_e32 v19, 0x3fb8aa3b, v20
	v_cmp_ge_i32_e32 vcc, v18, v66
	v_fma_f32 v20, v65, v70, -v77
	s_nop 0
	v_cndmask_b32_e32 v18, v230, v19, vcc
	v_exp_f32_e32 v82, v18
	v_or_b32_e32 v18, 0x53, v234
	v_fma_f32 v19, v64, v67, -v21
	v_mul_f32_e32 v19, 0x3fb8aa3b, v19
	v_cmp_le_i32_e32 vcc, v18, v66
	v_add_f32_e32 v76, v76, v82
	v_mul_f32_e32 v26, v26, v76
	v_cndmask_b32_e32 v19, v230, v19, vcc
	v_exp_f32_e32 v77, v19
	v_mul_f32_e32 v19, 0x3fb8aa3b, v20
	v_cmp_ge_i32_e32 vcc, v18, v66
	s_nop 1
	v_cndmask_b32_e32 v18, v230, v19, vcc
	v_exp_f32_e32 v83, v18
	v_lshlrev_b32_e32 v18, 2, v84
	v_add_u32_e32 v19, s44, v18
	v_add_u32_e32 v22, s45, v18
	ds_read_b128 v[18:21], v19
	ds_read_b128 v[22:25], v22
	v_cmp_le_i32_e32 vcc, v84, v66
	v_add_f32_e32 v76, v77, v83
	v_or_b32_e32 v77, 0x59, v234
	s_waitcnt lgkmcnt(0)
	v_fma_f32 v18, v64, v67, -v18
	v_fma_f32 v22, v65, v70, -v22
	v_mul_f32_e32 v18, 0x3fb8aa3b, v18
	v_cndmask_b32_e32 v18, v230, v18, vcc
	v_mul_f32_e32 v22, 0x3fb8aa3b, v22
	v_cmp_ge_i32_e32 vcc, v84, v66
	v_fma_f32 v19, v64, v67, -v19
	v_fma_f32 v23, v65, v70, -v23
	v_cndmask_b32_e32 v22, v230, v22, vcc
	v_mul_f32_e32 v19, 0x3fb8aa3b, v19
	v_cmp_le_i32_e32 vcc, v77, v66
	v_mul_f32_e32 v23, 0x3fb8aa3b, v23
	v_exp_f32_e32 v18, v18
	v_cndmask_b32_e32 v19, v230, v19, vcc
	v_cmp_ge_i32_e32 vcc, v77, v66
	v_exp_f32_e32 v22, v22
	v_exp_f32_e32 v19, v19
	v_cndmask_b32_e32 v23, v230, v23, vcc
	v_exp_f32_e32 v23, v23
	v_add_f32_e32 v18, v18, v22
	v_mul_f32_e32 v28, v28, v18
	v_fma_f32 v20, v64, v67, -v20
	v_add_f32_e32 v18, v19, v23
	v_or_b32_e32 v19, 0x5a, v234
	v_fma_f32 v22, v65, v70, -v24
	v_mul_f32_e32 v20, 0x3fb8aa3b, v20
	v_cmp_le_i32_e32 vcc, v19, v66
	v_mul_f32_e32 v22, 0x3fb8aa3b, v22
	v_fma_f32 v21, v64, v67, -v21
	v_cndmask_b32_e32 v20, v230, v20, vcc
	v_cmp_ge_i32_e32 vcc, v19, v66
	v_fma_f32 v23, v65, v70, -v25
	v_mul_f32_e32 v21, 0x3fb8aa3b, v21
	v_cndmask_b32_e32 v19, v230, v22, vcc
	v_or_b32_e32 v22, 0x5b, v234
	v_cmp_le_i32_e32 vcc, v22, v66
	v_mul_f32_e32 v23, 0x3fb8aa3b, v23
	v_exp_f32_e32 v20, v20
	v_cndmask_b32_e32 v21, v230, v21, vcc
	v_cmp_ge_i32_e32 vcc, v22, v66
	v_exp_f32_e32 v19, v19
	v_exp_f32_e32 v21, v21
	v_cndmask_b32_e32 v22, v230, v23, vcc
	v_exp_f32_e32 v22, v22
	v_mul_f32_e32 v29, v29, v18
	v_add_f32_e32 v18, v20, v19
	v_mul_f32_e32 v30, v30, v18
	v_add_f32_e32 v18, v21, v22
	v_mul_f32_e32 v27, v27, v76
	v_mul_f32_e32 v31, v31, v18
	v_or_b32_e32 v76, 0x60, v234
	v_lshlrev_b32_e32 v18, 2, v76
	v_add_u32_e32 v19, s44, v18
	v_add_u32_e32 v22, s45, v18
	ds_read_b128 v[18:21], v19
	ds_read_b128 v[22:25], v22
	v_cmp_le_i32_e32 vcc, v76, v66
	v_or_b32_e32 v84, 0x68, v234
	s_waitcnt lgkmcnt(0)
; #define FENCE() do { asm volatile("" ::: "memory"); __builtin_amdgcn_sched_barrier(0); } while (0)
; __device__ __forceinline__ int crow(int r, int hi) { return (r & 3) + 8 * (r >> 2) + 4 * hi; }
; __device__ __forceinline__ int crow(int r, int hi) { return (r & 3) + 8 * (r >> 2) + 4 * hi; }
; template <int DK, int DV, bool MLSTM>
; __device__ __forceinline__ void out_unit2(LAS unsigned char* lds, LAS unsigned char* ldstab, const OutArgs a, const int wv) {
;     ...
; #pragma unroll
;     for (int kb = 0; kb < 4; ++kb) {
; #pragma unroll
;         for (int r = 0; r < 16; ++r) { const int s = 32 * kb + crow(r, hi);
;             const float xf = a_fl - akf[s], xb = a_bl - akb[s];
;             const float wf = __expf((s <= l2) ? xf : -1.0e30f), wb = __expf((s >= l2) ? xb : -1.0e30f);
;             p[kb][r] *= (wf * rf + wb * rbk); }
;         FENCE(); }
	v_fma_f32 v18, v64, v67, -v18
	v_fma_f32 v22, v65, v70, -v22
	v_mul_f32_e32 v18, 0x3fb8aa3b, v18
	v_cndmask_b32_e32 v18, v230, v18, vcc
	v_mul_f32_e32 v22, 0x3fb8aa3b, v22
	v_cmp_ge_i32_e32 vcc, v76, v66
	v_or_b32_e32 v76, 0x61, v234
	v_fma_f32 v19, v64, v67, -v19
	v_cndmask_b32_e32 v22, v230, v22, vcc
	v_fma_f32 v23, v65, v70, -v23
	v_mul_f32_e32 v19, 0x3fb8aa3b, v19
	v_cmp_le_i32_e32 vcc, v76, v66
	v_mul_f32_e32 v23, 0x3fb8aa3b, v23
	v_exp_f32_e32 v18, v18
	v_cndmask_b32_e32 v19, v230, v19, vcc
	v_cmp_ge_i32_e32 vcc, v76, v66
	v_exp_f32_e32 v22, v22
	v_exp_f32_e32 v19, v19
	v_cndmask_b32_e32 v23, v230, v23, vcc
	v_exp_f32_e32 v23, v23
	v_add_f32_e32 v18, v18, v22
	v_mul_f32_e32 v76, v0, v18
	v_fma_f32 v18, v65, v70, -v24
	v_add_f32_e32 v0, v19, v23
	v_mul_f32_e32 v77, v1, v0
	v_or_b32_e32 v0, 0x62, v234
	v_fma_f32 v1, v64, v67, -v20
	v_mul_f32_e32 v1, 0x3fb8aa3b, v1
	v_cmp_le_i32_e32 vcc, v0, v66
	v_mul_f32_e32 v18, 0x3fb8aa3b, v18
	v_fma_f32 v19, v64, v67, -v21
	v_cndmask_b32_e32 v1, v230, v1, vcc
	v_cmp_ge_i32_e32 vcc, v0, v66
	v_mul_f32_e32 v19, 0x3fb8aa3b, v19
	v_fma_f32 v20, v65, v70, -v25
	v_cndmask_b32_e32 v0, v230, v18, vcc
	v_or_b32_e32 v18, 0x63, v234
	v_cmp_le_i32_e32 vcc, v18, v66
	v_exp_f32_e32 v1, v1
	v_exp_f32_e32 v0, v0
	v_cndmask_b32_e32 v19, v230, v19, vcc
	v_exp_f32_e32 v82, v19
	v_mul_f32_e32 v19, 0x3fb8aa3b, v20
	v_cmp_ge_i32_e32 vcc, v18, v66
	v_add_f32_e32 v0, v1, v0
	v_mul_f32_e32 v85, v2, v0
	v_cndmask_b32_e32 v18, v230, v19, vcc
	v_exp_f32_e32 v83, v18
	v_lshlrev_b32_e32 v18, 2, v84
	v_add_u32_e32 v19, s44, v18
	v_add_u32_e32 v22, s45, v18
	ds_read_b128 v[18:21], v19
	ds_read_b128 v[22:25], v22
	v_cmp_le_i32_e32 vcc, v84, v66
	v_add_f32_e32 v0, v82, v83
	v_or_b32_e32 v83, 0x70, v234
	s_waitcnt lgkmcnt(0)
	v_fma_f32 v1, v64, v67, -v18
	v_fma_f32 v2, v65, v70, -v22
	v_mul_f32_e32 v1, 0x3fb8aa3b, v1
	v_cndmask_b32_e32 v1, v230, v1, vcc
	v_mul_f32_e32 v2, 0x3fb8aa3b, v2
	v_cmp_ge_i32_e32 vcc, v84, v66
	v_or_b32_e32 v18, 0x69, v234
	v_fma_f32 v19, v64, v67, -v19
	v_cndmask_b32_e32 v2, v230, v2, vcc
	v_fma_f32 v22, v65, v70, -v23
	v_mul_f32_e32 v19, 0x3fb8aa3b, v19
	v_cmp_le_i32_e32 vcc, v18, v66
	v_mul_f32_e32 v22, 0x3fb8aa3b, v22
	v_exp_f32_e32 v1, v1
	v_cndmask_b32_e32 v19, v230, v19, vcc
	v_cmp_ge_i32_e32 vcc, v18, v66
	v_exp_f32_e32 v2, v2
	v_exp_f32_e32 v19, v19
	v_cndmask_b32_e32 v18, v230, v22, vcc
	v_exp_f32_e32 v18, v18
	v_mul_f32_e32 v22, v3, v0
	v_add_f32_e32 v0, v1, v2
	v_mul_f32_e32 v23, v4, v0
	v_add_f32_e32 v0, v19, v18
	v_mul_f32_e32 v82, v5, v0
	v_or_b32_e32 v0, 0x6a, v234
	v_fma_f32 v1, v64, v67, -v20
	v_mul_f32_e32 v1, 0x3fb8aa3b, v1
	v_cmp_le_i32_e32 vcc, v0, v66
	v_fma_f32 v2, v65, v70, -v24
	s_nop 0
	v_cndmask_b32_e32 v1, v230, v1, vcc
	v_exp_f32_e32 v4, v1
	v_mul_f32_e32 v1, 0x3fb8aa3b, v2
	v_cmp_ge_i32_e32 vcc, v0, v66
	v_fma_f32 v2, v65, v70, -v25
	s_nop 0
	v_cndmask_b32_e32 v0, v230, v1, vcc
	v_exp_f32_e32 v5, v0
	v_or_b32_e32 v0, 0x6b, v234
	v_fma_f32 v1, v64, v67, -v21
	v_mul_f32_e32 v1, 0x3fb8aa3b, v1
	v_cmp_le_i32_e32 vcc, v0, v66
	v_add_f32_e32 v4, v4, v5
	v_mul_f32_e32 v84, v6, v4
	v_cndmask_b32_e32 v1, v230, v1, vcc
	v_exp_f32_e32 v24, v1
	v_mul_f32_e32 v1, 0x3fb8aa3b, v2
	v_cmp_ge_i32_e32 vcc, v0, v66
	v_or_b32_e32 v6, 0x71, v234
	s_nop 0
	v_cndmask_b32_e32 v0, v230, v1, vcc
	v_exp_f32_e32 v25, v0
	v_lshlrev_b32_e32 v0, 2, v83
	v_add_u32_e32 v1, s44, v0
	v_add_u32_e32 v18, s45, v0
	ds_read_b128 v[0:3], v1
	ds_read_b128 v[18:21], v18
	v_cmp_le_i32_e32 vcc, v83, v66
	v_add_f32_e32 v4, v24, v25
	v_or_b32_e32 v25, 0x78, v234
	s_waitcnt lgkmcnt(0)
	v_fma_f32 v0, v64, v67, -v0
	v_fma_f32 v5, v65, v70, -v18
	v_mul_f32_e32 v0, 0x3fb8aa3b, v0
	v_cndmask_b32_e32 v0, v230, v0, vcc
	v_mul_f32_e32 v5, 0x3fb8aa3b, v5
	v_cmp_ge_i32_e32 vcc, v83, v66
	v_fma_f32 v1, v64, v67, -v1
	v_fma_f32 v18, v65, v70, -v19
	v_cndmask_b32_e32 v5, v230, v5, vcc
	v_mul_f32_e32 v1, 0x3fb8aa3b, v1
	v_cmp_le_i32_e32 vcc, v6, v66
	v_mul_f32_e32 v18, 0x3fb8aa3b, v18
	v_exp_f32_e32 v0, v0
	v_cndmask_b32_e32 v1, v230, v1, vcc
	v_cmp_ge_i32_e32 vcc, v6, v66
	v_exp_f32_e32 v5, v5
	v_exp_f32_e32 v1, v1
	v_cndmask_b32_e32 v6, v230, v18, vcc
	v_exp_f32_e32 v6, v6
	v_add_f32_e32 v0, v0, v5
	v_mul_f32_e32 v8, v8, v0
	v_mul_f32_e32 v18, v7, v4
	v_add_f32_e32 v0, v1, v6
	v_mul_f32_e32 v9, v9, v0
	v_or_b32_e32 v0, 0x72, v234
	v_fma_f32 v1, v64, v67, -v2
	v_mul_f32_e32 v1, 0x3fb8aa3b, v1
	v_cmp_le_i32_e32 vcc, v0, v66
	v_fma_f32 v2, v65, v70, -v20
	s_nop 0
	v_cndmask_b32_e32 v1, v230, v1, vcc
	v_exp_f32_e32 v19, v1
	v_mul_f32_e32 v1, 0x3fb8aa3b, v2
	v_cmp_ge_i32_e32 vcc, v0, v66
	v_fma_f32 v2, v65, v70, -v21
	s_nop 0
	v_cndmask_b32_e32 v0, v230, v1, vcc
	v_exp_f32_e32 v20, v0
	v_or_b32_e32 v0, 0x73, v234
	v_fma_f32 v1, v64, v67, -v3
	v_mul_f32_e32 v1, 0x3fb8aa3b, v1
	v_cmp_le_i32_e32 vcc, v0, v66
	v_add_f32_e32 v19, v19, v20
	v_or_b32_e32 v20, 0x79, v234
	v_cndmask_b32_e32 v1, v230, v1, vcc
	v_exp_f32_e32 v21, v1
	v_mul_f32_e32 v1, 0x3fb8aa3b, v2
	v_cmp_ge_i32_e32 vcc, v0, v66
	v_mul_f32_e32 v10, v10, v19
	s_nop 0
	v_cndmask_b32_e32 v0, v230, v1, vcc
	v_exp_f32_e32 v24, v0
	v_lshlrev_b32_e32 v0, 2, v25
	v_add_u32_e32 v1, s44, v0
	v_add_u32_e32 v4, s45, v0
	ds_read_b128 v[0:3], v1
	ds_read_b128 v[4:7], v4
	v_cmp_le_i32_e32 vcc, v25, v66
	v_add_f32_e32 v19, v21, v24
	s_waitcnt lgkmcnt(0)
; #define VM_WAIT() asm volatile("s_waitcnt vmcnt(0)" ::: "memory")
; #define FENCE() do { asm volatile("" ::: "memory"); __builtin_amdgcn_sched_barrier(0); } while (0)
; __device__ __forceinline__ int crow(int r, int hi) { return (r & 3) + 8 * (r >> 2) + 4 * hi; }
; __device__ __forceinline__ int crow(int r, int hi) { return (r & 3) + 8 * (r >> 2) + 4 * hi; }
; template <int DK, int DV, bool MLSTM>
; __device__ __forceinline__ void out_unit2(LAS unsigned char* lds, LAS unsigned char* ldstab, const OutArgs a, const int wv) {
;     ...
; #pragma unroll
;     for (int kb = 0; kb < 4; ++kb) {
; #pragma unroll
;         for (int r = 0; r < 16; ++r) { const int s = 32 * kb + crow(r, hi);
;             const float xf = a_fl - akf[s], xb = a_bl - akb[s];
;             const float wf = __expf((s <= l2) ? xf : -1.0e30f), wb = __expf((s >= l2) ? xb : -1.0e30f);
;             p[kb][r] *= (wf * rf + wb * rbk); }
;         FENCE(); }
;     const float qsf = __expf(a_fl) * rf, qsb = __expf(a_bl) * rbk;
;     bf16x8 pa[8];
;     ...
; #pragma unroll
;     for (int kb = 0; kb < 4; ++kb) { LA_PK4(p[kb], 0, pa[2 * kb]); LA_PK4(p[kb], 8, pa[2 * kb + 1]); }
;     ...
; #pragma unroll
;     for (int pc = 0; pc < 4; ++pc) {
;         VM_WAIT(); __syncthreads();
;         OUT_DMA(pc + 1);
;         const bf16x8 af0 = pa[2 * pc], af1 = pa[2 * pc + 1];
;         OUT_MMA(pc & 1);
	v_fma_f32 v0, v64, v67, -v0
	v_fma_f32 v4, v65, v70, -v4
	v_mul_f32_e32 v0, 0x3fb8aa3b, v0
	v_cndmask_b32_e32 v0, v230, v0, vcc
	v_mul_f32_e32 v4, 0x3fb8aa3b, v4
	v_cmp_ge_i32_e32 vcc, v25, v66
	v_fma_f32 v1, v64, v67, -v1
	v_fma_f32 v5, v65, v70, -v5
	v_cndmask_b32_e32 v4, v230, v4, vcc
	v_mul_f32_e32 v1, 0x3fb8aa3b, v1
	v_cmp_le_i32_e32 vcc, v20, v66
	v_mul_f32_e32 v5, 0x3fb8aa3b, v5
	v_exp_f32_e32 v0, v0
	v_cndmask_b32_e32 v1, v230, v1, vcc
	v_cmp_ge_i32_e32 vcc, v20, v66
	v_exp_f32_e32 v4, v4
	v_exp_f32_e32 v1, v1
	v_cndmask_b32_e32 v5, v230, v5, vcc
	v_exp_f32_e32 v5, v5
	v_add_f32_e32 v0, v0, v4
	v_or_b32_e32 v4, 0x7a, v234
	v_fma_f32 v2, v64, v67, -v2
	v_add_f32_e32 v1, v1, v5
	v_fma_f32 v5, v65, v70, -v6
	v_mul_f32_e32 v2, 0x3fb8aa3b, v2
	v_cmp_le_i32_e32 vcc, v4, v66
	v_mul_f32_e32 v5, 0x3fb8aa3b, v5
	v_fma_f32 v3, v64, v67, -v3
	v_cndmask_b32_e32 v2, v230, v2, vcc
	v_cmp_ge_i32_e32 vcc, v4, v66
	v_fma_f32 v6, v65, v70, -v7
	v_mul_f32_e32 v3, 0x3fb8aa3b, v3
	v_cndmask_b32_e32 v4, v230, v5, vcc
	v_or_b32_e32 v5, 0x7b, v234
	v_cmp_le_i32_e32 vcc, v5, v66
	v_mul_f32_e32 v6, 0x3fb8aa3b, v6
	v_exp_f32_e32 v2, v2
	v_cndmask_b32_e32 v3, v230, v3, vcc
	v_cmp_ge_i32_e32 vcc, v5, v66
	v_exp_f32_e32 v4, v4
	v_exp_f32_e32 v3, v3
	v_cndmask_b32_e32 v5, v230, v6, vcc
	v_exp_f32_e32 v5, v5
	v_add_f32_e32 v2, v2, v4
	v_mul_f32_e32 v11, v11, v19
	v_mul_f32_e32 v0, v12, v0
	v_add_f32_e32 v3, v3, v5
	v_mul_f32_e32 v1, v13, v1
	v_mul_f32_e32 v2, v14, v2
	v_mul_f32_e32 v3, v15, v3
	s_add_u32 s44, s37, 0x61000
	s_addc_u32 s45, s16, 0
	v_cvt_pk_bf16_f32 v64, v48, v49
	v_cvt_pk_bf16_f32 v65, v50, v51
	v_cvt_pk_bf16_f32 v66, v52, v53
	v_cvt_pk_bf16_f32 v67, v54, v72
	v_cvt_pk_bf16_f32 v152, v55, v56
	v_cvt_pk_bf16_f32 v153, v57, v58
	v_cvt_pk_bf16_f32 v154, v59, v60
	v_cvt_pk_bf16_f32 v155, v61, v62
	v_cvt_pk_bf16_f32 v148, v32, v33
	v_cvt_pk_bf16_f32 v149, v34, v35
	v_cvt_pk_bf16_f32 v150, v36, v37
	v_cvt_pk_bf16_f32 v151, v38, v63
	v_cvt_pk_bf16_f32 v144, v39, v40
	v_cvt_pk_bf16_f32 v145, v41, v42
	v_cvt_pk_bf16_f32 v146, v43, v44
	v_cvt_pk_bf16_f32 v147, v45, v46
	v_cvt_pk_bf16_f32 v140, v16, v17
	v_cvt_pk_bf16_f32 v141, v47, v79
	v_cvt_pk_bf16_f32 v142, v73, v78
	v_cvt_pk_bf16_f32 v143, v80, v81
	v_cvt_pk_bf16_f32 v136, v74, v75
	v_cvt_pk_bf16_f32 v137, v26, v27
	v_cvt_pk_bf16_f32 v138, v28, v29
	v_cvt_pk_bf16_f32 v139, v30, v31
	v_cvt_pk_bf16_f32 v132, v76, v77
	v_cvt_pk_bf16_f32 v133, v85, v22
	v_cvt_pk_bf16_f32 v134, v23, v82
	v_cvt_pk_bf16_f32 v135, v84, v18
	v_cvt_pk_bf16_f32 v128, v8, v9
	v_cvt_pk_bf16_f32 v129, v10, v11
	v_cvt_pk_bf16_f32 v130, v0, v1
	v_mov_b64_e32 v[0:1], s[44:45]
	v_cvt_pk_bf16_f32 v131, v2, v3
	v_mad_i64_i32 v[2:3], s[44:45], v182, s57, v[0:1]
	v_lshl_add_u64 v[2:3], v[2:3], 0, v[184:185]
	v_lshl_add_u64 v[2:3], v[2:3], 0, v[160:161]
	s_add_i32 s94, s6, s80
	v_lshl_add_u64 v[2:3], v[2:3], 0, v[156:157]
	s_mov_b32 m0, s94
	s_waitcnt vmcnt(0)
	s_waitcnt vmcnt(0)
	s_barrier
	global_load_lds_dwordx4 v[2:3], off
	v_mad_i64_i32 v[2:3], s[44:45], v186, s57, v[0:1]
	v_lshl_add_u64 v[2:3], v[2:3], 0, v[188:189]
	v_lshl_add_u64 v[2:3], v[2:3], 0, v[190:191]
	s_add_i32 s44, s7, s80
	v_lshl_add_u64 v[2:3], v[2:3], 0, v[192:193]
	s_mov_b32 m0, s44
	s_add_i32 s45, s36, s80
	global_load_lds_dwordx4 v[2:3], off
	v_mad_i64_i32 v[2:3], s[96:97], v194, s57, v[0:1]
	v_lshl_add_u64 v[2:3], v[2:3], 0, v[196:197]
	v_mad_i64_i32 v[0:1], s[96:97], v202, s57, v[0:1]
	v_lshl_add_u64 v[2:3], v[2:3], 0, v[198:199]
	v_lshl_add_u64 v[0:1], v[0:1], 0, v[204:205]
	v_lshl_add_u64 v[2:3], v[2:3], 0, v[200:201]
	s_mov_b32 m0, s45
	v_lshl_add_u64 v[0:1], v[0:1], 0, v[206:207]
	s_add_i32 s93, s38, s80
	global_load_lds_dwordx4 v[2:3], off
	v_lshl_add_u64 v[0:1], v[0:1], 0, v[208:209]
	s_mov_b32 m0, s93
	v_lshl_add_u64 v[2:3], s[4:5], 0, v[188:189]
	global_load_lds_dwordx4 v[0:1], off
	v_mul_f32_e32 v0, 0x3fb8aa3b, v69
	v_exp_f32_e32 v179, v0
	v_lshl_add_u64 v[0:1], s[4:5], 0, v[184:185]
	v_lshl_add_u64 v[0:1], v[0:1], 0, v[160:161]
	v_lshl_add_u64 v[0:1], v[0:1], 0, v[156:157]
	v_lshl_add_u64 v[2:3], v[2:3], 0, v[190:191]
	v_lshl_add_u64 v[4:5], s[4:5], 0, v[196:197]
	v_lshlrev_b64 v[210:211], 10, v[182:183]
	v_lshl_add_u64 v[2:3], v[2:3], 0, v[192:193]
	v_lshl_add_u64 v[4:5], v[4:5], 0, v[198:199]
	v_lshl_add_u64 v[6:7], s[4:5], 0, v[204:205]
	v_lshl_add_u64 v[222:223], v[0:1], 0, v[210:211]
	v_lshlrev_b64 v[212:213], 10, v[186:187]
	v_lshlrev_b64 v[214:215], 10, v[194:195]
	v_bitop3_b32 v183, v68, 16, s39 bitop3:0x36
	v_add_u32_e32 v195, s68, v175
	ds_read_b64_tr_b16 v[0:1], v195 offset:0
	v_lshl_add_u64 v[4:5], v[4:5], 0, v[200:201]
	v_lshl_add_u64 v[6:7], v[6:7], 0, v[206:207]
	v_lshl_add_u64 v[224:225], v[2:3], 0, v[212:213]
	v_lshlrev_b64 v[216:217], 10, v[202:203]
	v_add_u32_e32 v203, s81, v183
	ds_read_b64_tr_b16 v[2:3], v203 offset:0
	v_lshl_add_u64 v[6:7], v[6:7], 0, v[208:209]
	v_lshl_add_u64 v[218:219], v[4:5], 0, v[214:215]
	ds_read_b64_tr_b16 v[4:5], v195 offset:0x200
	v_lshl_add_u64 v[220:221], v[6:7], 0, v[216:217]
	ds_read_b64_tr_b16 v[6:7], v203 offset:0x200
	ds_read_b64_tr_b16 v[32:33], v195 offset:0x400
	ds_read_b64_tr_b16 v[34:35], v203 offset:0x400
	ds_read_b64_tr_b16 v[48:49], v195 offset:0x600
	ds_read_b64_tr_b16 v[50:51], v203 offset:0x600
	s_waitcnt lgkmcnt(0)
; #define VM_WAIT() asm volatile("s_waitcnt vmcnt(0)" ::: "memory")
; template <int DK, int DV, bool MLSTM>
; __device__ __forceinline__ void out_unit2(LAS unsigned char* lds, LAS unsigned char* ldstab, const OutArgs a, const int wv) {
;     ...
; #pragma unroll
;     for (int kb = 0; kb < 4; ++kb) { LA_PK4(p[kb], 0, pa[2 * kb]); LA_PK4(p[kb], 8, pa[2 * kb + 1]); }
;     ...
; #pragma unroll
;     for (int pc = 0; pc < 4; ++pc) {
;         VM_WAIT(); __syncthreads();
;         OUT_DMA(pc + 1);
;         const bf16x8 af0 = pa[2 * pc], af1 = pa[2 * pc + 1];
;         OUT_MMA(pc & 1);
	v_permlane32_swap_b32_e32 v64, v66
	v_permlane32_swap_b32_e32 v65, v67
	v_permlane32_swap_b32_e32 v144, v146
	v_permlane32_swap_b32_e32 v140, v142
	v_permlane32_swap_b32_e32 v136, v138
	v_permlane32_swap_b32_e32 v132, v134
	v_add_u32_e32 v181, 0x100, v183
	v_mul_f32_e32 v235, 0x3fb8aa3b, v71
	v_permlane32_swap_b32_e32 v152, v154
	v_permlane32_swap_b32_e32 v153, v155
	v_permlane32_swap_b32_e32 v148, v150
	v_permlane32_swap_b32_e32 v149, v151
	v_permlane32_swap_b32_e32 v145, v147
	v_permlane32_swap_b32_e32 v141, v143
	v_permlane32_swap_b32_e32 v137, v139
	v_permlane32_swap_b32_e32 v133, v135
	v_permlane32_swap_b32_e32 v128, v130
	v_permlane32_swap_b32_e32 v129, v131
	ds_read_b64_tr_b16 v[68:69], v195 offset:0x1000
	ds_read_b64_tr_b16 v[70:71], v203 offset:0x1000
	ds_read_b64_tr_b16 v[72:73], v195 offset:0x1200
	v_mfma_f32_32x32x16_bf16 v[16:31], v[64:67], v[0:3], 0
	ds_read_b64_tr_b16 v[74:75], v203 offset:0x1200
	ds_read_b64_tr_b16 v[76:77], v195 offset:0x1400
	ds_read_b64_tr_b16 v[78:79], v203 offset:0x1400
	ds_read_b64_tr_b16 v[80:81], v195 offset:0x1600
	ds_read_b64_tr_b16 v[82:83], v203 offset:0x1600
	s_waitcnt lgkmcnt(0)
	v_mfma_f32_32x32x16_bf16 v[0:15], v[64:67], v[4:7], 0
	v_mfma_f32_32x32x16_bf16 v[32:47], v[64:67], v[32:35], 0
	v_mfma_f32_32x32x16_bf16 v[48:63], v[64:67], v[48:51], 0
	v_mfma_f32_32x32x16_bf16 v[16:31], v[152:155], v[68:71], v[16:31]
	v_add_u32_e32 v252, s70, v175
	ds_read_b64_tr_b16 v[68:69], v252 offset:0
	v_add_u32_e32 v253, s82, v183
	ds_read_b64_tr_b16 v[70:71], v253 offset:0
	v_mfma_f32_32x32x16_bf16 v[0:15], v[152:155], v[72:75], v[0:15]
	ds_read_b64_tr_b16 v[72:73], v252 offset:0x200
	ds_read_b64_tr_b16 v[74:75], v253 offset:0x200
	v_mfma_f32_32x32x16_bf16 v[32:47], v[152:155], v[76:79], v[32:47]
	ds_read_b64_tr_b16 v[76:77], v252 offset:0x400
	ds_read_b64_tr_b16 v[78:79], v253 offset:0x400
	ds_read_b64_tr_b16 v[236:237], v252 offset:0x600
	ds_read_b64_tr_b16 v[238:239], v253 offset:0x600
	s_waitcnt lgkmcnt(0)
	v_mfma_f32_32x32x16_bf16 v[48:63], v[152:155], v[80:83], v[48:63]
	v_mfma_f32_32x32x16_bf16 v[96:111], v[64:67], v[68:71], 0
	v_mfma_f32_32x32x16_bf16 v[112:127], v[64:67], v[72:75], 0
	v_mfma_f32_32x32x16_bf16 v[80:95], v[64:67], v[76:79], 0
	v_mfma_f32_32x32x16_bf16 v[64:79], v[64:67], v[236:239], 0
	ds_read_b64_tr_b16 v[236:237], v252 offset:0x1000
	ds_read_b64_tr_b16 v[238:239], v253 offset:0x1000
	ds_read_b64_tr_b16 v[240:241], v252 offset:0x1200
	ds_read_b64_tr_b16 v[242:243], v253 offset:0x1200
	ds_read_b64_tr_b16 v[244:245], v252 offset:0x1400
	ds_read_b64_tr_b16 v[246:247], v253 offset:0x1400
	ds_read_b64_tr_b16 v[248:249], v252 offset:0x1600
	ds_read_b64_tr_b16 v[250:251], v253 offset:0x1600
	s_waitcnt lgkmcnt(0)
	s_add_u32 s96, s37, 0xc1000
	s_addc_u32 s97, s16, 0
	v_mfma_f32_32x32x16_bf16 v[96:111], v[152:155], v[236:239], v[96:111]
	v_mov_b64_e32 v[236:237], s[96:97]
	v_mad_i64_i32 v[238:239], s[96:97], v182, s57, v[236:237]
	v_lshl_add_u64 v[238:239], v[238:239], 0, v[184:185]
	v_lshl_add_u64 v[238:239], v[238:239], 0, v[160:161]
	s_mov_b32 m0, s40
	v_lshl_add_u64 v[238:239], v[238:239], 0, v[156:157]
	s_waitcnt vmcnt(0)
	s_waitcnt vmcnt(0) lgkmcnt(0)
	s_barrier
	global_load_lds_dwordx4 v[238:239], off
	v_mad_i64_i32 v[238:239], s[96:97], v186, s57, v[236:237]
	v_lshl_add_u64 v[238:239], v[238:239], 0, v[188:189]
	v_lshl_add_u64 v[238:239], v[238:239], 0, v[190:191]
	v_lshl_add_u64 v[238:239], v[238:239], 0, v[192:193]
	s_mov_b32 m0, s41
	v_mfma_f32_32x32x16_bf16 v[112:127], v[152:155], v[240:243], v[112:127]
	global_load_lds_dwordx4 v[238:239], off
	v_mad_i64_i32 v[238:239], s[96:97], v194, s57, v[236:237]
	v_lshl_add_u64 v[238:239], v[238:239], 0, v[196:197]
	v_mad_i64_i32 v[236:237], s[96:97], v202, s57, v[236:237]
	v_lshl_add_u64 v[238:239], v[238:239], 0, v[198:199]
	v_lshl_add_u64 v[236:237], v[236:237], 0, v[204:205]
	v_lshl_add_u64 v[238:239], v[238:239], 0, v[200:201]
	s_mov_b32 m0, s42
	v_lshl_add_u64 v[236:237], v[236:237], 0, v[206:207]
	global_load_lds_dwordx4 v[238:239], off
	v_lshl_add_u64 v[236:237], v[236:237], 0, v[208:209]
	s_mov_b32 m0, s43
	v_mfma_f32_32x32x16_bf16 v[80:95], v[152:155], v[244:247], v[80:95]
	global_load_lds_dwordx4 v[236:237], off
	v_add_u32_e32 v254, s80, v175
	v_add_u32_e32 v255, s83, v183
	v_mfma_f32_32x32x16_bf16 v[64:79], v[152:155], v[248:251], v[64:79]
	ds_read_b64_tr_b16 v[152:153], v254 offset:0
	ds_read_b64_tr_b16 v[154:155], v255 offset:0
	ds_read_b64_tr_b16 v[236:237], v254 offset:0x200
	ds_read_b64_tr_b16 v[238:239], v255 offset:0x200
	ds_read_b64_tr_b16 v[240:241], v254 offset:0x400
	ds_read_b64_tr_b16 v[242:243], v255 offset:0x400
	ds_read_b64_tr_b16 v[244:245], v254 offset:0x600
	ds_read_b64_tr_b16 v[246:247], v255 offset:0x600
	s_waitcnt lgkmcnt(0)
	s_nop 0
	v_mfma_f32_32x32x16_bf16 v[16:31], v[148:151], v[152:155], v[16:31]
	ds_read_b64_tr_b16 v[152:153], v254 offset:0x1000
	ds_read_b64_tr_b16 v[154:155], v255 offset:0x1000
	v_mfma_f32_32x32x16_bf16 v[0:15], v[148:151], v[236:239], v[0:15]
	ds_read_b64_tr_b16 v[236:237], v254 offset:0x1200
	ds_read_b64_tr_b16 v[238:239], v255 offset:0x1200
	v_mfma_f32_32x32x16_bf16 v[32:47], v[148:151], v[240:243], v[32:47]
	ds_read_b64_tr_b16 v[240:241], v254 offset:0x1400
	ds_read_b64_tr_b16 v[242:243], v255 offset:0x1400
	ds_read_b64_tr_b16 v[248:249], v254 offset:0x1600
	ds_read_b64_tr_b16 v[250:251], v255 offset:0x1600
	s_waitcnt lgkmcnt(0)
; #define VM_WAIT() asm volatile("s_waitcnt vmcnt(0)" ::: "memory")
; template <int DK, int DV, bool MLSTM>
; __device__ __forceinline__ void out_unit2(LAS unsigned char* lds, LAS unsigned char* ldstab, const OutArgs a, const int wv) {
;     ...
; #pragma unroll
;     for (int pc = 0; pc < 4; ++pc) {
;         VM_WAIT(); __syncthreads();
;         OUT_DMA(pc + 1);
;         const bf16x8 af0 = pa[2 * pc], af1 = pa[2 * pc + 1];
;         OUT_MMA(pc & 1);
	v_mfma_f32_32x32x16_bf16 v[48:63], v[148:151], v[244:247], v[48:63]
	v_mfma_f32_32x32x16_bf16 v[16:31], v[144:147], v[152:155], v[16:31]
	v_add_u32_e32 v226, s84, v175
	ds_read_b64_tr_b16 v[152:153], v226 offset:0
	v_add_u32_e32 v227, s85, v183
	ds_read_b64_tr_b16 v[154:155], v227 offset:0
	v_mfma_f32_32x32x16_bf16 v[0:15], v[144:147], v[236:239], v[0:15]
	ds_read_b64_tr_b16 v[236:237], v226 offset:0x200
	ds_read_b64_tr_b16 v[238:239], v227 offset:0x200
	v_mfma_f32_32x32x16_bf16 v[32:47], v[144:147], v[240:243], v[32:47]
	ds_read_b64_tr_b16 v[240:241], v226 offset:0x400
	ds_read_b64_tr_b16 v[242:243], v227 offset:0x400
	ds_read_b64_tr_b16 v[244:245], v226 offset:0x600
	ds_read_b64_tr_b16 v[246:247], v227 offset:0x600
	s_waitcnt lgkmcnt(0)
	v_mfma_f32_32x32x16_bf16 v[48:63], v[144:147], v[248:251], v[48:63]
	v_mfma_f32_32x32x16_bf16 v[96:111], v[148:151], v[152:155], v[96:111]
	ds_read_b64_tr_b16 v[152:153], v226 offset:0x1000
	ds_read_b64_tr_b16 v[154:155], v227 offset:0x1000
	v_mfma_f32_32x32x16_bf16 v[112:127], v[148:151], v[236:239], v[112:127]
	ds_read_b64_tr_b16 v[236:237], v226 offset:0x1200
	ds_read_b64_tr_b16 v[238:239], v227 offset:0x1200
	v_mfma_f32_32x32x16_bf16 v[80:95], v[148:151], v[240:243], v[80:95]
	ds_read_b64_tr_b16 v[240:241], v226 offset:0x1400
	ds_read_b64_tr_b16 v[242:243], v227 offset:0x1400
	ds_read_b64_tr_b16 v[248:249], v226 offset:0x1600
	ds_read_b64_tr_b16 v[250:251], v227 offset:0x1600
	s_waitcnt lgkmcnt(0)
	v_mfma_f32_32x32x16_bf16 v[64:79], v[148:151], v[244:247], v[64:79]
	s_mov_b32 m0, s94
	s_add_u32 s94, s37, 0x121000
	s_addc_u32 s95, s16, 0
	v_mov_b64_e32 v[148:149], s[94:95]
	v_mad_i64_i32 v[150:151], s[94:95], v182, s57, v[148:149]
	v_lshl_add_u64 v[150:151], v[150:151], 0, v[184:185]
	v_lshl_add_u64 v[150:151], v[150:151], 0, v[160:161]
	v_lshl_add_u64 v[150:151], v[150:151], 0, v[156:157]
	s_waitcnt vmcnt(0)
	s_waitcnt vmcnt(0) lgkmcnt(0)
	s_barrier
	global_load_lds_dwordx4 v[150:151], off
	v_mad_i64_i32 v[150:151], s[94:95], v186, s57, v[148:149]
	v_lshl_add_u64 v[150:151], v[150:151], 0, v[188:189]
	v_lshl_add_u64 v[150:151], v[150:151], 0, v[190:191]
	v_lshl_add_u64 v[150:151], v[150:151], 0, v[192:193]
	s_mov_b32 m0, s44
	v_mfma_f32_32x32x16_bf16 v[96:111], v[144:147], v[152:155], v[96:111]
	global_load_lds_dwordx4 v[150:151], off
	v_mad_i64_i32 v[150:151], s[94:95], v194, s57, v[148:149]
	v_lshl_add_u64 v[150:151], v[150:151], 0, v[196:197]
	s_mov_b32 m0, s45
	v_mad_i64_i32 v[148:149], s[44:45], v202, s57, v[148:149]
	v_lshl_add_u64 v[150:151], v[150:151], 0, v[198:199]
	v_lshl_add_u64 v[148:149], v[148:149], 0, v[204:205]
	v_lshl_add_u64 v[150:151], v[150:151], 0, v[200:201]
	v_lshl_add_u64 v[148:149], v[148:149], 0, v[206:207]
	global_load_lds_dwordx4 v[150:151], off
	v_lshl_add_u64 v[148:149], v[148:149], 0, v[208:209]
	s_mov_b32 m0, s93
	v_mfma_f32_32x32x16_bf16 v[112:127], v[144:147], v[236:239], v[112:127]
	global_load_lds_dwordx4 v[148:149], off
	v_mfma_f32_32x32x16_bf16 v[80:95], v[144:147], v[240:243], v[80:95]
	v_mfma_f32_32x32x16_bf16 v[64:79], v[144:147], v[248:251], v[64:79]
	ds_read_b64_tr_b16 v[144:145], v195 offset:0
	ds_read_b64_tr_b16 v[146:147], v203 offset:0
	ds_read_b64_tr_b16 v[148:149], v195 offset:0x200
	ds_read_b64_tr_b16 v[150:151], v203 offset:0x200
	ds_read_b64_tr_b16 v[152:153], v195 offset:0x400
	ds_read_b64_tr_b16 v[154:155], v203 offset:0x400
	ds_read_b64_tr_b16 v[182:183], v195 offset:0x600
	ds_read_b64_tr_b16 v[184:185], v203 offset:0x600
	s_waitcnt lgkmcnt(0)
	s_nop 0
	v_mfma_f32_32x32x16_bf16 v[16:31], v[140:143], v[144:147], v[16:31]
	ds_read_b64_tr_b16 v[144:145], v195 offset:0x1000
	ds_read_b64_tr_b16 v[146:147], v203 offset:0x1000
	v_mfma_f32_32x32x16_bf16 v[0:15], v[140:143], v[148:151], v[0:15]
	ds_read_b64_tr_b16 v[148:149], v195 offset:0x1200
	ds_read_b64_tr_b16 v[150:151], v203 offset:0x1200
	v_mfma_f32_32x32x16_bf16 v[32:47], v[140:143], v[152:155], v[32:47]
	ds_read_b64_tr_b16 v[152:153], v195 offset:0x1400
	ds_read_b64_tr_b16 v[154:155], v203 offset:0x1400
	ds_read_b64_tr_b16 v[186:187], v195 offset:0x1600
	ds_read_b64_tr_b16 v[188:189], v203 offset:0x1600
	s_waitcnt lgkmcnt(0)
	v_mfma_f32_32x32x16_bf16 v[48:63], v[140:143], v[182:185], v[48:63]
	v_mfma_f32_32x32x16_bf16 v[16:31], v[136:139], v[144:147], v[16:31]
	ds_read_b64_tr_b16 v[144:145], v252 offset:0
	ds_read_b64_tr_b16 v[146:147], v253 offset:0
	v_mfma_f32_32x32x16_bf16 v[0:15], v[136:139], v[148:151], v[0:15]
	ds_read_b64_tr_b16 v[148:149], v252 offset:0x200
	ds_read_b64_tr_b16 v[150:151], v253 offset:0x200
	v_mfma_f32_32x32x16_bf16 v[32:47], v[136:139], v[152:155], v[32:47]
	ds_read_b64_tr_b16 v[152:153], v252 offset:0x400
	ds_read_b64_tr_b16 v[154:155], v253 offset:0x400
	ds_read_b64_tr_b16 v[182:183], v252 offset:0x600
	ds_read_b64_tr_b16 v[184:185], v253 offset:0x600
	s_waitcnt lgkmcnt(0)
	v_mfma_f32_32x32x16_bf16 v[48:63], v[136:139], v[186:189], v[48:63]
	v_mfma_f32_32x32x16_bf16 v[96:111], v[140:143], v[144:147], v[96:111]
	ds_read_b64_tr_b16 v[144:145], v252 offset:0x1000
	ds_read_b64_tr_b16 v[146:147], v253 offset:0x1000
	v_mfma_f32_32x32x16_bf16 v[112:127], v[140:143], v[148:151], v[112:127]
	ds_read_b64_tr_b16 v[148:149], v252 offset:0x1200
	ds_read_b64_tr_b16 v[150:151], v253 offset:0x1200
	v_mfma_f32_32x32x16_bf16 v[80:95], v[140:143], v[152:155], v[80:95]
	ds_read_b64_tr_b16 v[152:153], v252 offset:0x1400
	ds_read_b64_tr_b16 v[154:155], v253 offset:0x1400
	ds_read_b64_tr_b16 v[186:187], v252 offset:0x1600
	ds_read_b64_tr_b16 v[188:189], v253 offset:0x1600
	s_waitcnt lgkmcnt(0)
	v_mfma_f32_32x32x16_bf16 v[64:79], v[140:143], v[182:185], v[64:79]
	s_mov_b32 m0, s40
	s_waitcnt vmcnt(0)
	s_waitcnt vmcnt(0) lgkmcnt(0)
	s_barrier
; #define VM_WAIT() asm volatile("s_waitcnt vmcnt(0)" ::: "memory")
; template <int DK, int DV, bool MLSTM>
; __device__ __forceinline__ void out_unit2(LAS unsigned char* lds, LAS unsigned char* ldstab, const OutArgs a, const int wv) {
;     ...
; #pragma unroll
;     for (int pc = 0; pc < 4; ++pc) {
;         VM_WAIT(); __syncthreads();
;         OUT_DMA(pc + 1);
;         const bf16x8 af0 = pa[2 * pc], af1 = pa[2 * pc + 1];
;         OUT_MMA(pc & 1);
;     }
; #pragma unroll 1
;     for (int pc = 4; pc < 4 + 2 * NCP; ++pc) {
;         VM_WAIT(); __syncthreads();
;         if (pc + 1 < 4 + 2 * NCP) OUT_DMA(pc + 1);
;         const int cq = pc - 4, dirb = cq >= NCP, cp = dirb ? cq - NCP : cq;
;         const float qs = dirb ? qsb : qsf;
;         const unsigned qa = QP + (cp >> 2) * 32768u + 512u * (cp & 3) + 8192u * rb;
;         const bf16x8 af0 = scale_frag(lds_r128(qa + rb0), qs), af1 = scale_frag(lds_r128(qa + rb1), qs);
	global_load_lds_dwordx4 v[222:223], off
	s_mov_b32 m0, s41
	v_mfma_f32_32x32x16_bf16 v[96:111], v[136:139], v[144:147], v[96:111]
	global_load_lds_dwordx4 v[224:225], off
	s_mov_b32 m0, s42
	s_nop 0
	global_load_lds_dwordx4 v[218:219], off
	s_mov_b32 m0, s43
	v_mfma_f32_32x32x16_bf16 v[112:127], v[136:139], v[148:151], v[112:127]
	global_load_lds_dwordx4 v[220:221], off
	ds_read_b64_tr_b16 v[140:141], v254 offset:0
	ds_read_b64_tr_b16 v[142:143], v255 offset:0
	ds_read_b64_tr_b16 v[144:145], v254 offset:0x200
	ds_read_b64_tr_b16 v[146:147], v255 offset:0x200
	ds_read_b64_tr_b16 v[148:149], v254 offset:0x400
	v_mfma_f32_32x32x16_bf16 v[80:95], v[136:139], v[152:155], v[80:95]
	ds_read_b64_tr_b16 v[150:151], v255 offset:0x400
	ds_read_b64_tr_b16 v[152:153], v254 offset:0x600
	ds_read_b64_tr_b16 v[154:155], v255 offset:0x600
	s_waitcnt lgkmcnt(0)
	v_mfma_f32_32x32x16_bf16 v[64:79], v[136:139], v[186:189], v[64:79]
	ds_read_b64_tr_b16 v[136:137], v254 offset:0x1000
	ds_read_b64_tr_b16 v[138:139], v255 offset:0x1000
	v_mfma_f32_32x32x16_bf16 v[16:31], v[132:135], v[140:143], v[16:31]
	ds_read_b64_tr_b16 v[140:141], v254 offset:0x1200
	ds_read_b64_tr_b16 v[142:143], v255 offset:0x1200
	v_mfma_f32_32x32x16_bf16 v[0:15], v[132:135], v[144:147], v[0:15]
	ds_read_b64_tr_b16 v[144:145], v254 offset:0x1400
	ds_read_b64_tr_b16 v[146:147], v255 offset:0x1400
	v_mfma_f32_32x32x16_bf16 v[32:47], v[132:135], v[148:151], v[32:47]
	ds_read_b64_tr_b16 v[148:149], v254 offset:0x1600
	ds_read_b64_tr_b16 v[150:151], v255 offset:0x1600
	s_waitcnt lgkmcnt(0)
	v_mfma_f32_32x32x16_bf16 v[48:63], v[132:135], v[152:155], v[48:63]
	v_mfma_f32_32x32x16_bf16 v[16:31], v[128:131], v[136:139], v[16:31]
	ds_read_b64_tr_b16 v[136:137], v226 offset:0
	ds_read_b64_tr_b16 v[138:139], v227 offset:0
	v_mfma_f32_32x32x16_bf16 v[0:15], v[128:131], v[140:143], v[0:15]
	ds_read_b64_tr_b16 v[140:141], v226 offset:0x200
	ds_read_b64_tr_b16 v[142:143], v227 offset:0x200
	v_mfma_f32_32x32x16_bf16 v[32:47], v[128:131], v[144:147], v[32:47]
	ds_read_b64_tr_b16 v[144:145], v226 offset:0x400
	ds_read_b64_tr_b16 v[146:147], v227 offset:0x400
	ds_read_b64_tr_b16 v[152:153], v226 offset:0x600
	ds_read_b64_tr_b16 v[154:155], v227 offset:0x600
	s_waitcnt lgkmcnt(0)
	v_mfma_f32_32x32x16_bf16 v[48:63], v[128:131], v[148:151], v[48:63]
	v_mfma_f32_32x32x16_bf16 v[96:111], v[132:135], v[136:139], v[96:111]
	ds_read_b64_tr_b16 v[136:137], v226 offset:0x1000
	ds_read_b64_tr_b16 v[138:139], v227 offset:0x1000
	v_mfma_f32_32x32x16_bf16 v[112:127], v[132:135], v[140:143], v[112:127]
	ds_read_b64_tr_b16 v[140:141], v226 offset:0x1200
	ds_read_b64_tr_b16 v[142:143], v227 offset:0x1200
	v_mfma_f32_32x32x16_bf16 v[80:95], v[132:135], v[144:147], v[80:95]
	ds_read_b64_tr_b16 v[146:147], v226 offset:0x1400
	ds_read_b64_tr_b16 v[148:149], v227 offset:0x1400
	ds_read_b64_tr_b16 v[182:183], v226 offset:0x1600
	ds_read_b64_tr_b16 v[184:185], v227 offset:0x1600
	s_waitcnt lgkmcnt(0)
	v_mfma_f32_32x32x16_bf16 v[64:79], v[132:135], v[152:155], v[64:79]
	v_mfma_f32_32x32x16_bf16 v[96:111], v[128:131], v[136:139], v[96:111]
	v_add_u32_e32 v226, s13, v173
	v_add_u32_e32 v227, s13, v177
	ds_read_b128 v[236:239], v226 offset:0
	ds_read_b128 v[240:243], v227 offset:0
	ds_read_b128 v[244:247], v226 offset:512
	ds_read_b128 v[248:251], v227 offset:512
	ds_read_b128 v[252:255], v226 offset:1024
	ds_read_b128 v[218:221], v227 offset:1024
	ds_read_b128 v[222:225], v226 offset:1536
	ds_read_b128 v[206:209], v227 offset:1536
	v_exp_f32_e32 v144, v235
	s_mov_b32 s37, 0x28000
	s_movk_i32 s39, 0x800
	v_lshlrev_b32_e32 v160, 1, v162
	v_lshlrev_b32_e32 v132, 1, v170
	v_lshlrev_b32_e32 v134, 1, v172
	v_lshlrev_b32_e32 v136, 1, v174
	v_mfma_f32_32x32x16_bf16 v[112:127], v[128:131], v[140:143], v[112:127]
	v_lshlrev_b32_e32 v138, 1, v176
	v_lshlrev_b32_e32 v140, 1, v178
	v_lshlrev_b32_e32 v142, 1, v180
	v_mfma_f32_32x32x16_bf16 v[80:95], v[128:131], v[146:149], v[80:95]
	v_mfma_f32_32x32x16_bf16 v[64:79], v[128:131], v[182:185], v[64:79]
	v_lshl_add_u64 v[198:199], v[158:159], 1, v[210:211]
	v_lshl_add_u64 v[198:199], v[198:199], 0, v[160:161]
	v_mov_b32_e32 v157, v161
	v_lshl_add_u64 v[198:199], v[198:199], 0, v[156:157]
	v_mov_b32_e32 v133, v161
	v_mov_b32_e32 v135, v161
	v_lshl_add_u64 v[200:201], v[164:165], 1, v[212:213]
	v_lshl_add_u64 v[200:201], v[200:201], 0, v[132:133]
	v_lshl_add_u64 v[200:201], v[200:201], 0, v[134:135]
	v_mov_b32_e32 v137, v161
	v_mov_b32_e32 v139, v161
	v_lshl_add_u64 v[202:203], v[166:167], 1, v[214:215]
	v_lshl_add_u64 v[202:203], v[202:203], 0, v[136:137]
	v_lshl_add_u64 v[202:203], v[202:203], 0, v[138:139]
	v_mov_b32_e32 v141, v161
	v_mov_b32_e32 v143, v161
	v_lshl_add_u64 v[204:205], v[168:169], 1, v[216:217]
	v_lshl_add_u64 v[204:205], v[204:205], 0, v[140:141]
	v_lshl_add_u64 v[204:205], v[204:205], 0, v[142:143]
	s_waitcnt vmcnt(0) lgkmcnt(0)
	s_barrier
; #define VM_WAIT() asm volatile("s_waitcnt vmcnt(0)" ::: "memory")
; template <int DK, int DV, bool MLSTM>
; __device__ __forceinline__ void out_unit2(LAS unsigned char* lds, LAS unsigned char* ldstab, const OutArgs a, const int wv) {
;     ...
; #pragma unroll 1
;     for (int pc = 4; pc < 4 + 2 * NCP; ++pc) {
;         VM_WAIT(); __syncthreads();
;         if (pc + 1 < 4 + 2 * NCP) OUT_DMA(pc + 1);
;         const int cq = pc - 4, dirb = cq >= NCP, cp = dirb ? cq - NCP : cq;
;         const float qs = dirb ? qsb : qsf;
;         const unsigned qa = QP + (cp >> 2) * 32768u + 512u * (cp & 3) + 8192u * rb;
;         const bf16x8 af0 = scale_frag(lds_r128(qa + rb0), qs), af1 = scale_frag(lds_r128(qa + rb1), qs);
;         OUT_MMA(pc & 1);
	s_add_u32 s40, s4, 0x8000
	s_addc_u32 s41, s5, 0
	v_lshl_add_u64 v[128:129], s[40:41], 0, v[198:199]
	v_lshl_add_u64 v[130:131], s[40:41], 0, v[200:201]
	v_lshl_add_u64 v[146:147], s[40:41], 0, v[202:203]
	v_lshl_add_u64 v[148:149], s[40:41], 0, v[204:205]
	s_add_i32 m0, s6, 0x18000
	s_nop 0
	global_load_lds_dwordx4 v[128:129], off
	s_add_i32 m0, s7, 0x18000
	s_nop 0
	global_load_lds_dwordx4 v[130:131], off
	s_add_i32 m0, s36, 0x18000
	s_nop 0
	global_load_lds_dwordx4 v[146:147], off
	s_add_i32 m0, s38, 0x18000
	s_nop 0
	global_load_lds_dwordx4 v[148:149], off
	s_add_u32 s40, s4, 0x10000
	s_addc_u32 s41, s5, 0
	v_lshl_add_u64 v[128:129], s[40:41], 0, v[198:199]
	v_lshl_add_u64 v[130:131], s[40:41], 0, v[200:201]
	v_lshl_add_u64 v[146:147], s[40:41], 0, v[202:203]
	v_lshl_add_u64 v[148:149], s[40:41], 0, v[204:205]
	s_mov_b32 m0, s6
	s_nop 0
	global_load_lds_dwordx4 v[128:129], off
	s_mov_b32 m0, s7
	s_nop 0
	global_load_lds_dwordx4 v[130:131], off
	s_mov_b32 m0, s36
	s_nop 0
	global_load_lds_dwordx4 v[146:147], off
	s_mov_b32 m0, s38
	s_nop 0
	global_load_lds_dwordx4 v[148:149], off
	v_lshlrev_b32_e32 v135, 16, v236
	v_and_b32_e32 v137, 0xffff0000, v236
	v_mul_f32_e32 v135, v179, v135
	v_mul_f32_e32 v137, v179, v137
	v_cvt_pk_bf16_f32 v128, v135, v137
	v_lshlrev_b32_e32 v135, 16, v237
	v_and_b32_e32 v137, 0xffff0000, v237
	v_mul_f32_e32 v135, v179, v135
	v_mul_f32_e32 v137, v179, v137
	v_cvt_pk_bf16_f32 v129, v135, v137
	v_lshlrev_b32_e32 v135, 16, v238
	v_and_b32_e32 v137, 0xffff0000, v238
	v_mul_f32_e32 v135, v179, v135
	v_mul_f32_e32 v137, v179, v137
	v_cvt_pk_bf16_f32 v130, v135, v137
	v_lshlrev_b32_e32 v135, 16, v239
	v_and_b32_e32 v137, 0xffff0000, v239
	v_mul_f32_e32 v135, v179, v135
	v_mul_f32_e32 v137, v179, v137
	v_cvt_pk_bf16_f32 v131, v135, v137
	v_lshlrev_b32_e32 v135, 16, v240
	v_and_b32_e32 v137, 0xffff0000, v240
	v_mul_f32_e32 v135, v179, v135
	v_mul_f32_e32 v137, v179, v137
	v_cvt_pk_bf16_f32 v146, v135, v137
	v_lshlrev_b32_e32 v135, 16, v241
	v_and_b32_e32 v137, 0xffff0000, v241
	v_mul_f32_e32 v135, v179, v135
	v_mul_f32_e32 v137, v179, v137
	v_cvt_pk_bf16_f32 v147, v135, v137
	v_lshlrev_b32_e32 v135, 16, v242
	v_and_b32_e32 v137, 0xffff0000, v242
	v_mul_f32_e32 v135, v179, v135
	v_mul_f32_e32 v137, v179, v137
	v_cvt_pk_bf16_f32 v148, v135, v137
	v_lshlrev_b32_e32 v135, 16, v243
	v_and_b32_e32 v137, 0xffff0000, v243
	v_mul_f32_e32 v135, v179, v135
	v_mul_f32_e32 v137, v179, v137
	v_cvt_pk_bf16_f32 v149, v135, v137
	v_add_u32_e32 v133, 0x10000, v175
	ds_read_b64_tr_b16 v[150:151], v133 offset:0
	v_add_u32_e32 v135, 0x10000, v181
	ds_read_b64_tr_b16 v[152:153], v135 offset:0
	ds_read_b64_tr_b16 v[182:183], v133 offset:0x200
	ds_read_b64_tr_b16 v[184:185], v135 offset:0x200
	ds_read_b64_tr_b16 v[186:187], v133 offset:0x400
	ds_read_b64_tr_b16 v[188:189], v135 offset:0x400
	ds_read_b64_tr_b16 v[190:191], v133 offset:0x600
	ds_read_b64_tr_b16 v[192:193], v135 offset:0x600
	s_waitcnt lgkmcnt(0)
	s_nop 0
	v_mfma_f32_32x32x16_bf16 v[16:31], v[128:131], v[150:153], v[16:31]
	ds_read_b64_tr_b16 v[150:151], v133 offset:0x1000
	ds_read_b64_tr_b16 v[152:153], v135 offset:0x1000
	v_mfma_f32_32x32x16_bf16 v[0:15], v[128:131], v[182:185], v[0:15]
	ds_read_b64_tr_b16 v[182:183], v133 offset:0x1200
	ds_read_b64_tr_b16 v[184:185], v135 offset:0x1200
	v_mfma_f32_32x32x16_bf16 v[32:47], v[128:131], v[186:189], v[32:47]
	ds_read_b64_tr_b16 v[186:187], v133 offset:0x1400
	ds_read_b64_tr_b16 v[188:189], v135 offset:0x1400
	ds_read_b64_tr_b16 v[194:195], v133 offset:0x1600
	ds_read_b64_tr_b16 v[196:197], v135 offset:0x1600
	s_waitcnt lgkmcnt(0)
	v_mfma_f32_32x32x16_bf16 v[48:63], v[128:131], v[190:193], v[48:63]
	v_mfma_f32_32x32x16_bf16 v[16:31], v[146:149], v[150:153], v[16:31]
	v_add_u32_e32 v133, 0x2000, v133
	ds_read_b64_tr_b16 v[150:151], v133 offset:0
	v_add_u32_e32 v135, 0x2000, v135
	ds_read_b64_tr_b16 v[152:153], v135 offset:0
	v_mfma_f32_32x32x16_bf16 v[0:15], v[146:149], v[182:185], v[0:15]
	ds_read_b64_tr_b16 v[182:183], v133 offset:0x200
	ds_read_b64_tr_b16 v[184:185], v135 offset:0x200
	v_mfma_f32_32x32x16_bf16 v[32:47], v[146:149], v[186:189], v[32:47]
	ds_read_b64_tr_b16 v[186:187], v133 offset:0x400
	ds_read_b64_tr_b16 v[188:189], v135 offset:0x400
	ds_read_b64_tr_b16 v[190:191], v133 offset:0x600
	ds_read_b64_tr_b16 v[192:193], v135 offset:0x600
	s_waitcnt lgkmcnt(0)
	v_mfma_f32_32x32x16_bf16 v[48:63], v[146:149], v[194:197], v[48:63]
	v_mfma_f32_32x32x16_bf16 v[96:111], v[128:131], v[150:153], v[96:111]
	ds_read_b64_tr_b16 v[150:151], v133 offset:0x1000
	ds_read_b64_tr_b16 v[152:153], v135 offset:0x1000
	v_mfma_f32_32x32x16_bf16 v[112:127], v[128:131], v[182:185], v[112:127]
	ds_read_b64_tr_b16 v[182:183], v133 offset:0x1200
	ds_read_b64_tr_b16 v[184:185], v135 offset:0x1200
	v_mfma_f32_32x32x16_bf16 v[80:95], v[128:131], v[186:189], v[80:95]
	ds_read_b64_tr_b16 v[186:187], v133 offset:0x1400
	ds_read_b64_tr_b16 v[188:189], v135 offset:0x1400
	ds_read_b64_tr_b16 v[194:195], v133 offset:0x1600
	ds_read_b64_tr_b16 v[196:197], v135 offset:0x1600
	s_waitcnt lgkmcnt(0)
	v_mfma_f32_32x32x16_bf16 v[64:79], v[128:131], v[190:193], v[64:79]
	v_mfma_f32_32x32x16_bf16 v[96:111], v[146:149], v[150:153], v[96:111]
	v_mfma_f32_32x32x16_bf16 v[112:127], v[146:149], v[182:185], v[112:127]
	v_mfma_f32_32x32x16_bf16 v[80:95], v[146:149], v[186:189], v[80:95]
	v_mfma_f32_32x32x16_bf16 v[64:79], v[146:149], v[194:197], v[64:79]
	s_waitcnt vmcnt(4) lgkmcnt(0)
	s_barrier
; #define VM_WAIT() asm volatile("s_waitcnt vmcnt(0)" ::: "memory")
; template <int DK, int DV, bool MLSTM>
; __device__ __forceinline__ void out_unit2(LAS unsigned char* lds, LAS unsigned char* ldstab, const OutArgs a, const int wv) {
;     ...
; #pragma unroll 1
;     for (int pc = 4; pc < 4 + 2 * NCP; ++pc) {
;         VM_WAIT(); __syncthreads();
;         if (pc + 1 < 4 + 2 * NCP) OUT_DMA(pc + 1);
;         const int cq = pc - 4, dirb = cq >= NCP, cp = dirb ? cq - NCP : cq;
;         const float qs = dirb ? qsb : qsf;
;         const unsigned qa = QP + (cp >> 2) * 32768u + 512u * (cp & 3) + 8192u * rb;
;         const bf16x8 af0 = scale_frag(lds_r128(qa + rb0), qs), af1 = scale_frag(lds_r128(qa + rb1), qs);
;         OUT_MMA(pc & 1);
	s_add_u32 s40, s4, 0x18000
	s_addc_u32 s41, s5, 0
	v_lshl_add_u64 v[128:129], s[40:41], 0, v[198:199]
	v_lshl_add_u64 v[130:131], s[40:41], 0, v[200:201]
	v_lshl_add_u64 v[146:147], s[40:41], 0, v[202:203]
	v_lshl_add_u64 v[148:149], s[40:41], 0, v[204:205]
	s_add_i32 m0, s6, 0x10000
	s_nop 0
	global_load_lds_dwordx4 v[128:129], off
	s_add_i32 m0, s7, 0x10000
	s_nop 0
	global_load_lds_dwordx4 v[130:131], off
	s_add_i32 m0, s36, 0x10000
	s_nop 0
	global_load_lds_dwordx4 v[146:147], off
	s_add_i32 m0, s38, 0x10000
	s_nop 0
	global_load_lds_dwordx4 v[148:149], off
	v_lshlrev_b32_e32 v135, 16, v244
	v_and_b32_e32 v137, 0xffff0000, v244
	v_mul_f32_e32 v135, v179, v135
	v_mul_f32_e32 v137, v179, v137
	v_cvt_pk_bf16_f32 v128, v135, v137
	v_lshlrev_b32_e32 v135, 16, v245
	v_and_b32_e32 v137, 0xffff0000, v245
	v_mul_f32_e32 v135, v179, v135
	v_mul_f32_e32 v137, v179, v137
	v_cvt_pk_bf16_f32 v129, v135, v137
	v_lshlrev_b32_e32 v135, 16, v246
	v_and_b32_e32 v137, 0xffff0000, v246
	v_mul_f32_e32 v135, v179, v135
	v_mul_f32_e32 v137, v179, v137
	v_cvt_pk_bf16_f32 v130, v135, v137
	v_lshlrev_b32_e32 v135, 16, v247
	v_and_b32_e32 v137, 0xffff0000, v247
	v_mul_f32_e32 v135, v179, v135
	v_mul_f32_e32 v137, v179, v137
	v_cvt_pk_bf16_f32 v131, v135, v137
	v_lshlrev_b32_e32 v135, 16, v248
	v_and_b32_e32 v137, 0xffff0000, v248
	v_mul_f32_e32 v135, v179, v135
	v_mul_f32_e32 v137, v179, v137
	v_cvt_pk_bf16_f32 v146, v135, v137
	v_lshlrev_b32_e32 v135, 16, v249
	v_and_b32_e32 v137, 0xffff0000, v249
	v_mul_f32_e32 v135, v179, v135
	v_mul_f32_e32 v137, v179, v137
	v_cvt_pk_bf16_f32 v147, v135, v137
	v_lshlrev_b32_e32 v135, 16, v250
	v_and_b32_e32 v137, 0xffff0000, v250
	v_mul_f32_e32 v135, v179, v135
	v_mul_f32_e32 v137, v179, v137
	v_cvt_pk_bf16_f32 v148, v135, v137
	v_lshlrev_b32_e32 v135, 16, v251
	v_and_b32_e32 v137, 0xffff0000, v251
	v_mul_f32_e32 v135, v179, v135
	v_mul_f32_e32 v137, v179, v137
	v_cvt_pk_bf16_f32 v149, v135, v137
	v_add_u32_e32 v133, 0x18000, v175
	ds_read_b64_tr_b16 v[150:151], v133 offset:0
	v_add_u32_e32 v135, 0x18000, v181
	ds_read_b64_tr_b16 v[152:153], v135 offset:0
	ds_read_b64_tr_b16 v[182:183], v133 offset:0x200
	ds_read_b64_tr_b16 v[184:185], v135 offset:0x200
	ds_read_b64_tr_b16 v[186:187], v133 offset:0x400
	ds_read_b64_tr_b16 v[188:189], v135 offset:0x400
	ds_read_b64_tr_b16 v[190:191], v133 offset:0x600
	ds_read_b64_tr_b16 v[192:193], v135 offset:0x600
	s_waitcnt lgkmcnt(0)
	s_nop 0
	v_mfma_f32_32x32x16_bf16 v[16:31], v[128:131], v[150:153], v[16:31]
	ds_read_b64_tr_b16 v[150:151], v133 offset:0x1000
	ds_read_b64_tr_b16 v[152:153], v135 offset:0x1000
	v_mfma_f32_32x32x16_bf16 v[0:15], v[128:131], v[182:185], v[0:15]
	ds_read_b64_tr_b16 v[182:183], v133 offset:0x1200
	ds_read_b64_tr_b16 v[184:185], v135 offset:0x1200
	v_mfma_f32_32x32x16_bf16 v[32:47], v[128:131], v[186:189], v[32:47]
	ds_read_b64_tr_b16 v[186:187], v133 offset:0x1400
	ds_read_b64_tr_b16 v[188:189], v135 offset:0x1400
	ds_read_b64_tr_b16 v[194:195], v133 offset:0x1600
	ds_read_b64_tr_b16 v[196:197], v135 offset:0x1600
	s_waitcnt lgkmcnt(0)
	v_mfma_f32_32x32x16_bf16 v[48:63], v[128:131], v[190:193], v[48:63]
	v_mfma_f32_32x32x16_bf16 v[16:31], v[146:149], v[150:153], v[16:31]
	v_add_u32_e32 v133, 0x2000, v133
	ds_read_b64_tr_b16 v[150:151], v133 offset:0
	v_add_u32_e32 v135, 0x2000, v135
	ds_read_b64_tr_b16 v[152:153], v135 offset:0
	v_mfma_f32_32x32x16_bf16 v[0:15], v[146:149], v[182:185], v[0:15]
	ds_read_b64_tr_b16 v[182:183], v133 offset:0x200
	ds_read_b64_tr_b16 v[184:185], v135 offset:0x200
	v_mfma_f32_32x32x16_bf16 v[32:47], v[146:149], v[186:189], v[32:47]
	ds_read_b64_tr_b16 v[186:187], v133 offset:0x400
	ds_read_b64_tr_b16 v[188:189], v135 offset:0x400
	ds_read_b64_tr_b16 v[190:191], v133 offset:0x600
	ds_read_b64_tr_b16 v[192:193], v135 offset:0x600
	s_waitcnt lgkmcnt(0)
	v_mfma_f32_32x32x16_bf16 v[48:63], v[146:149], v[194:197], v[48:63]
	v_mfma_f32_32x32x16_bf16 v[96:111], v[128:131], v[150:153], v[96:111]
	ds_read_b64_tr_b16 v[150:151], v133 offset:0x1000
	ds_read_b64_tr_b16 v[152:153], v135 offset:0x1000
	v_mfma_f32_32x32x16_bf16 v[112:127], v[128:131], v[182:185], v[112:127]
	ds_read_b64_tr_b16 v[182:183], v133 offset:0x1200
	ds_read_b64_tr_b16 v[184:185], v135 offset:0x1200
	v_mfma_f32_32x32x16_bf16 v[80:95], v[128:131], v[186:189], v[80:95]
	ds_read_b64_tr_b16 v[186:187], v133 offset:0x1400
	ds_read_b64_tr_b16 v[188:189], v135 offset:0x1400
	ds_read_b64_tr_b16 v[194:195], v133 offset:0x1600
	ds_read_b64_tr_b16 v[196:197], v135 offset:0x1600
	s_waitcnt lgkmcnt(0)
	v_mfma_f32_32x32x16_bf16 v[64:79], v[128:131], v[190:193], v[64:79]
	v_mfma_f32_32x32x16_bf16 v[96:111], v[146:149], v[150:153], v[96:111]
	v_mfma_f32_32x32x16_bf16 v[112:127], v[146:149], v[182:185], v[112:127]
	v_mfma_f32_32x32x16_bf16 v[80:95], v[146:149], v[186:189], v[80:95]
	v_mfma_f32_32x32x16_bf16 v[64:79], v[146:149], v[194:197], v[64:79]
	s_waitcnt vmcnt(4) lgkmcnt(0)
	s_barrier
; #define VM_WAIT() asm volatile("s_waitcnt vmcnt(0)" ::: "memory")
; template <int DK, int DV, bool MLSTM>
; __device__ __forceinline__ void out_unit2(LAS unsigned char* lds, LAS unsigned char* ldstab, const OutArgs a, const int wv) {
;     ...
; #pragma unroll 1
;     for (int pc = 4; pc < 4 + 2 * NCP; ++pc) {
;         VM_WAIT(); __syncthreads();
;         if (pc + 1 < 4 + 2 * NCP) OUT_DMA(pc + 1);
;         const int cq = pc - 4, dirb = cq >= NCP, cp = dirb ? cq - NCP : cq;
;         const float qs = dirb ? qsb : qsf;
;         const unsigned qa = QP + (cp >> 2) * 32768u + 512u * (cp & 3) + 8192u * rb;
;         const bf16x8 af0 = scale_frag(lds_r128(qa + rb0), qs), af1 = scale_frag(lds_r128(qa + rb1), qs);
;         OUT_MMA(pc & 1);
	s_add_u32 s40, s4, 0x20000
	s_addc_u32 s41, s5, 0
	v_lshl_add_u64 v[128:129], s[40:41], 0, v[198:199]
	v_lshl_add_u64 v[130:131], s[40:41], 0, v[200:201]
	v_lshl_add_u64 v[146:147], s[40:41], 0, v[202:203]
	v_lshl_add_u64 v[148:149], s[40:41], 0, v[204:205]
	s_add_i32 m0, s6, 0x18000
	s_nop 0
	global_load_lds_dwordx4 v[128:129], off
	s_add_i32 m0, s7, 0x18000
	s_nop 0
	global_load_lds_dwordx4 v[130:131], off
	s_add_i32 m0, s36, 0x18000
	s_nop 0
	global_load_lds_dwordx4 v[146:147], off
	s_add_i32 m0, s38, 0x18000
	s_nop 0
	global_load_lds_dwordx4 v[148:149], off
	v_lshlrev_b32_e32 v135, 16, v252
	v_and_b32_e32 v137, 0xffff0000, v252
	v_mul_f32_e32 v135, v179, v135
	v_mul_f32_e32 v137, v179, v137
	v_cvt_pk_bf16_f32 v128, v135, v137
	v_lshlrev_b32_e32 v135, 16, v253
	v_and_b32_e32 v137, 0xffff0000, v253
	v_mul_f32_e32 v135, v179, v135
	v_mul_f32_e32 v137, v179, v137
	v_cvt_pk_bf16_f32 v129, v135, v137
	v_lshlrev_b32_e32 v135, 16, v254
	v_and_b32_e32 v137, 0xffff0000, v254
	v_mul_f32_e32 v135, v179, v135
	v_mul_f32_e32 v137, v179, v137
	v_cvt_pk_bf16_f32 v130, v135, v137
	v_lshlrev_b32_e32 v135, 16, v255
	v_and_b32_e32 v137, 0xffff0000, v255
	v_mul_f32_e32 v135, v179, v135
	v_mul_f32_e32 v137, v179, v137
	v_cvt_pk_bf16_f32 v131, v135, v137
	v_lshlrev_b32_e32 v135, 16, v218
	v_and_b32_e32 v137, 0xffff0000, v218
	v_mul_f32_e32 v135, v179, v135
	v_mul_f32_e32 v137, v179, v137
	v_cvt_pk_bf16_f32 v146, v135, v137
	v_lshlrev_b32_e32 v135, 16, v219
	v_and_b32_e32 v137, 0xffff0000, v219
	v_mul_f32_e32 v135, v179, v135
	v_mul_f32_e32 v137, v179, v137
	v_cvt_pk_bf16_f32 v147, v135, v137
	v_lshlrev_b32_e32 v135, 16, v220
	v_and_b32_e32 v137, 0xffff0000, v220
	v_mul_f32_e32 v135, v179, v135
	v_mul_f32_e32 v137, v179, v137
	v_cvt_pk_bf16_f32 v148, v135, v137
	v_lshlrev_b32_e32 v135, 16, v221
	v_and_b32_e32 v137, 0xffff0000, v221
	v_mul_f32_e32 v135, v179, v135
	v_mul_f32_e32 v137, v179, v137
	v_cvt_pk_bf16_f32 v149, v135, v137
	v_mov_b32_e32 v133, v175
	ds_read_b64_tr_b16 v[150:151], v133 offset:0
	v_mov_b32_e32 v135, v181
	ds_read_b64_tr_b16 v[152:153], v135 offset:0
	ds_read_b64_tr_b16 v[182:183], v133 offset:0x200
	ds_read_b64_tr_b16 v[184:185], v135 offset:0x200
	ds_read_b64_tr_b16 v[186:187], v133 offset:0x400
	ds_read_b64_tr_b16 v[188:189], v135 offset:0x400
	ds_read_b64_tr_b16 v[190:191], v133 offset:0x600
	ds_read_b64_tr_b16 v[192:193], v135 offset:0x600
	s_waitcnt lgkmcnt(0)
	s_nop 0
	v_mfma_f32_32x32x16_bf16 v[16:31], v[128:131], v[150:153], v[16:31]
	ds_read_b64_tr_b16 v[150:151], v133 offset:0x1000
	ds_read_b64_tr_b16 v[152:153], v135 offset:0x1000
	v_mfma_f32_32x32x16_bf16 v[0:15], v[128:131], v[182:185], v[0:15]
	ds_read_b64_tr_b16 v[182:183], v133 offset:0x1200
	ds_read_b64_tr_b16 v[184:185], v135 offset:0x1200
	v_mfma_f32_32x32x16_bf16 v[32:47], v[128:131], v[186:189], v[32:47]
	ds_read_b64_tr_b16 v[186:187], v133 offset:0x1400
	ds_read_b64_tr_b16 v[188:189], v135 offset:0x1400
	ds_read_b64_tr_b16 v[194:195], v133 offset:0x1600
	ds_read_b64_tr_b16 v[196:197], v135 offset:0x1600
	s_waitcnt lgkmcnt(0)
	v_mfma_f32_32x32x16_bf16 v[48:63], v[128:131], v[190:193], v[48:63]
	v_mfma_f32_32x32x16_bf16 v[16:31], v[146:149], v[150:153], v[16:31]
	v_add_u32_e32 v133, 0x2000, v133
	ds_read_b64_tr_b16 v[150:151], v133 offset:0
	v_add_u32_e32 v135, 0x2000, v135
	ds_read_b64_tr_b16 v[152:153], v135 offset:0
	v_mfma_f32_32x32x16_bf16 v[0:15], v[146:149], v[182:185], v[0:15]
	ds_read_b64_tr_b16 v[182:183], v133 offset:0x200
	ds_read_b64_tr_b16 v[184:185], v135 offset:0x200
	v_mfma_f32_32x32x16_bf16 v[32:47], v[146:149], v[186:189], v[32:47]
	ds_read_b64_tr_b16 v[186:187], v133 offset:0x400
	ds_read_b64_tr_b16 v[188:189], v135 offset:0x400
	ds_read_b64_tr_b16 v[190:191], v133 offset:0x600
	ds_read_b64_tr_b16 v[192:193], v135 offset:0x600
	s_waitcnt lgkmcnt(0)
	v_mfma_f32_32x32x16_bf16 v[48:63], v[146:149], v[194:197], v[48:63]
	v_mfma_f32_32x32x16_bf16 v[96:111], v[128:131], v[150:153], v[96:111]
	ds_read_b64_tr_b16 v[150:151], v133 offset:0x1000
	ds_read_b64_tr_b16 v[152:153], v135 offset:0x1000
	v_mfma_f32_32x32x16_bf16 v[112:127], v[128:131], v[182:185], v[112:127]
	ds_read_b64_tr_b16 v[182:183], v133 offset:0x1200
	ds_read_b64_tr_b16 v[184:185], v135 offset:0x1200
	v_mfma_f32_32x32x16_bf16 v[80:95], v[128:131], v[186:189], v[80:95]
	ds_read_b64_tr_b16 v[186:187], v133 offset:0x1400
	ds_read_b64_tr_b16 v[188:189], v135 offset:0x1400
	ds_read_b64_tr_b16 v[194:195], v133 offset:0x1600
	ds_read_b64_tr_b16 v[196:197], v135 offset:0x1600
	s_waitcnt lgkmcnt(0)
	v_mfma_f32_32x32x16_bf16 v[64:79], v[128:131], v[190:193], v[64:79]
	v_mfma_f32_32x32x16_bf16 v[96:111], v[146:149], v[150:153], v[96:111]
	v_mfma_f32_32x32x16_bf16 v[112:127], v[146:149], v[182:185], v[112:127]
	v_mfma_f32_32x32x16_bf16 v[80:95], v[146:149], v[186:189], v[80:95]
	v_mfma_f32_32x32x16_bf16 v[64:79], v[146:149], v[194:197], v[64:79]
	s_waitcnt vmcnt(4) lgkmcnt(0)
	s_barrier
; #define VM_WAIT() asm volatile("s_waitcnt vmcnt(0)" ::: "memory")
; template <int DK, int DV, bool MLSTM>
; __device__ __forceinline__ void out_unit2(LAS unsigned char* lds, LAS unsigned char* ldstab, const OutArgs a, const int wv) {
;     ...
; #pragma unroll 1
;     for (int pc = 4; pc < 4 + 2 * NCP; ++pc) {
;         VM_WAIT(); __syncthreads();
;         if (pc + 1 < 4 + 2 * NCP) OUT_DMA(pc + 1);
;         const int cq = pc - 4, dirb = cq >= NCP, cp = dirb ? cq - NCP : cq;
;         const float qs = dirb ? qsb : qsf;
;         const unsigned qa = QP + (cp >> 2) * 32768u + 512u * (cp & 3) + 8192u * rb;
;         const bf16x8 af0 = scale_frag(lds_r128(qa + rb0), qs), af1 = scale_frag(lds_r128(qa + rb1), qs);
;         OUT_MMA(pc & 1);
	s_add_u32 s40, s4, 0x28000
	s_addc_u32 s41, s5, 0
	v_lshl_add_u64 v[128:129], s[40:41], 0, v[198:199]
	v_lshl_add_u64 v[130:131], s[40:41], 0, v[200:201]
	v_lshl_add_u64 v[146:147], s[40:41], 0, v[202:203]
	v_lshl_add_u64 v[148:149], s[40:41], 0, v[204:205]
	s_mov_b32 m0, s6
	s_nop 0
	global_load_lds_dwordx4 v[128:129], off
	s_mov_b32 m0, s7
	s_nop 0
	global_load_lds_dwordx4 v[130:131], off
	s_mov_b32 m0, s36
	s_nop 0
	global_load_lds_dwordx4 v[146:147], off
	s_mov_b32 m0, s38
	s_nop 0
	global_load_lds_dwordx4 v[148:149], off
	v_lshlrev_b32_e32 v135, 16, v222
	v_and_b32_e32 v137, 0xffff0000, v222
	v_mul_f32_e32 v135, v179, v135
	v_mul_f32_e32 v137, v179, v137
	v_cvt_pk_bf16_f32 v128, v135, v137
	v_lshlrev_b32_e32 v135, 16, v223
	v_and_b32_e32 v137, 0xffff0000, v223
	v_mul_f32_e32 v135, v179, v135
	v_mul_f32_e32 v137, v179, v137
	v_cvt_pk_bf16_f32 v129, v135, v137
	v_lshlrev_b32_e32 v135, 16, v224
	v_and_b32_e32 v137, 0xffff0000, v224
	v_mul_f32_e32 v135, v179, v135
	v_mul_f32_e32 v137, v179, v137
	v_cvt_pk_bf16_f32 v130, v135, v137
	v_lshlrev_b32_e32 v135, 16, v225
	v_and_b32_e32 v137, 0xffff0000, v225
	v_mul_f32_e32 v135, v179, v135
	v_mul_f32_e32 v137, v179, v137
	v_cvt_pk_bf16_f32 v131, v135, v137
	v_lshlrev_b32_e32 v135, 16, v206
	v_and_b32_e32 v137, 0xffff0000, v206
	v_mul_f32_e32 v135, v179, v135
	v_mul_f32_e32 v137, v179, v137
	v_cvt_pk_bf16_f32 v146, v135, v137
	v_lshlrev_b32_e32 v135, 16, v207
	v_and_b32_e32 v137, 0xffff0000, v207
	v_mul_f32_e32 v135, v179, v135
	v_mul_f32_e32 v137, v179, v137
	v_cvt_pk_bf16_f32 v147, v135, v137
	v_lshlrev_b32_e32 v135, 16, v208
	v_and_b32_e32 v137, 0xffff0000, v208
	v_mul_f32_e32 v135, v179, v135
	v_mul_f32_e32 v137, v179, v137
	v_cvt_pk_bf16_f32 v148, v135, v137
	v_lshlrev_b32_e32 v135, 16, v209
	v_and_b32_e32 v137, 0xffff0000, v209
	v_mul_f32_e32 v135, v179, v135
	v_mul_f32_e32 v137, v179, v137
	v_cvt_pk_bf16_f32 v149, v135, v137
	v_add_u32_e32 v133, 0x10000, v175
	ds_read_b64_tr_b16 v[150:151], v133 offset:0
	v_add_u32_e32 v135, 0x10000, v181
	ds_read_b64_tr_b16 v[152:153], v135 offset:0
	ds_read_b64_tr_b16 v[182:183], v133 offset:0x200
	ds_read_b64_tr_b16 v[184:185], v135 offset:0x200
	ds_read_b64_tr_b16 v[186:187], v133 offset:0x400
	ds_read_b64_tr_b16 v[188:189], v135 offset:0x400
	ds_read_b64_tr_b16 v[190:191], v133 offset:0x600
	ds_read_b64_tr_b16 v[192:193], v135 offset:0x600
	s_waitcnt lgkmcnt(0)
	s_nop 0
	v_mfma_f32_32x32x16_bf16 v[16:31], v[128:131], v[150:153], v[16:31]
	ds_read_b64_tr_b16 v[150:151], v133 offset:0x1000
	ds_read_b64_tr_b16 v[152:153], v135 offset:0x1000
	v_mfma_f32_32x32x16_bf16 v[0:15], v[128:131], v[182:185], v[0:15]
	ds_read_b64_tr_b16 v[182:183], v133 offset:0x1200
	ds_read_b64_tr_b16 v[184:185], v135 offset:0x1200
	v_mfma_f32_32x32x16_bf16 v[32:47], v[128:131], v[186:189], v[32:47]
	ds_read_b64_tr_b16 v[186:187], v133 offset:0x1400
	ds_read_b64_tr_b16 v[188:189], v135 offset:0x1400
	ds_read_b64_tr_b16 v[194:195], v133 offset:0x1600
	ds_read_b64_tr_b16 v[196:197], v135 offset:0x1600
	s_waitcnt lgkmcnt(0)
	v_mfma_f32_32x32x16_bf16 v[48:63], v[128:131], v[190:193], v[48:63]
	v_mfma_f32_32x32x16_bf16 v[16:31], v[146:149], v[150:153], v[16:31]
	v_add_u32_e32 v133, 0x2000, v133
	ds_read_b64_tr_b16 v[150:151], v133 offset:0
	v_add_u32_e32 v135, 0x2000, v135
	ds_read_b64_tr_b16 v[152:153], v135 offset:0
	v_mfma_f32_32x32x16_bf16 v[0:15], v[146:149], v[182:185], v[0:15]
	ds_read_b64_tr_b16 v[182:183], v133 offset:0x200
	ds_read_b64_tr_b16 v[184:185], v135 offset:0x200
	v_mfma_f32_32x32x16_bf16 v[32:47], v[146:149], v[186:189], v[32:47]
	ds_read_b64_tr_b16 v[186:187], v133 offset:0x400
	ds_read_b64_tr_b16 v[188:189], v135 offset:0x400
	ds_read_b64_tr_b16 v[190:191], v133 offset:0x600
	ds_read_b64_tr_b16 v[192:193], v135 offset:0x600
	s_waitcnt lgkmcnt(0)
	v_mfma_f32_32x32x16_bf16 v[48:63], v[146:149], v[194:197], v[48:63]
	v_mfma_f32_32x32x16_bf16 v[96:111], v[128:131], v[150:153], v[96:111]
	ds_read_b64_tr_b16 v[150:151], v133 offset:0x1000
	ds_read_b64_tr_b16 v[152:153], v135 offset:0x1000
	v_mfma_f32_32x32x16_bf16 v[112:127], v[128:131], v[182:185], v[112:127]
	ds_read_b64_tr_b16 v[182:183], v133 offset:0x1200
	ds_read_b64_tr_b16 v[184:185], v135 offset:0x1200
	v_mfma_f32_32x32x16_bf16 v[80:95], v[128:131], v[186:189], v[80:95]
	ds_read_b64_tr_b16 v[186:187], v133 offset:0x1400
	ds_read_b64_tr_b16 v[188:189], v135 offset:0x1400
	ds_read_b64_tr_b16 v[194:195], v133 offset:0x1600
	ds_read_b64_tr_b16 v[196:197], v135 offset:0x1600
	s_waitcnt lgkmcnt(0)
	v_mfma_f32_32x32x16_bf16 v[64:79], v[128:131], v[190:193], v[64:79]
	v_mfma_f32_32x32x16_bf16 v[96:111], v[146:149], v[150:153], v[96:111]
	v_mfma_f32_32x32x16_bf16 v[112:127], v[146:149], v[182:185], v[112:127]
	v_mfma_f32_32x32x16_bf16 v[80:95], v[146:149], v[186:189], v[80:95]
	v_mfma_f32_32x32x16_bf16 v[64:79], v[146:149], v[194:197], v[64:79]
	s_waitcnt vmcnt(4) lgkmcnt(0)
	s_barrier
; #define VM_WAIT() asm volatile("s_waitcnt vmcnt(0)" ::: "memory")
; template <int DK, int DV, bool MLSTM>
; __device__ __forceinline__ void out_unit2(LAS unsigned char* lds, LAS unsigned char* ldstab, const OutArgs a, const int wv) {
;     ...
; #pragma unroll 1
;     for (int pc = 4; pc < 4 + 2 * NCP; ++pc) {
;         VM_WAIT(); __syncthreads();
;         if (pc + 1 < 4 + 2 * NCP) OUT_DMA(pc + 1);
;         const int cq = pc - 4, dirb = cq >= NCP, cp = dirb ? cq - NCP : cq;
;         const float qs = dirb ? qsb : qsf;
;         const unsigned qa = QP + (cp >> 2) * 32768u + 512u * (cp & 3) + 8192u * rb;
;         const bf16x8 af0 = scale_frag(lds_r128(qa + rb0), qs), af1 = scale_frag(lds_r128(qa + rb1), qs);
;         OUT_MMA(pc & 1);
	s_add_u32 s40, s4, 0x30000
	s_addc_u32 s41, s5, 0
	v_lshl_add_u64 v[128:129], s[40:41], 0, v[198:199]
	v_lshl_add_u64 v[130:131], s[40:41], 0, v[200:201]
	v_lshl_add_u64 v[146:147], s[40:41], 0, v[202:203]
	v_lshl_add_u64 v[148:149], s[40:41], 0, v[204:205]
	s_add_i32 m0, s6, 0x10000
	s_nop 0
	global_load_lds_dwordx4 v[128:129], off
	s_add_i32 m0, s7, 0x10000
	s_nop 0
	global_load_lds_dwordx4 v[130:131], off
	s_add_i32 m0, s36, 0x10000
	s_nop 0
	global_load_lds_dwordx4 v[146:147], off
	s_add_i32 m0, s38, 0x10000
	s_nop 0
	global_load_lds_dwordx4 v[148:149], off
	v_add_u32_e32 v133, s13, v173
	v_add_u32_e32 v135, s13, v177
	ds_read_b128 v[128:131], v133 offset:32768
	ds_read_b128 v[146:149], v135 offset:32768
	s_waitcnt lgkmcnt(0)
	v_lshlrev_b32_e32 v135, 16, v128
	v_and_b32_e32 v137, 0xffff0000, v128
	v_mul_f32_e32 v135, v179, v135
	v_mul_f32_e32 v137, v179, v137
	v_cvt_pk_bf16_f32 v128, v135, v137
	v_lshlrev_b32_e32 v135, 16, v129
	v_and_b32_e32 v137, 0xffff0000, v129
	v_mul_f32_e32 v135, v179, v135
	v_mul_f32_e32 v137, v179, v137
	v_cvt_pk_bf16_f32 v129, v135, v137
	v_lshlrev_b32_e32 v135, 16, v130
	v_and_b32_e32 v137, 0xffff0000, v130
	v_mul_f32_e32 v135, v179, v135
	v_mul_f32_e32 v137, v179, v137
	v_cvt_pk_bf16_f32 v130, v135, v137
	v_lshlrev_b32_e32 v135, 16, v131
	v_and_b32_e32 v137, 0xffff0000, v131
	v_mul_f32_e32 v135, v179, v135
	v_mul_f32_e32 v137, v179, v137
	v_cvt_pk_bf16_f32 v131, v135, v137
	v_lshlrev_b32_e32 v135, 16, v146
	v_and_b32_e32 v137, 0xffff0000, v146
	v_mul_f32_e32 v135, v179, v135
	v_mul_f32_e32 v137, v179, v137
	v_cvt_pk_bf16_f32 v146, v135, v137
	v_lshlrev_b32_e32 v135, 16, v147
	v_and_b32_e32 v137, 0xffff0000, v147
	v_mul_f32_e32 v135, v179, v135
	v_mul_f32_e32 v137, v179, v137
	v_cvt_pk_bf16_f32 v147, v135, v137
	v_lshlrev_b32_e32 v135, 16, v148
	v_and_b32_e32 v137, 0xffff0000, v148
	v_mul_f32_e32 v135, v179, v135
	v_mul_f32_e32 v137, v179, v137
	v_cvt_pk_bf16_f32 v148, v135, v137
	v_lshlrev_b32_e32 v135, 16, v149
	v_and_b32_e32 v137, 0xffff0000, v149
	v_mul_f32_e32 v135, v179, v135
	v_mul_f32_e32 v137, v179, v137
	v_cvt_pk_bf16_f32 v149, v135, v137
	v_add_u32_e32 v133, 0x18000, v175
	ds_read_b64_tr_b16 v[150:151], v133 offset:0
	v_add_u32_e32 v135, 0x18000, v181
	ds_read_b64_tr_b16 v[152:153], v135 offset:0
	ds_read_b64_tr_b16 v[182:183], v133 offset:0x200
	ds_read_b64_tr_b16 v[184:185], v135 offset:0x200
	ds_read_b64_tr_b16 v[186:187], v133 offset:0x400
	ds_read_b64_tr_b16 v[188:189], v135 offset:0x400
	ds_read_b64_tr_b16 v[190:191], v133 offset:0x600
	ds_read_b64_tr_b16 v[192:193], v135 offset:0x600
	s_waitcnt lgkmcnt(0)
	s_nop 0
	v_mfma_f32_32x32x16_bf16 v[16:31], v[128:131], v[150:153], v[16:31]
	ds_read_b64_tr_b16 v[150:151], v133 offset:0x1000
	ds_read_b64_tr_b16 v[152:153], v135 offset:0x1000
	v_mfma_f32_32x32x16_bf16 v[0:15], v[128:131], v[182:185], v[0:15]
	ds_read_b64_tr_b16 v[182:183], v133 offset:0x1200
	ds_read_b64_tr_b16 v[184:185], v135 offset:0x1200
	v_mfma_f32_32x32x16_bf16 v[32:47], v[128:131], v[186:189], v[32:47]
	ds_read_b64_tr_b16 v[186:187], v133 offset:0x1400
	ds_read_b64_tr_b16 v[188:189], v135 offset:0x1400
	ds_read_b64_tr_b16 v[194:195], v133 offset:0x1600
	ds_read_b64_tr_b16 v[196:197], v135 offset:0x1600
	s_waitcnt lgkmcnt(0)
	v_mfma_f32_32x32x16_bf16 v[48:63], v[128:131], v[190:193], v[48:63]
	v_mfma_f32_32x32x16_bf16 v[16:31], v[146:149], v[150:153], v[16:31]
	v_add_u32_e32 v133, 0x2000, v133
	ds_read_b64_tr_b16 v[150:151], v133 offset:0
	v_add_u32_e32 v135, 0x2000, v135
	ds_read_b64_tr_b16 v[152:153], v135 offset:0
	v_mfma_f32_32x32x16_bf16 v[0:15], v[146:149], v[182:185], v[0:15]
	ds_read_b64_tr_b16 v[182:183], v133 offset:0x200
	ds_read_b64_tr_b16 v[184:185], v135 offset:0x200
	v_mfma_f32_32x32x16_bf16 v[32:47], v[146:149], v[186:189], v[32:47]
	ds_read_b64_tr_b16 v[186:187], v133 offset:0x400
	ds_read_b64_tr_b16 v[188:189], v135 offset:0x400
	ds_read_b64_tr_b16 v[190:191], v133 offset:0x600
	ds_read_b64_tr_b16 v[192:193], v135 offset:0x600
	s_waitcnt lgkmcnt(0)
	v_mfma_f32_32x32x16_bf16 v[48:63], v[146:149], v[194:197], v[48:63]
	v_mfma_f32_32x32x16_bf16 v[96:111], v[128:131], v[150:153], v[96:111]
	ds_read_b64_tr_b16 v[150:151], v133 offset:0x1000
	ds_read_b64_tr_b16 v[152:153], v135 offset:0x1000
	v_mfma_f32_32x32x16_bf16 v[112:127], v[128:131], v[182:185], v[112:127]
	ds_read_b64_tr_b16 v[182:183], v133 offset:0x1200
	ds_read_b64_tr_b16 v[184:185], v135 offset:0x1200
	v_mfma_f32_32x32x16_bf16 v[80:95], v[128:131], v[186:189], v[80:95]
	ds_read_b64_tr_b16 v[186:187], v133 offset:0x1400
	ds_read_b64_tr_b16 v[188:189], v135 offset:0x1400
	ds_read_b64_tr_b16 v[194:195], v133 offset:0x1600
	ds_read_b64_tr_b16 v[196:197], v135 offset:0x1600
	s_waitcnt lgkmcnt(0)
	v_mfma_f32_32x32x16_bf16 v[64:79], v[128:131], v[190:193], v[64:79]
	v_mfma_f32_32x32x16_bf16 v[96:111], v[146:149], v[150:153], v[96:111]
	v_mfma_f32_32x32x16_bf16 v[112:127], v[146:149], v[182:185], v[112:127]
	v_mfma_f32_32x32x16_bf16 v[80:95], v[146:149], v[186:189], v[80:95]
	v_mfma_f32_32x32x16_bf16 v[64:79], v[146:149], v[194:197], v[64:79]
	s_waitcnt vmcnt(4) lgkmcnt(0)
	s_barrier
; #define VM_WAIT() asm volatile("s_waitcnt vmcnt(0)" ::: "memory")
; template <int DK, int DV, bool MLSTM>
; __device__ __forceinline__ void out_unit2(LAS unsigned char* lds, LAS unsigned char* ldstab, const OutArgs a, const int wv) {
;     ...
; #pragma unroll 1
;     for (int pc = 4; pc < 4 + 2 * NCP; ++pc) {
;         VM_WAIT(); __syncthreads();
;         if (pc + 1 < 4 + 2 * NCP) OUT_DMA(pc + 1);
;         const int cq = pc - 4, dirb = cq >= NCP, cp = dirb ? cq - NCP : cq;
;         const float qs = dirb ? qsb : qsf;
;         const unsigned qa = QP + (cp >> 2) * 32768u + 512u * (cp & 3) + 8192u * rb;
;         const bf16x8 af0 = scale_frag(lds_r128(qa + rb0), qs), af1 = scale_frag(lds_r128(qa + rb1), qs);
;         OUT_MMA(pc & 1);
	s_add_u32 s40, s4, 0x38000
	s_addc_u32 s41, s5, 0
	v_lshl_add_u64 v[128:129], s[40:41], 0, v[198:199]
	v_lshl_add_u64 v[130:131], s[40:41], 0, v[200:201]
	v_lshl_add_u64 v[146:147], s[40:41], 0, v[202:203]
	v_lshl_add_u64 v[148:149], s[40:41], 0, v[204:205]
	s_add_i32 m0, s6, 0x18000
	s_nop 0
	global_load_lds_dwordx4 v[128:129], off
	s_add_i32 m0, s7, 0x18000
	s_nop 0
	global_load_lds_dwordx4 v[130:131], off
	s_add_i32 m0, s36, 0x18000
	s_nop 0
	global_load_lds_dwordx4 v[146:147], off
	s_add_i32 m0, s38, 0x18000
	s_nop 0
	global_load_lds_dwordx4 v[148:149], off
	v_add_u32_e32 v133, s13, v173
	v_add_u32_e32 v135, s13, v177
	ds_read_b128 v[128:131], v133 offset:33280
	ds_read_b128 v[146:149], v135 offset:33280
	s_waitcnt lgkmcnt(0)
	v_lshlrev_b32_e32 v135, 16, v128
	v_and_b32_e32 v137, 0xffff0000, v128
	v_mul_f32_e32 v135, v179, v135
	v_mul_f32_e32 v137, v179, v137
	v_cvt_pk_bf16_f32 v128, v135, v137
	v_lshlrev_b32_e32 v135, 16, v129
	v_and_b32_e32 v137, 0xffff0000, v129
	v_mul_f32_e32 v135, v179, v135
	v_mul_f32_e32 v137, v179, v137
	v_cvt_pk_bf16_f32 v129, v135, v137
	v_lshlrev_b32_e32 v135, 16, v130
	v_and_b32_e32 v137, 0xffff0000, v130
	v_mul_f32_e32 v135, v179, v135
	v_mul_f32_e32 v137, v179, v137
	v_cvt_pk_bf16_f32 v130, v135, v137
	v_lshlrev_b32_e32 v135, 16, v131
	v_and_b32_e32 v137, 0xffff0000, v131
	v_mul_f32_e32 v135, v179, v135
	v_mul_f32_e32 v137, v179, v137
	v_cvt_pk_bf16_f32 v131, v135, v137
	v_lshlrev_b32_e32 v135, 16, v146
	v_and_b32_e32 v137, 0xffff0000, v146
	v_mul_f32_e32 v135, v179, v135
	v_mul_f32_e32 v137, v179, v137
	v_cvt_pk_bf16_f32 v146, v135, v137
	v_lshlrev_b32_e32 v135, 16, v147
	v_and_b32_e32 v137, 0xffff0000, v147
	v_mul_f32_e32 v135, v179, v135
	v_mul_f32_e32 v137, v179, v137
	v_cvt_pk_bf16_f32 v147, v135, v137
	v_lshlrev_b32_e32 v135, 16, v148
	v_and_b32_e32 v137, 0xffff0000, v148
	v_mul_f32_e32 v135, v179, v135
	v_mul_f32_e32 v137, v179, v137
	v_cvt_pk_bf16_f32 v148, v135, v137
	v_lshlrev_b32_e32 v135, 16, v149
	v_and_b32_e32 v137, 0xffff0000, v149
	v_mul_f32_e32 v135, v179, v135
	v_mul_f32_e32 v137, v179, v137
	v_cvt_pk_bf16_f32 v149, v135, v137
	v_mov_b32_e32 v133, v175
	ds_read_b64_tr_b16 v[150:151], v133 offset:0
	v_mov_b32_e32 v135, v181
	ds_read_b64_tr_b16 v[152:153], v135 offset:0
	ds_read_b64_tr_b16 v[182:183], v133 offset:0x200
	ds_read_b64_tr_b16 v[184:185], v135 offset:0x200
	ds_read_b64_tr_b16 v[186:187], v133 offset:0x400
	ds_read_b64_tr_b16 v[188:189], v135 offset:0x400
	ds_read_b64_tr_b16 v[190:191], v133 offset:0x600
	ds_read_b64_tr_b16 v[192:193], v135 offset:0x600
	s_waitcnt lgkmcnt(0)
	s_nop 0
	v_mfma_f32_32x32x16_bf16 v[16:31], v[128:131], v[150:153], v[16:31]
	ds_read_b64_tr_b16 v[150:151], v133 offset:0x1000
	ds_read_b64_tr_b16 v[152:153], v135 offset:0x1000
	v_mfma_f32_32x32x16_bf16 v[0:15], v[128:131], v[182:185], v[0:15]
	ds_read_b64_tr_b16 v[182:183], v133 offset:0x1200
	ds_read_b64_tr_b16 v[184:185], v135 offset:0x1200
	v_mfma_f32_32x32x16_bf16 v[32:47], v[128:131], v[186:189], v[32:47]
	ds_read_b64_tr_b16 v[186:187], v133 offset:0x1400
	ds_read_b64_tr_b16 v[188:189], v135 offset:0x1400
	ds_read_b64_tr_b16 v[194:195], v133 offset:0x1600
	ds_read_b64_tr_b16 v[196:197], v135 offset:0x1600
	s_waitcnt lgkmcnt(0)
	v_mfma_f32_32x32x16_bf16 v[48:63], v[128:131], v[190:193], v[48:63]
	v_mfma_f32_32x32x16_bf16 v[16:31], v[146:149], v[150:153], v[16:31]
	v_add_u32_e32 v133, 0x2000, v133
	ds_read_b64_tr_b16 v[150:151], v133 offset:0
	v_add_u32_e32 v135, 0x2000, v135
	ds_read_b64_tr_b16 v[152:153], v135 offset:0
	v_mfma_f32_32x32x16_bf16 v[0:15], v[146:149], v[182:185], v[0:15]
	ds_read_b64_tr_b16 v[182:183], v133 offset:0x200
	ds_read_b64_tr_b16 v[184:185], v135 offset:0x200
	v_mfma_f32_32x32x16_bf16 v[32:47], v[146:149], v[186:189], v[32:47]
	ds_read_b64_tr_b16 v[186:187], v133 offset:0x400
	ds_read_b64_tr_b16 v[188:189], v135 offset:0x400
	ds_read_b64_tr_b16 v[190:191], v133 offset:0x600
	ds_read_b64_tr_b16 v[192:193], v135 offset:0x600
	s_waitcnt lgkmcnt(0)
	v_mfma_f32_32x32x16_bf16 v[48:63], v[146:149], v[194:197], v[48:63]
	v_mfma_f32_32x32x16_bf16 v[96:111], v[128:131], v[150:153], v[96:111]
	ds_read_b64_tr_b16 v[150:151], v133 offset:0x1000
	ds_read_b64_tr_b16 v[152:153], v135 offset:0x1000
	v_mfma_f32_32x32x16_bf16 v[112:127], v[128:131], v[182:185], v[112:127]
	ds_read_b64_tr_b16 v[182:183], v133 offset:0x1200
	ds_read_b64_tr_b16 v[184:185], v135 offset:0x1200
	v_mfma_f32_32x32x16_bf16 v[80:95], v[128:131], v[186:189], v[80:95]
	ds_read_b64_tr_b16 v[186:187], v133 offset:0x1400
	ds_read_b64_tr_b16 v[188:189], v135 offset:0x1400
	ds_read_b64_tr_b16 v[194:195], v133 offset:0x1600
	ds_read_b64_tr_b16 v[196:197], v135 offset:0x1600
	s_waitcnt lgkmcnt(0)
	v_mfma_f32_32x32x16_bf16 v[64:79], v[128:131], v[190:193], v[64:79]
	v_mfma_f32_32x32x16_bf16 v[96:111], v[146:149], v[150:153], v[96:111]
	v_mfma_f32_32x32x16_bf16 v[112:127], v[146:149], v[182:185], v[112:127]
	v_mfma_f32_32x32x16_bf16 v[80:95], v[146:149], v[186:189], v[80:95]
	v_mfma_f32_32x32x16_bf16 v[64:79], v[146:149], v[194:197], v[64:79]
	s_waitcnt vmcnt(4) lgkmcnt(0)
	s_barrier
; #define VM_WAIT() asm volatile("s_waitcnt vmcnt(0)" ::: "memory")
; template <int DK, int DV, bool MLSTM>
; __device__ __forceinline__ void out_unit2(LAS unsigned char* lds, LAS unsigned char* ldstab, const OutArgs a, const int wv) {
;     ...
; #pragma unroll 1
;     for (int pc = 4; pc < 4 + 2 * NCP; ++pc) {
;         VM_WAIT(); __syncthreads();
;         if (pc + 1 < 4 + 2 * NCP) OUT_DMA(pc + 1);
;         const int cq = pc - 4, dirb = cq >= NCP, cp = dirb ? cq - NCP : cq;
;         const float qs = dirb ? qsb : qsf;
;         const unsigned qa = QP + (cp >> 2) * 32768u + 512u * (cp & 3) + 8192u * rb;
;         const bf16x8 af0 = scale_frag(lds_r128(qa + rb0), qs), af1 = scale_frag(lds_r128(qa + rb1), qs);
;         OUT_MMA(pc & 1);
	s_add_u32 s40, s11, 0x0
	s_addc_u32 s41, s12, 0
	v_lshl_add_u64 v[128:129], s[40:41], 0, v[198:199]
	v_lshl_add_u64 v[130:131], s[40:41], 0, v[200:201]
	v_lshl_add_u64 v[146:147], s[40:41], 0, v[202:203]
	v_lshl_add_u64 v[148:149], s[40:41], 0, v[204:205]
	s_mov_b32 m0, s6
	s_nop 0
	global_load_lds_dwordx4 v[128:129], off
	s_mov_b32 m0, s7
	s_nop 0
	global_load_lds_dwordx4 v[130:131], off
	s_mov_b32 m0, s36
	s_nop 0
	global_load_lds_dwordx4 v[146:147], off
	s_mov_b32 m0, s38
	s_nop 0
	global_load_lds_dwordx4 v[148:149], off
	v_add_u32_e32 v133, s13, v173
	v_add_u32_e32 v135, s13, v177
	ds_read_b128 v[128:131], v133 offset:33792
	ds_read_b128 v[146:149], v135 offset:33792
	s_waitcnt lgkmcnt(0)
	v_lshlrev_b32_e32 v135, 16, v128
	v_and_b32_e32 v137, 0xffff0000, v128
	v_mul_f32_e32 v135, v179, v135
	v_mul_f32_e32 v137, v179, v137
	v_cvt_pk_bf16_f32 v128, v135, v137
	v_lshlrev_b32_e32 v135, 16, v129
	v_and_b32_e32 v137, 0xffff0000, v129
	v_mul_f32_e32 v135, v179, v135
	v_mul_f32_e32 v137, v179, v137
	v_cvt_pk_bf16_f32 v129, v135, v137
	v_lshlrev_b32_e32 v135, 16, v130
	v_and_b32_e32 v137, 0xffff0000, v130
	v_mul_f32_e32 v135, v179, v135
	v_mul_f32_e32 v137, v179, v137
	v_cvt_pk_bf16_f32 v130, v135, v137
	v_lshlrev_b32_e32 v135, 16, v131
	v_and_b32_e32 v137, 0xffff0000, v131
	v_mul_f32_e32 v135, v179, v135
	v_mul_f32_e32 v137, v179, v137
	v_cvt_pk_bf16_f32 v131, v135, v137
	v_lshlrev_b32_e32 v135, 16, v146
	v_and_b32_e32 v137, 0xffff0000, v146
	v_mul_f32_e32 v135, v179, v135
	v_mul_f32_e32 v137, v179, v137
	v_cvt_pk_bf16_f32 v146, v135, v137
	v_lshlrev_b32_e32 v135, 16, v147
	v_and_b32_e32 v137, 0xffff0000, v147
	v_mul_f32_e32 v135, v179, v135
	v_mul_f32_e32 v137, v179, v137
	v_cvt_pk_bf16_f32 v147, v135, v137
	v_lshlrev_b32_e32 v135, 16, v148
	v_and_b32_e32 v137, 0xffff0000, v148
	v_mul_f32_e32 v135, v179, v135
	v_mul_f32_e32 v137, v179, v137
	v_cvt_pk_bf16_f32 v148, v135, v137
	v_lshlrev_b32_e32 v135, 16, v149
	v_and_b32_e32 v137, 0xffff0000, v149
	v_mul_f32_e32 v135, v179, v135
	v_mul_f32_e32 v137, v179, v137
	v_cvt_pk_bf16_f32 v149, v135, v137
	v_add_u32_e32 v133, 0x10000, v175
	ds_read_b64_tr_b16 v[150:151], v133 offset:0
	v_add_u32_e32 v135, 0x10000, v181
	ds_read_b64_tr_b16 v[152:153], v135 offset:0
	ds_read_b64_tr_b16 v[182:183], v133 offset:0x200
	ds_read_b64_tr_b16 v[184:185], v135 offset:0x200
	ds_read_b64_tr_b16 v[186:187], v133 offset:0x400
	ds_read_b64_tr_b16 v[188:189], v135 offset:0x400
	ds_read_b64_tr_b16 v[190:191], v133 offset:0x600
	ds_read_b64_tr_b16 v[192:193], v135 offset:0x600
	s_waitcnt lgkmcnt(0)
	s_nop 0
	v_mfma_f32_32x32x16_bf16 v[16:31], v[128:131], v[150:153], v[16:31]
	ds_read_b64_tr_b16 v[150:151], v133 offset:0x1000
	ds_read_b64_tr_b16 v[152:153], v135 offset:0x1000
	v_mfma_f32_32x32x16_bf16 v[0:15], v[128:131], v[182:185], v[0:15]
	ds_read_b64_tr_b16 v[182:183], v133 offset:0x1200
	ds_read_b64_tr_b16 v[184:185], v135 offset:0x1200
	v_mfma_f32_32x32x16_bf16 v[32:47], v[128:131], v[186:189], v[32:47]
	ds_read_b64_tr_b16 v[186:187], v133 offset:0x1400
	ds_read_b64_tr_b16 v[188:189], v135 offset:0x1400
	ds_read_b64_tr_b16 v[194:195], v133 offset:0x1600
	ds_read_b64_tr_b16 v[196:197], v135 offset:0x1600
	s_waitcnt lgkmcnt(0)
	v_mfma_f32_32x32x16_bf16 v[48:63], v[128:131], v[190:193], v[48:63]
	v_mfma_f32_32x32x16_bf16 v[16:31], v[146:149], v[150:153], v[16:31]
	v_add_u32_e32 v133, 0x2000, v133
	ds_read_b64_tr_b16 v[150:151], v133 offset:0
	v_add_u32_e32 v135, 0x2000, v135
	ds_read_b64_tr_b16 v[152:153], v135 offset:0
	v_mfma_f32_32x32x16_bf16 v[0:15], v[146:149], v[182:185], v[0:15]
	ds_read_b64_tr_b16 v[182:183], v133 offset:0x200
	ds_read_b64_tr_b16 v[184:185], v135 offset:0x200
	v_mfma_f32_32x32x16_bf16 v[32:47], v[146:149], v[186:189], v[32:47]
	ds_read_b64_tr_b16 v[186:187], v133 offset:0x400
	ds_read_b64_tr_b16 v[188:189], v135 offset:0x400
	ds_read_b64_tr_b16 v[190:191], v133 offset:0x600
	ds_read_b64_tr_b16 v[192:193], v135 offset:0x600
	s_waitcnt lgkmcnt(0)
	v_mfma_f32_32x32x16_bf16 v[48:63], v[146:149], v[194:197], v[48:63]
	v_mfma_f32_32x32x16_bf16 v[96:111], v[128:131], v[150:153], v[96:111]
	ds_read_b64_tr_b16 v[150:151], v133 offset:0x1000
	ds_read_b64_tr_b16 v[152:153], v135 offset:0x1000
	v_mfma_f32_32x32x16_bf16 v[112:127], v[128:131], v[182:185], v[112:127]
	ds_read_b64_tr_b16 v[182:183], v133 offset:0x1200
	ds_read_b64_tr_b16 v[184:185], v135 offset:0x1200
	v_mfma_f32_32x32x16_bf16 v[80:95], v[128:131], v[186:189], v[80:95]
	ds_read_b64_tr_b16 v[186:187], v133 offset:0x1400
	ds_read_b64_tr_b16 v[188:189], v135 offset:0x1400
	ds_read_b64_tr_b16 v[194:195], v133 offset:0x1600
	ds_read_b64_tr_b16 v[196:197], v135 offset:0x1600
	s_waitcnt lgkmcnt(0)
	v_mfma_f32_32x32x16_bf16 v[64:79], v[128:131], v[190:193], v[64:79]
	v_mfma_f32_32x32x16_bf16 v[96:111], v[146:149], v[150:153], v[96:111]
	v_mfma_f32_32x32x16_bf16 v[112:127], v[146:149], v[182:185], v[112:127]
	v_mfma_f32_32x32x16_bf16 v[80:95], v[146:149], v[186:189], v[80:95]
	v_mfma_f32_32x32x16_bf16 v[64:79], v[146:149], v[194:197], v[64:79]
	s_waitcnt vmcnt(4) lgkmcnt(0)
	s_barrier
; #define VM_WAIT() asm volatile("s_waitcnt vmcnt(0)" ::: "memory")
; template <int DK, int DV, bool MLSTM>
; __device__ __forceinline__ void out_unit2(LAS unsigned char* lds, LAS unsigned char* ldstab, const OutArgs a, const int wv) {
;     ...
; #pragma unroll 1
;     for (int pc = 4; pc < 4 + 2 * NCP; ++pc) {
;         VM_WAIT(); __syncthreads();
;         if (pc + 1 < 4 + 2 * NCP) OUT_DMA(pc + 1);
;         const int cq = pc - 4, dirb = cq >= NCP, cp = dirb ? cq - NCP : cq;
;         const float qs = dirb ? qsb : qsf;
;         const unsigned qa = QP + (cp >> 2) * 32768u + 512u * (cp & 3) + 8192u * rb;
;         const bf16x8 af0 = scale_frag(lds_r128(qa + rb0), qs), af1 = scale_frag(lds_r128(qa + rb1), qs);
;         OUT_MMA(pc & 1);
	s_add_u32 s40, s11, 0x8000
	s_addc_u32 s41, s12, 0
	v_lshl_add_u64 v[128:129], s[40:41], 0, v[198:199]
	v_lshl_add_u64 v[130:131], s[40:41], 0, v[200:201]
	v_lshl_add_u64 v[146:147], s[40:41], 0, v[202:203]
	v_lshl_add_u64 v[148:149], s[40:41], 0, v[204:205]
	s_add_i32 m0, s6, 0x10000
	s_nop 0
	global_load_lds_dwordx4 v[128:129], off
	s_add_i32 m0, s7, 0x10000
	s_nop 0
	global_load_lds_dwordx4 v[130:131], off
	s_add_i32 m0, s36, 0x10000
	s_nop 0
	global_load_lds_dwordx4 v[146:147], off
	s_add_i32 m0, s38, 0x10000
	s_nop 0
	global_load_lds_dwordx4 v[148:149], off
	v_add_u32_e32 v133, s13, v173
	v_add_u32_e32 v135, s13, v177
	ds_read_b128 v[128:131], v133 offset:34304
	ds_read_b128 v[146:149], v135 offset:34304
	s_waitcnt lgkmcnt(0)
	v_lshlrev_b32_e32 v135, 16, v128
	v_and_b32_e32 v137, 0xffff0000, v128
	v_mul_f32_e32 v135, v179, v135
	v_mul_f32_e32 v137, v179, v137
	v_cvt_pk_bf16_f32 v128, v135, v137
	v_lshlrev_b32_e32 v135, 16, v129
	v_and_b32_e32 v137, 0xffff0000, v129
	v_mul_f32_e32 v135, v179, v135
	v_mul_f32_e32 v137, v179, v137
	v_cvt_pk_bf16_f32 v129, v135, v137
	v_lshlrev_b32_e32 v135, 16, v130
	v_and_b32_e32 v137, 0xffff0000, v130
	v_mul_f32_e32 v135, v179, v135
	v_mul_f32_e32 v137, v179, v137
	v_cvt_pk_bf16_f32 v130, v135, v137
	v_lshlrev_b32_e32 v135, 16, v131
	v_and_b32_e32 v137, 0xffff0000, v131
	v_mul_f32_e32 v135, v179, v135
	v_mul_f32_e32 v137, v179, v137
	v_cvt_pk_bf16_f32 v131, v135, v137
	v_lshlrev_b32_e32 v135, 16, v146
	v_and_b32_e32 v137, 0xffff0000, v146
	v_mul_f32_e32 v135, v179, v135
	v_mul_f32_e32 v137, v179, v137
	v_cvt_pk_bf16_f32 v146, v135, v137
	v_lshlrev_b32_e32 v135, 16, v147
	v_and_b32_e32 v137, 0xffff0000, v147
	v_mul_f32_e32 v135, v179, v135
	v_mul_f32_e32 v137, v179, v137
	v_cvt_pk_bf16_f32 v147, v135, v137
	v_lshlrev_b32_e32 v135, 16, v148
	v_and_b32_e32 v137, 0xffff0000, v148
	v_mul_f32_e32 v135, v179, v135
	v_mul_f32_e32 v137, v179, v137
	v_cvt_pk_bf16_f32 v148, v135, v137
	v_lshlrev_b32_e32 v135, 16, v149
	v_and_b32_e32 v137, 0xffff0000, v149
	v_mul_f32_e32 v135, v179, v135
	v_mul_f32_e32 v137, v179, v137
	v_cvt_pk_bf16_f32 v149, v135, v137
	v_add_u32_e32 v133, 0x18000, v175
	ds_read_b64_tr_b16 v[150:151], v133 offset:0
	v_add_u32_e32 v135, 0x18000, v181
	ds_read_b64_tr_b16 v[152:153], v135 offset:0
	ds_read_b64_tr_b16 v[182:183], v133 offset:0x200
	ds_read_b64_tr_b16 v[184:185], v135 offset:0x200
	ds_read_b64_tr_b16 v[186:187], v133 offset:0x400
	ds_read_b64_tr_b16 v[188:189], v135 offset:0x400
	ds_read_b64_tr_b16 v[190:191], v133 offset:0x600
	ds_read_b64_tr_b16 v[192:193], v135 offset:0x600
	s_waitcnt lgkmcnt(0)
	s_nop 0
	v_mfma_f32_32x32x16_bf16 v[16:31], v[128:131], v[150:153], v[16:31]
	ds_read_b64_tr_b16 v[150:151], v133 offset:0x1000
	ds_read_b64_tr_b16 v[152:153], v135 offset:0x1000
	v_mfma_f32_32x32x16_bf16 v[0:15], v[128:131], v[182:185], v[0:15]
	ds_read_b64_tr_b16 v[182:183], v133 offset:0x1200
	ds_read_b64_tr_b16 v[184:185], v135 offset:0x1200
	v_mfma_f32_32x32x16_bf16 v[32:47], v[128:131], v[186:189], v[32:47]
	ds_read_b64_tr_b16 v[186:187], v133 offset:0x1400
	ds_read_b64_tr_b16 v[188:189], v135 offset:0x1400
	ds_read_b64_tr_b16 v[194:195], v133 offset:0x1600
	ds_read_b64_tr_b16 v[196:197], v135 offset:0x1600
	s_waitcnt lgkmcnt(0)
	v_mfma_f32_32x32x16_bf16 v[48:63], v[128:131], v[190:193], v[48:63]
	v_mfma_f32_32x32x16_bf16 v[16:31], v[146:149], v[150:153], v[16:31]
	v_add_u32_e32 v133, 0x2000, v133
	ds_read_b64_tr_b16 v[150:151], v133 offset:0
	v_add_u32_e32 v135, 0x2000, v135
	ds_read_b64_tr_b16 v[152:153], v135 offset:0
	v_mfma_f32_32x32x16_bf16 v[0:15], v[146:149], v[182:185], v[0:15]
	ds_read_b64_tr_b16 v[182:183], v133 offset:0x200
	ds_read_b64_tr_b16 v[184:185], v135 offset:0x200
	v_mfma_f32_32x32x16_bf16 v[32:47], v[146:149], v[186:189], v[32:47]
	ds_read_b64_tr_b16 v[186:187], v133 offset:0x400
	ds_read_b64_tr_b16 v[188:189], v135 offset:0x400
	ds_read_b64_tr_b16 v[190:191], v133 offset:0x600
	ds_read_b64_tr_b16 v[192:193], v135 offset:0x600
	s_waitcnt lgkmcnt(0)
	v_mfma_f32_32x32x16_bf16 v[48:63], v[146:149], v[194:197], v[48:63]
	v_mfma_f32_32x32x16_bf16 v[96:111], v[128:131], v[150:153], v[96:111]
	ds_read_b64_tr_b16 v[150:151], v133 offset:0x1000
	ds_read_b64_tr_b16 v[152:153], v135 offset:0x1000
	v_mfma_f32_32x32x16_bf16 v[112:127], v[128:131], v[182:185], v[112:127]
	ds_read_b64_tr_b16 v[182:183], v133 offset:0x1200
	ds_read_b64_tr_b16 v[184:185], v135 offset:0x1200
	v_mfma_f32_32x32x16_bf16 v[80:95], v[128:131], v[186:189], v[80:95]
	ds_read_b64_tr_b16 v[186:187], v133 offset:0x1400
	ds_read_b64_tr_b16 v[188:189], v135 offset:0x1400
	ds_read_b64_tr_b16 v[194:195], v133 offset:0x1600
	ds_read_b64_tr_b16 v[196:197], v135 offset:0x1600
	s_waitcnt lgkmcnt(0)
	v_mfma_f32_32x32x16_bf16 v[64:79], v[128:131], v[190:193], v[64:79]
	v_mfma_f32_32x32x16_bf16 v[96:111], v[146:149], v[150:153], v[96:111]
	v_mfma_f32_32x32x16_bf16 v[112:127], v[146:149], v[182:185], v[112:127]
	v_mfma_f32_32x32x16_bf16 v[80:95], v[146:149], v[186:189], v[80:95]
	v_mfma_f32_32x32x16_bf16 v[64:79], v[146:149], v[194:197], v[64:79]
	s_waitcnt vmcnt(4) lgkmcnt(0)
	s_barrier
; #define VM_WAIT() asm volatile("s_waitcnt vmcnt(0)" ::: "memory")
; template <int DK, int DV, bool MLSTM>
; __device__ __forceinline__ void out_unit2(LAS unsigned char* lds, LAS unsigned char* ldstab, const OutArgs a, const int wv) {
;     ...
; #pragma unroll 1
;     for (int pc = 4; pc < 4 + 2 * NCP; ++pc) {
;         VM_WAIT(); __syncthreads();
;         if (pc + 1 < 4 + 2 * NCP) OUT_DMA(pc + 1);
;         const int cq = pc - 4, dirb = cq >= NCP, cp = dirb ? cq - NCP : cq;
;         const float qs = dirb ? qsb : qsf;
;         const unsigned qa = QP + (cp >> 2) * 32768u + 512u * (cp & 3) + 8192u * rb;
;         const bf16x8 af0 = scale_frag(lds_r128(qa + rb0), qs), af1 = scale_frag(lds_r128(qa + rb1), qs);
;         OUT_MMA(pc & 1);
	s_add_u32 s40, s11, 0x10000
	s_addc_u32 s41, s12, 0
	v_lshl_add_u64 v[128:129], s[40:41], 0, v[198:199]
	v_lshl_add_u64 v[130:131], s[40:41], 0, v[200:201]
	v_lshl_add_u64 v[146:147], s[40:41], 0, v[202:203]
	v_lshl_add_u64 v[148:149], s[40:41], 0, v[204:205]
	s_add_i32 m0, s6, 0x18000
	s_nop 0
	global_load_lds_dwordx4 v[128:129], off
	s_add_i32 m0, s7, 0x18000
	s_nop 0
	global_load_lds_dwordx4 v[130:131], off
	s_add_i32 m0, s36, 0x18000
	s_nop 0
	global_load_lds_dwordx4 v[146:147], off
	s_add_i32 m0, s38, 0x18000
	s_nop 0
	global_load_lds_dwordx4 v[148:149], off
	v_lshlrev_b32_e32 v135, 16, v236
	v_and_b32_e32 v137, 0xffff0000, v236
	v_mul_f32_e32 v135, v144, v135
	v_mul_f32_e32 v137, v144, v137
	v_cvt_pk_bf16_f32 v128, v135, v137
	v_lshlrev_b32_e32 v135, 16, v237
	v_and_b32_e32 v137, 0xffff0000, v237
	v_mul_f32_e32 v135, v144, v135
	v_mul_f32_e32 v137, v144, v137
	v_cvt_pk_bf16_f32 v129, v135, v137
	v_lshlrev_b32_e32 v135, 16, v238
	v_and_b32_e32 v137, 0xffff0000, v238
	v_mul_f32_e32 v135, v144, v135
	v_mul_f32_e32 v137, v144, v137
	v_cvt_pk_bf16_f32 v130, v135, v137
	v_lshlrev_b32_e32 v135, 16, v239
	v_and_b32_e32 v137, 0xffff0000, v239
	v_mul_f32_e32 v135, v144, v135
	v_mul_f32_e32 v137, v144, v137
	v_cvt_pk_bf16_f32 v131, v135, v137
	v_lshlrev_b32_e32 v135, 16, v240
	v_and_b32_e32 v137, 0xffff0000, v240
	v_mul_f32_e32 v135, v144, v135
	v_mul_f32_e32 v137, v144, v137
	v_cvt_pk_bf16_f32 v146, v135, v137
	v_lshlrev_b32_e32 v135, 16, v241
	v_and_b32_e32 v137, 0xffff0000, v241
	v_mul_f32_e32 v135, v144, v135
	v_mul_f32_e32 v137, v144, v137
	v_cvt_pk_bf16_f32 v147, v135, v137
	v_lshlrev_b32_e32 v135, 16, v242
	v_and_b32_e32 v137, 0xffff0000, v242
	v_mul_f32_e32 v135, v144, v135
	v_mul_f32_e32 v137, v144, v137
	v_cvt_pk_bf16_f32 v148, v135, v137
	v_lshlrev_b32_e32 v135, 16, v243
	v_and_b32_e32 v137, 0xffff0000, v243
	v_mul_f32_e32 v135, v144, v135
	v_mul_f32_e32 v137, v144, v137
	v_cvt_pk_bf16_f32 v149, v135, v137
	v_mov_b32_e32 v133, v175
	ds_read_b64_tr_b16 v[150:151], v133 offset:0
	v_mov_b32_e32 v135, v181
	ds_read_b64_tr_b16 v[152:153], v135 offset:0
	ds_read_b64_tr_b16 v[182:183], v133 offset:0x200
	ds_read_b64_tr_b16 v[184:185], v135 offset:0x200
	ds_read_b64_tr_b16 v[186:187], v133 offset:0x400
	ds_read_b64_tr_b16 v[188:189], v135 offset:0x400
	ds_read_b64_tr_b16 v[190:191], v133 offset:0x600
	ds_read_b64_tr_b16 v[192:193], v135 offset:0x600
	s_waitcnt lgkmcnt(0)
	s_nop 0
	v_mfma_f32_32x32x16_bf16 v[16:31], v[128:131], v[150:153], v[16:31]
	ds_read_b64_tr_b16 v[150:151], v133 offset:0x1000
	ds_read_b64_tr_b16 v[152:153], v135 offset:0x1000
	v_mfma_f32_32x32x16_bf16 v[0:15], v[128:131], v[182:185], v[0:15]
	ds_read_b64_tr_b16 v[182:183], v133 offset:0x1200
	ds_read_b64_tr_b16 v[184:185], v135 offset:0x1200
	v_mfma_f32_32x32x16_bf16 v[32:47], v[128:131], v[186:189], v[32:47]
	ds_read_b64_tr_b16 v[186:187], v133 offset:0x1400
	ds_read_b64_tr_b16 v[188:189], v135 offset:0x1400
	ds_read_b64_tr_b16 v[194:195], v133 offset:0x1600
	ds_read_b64_tr_b16 v[196:197], v135 offset:0x1600
	s_waitcnt lgkmcnt(0)
	v_mfma_f32_32x32x16_bf16 v[48:63], v[128:131], v[190:193], v[48:63]
	v_mfma_f32_32x32x16_bf16 v[16:31], v[146:149], v[150:153], v[16:31]
	v_add_u32_e32 v133, 0x2000, v133
	ds_read_b64_tr_b16 v[150:151], v133 offset:0
	v_add_u32_e32 v135, 0x2000, v135
	ds_read_b64_tr_b16 v[152:153], v135 offset:0
	v_mfma_f32_32x32x16_bf16 v[0:15], v[146:149], v[182:185], v[0:15]
	ds_read_b64_tr_b16 v[182:183], v133 offset:0x200
	ds_read_b64_tr_b16 v[184:185], v135 offset:0x200
	v_mfma_f32_32x32x16_bf16 v[32:47], v[146:149], v[186:189], v[32:47]
	ds_read_b64_tr_b16 v[186:187], v133 offset:0x400
	ds_read_b64_tr_b16 v[188:189], v135 offset:0x400
	ds_read_b64_tr_b16 v[190:191], v133 offset:0x600
	ds_read_b64_tr_b16 v[192:193], v135 offset:0x600
	s_waitcnt lgkmcnt(0)
	v_mfma_f32_32x32x16_bf16 v[48:63], v[146:149], v[194:197], v[48:63]
	v_mfma_f32_32x32x16_bf16 v[96:111], v[128:131], v[150:153], v[96:111]
	ds_read_b64_tr_b16 v[150:151], v133 offset:0x1000
	ds_read_b64_tr_b16 v[152:153], v135 offset:0x1000
	v_mfma_f32_32x32x16_bf16 v[112:127], v[128:131], v[182:185], v[112:127]
	ds_read_b64_tr_b16 v[182:183], v133 offset:0x1200
	ds_read_b64_tr_b16 v[184:185], v135 offset:0x1200
	v_mfma_f32_32x32x16_bf16 v[80:95], v[128:131], v[186:189], v[80:95]
	ds_read_b64_tr_b16 v[186:187], v133 offset:0x1400
	ds_read_b64_tr_b16 v[188:189], v135 offset:0x1400
	ds_read_b64_tr_b16 v[194:195], v133 offset:0x1600
	ds_read_b64_tr_b16 v[196:197], v135 offset:0x1600
	s_waitcnt lgkmcnt(0)
	v_mfma_f32_32x32x16_bf16 v[64:79], v[128:131], v[190:193], v[64:79]
	v_mfma_f32_32x32x16_bf16 v[96:111], v[146:149], v[150:153], v[96:111]
	v_mfma_f32_32x32x16_bf16 v[112:127], v[146:149], v[182:185], v[112:127]
	v_mfma_f32_32x32x16_bf16 v[80:95], v[146:149], v[186:189], v[80:95]
	v_mfma_f32_32x32x16_bf16 v[64:79], v[146:149], v[194:197], v[64:79]
	s_waitcnt vmcnt(4) lgkmcnt(0)
	s_barrier
; #define VM_WAIT() asm volatile("s_waitcnt vmcnt(0)" ::: "memory")
; template <int DK, int DV, bool MLSTM>
; __device__ __forceinline__ void out_unit2(LAS unsigned char* lds, LAS unsigned char* ldstab, const OutArgs a, const int wv) {
;     ...
;     for (int pc = 4; pc < 4 + 2 * NCP; ++pc) {
;         VM_WAIT(); __syncthreads();
;         if (pc + 1 < 4 + 2 * NCP) OUT_DMA(pc + 1);
;         const int cq = pc - 4, dirb = cq >= NCP, cp = dirb ? cq - NCP : cq;
;         const float qs = dirb ? qsb : qsf;
;         const unsigned qa = QP + (cp >> 2) * 32768u + 512u * (cp & 3) + 8192u * rb;
;         const bf16x8 af0 = scale_frag(lds_r128(qa + rb0), qs), af1 = scale_frag(lds_r128(qa + rb1), qs);
;         OUT_MMA(pc & 1);
;     }
	s_add_u32 s40, s11, 0x18000
	s_addc_u32 s41, s12, 0
	v_lshl_add_u64 v[128:129], s[40:41], 0, v[198:199]
	v_lshl_add_u64 v[130:131], s[40:41], 0, v[200:201]
	v_lshl_add_u64 v[146:147], s[40:41], 0, v[202:203]
	v_lshl_add_u64 v[148:149], s[40:41], 0, v[204:205]
	s_mov_b32 m0, s6
	s_nop 0
	global_load_lds_dwordx4 v[128:129], off
	s_mov_b32 m0, s7
	s_nop 0
	global_load_lds_dwordx4 v[130:131], off
	s_mov_b32 m0, s36
	s_nop 0
	global_load_lds_dwordx4 v[146:147], off
	s_mov_b32 m0, s38
	s_nop 0
	global_load_lds_dwordx4 v[148:149], off
	v_lshlrev_b32_e32 v135, 16, v244
	v_and_b32_e32 v137, 0xffff0000, v244
	v_mul_f32_e32 v135, v144, v135
	v_mul_f32_e32 v137, v144, v137
	v_cvt_pk_bf16_f32 v128, v135, v137
	v_lshlrev_b32_e32 v135, 16, v245
	v_and_b32_e32 v137, 0xffff0000, v245
	v_mul_f32_e32 v135, v144, v135
	v_mul_f32_e32 v137, v144, v137
	v_cvt_pk_bf16_f32 v129, v135, v137
	v_lshlrev_b32_e32 v135, 16, v246
	v_and_b32_e32 v137, 0xffff0000, v246
	v_mul_f32_e32 v135, v144, v135
	v_mul_f32_e32 v137, v144, v137
	v_cvt_pk_bf16_f32 v130, v135, v137
	v_lshlrev_b32_e32 v135, 16, v247
	v_and_b32_e32 v137, 0xffff0000, v247
	v_mul_f32_e32 v135, v144, v135
	v_mul_f32_e32 v137, v144, v137
	v_cvt_pk_bf16_f32 v131, v135, v137
	v_lshlrev_b32_e32 v135, 16, v248
	v_and_b32_e32 v137, 0xffff0000, v248
	v_mul_f32_e32 v135, v144, v135
	v_mul_f32_e32 v137, v144, v137
	v_cvt_pk_bf16_f32 v146, v135, v137
	v_lshlrev_b32_e32 v135, 16, v249
	v_and_b32_e32 v137, 0xffff0000, v249
	v_mul_f32_e32 v135, v144, v135
	v_mul_f32_e32 v137, v144, v137
	v_cvt_pk_bf16_f32 v147, v135, v137
	v_lshlrev_b32_e32 v135, 16, v250
	v_and_b32_e32 v137, 0xffff0000, v250
	v_mul_f32_e32 v135, v144, v135
	v_mul_f32_e32 v137, v144, v137
	v_cvt_pk_bf16_f32 v148, v135, v137
	v_lshlrev_b32_e32 v135, 16, v251
	v_and_b32_e32 v137, 0xffff0000, v251
	v_mul_f32_e32 v135, v144, v135
	v_mul_f32_e32 v137, v144, v137
	v_cvt_pk_bf16_f32 v149, v135, v137
	v_add_u32_e32 v133, 0x10000, v175
	ds_read_b64_tr_b16 v[150:151], v133 offset:0
	v_add_u32_e32 v135, 0x10000, v181
	ds_read_b64_tr_b16 v[152:153], v135 offset:0
	ds_read_b64_tr_b16 v[182:183], v133 offset:0x200
	ds_read_b64_tr_b16 v[184:185], v135 offset:0x200
	ds_read_b64_tr_b16 v[186:187], v133 offset:0x400
	ds_read_b64_tr_b16 v[188:189], v135 offset:0x400
	ds_read_b64_tr_b16 v[190:191], v133 offset:0x600
	ds_read_b64_tr_b16 v[192:193], v135 offset:0x600
	s_waitcnt lgkmcnt(0)
	s_nop 0
	v_mfma_f32_32x32x16_bf16 v[16:31], v[128:131], v[150:153], v[16:31]
	ds_read_b64_tr_b16 v[150:151], v133 offset:0x1000
	ds_read_b64_tr_b16 v[152:153], v135 offset:0x1000
	v_mfma_f32_32x32x16_bf16 v[0:15], v[128:131], v[182:185], v[0:15]
	ds_read_b64_tr_b16 v[182:183], v133 offset:0x1200
	ds_read_b64_tr_b16 v[184:185], v135 offset:0x1200
	v_mfma_f32_32x32x16_bf16 v[32:47], v[128:131], v[186:189], v[32:47]
	ds_read_b64_tr_b16 v[186:187], v133 offset:0x1400
	ds_read_b64_tr_b16 v[188:189], v135 offset:0x1400
	ds_read_b64_tr_b16 v[194:195], v133 offset:0x1600
	ds_read_b64_tr_b16 v[196:197], v135 offset:0x1600
	s_waitcnt lgkmcnt(0)
	v_mfma_f32_32x32x16_bf16 v[48:63], v[128:131], v[190:193], v[48:63]
	v_mfma_f32_32x32x16_bf16 v[16:31], v[146:149], v[150:153], v[16:31]
	v_add_u32_e32 v133, 0x2000, v133
	ds_read_b64_tr_b16 v[150:151], v133 offset:0
	v_add_u32_e32 v135, 0x2000, v135
	ds_read_b64_tr_b16 v[152:153], v135 offset:0
	v_mfma_f32_32x32x16_bf16 v[0:15], v[146:149], v[182:185], v[0:15]
	ds_read_b64_tr_b16 v[182:183], v133 offset:0x200
	ds_read_b64_tr_b16 v[184:185], v135 offset:0x200
	v_mfma_f32_32x32x16_bf16 v[32:47], v[146:149], v[186:189], v[32:47]
	ds_read_b64_tr_b16 v[186:187], v133 offset:0x400
	ds_read_b64_tr_b16 v[188:189], v135 offset:0x400
	ds_read_b64_tr_b16 v[190:191], v133 offset:0x600
	ds_read_b64_tr_b16 v[192:193], v135 offset:0x600
	s_waitcnt lgkmcnt(0)
	v_mfma_f32_32x32x16_bf16 v[48:63], v[146:149], v[194:197], v[48:63]
	v_mfma_f32_32x32x16_bf16 v[96:111], v[128:131], v[150:153], v[96:111]
	ds_read_b64_tr_b16 v[150:151], v133 offset:0x1000
	ds_read_b64_tr_b16 v[152:153], v135 offset:0x1000
	v_mfma_f32_32x32x16_bf16 v[112:127], v[128:131], v[182:185], v[112:127]
	ds_read_b64_tr_b16 v[182:183], v133 offset:0x1200
	ds_read_b64_tr_b16 v[184:185], v135 offset:0x1200
	v_mfma_f32_32x32x16_bf16 v[80:95], v[128:131], v[186:189], v[80:95]
	ds_read_b64_tr_b16 v[186:187], v133 offset:0x1400
	ds_read_b64_tr_b16 v[188:189], v135 offset:0x1400
	ds_read_b64_tr_b16 v[194:195], v133 offset:0x1600
	ds_read_b64_tr_b16 v[196:197], v135 offset:0x1600
	s_waitcnt lgkmcnt(0)
	v_mfma_f32_32x32x16_bf16 v[64:79], v[128:131], v[190:193], v[64:79]
	v_mfma_f32_32x32x16_bf16 v[96:111], v[146:149], v[150:153], v[96:111]
	v_mfma_f32_32x32x16_bf16 v[112:127], v[146:149], v[182:185], v[112:127]
	v_mfma_f32_32x32x16_bf16 v[80:95], v[146:149], v[186:189], v[80:95]
	v_mfma_f32_32x32x16_bf16 v[64:79], v[146:149], v[194:197], v[64:79]
	s_waitcnt vmcnt(4) lgkmcnt(0)
	s_barrier
; #define VM_WAIT() asm volatile("s_waitcnt vmcnt(0)" ::: "memory")
; template <int DK, int DV, bool MLSTM>
; __device__ __forceinline__ void out_unit2(LAS unsigned char* lds, LAS unsigned char* ldstab, const OutArgs a, const int wv) {
;     ...
;     for (int pc = 4; pc < 4 + 2 * NCP; ++pc) {
;         VM_WAIT(); __syncthreads();
;         if (pc + 1 < 4 + 2 * NCP) OUT_DMA(pc + 1);
;         const int cq = pc - 4, dirb = cq >= NCP, cp = dirb ? cq - NCP : cq;
;         const float qs = dirb ? qsb : qsf;
;         const unsigned qa = QP + (cp >> 2) * 32768u + 512u * (cp & 3) + 8192u * rb;
;         const bf16x8 af0 = scale_frag(lds_r128(qa + rb0), qs), af1 = scale_frag(lds_r128(qa + rb1), qs);
;         OUT_MMA(pc & 1);
;     }
	s_add_u32 s40, s11, 0x20000
	s_addc_u32 s41, s12, 0
	v_lshl_add_u64 v[128:129], s[40:41], 0, v[198:199]
	v_lshl_add_u64 v[130:131], s[40:41], 0, v[200:201]
	v_lshl_add_u64 v[146:147], s[40:41], 0, v[202:203]
	v_lshl_add_u64 v[148:149], s[40:41], 0, v[204:205]
	s_add_i32 m0, s6, 0x10000
	s_nop 0
	global_load_lds_dwordx4 v[128:129], off
	s_add_i32 m0, s7, 0x10000
	s_nop 0
	global_load_lds_dwordx4 v[130:131], off
	s_add_i32 m0, s36, 0x10000
	s_nop 0
	global_load_lds_dwordx4 v[146:147], off
	s_add_i32 m0, s38, 0x10000
	s_nop 0
	global_load_lds_dwordx4 v[148:149], off
	v_lshlrev_b32_e32 v135, 16, v252
	v_and_b32_e32 v137, 0xffff0000, v252
	v_mul_f32_e32 v135, v144, v135
	v_mul_f32_e32 v137, v144, v137
	v_cvt_pk_bf16_f32 v128, v135, v137
	v_lshlrev_b32_e32 v135, 16, v253
	v_and_b32_e32 v137, 0xffff0000, v253
	v_mul_f32_e32 v135, v144, v135
	v_mul_f32_e32 v137, v144, v137
	v_cvt_pk_bf16_f32 v129, v135, v137
	v_lshlrev_b32_e32 v135, 16, v254
	v_and_b32_e32 v137, 0xffff0000, v254
	v_mul_f32_e32 v135, v144, v135
	v_mul_f32_e32 v137, v144, v137
	v_cvt_pk_bf16_f32 v130, v135, v137
	v_lshlrev_b32_e32 v135, 16, v255
	v_and_b32_e32 v137, 0xffff0000, v255
	v_mul_f32_e32 v135, v144, v135
	v_mul_f32_e32 v137, v144, v137
	v_cvt_pk_bf16_f32 v131, v135, v137
	v_lshlrev_b32_e32 v135, 16, v218
	v_and_b32_e32 v137, 0xffff0000, v218
	v_mul_f32_e32 v135, v144, v135
	v_mul_f32_e32 v137, v144, v137
	v_cvt_pk_bf16_f32 v146, v135, v137
	v_lshlrev_b32_e32 v135, 16, v219
	v_and_b32_e32 v137, 0xffff0000, v219
	v_mul_f32_e32 v135, v144, v135
	v_mul_f32_e32 v137, v144, v137
	v_cvt_pk_bf16_f32 v147, v135, v137
	v_lshlrev_b32_e32 v135, 16, v220
	v_and_b32_e32 v137, 0xffff0000, v220
	v_mul_f32_e32 v135, v144, v135
	v_mul_f32_e32 v137, v144, v137
	v_cvt_pk_bf16_f32 v148, v135, v137
	v_lshlrev_b32_e32 v135, 16, v221
	v_and_b32_e32 v137, 0xffff0000, v221
	v_mul_f32_e32 v135, v144, v135
	v_mul_f32_e32 v137, v144, v137
	v_cvt_pk_bf16_f32 v149, v135, v137
	v_add_u32_e32 v133, 0x18000, v175
	ds_read_b64_tr_b16 v[150:151], v133 offset:0
	v_add_u32_e32 v135, 0x18000, v181
	ds_read_b64_tr_b16 v[152:153], v135 offset:0
	ds_read_b64_tr_b16 v[182:183], v133 offset:0x200
	ds_read_b64_tr_b16 v[184:185], v135 offset:0x200
	ds_read_b64_tr_b16 v[186:187], v133 offset:0x400
	ds_read_b64_tr_b16 v[188:189], v135 offset:0x400
	ds_read_b64_tr_b16 v[190:191], v133 offset:0x600
	ds_read_b64_tr_b16 v[192:193], v135 offset:0x600
	s_waitcnt lgkmcnt(0)
	s_nop 0
	v_mfma_f32_32x32x16_bf16 v[16:31], v[128:131], v[150:153], v[16:31]
	ds_read_b64_tr_b16 v[150:151], v133 offset:0x1000
	ds_read_b64_tr_b16 v[152:153], v135 offset:0x1000
	v_mfma_f32_32x32x16_bf16 v[0:15], v[128:131], v[182:185], v[0:15]
	ds_read_b64_tr_b16 v[182:183], v133 offset:0x1200
	ds_read_b64_tr_b16 v[184:185], v135 offset:0x1200
	v_mfma_f32_32x32x16_bf16 v[32:47], v[128:131], v[186:189], v[32:47]
	ds_read_b64_tr_b16 v[186:187], v133 offset:0x1400
	ds_read_b64_tr_b16 v[188:189], v135 offset:0x1400
	ds_read_b64_tr_b16 v[194:195], v133 offset:0x1600
	ds_read_b64_tr_b16 v[196:197], v135 offset:0x1600
	s_waitcnt lgkmcnt(0)
	v_mfma_f32_32x32x16_bf16 v[48:63], v[128:131], v[190:193], v[48:63]
	v_mfma_f32_32x32x16_bf16 v[16:31], v[146:149], v[150:153], v[16:31]
	v_add_u32_e32 v133, 0x2000, v133
	ds_read_b64_tr_b16 v[150:151], v133 offset:0
	v_add_u32_e32 v135, 0x2000, v135
	ds_read_b64_tr_b16 v[152:153], v135 offset:0
	v_mfma_f32_32x32x16_bf16 v[0:15], v[146:149], v[182:185], v[0:15]
	ds_read_b64_tr_b16 v[182:183], v133 offset:0x200
	ds_read_b64_tr_b16 v[184:185], v135 offset:0x200
	v_mfma_f32_32x32x16_bf16 v[32:47], v[146:149], v[186:189], v[32:47]
	ds_read_b64_tr_b16 v[186:187], v133 offset:0x400
	ds_read_b64_tr_b16 v[188:189], v135 offset:0x400
	ds_read_b64_tr_b16 v[190:191], v133 offset:0x600
	ds_read_b64_tr_b16 v[192:193], v135 offset:0x600
	s_waitcnt lgkmcnt(0)
	v_mfma_f32_32x32x16_bf16 v[48:63], v[146:149], v[194:197], v[48:63]
	v_mfma_f32_32x32x16_bf16 v[96:111], v[128:131], v[150:153], v[96:111]
	ds_read_b64_tr_b16 v[150:151], v133 offset:0x1000
	ds_read_b64_tr_b16 v[152:153], v135 offset:0x1000
	v_mfma_f32_32x32x16_bf16 v[112:127], v[128:131], v[182:185], v[112:127]
	ds_read_b64_tr_b16 v[182:183], v133 offset:0x1200
	ds_read_b64_tr_b16 v[184:185], v135 offset:0x1200
	v_mfma_f32_32x32x16_bf16 v[80:95], v[128:131], v[186:189], v[80:95]
	ds_read_b64_tr_b16 v[186:187], v133 offset:0x1400
	ds_read_b64_tr_b16 v[188:189], v135 offset:0x1400
	ds_read_b64_tr_b16 v[194:195], v133 offset:0x1600
	ds_read_b64_tr_b16 v[196:197], v135 offset:0x1600
	s_waitcnt lgkmcnt(0)
	v_mfma_f32_32x32x16_bf16 v[64:79], v[128:131], v[190:193], v[64:79]
	v_mfma_f32_32x32x16_bf16 v[96:111], v[146:149], v[150:153], v[96:111]
	v_mfma_f32_32x32x16_bf16 v[112:127], v[146:149], v[182:185], v[112:127]
	v_mfma_f32_32x32x16_bf16 v[80:95], v[146:149], v[186:189], v[80:95]
	v_mfma_f32_32x32x16_bf16 v[64:79], v[146:149], v[194:197], v[64:79]
	s_waitcnt vmcnt(4) lgkmcnt(0)
	s_barrier
; #define VM_WAIT() asm volatile("s_waitcnt vmcnt(0)" ::: "memory")
; template <int DK, int DV, bool MLSTM>
; __device__ __forceinline__ void out_unit2(LAS unsigned char* lds, LAS unsigned char* ldstab, const OutArgs a, const int wv) {
;     ...
;     for (int pc = 4; pc < 4 + 2 * NCP; ++pc) {
;         VM_WAIT(); __syncthreads();
;         if (pc + 1 < 4 + 2 * NCP) OUT_DMA(pc + 1);
;         const int cq = pc - 4, dirb = cq >= NCP, cp = dirb ? cq - NCP : cq;
;         const float qs = dirb ? qsb : qsf;
;         const unsigned qa = QP + (cp >> 2) * 32768u + 512u * (cp & 3) + 8192u * rb;
;         const bf16x8 af0 = scale_frag(lds_r128(qa + rb0), qs), af1 = scale_frag(lds_r128(qa + rb1), qs);
;         OUT_MMA(pc & 1);
;     }
	s_add_u32 s40, s11, 0x28000
	s_addc_u32 s41, s12, 0
	v_lshl_add_u64 v[128:129], s[40:41], 0, v[198:199]
	v_lshl_add_u64 v[130:131], s[40:41], 0, v[200:201]
	v_lshl_add_u64 v[146:147], s[40:41], 0, v[202:203]
	v_lshl_add_u64 v[148:149], s[40:41], 0, v[204:205]
	s_add_i32 m0, s6, 0x18000
	s_nop 0
	global_load_lds_dwordx4 v[128:129], off
	s_add_i32 m0, s7, 0x18000
	s_nop 0
	global_load_lds_dwordx4 v[130:131], off
	s_add_i32 m0, s36, 0x18000
	s_nop 0
	global_load_lds_dwordx4 v[146:147], off
	s_add_i32 m0, s38, 0x18000
	s_nop 0
	global_load_lds_dwordx4 v[148:149], off
	v_lshlrev_b32_e32 v135, 16, v222
	v_and_b32_e32 v137, 0xffff0000, v222
	v_mul_f32_e32 v135, v144, v135
	v_mul_f32_e32 v137, v144, v137
	v_cvt_pk_bf16_f32 v128, v135, v137
	v_lshlrev_b32_e32 v135, 16, v223
	v_and_b32_e32 v137, 0xffff0000, v223
	v_mul_f32_e32 v135, v144, v135
	v_mul_f32_e32 v137, v144, v137
	v_cvt_pk_bf16_f32 v129, v135, v137
	v_lshlrev_b32_e32 v135, 16, v224
	v_and_b32_e32 v137, 0xffff0000, v224
	v_mul_f32_e32 v135, v144, v135
	v_mul_f32_e32 v137, v144, v137
	v_cvt_pk_bf16_f32 v130, v135, v137
	v_lshlrev_b32_e32 v135, 16, v225
	v_and_b32_e32 v137, 0xffff0000, v225
	v_mul_f32_e32 v135, v144, v135
	v_mul_f32_e32 v137, v144, v137
	v_cvt_pk_bf16_f32 v131, v135, v137
	v_lshlrev_b32_e32 v135, 16, v206
	v_and_b32_e32 v137, 0xffff0000, v206
	v_mul_f32_e32 v135, v144, v135
	v_mul_f32_e32 v137, v144, v137
	v_cvt_pk_bf16_f32 v146, v135, v137
	v_lshlrev_b32_e32 v135, 16, v207
	v_and_b32_e32 v137, 0xffff0000, v207
	v_mul_f32_e32 v135, v144, v135
	v_mul_f32_e32 v137, v144, v137
	v_cvt_pk_bf16_f32 v147, v135, v137
	v_lshlrev_b32_e32 v135, 16, v208
	v_and_b32_e32 v137, 0xffff0000, v208
	v_mul_f32_e32 v135, v144, v135
	v_mul_f32_e32 v137, v144, v137
	v_cvt_pk_bf16_f32 v148, v135, v137
	v_lshlrev_b32_e32 v135, 16, v209
	v_and_b32_e32 v137, 0xffff0000, v209
	v_mul_f32_e32 v135, v144, v135
	v_mul_f32_e32 v137, v144, v137
	v_cvt_pk_bf16_f32 v149, v135, v137
	v_mov_b32_e32 v133, v175
	ds_read_b64_tr_b16 v[150:151], v133 offset:0
	v_mov_b32_e32 v135, v181
	ds_read_b64_tr_b16 v[152:153], v135 offset:0
	ds_read_b64_tr_b16 v[182:183], v133 offset:0x200
	ds_read_b64_tr_b16 v[184:185], v135 offset:0x200
	ds_read_b64_tr_b16 v[186:187], v133 offset:0x400
	ds_read_b64_tr_b16 v[188:189], v135 offset:0x400
	ds_read_b64_tr_b16 v[190:191], v133 offset:0x600
	ds_read_b64_tr_b16 v[192:193], v135 offset:0x600
	s_waitcnt lgkmcnt(0)
	s_nop 0
	v_mfma_f32_32x32x16_bf16 v[16:31], v[128:131], v[150:153], v[16:31]
	ds_read_b64_tr_b16 v[150:151], v133 offset:0x1000
	ds_read_b64_tr_b16 v[152:153], v135 offset:0x1000
	v_mfma_f32_32x32x16_bf16 v[0:15], v[128:131], v[182:185], v[0:15]
	ds_read_b64_tr_b16 v[182:183], v133 offset:0x1200
	ds_read_b64_tr_b16 v[184:185], v135 offset:0x1200
	v_mfma_f32_32x32x16_bf16 v[32:47], v[128:131], v[186:189], v[32:47]
	ds_read_b64_tr_b16 v[186:187], v133 offset:0x1400
	ds_read_b64_tr_b16 v[188:189], v135 offset:0x1400
	ds_read_b64_tr_b16 v[194:195], v133 offset:0x1600
	ds_read_b64_tr_b16 v[196:197], v135 offset:0x1600
	s_waitcnt lgkmcnt(0)
	v_mfma_f32_32x32x16_bf16 v[48:63], v[128:131], v[190:193], v[48:63]
	v_mfma_f32_32x32x16_bf16 v[16:31], v[146:149], v[150:153], v[16:31]
	v_add_u32_e32 v133, 0x2000, v133
	ds_read_b64_tr_b16 v[150:151], v133 offset:0
	v_add_u32_e32 v135, 0x2000, v135
	ds_read_b64_tr_b16 v[152:153], v135 offset:0
	v_mfma_f32_32x32x16_bf16 v[0:15], v[146:149], v[182:185], v[0:15]
	ds_read_b64_tr_b16 v[182:183], v133 offset:0x200
	ds_read_b64_tr_b16 v[184:185], v135 offset:0x200
	v_mfma_f32_32x32x16_bf16 v[32:47], v[146:149], v[186:189], v[32:47]
	ds_read_b64_tr_b16 v[186:187], v133 offset:0x400
	ds_read_b64_tr_b16 v[188:189], v135 offset:0x400
	ds_read_b64_tr_b16 v[190:191], v133 offset:0x600
	ds_read_b64_tr_b16 v[192:193], v135 offset:0x600
	s_waitcnt lgkmcnt(0)
	v_mfma_f32_32x32x16_bf16 v[48:63], v[146:149], v[194:197], v[48:63]
	v_mfma_f32_32x32x16_bf16 v[96:111], v[128:131], v[150:153], v[96:111]
	ds_read_b64_tr_b16 v[150:151], v133 offset:0x1000
	ds_read_b64_tr_b16 v[152:153], v135 offset:0x1000
	v_mfma_f32_32x32x16_bf16 v[112:127], v[128:131], v[182:185], v[112:127]
	ds_read_b64_tr_b16 v[182:183], v133 offset:0x1200
	ds_read_b64_tr_b16 v[184:185], v135 offset:0x1200
	v_mfma_f32_32x32x16_bf16 v[80:95], v[128:131], v[186:189], v[80:95]
	ds_read_b64_tr_b16 v[186:187], v133 offset:0x1400
	ds_read_b64_tr_b16 v[188:189], v135 offset:0x1400
	ds_read_b64_tr_b16 v[194:195], v133 offset:0x1600
	ds_read_b64_tr_b16 v[196:197], v135 offset:0x1600
	s_waitcnt lgkmcnt(0)
	v_mfma_f32_32x32x16_bf16 v[64:79], v[128:131], v[190:193], v[64:79]
	v_mfma_f32_32x32x16_bf16 v[96:111], v[146:149], v[150:153], v[96:111]
	v_mfma_f32_32x32x16_bf16 v[112:127], v[146:149], v[182:185], v[112:127]
	v_mfma_f32_32x32x16_bf16 v[80:95], v[146:149], v[186:189], v[80:95]
	v_mfma_f32_32x32x16_bf16 v[64:79], v[146:149], v[194:197], v[64:79]
	s_waitcnt vmcnt(4) lgkmcnt(0)
	s_barrier
; #define VM_WAIT() asm volatile("s_waitcnt vmcnt(0)" ::: "memory")
; template <int DK, int DV, bool MLSTM>
; __device__ __forceinline__ void out_unit2(LAS unsigned char* lds, LAS unsigned char* ldstab, const OutArgs a, const int wv) {
;     ...
;     for (int pc = 4; pc < 4 + 2 * NCP; ++pc) {
;         VM_WAIT(); __syncthreads();
;         if (pc + 1 < 4 + 2 * NCP) OUT_DMA(pc + 1);
;         const int cq = pc - 4, dirb = cq >= NCP, cp = dirb ? cq - NCP : cq;
;         const float qs = dirb ? qsb : qsf;
;         const unsigned qa = QP + (cp >> 2) * 32768u + 512u * (cp & 3) + 8192u * rb;
;         const bf16x8 af0 = scale_frag(lds_r128(qa + rb0), qs), af1 = scale_frag(lds_r128(qa + rb1), qs);
;         OUT_MMA(pc & 1);
;     }
	s_add_u32 s40, s11, 0x30000
	s_addc_u32 s41, s12, 0
	v_lshl_add_u64 v[128:129], s[40:41], 0, v[198:199]
	v_lshl_add_u64 v[130:131], s[40:41], 0, v[200:201]
	v_lshl_add_u64 v[146:147], s[40:41], 0, v[202:203]
	v_lshl_add_u64 v[148:149], s[40:41], 0, v[204:205]
	s_mov_b32 m0, s6
	s_nop 0
	global_load_lds_dwordx4 v[128:129], off
	s_mov_b32 m0, s7
	s_nop 0
	global_load_lds_dwordx4 v[130:131], off
	s_mov_b32 m0, s36
	s_nop 0
	global_load_lds_dwordx4 v[146:147], off
	s_mov_b32 m0, s38
	s_nop 0
	global_load_lds_dwordx4 v[148:149], off
	v_add_u32_e32 v133, s13, v173
	v_add_u32_e32 v135, s13, v177
	ds_read_b128 v[128:131], v133 offset:32768
	ds_read_b128 v[146:149], v135 offset:32768
	s_waitcnt lgkmcnt(0)
	v_lshlrev_b32_e32 v135, 16, v128
	v_and_b32_e32 v137, 0xffff0000, v128
	v_mul_f32_e32 v135, v144, v135
	v_mul_f32_e32 v137, v144, v137
	v_cvt_pk_bf16_f32 v128, v135, v137
	v_lshlrev_b32_e32 v135, 16, v129
	v_and_b32_e32 v137, 0xffff0000, v129
	v_mul_f32_e32 v135, v144, v135
	v_mul_f32_e32 v137, v144, v137
	v_cvt_pk_bf16_f32 v129, v135, v137
	v_lshlrev_b32_e32 v135, 16, v130
	v_and_b32_e32 v137, 0xffff0000, v130
	v_mul_f32_e32 v135, v144, v135
	v_mul_f32_e32 v137, v144, v137
	v_cvt_pk_bf16_f32 v130, v135, v137
	v_lshlrev_b32_e32 v135, 16, v131
	v_and_b32_e32 v137, 0xffff0000, v131
	v_mul_f32_e32 v135, v144, v135
	v_mul_f32_e32 v137, v144, v137
	v_cvt_pk_bf16_f32 v131, v135, v137
	v_lshlrev_b32_e32 v135, 16, v146
	v_and_b32_e32 v137, 0xffff0000, v146
	v_mul_f32_e32 v135, v144, v135
	v_mul_f32_e32 v137, v144, v137
	v_cvt_pk_bf16_f32 v146, v135, v137
	v_lshlrev_b32_e32 v135, 16, v147
	v_and_b32_e32 v137, 0xffff0000, v147
	v_mul_f32_e32 v135, v144, v135
	v_mul_f32_e32 v137, v144, v137
	v_cvt_pk_bf16_f32 v147, v135, v137
	v_lshlrev_b32_e32 v135, 16, v148
	v_and_b32_e32 v137, 0xffff0000, v148
	v_mul_f32_e32 v135, v144, v135
	v_mul_f32_e32 v137, v144, v137
	v_cvt_pk_bf16_f32 v148, v135, v137
	v_lshlrev_b32_e32 v135, 16, v149
	v_and_b32_e32 v137, 0xffff0000, v149
	v_mul_f32_e32 v135, v144, v135
	v_mul_f32_e32 v137, v144, v137
	v_cvt_pk_bf16_f32 v149, v135, v137
	v_add_u32_e32 v133, 0x10000, v175
	ds_read_b64_tr_b16 v[150:151], v133 offset:0
	v_add_u32_e32 v135, 0x10000, v181
	ds_read_b64_tr_b16 v[152:153], v135 offset:0
	ds_read_b64_tr_b16 v[182:183], v133 offset:0x200
	ds_read_b64_tr_b16 v[184:185], v135 offset:0x200
	ds_read_b64_tr_b16 v[186:187], v133 offset:0x400
	ds_read_b64_tr_b16 v[188:189], v135 offset:0x400
	ds_read_b64_tr_b16 v[190:191], v133 offset:0x600
	ds_read_b64_tr_b16 v[192:193], v135 offset:0x600
	s_waitcnt lgkmcnt(0)
	s_nop 0
	v_mfma_f32_32x32x16_bf16 v[16:31], v[128:131], v[150:153], v[16:31]
	ds_read_b64_tr_b16 v[150:151], v133 offset:0x1000
	ds_read_b64_tr_b16 v[152:153], v135 offset:0x1000
	v_mfma_f32_32x32x16_bf16 v[0:15], v[128:131], v[182:185], v[0:15]
	ds_read_b64_tr_b16 v[182:183], v133 offset:0x1200
	ds_read_b64_tr_b16 v[184:185], v135 offset:0x1200
	v_mfma_f32_32x32x16_bf16 v[32:47], v[128:131], v[186:189], v[32:47]
	ds_read_b64_tr_b16 v[186:187], v133 offset:0x1400
	ds_read_b64_tr_b16 v[188:189], v135 offset:0x1400
	ds_read_b64_tr_b16 v[194:195], v133 offset:0x1600
	ds_read_b64_tr_b16 v[196:197], v135 offset:0x1600
	s_waitcnt lgkmcnt(0)
	v_mfma_f32_32x32x16_bf16 v[48:63], v[128:131], v[190:193], v[48:63]
	v_mfma_f32_32x32x16_bf16 v[16:31], v[146:149], v[150:153], v[16:31]
	v_add_u32_e32 v133, 0x2000, v133
	ds_read_b64_tr_b16 v[150:151], v133 offset:0
	v_add_u32_e32 v135, 0x2000, v135
	ds_read_b64_tr_b16 v[152:153], v135 offset:0
	v_mfma_f32_32x32x16_bf16 v[0:15], v[146:149], v[182:185], v[0:15]
	ds_read_b64_tr_b16 v[182:183], v133 offset:0x200
	ds_read_b64_tr_b16 v[184:185], v135 offset:0x200
	v_mfma_f32_32x32x16_bf16 v[32:47], v[146:149], v[186:189], v[32:47]
	ds_read_b64_tr_b16 v[186:187], v133 offset:0x400
	ds_read_b64_tr_b16 v[188:189], v135 offset:0x400
	ds_read_b64_tr_b16 v[190:191], v133 offset:0x600
	ds_read_b64_tr_b16 v[192:193], v135 offset:0x600
	s_waitcnt lgkmcnt(0)
	v_mfma_f32_32x32x16_bf16 v[48:63], v[146:149], v[194:197], v[48:63]
	v_mfma_f32_32x32x16_bf16 v[96:111], v[128:131], v[150:153], v[96:111]
	ds_read_b64_tr_b16 v[150:151], v133 offset:0x1000
	ds_read_b64_tr_b16 v[152:153], v135 offset:0x1000
	v_mfma_f32_32x32x16_bf16 v[112:127], v[128:131], v[182:185], v[112:127]
	ds_read_b64_tr_b16 v[182:183], v133 offset:0x1200
	ds_read_b64_tr_b16 v[184:185], v135 offset:0x1200
	v_mfma_f32_32x32x16_bf16 v[80:95], v[128:131], v[186:189], v[80:95]
	ds_read_b64_tr_b16 v[186:187], v133 offset:0x1400
	ds_read_b64_tr_b16 v[188:189], v135 offset:0x1400
	ds_read_b64_tr_b16 v[194:195], v133 offset:0x1600
	ds_read_b64_tr_b16 v[196:197], v135 offset:0x1600
	s_waitcnt lgkmcnt(0)
	v_mfma_f32_32x32x16_bf16 v[64:79], v[128:131], v[190:193], v[64:79]
	v_mfma_f32_32x32x16_bf16 v[96:111], v[146:149], v[150:153], v[96:111]
	v_mfma_f32_32x32x16_bf16 v[112:127], v[146:149], v[182:185], v[112:127]
	v_mfma_f32_32x32x16_bf16 v[80:95], v[146:149], v[186:189], v[80:95]
	v_mfma_f32_32x32x16_bf16 v[64:79], v[146:149], v[194:197], v[64:79]
	s_waitcnt vmcnt(4) lgkmcnt(0)
	s_barrier
; #define VM_WAIT() asm volatile("s_waitcnt vmcnt(0)" ::: "memory")
; template <int DK, int DV, bool MLSTM>
; __device__ __forceinline__ void out_unit2(LAS unsigned char* lds, LAS unsigned char* ldstab, const OutArgs a, const int wv) {
;     ...
;     for (int pc = 4; pc < 4 + 2 * NCP; ++pc) {
;         VM_WAIT(); __syncthreads();
;         if (pc + 1 < 4 + 2 * NCP) OUT_DMA(pc + 1);
;         const int cq = pc - 4, dirb = cq >= NCP, cp = dirb ? cq - NCP : cq;
;         const float qs = dirb ? qsb : qsf;
;         const unsigned qa = QP + (cp >> 2) * 32768u + 512u * (cp & 3) + 8192u * rb;
;         const bf16x8 af0 = scale_frag(lds_r128(qa + rb0), qs), af1 = scale_frag(lds_r128(qa + rb1), qs);
;         OUT_MMA(pc & 1);
;     }
	s_add_u32 s40, s11, 0x38000
	s_addc_u32 s41, s12, 0
	v_lshl_add_u64 v[128:129], s[40:41], 0, v[198:199]
	v_lshl_add_u64 v[130:131], s[40:41], 0, v[200:201]
	v_lshl_add_u64 v[146:147], s[40:41], 0, v[202:203]
	v_lshl_add_u64 v[148:149], s[40:41], 0, v[204:205]
	s_add_i32 m0, s6, 0x10000
	s_nop 0
	global_load_lds_dwordx4 v[128:129], off
	s_add_i32 m0, s7, 0x10000
	s_nop 0
	global_load_lds_dwordx4 v[130:131], off
	s_add_i32 m0, s36, 0x10000
	s_nop 0
	global_load_lds_dwordx4 v[146:147], off
	s_add_i32 m0, s38, 0x10000
	s_nop 0
	global_load_lds_dwordx4 v[148:149], off
	v_add_u32_e32 v133, s13, v173
	v_add_u32_e32 v135, s13, v177
	ds_read_b128 v[128:131], v133 offset:33280
	ds_read_b128 v[146:149], v135 offset:33280
	s_waitcnt lgkmcnt(0)
	v_lshlrev_b32_e32 v135, 16, v128
	v_and_b32_e32 v137, 0xffff0000, v128
	v_mul_f32_e32 v135, v144, v135
	v_mul_f32_e32 v137, v144, v137
	v_cvt_pk_bf16_f32 v128, v135, v137
	v_lshlrev_b32_e32 v135, 16, v129
	v_and_b32_e32 v137, 0xffff0000, v129
	v_mul_f32_e32 v135, v144, v135
	v_mul_f32_e32 v137, v144, v137
	v_cvt_pk_bf16_f32 v129, v135, v137
	v_lshlrev_b32_e32 v135, 16, v130
	v_and_b32_e32 v137, 0xffff0000, v130
	v_mul_f32_e32 v135, v144, v135
	v_mul_f32_e32 v137, v144, v137
	v_cvt_pk_bf16_f32 v130, v135, v137
	v_lshlrev_b32_e32 v135, 16, v131
	v_and_b32_e32 v137, 0xffff0000, v131
	v_mul_f32_e32 v135, v144, v135
	v_mul_f32_e32 v137, v144, v137
	v_cvt_pk_bf16_f32 v131, v135, v137
	v_lshlrev_b32_e32 v135, 16, v146
	v_and_b32_e32 v137, 0xffff0000, v146
	v_mul_f32_e32 v135, v144, v135
	v_mul_f32_e32 v137, v144, v137
	v_cvt_pk_bf16_f32 v146, v135, v137
	v_lshlrev_b32_e32 v135, 16, v147
	v_and_b32_e32 v137, 0xffff0000, v147
	v_mul_f32_e32 v135, v144, v135
	v_mul_f32_e32 v137, v144, v137
	v_cvt_pk_bf16_f32 v147, v135, v137
	v_lshlrev_b32_e32 v135, 16, v148
	v_and_b32_e32 v137, 0xffff0000, v148
	v_mul_f32_e32 v135, v144, v135
	v_mul_f32_e32 v137, v144, v137
	v_cvt_pk_bf16_f32 v148, v135, v137
	v_lshlrev_b32_e32 v135, 16, v149
	v_and_b32_e32 v137, 0xffff0000, v149
	v_mul_f32_e32 v135, v144, v135
	v_mul_f32_e32 v137, v144, v137
	v_cvt_pk_bf16_f32 v149, v135, v137
	v_add_u32_e32 v133, 0x18000, v175
	ds_read_b64_tr_b16 v[150:151], v133 offset:0
	v_add_u32_e32 v135, 0x18000, v181
	ds_read_b64_tr_b16 v[152:153], v135 offset:0
	ds_read_b64_tr_b16 v[182:183], v133 offset:0x200
	ds_read_b64_tr_b16 v[184:185], v135 offset:0x200
	ds_read_b64_tr_b16 v[186:187], v133 offset:0x400
	ds_read_b64_tr_b16 v[188:189], v135 offset:0x400
	ds_read_b64_tr_b16 v[190:191], v133 offset:0x600
	ds_read_b64_tr_b16 v[192:193], v135 offset:0x600
	s_waitcnt lgkmcnt(0)
	s_nop 0
	v_mfma_f32_32x32x16_bf16 v[16:31], v[128:131], v[150:153], v[16:31]
	ds_read_b64_tr_b16 v[150:151], v133 offset:0x1000
	ds_read_b64_tr_b16 v[152:153], v135 offset:0x1000
	v_mfma_f32_32x32x16_bf16 v[0:15], v[128:131], v[182:185], v[0:15]
	ds_read_b64_tr_b16 v[182:183], v133 offset:0x1200
	ds_read_b64_tr_b16 v[184:185], v135 offset:0x1200
	v_mfma_f32_32x32x16_bf16 v[32:47], v[128:131], v[186:189], v[32:47]
	ds_read_b64_tr_b16 v[186:187], v133 offset:0x1400
	ds_read_b64_tr_b16 v[188:189], v135 offset:0x1400
	ds_read_b64_tr_b16 v[194:195], v133 offset:0x1600
	ds_read_b64_tr_b16 v[196:197], v135 offset:0x1600
	s_waitcnt lgkmcnt(0)
	v_mfma_f32_32x32x16_bf16 v[48:63], v[128:131], v[190:193], v[48:63]
	v_mfma_f32_32x32x16_bf16 v[16:31], v[146:149], v[150:153], v[16:31]
	v_add_u32_e32 v133, 0x2000, v133
	ds_read_b64_tr_b16 v[150:151], v133 offset:0
	v_add_u32_e32 v135, 0x2000, v135
	ds_read_b64_tr_b16 v[152:153], v135 offset:0
	v_mfma_f32_32x32x16_bf16 v[0:15], v[146:149], v[182:185], v[0:15]
	ds_read_b64_tr_b16 v[182:183], v133 offset:0x200
	ds_read_b64_tr_b16 v[184:185], v135 offset:0x200
	v_mfma_f32_32x32x16_bf16 v[32:47], v[146:149], v[186:189], v[32:47]
	ds_read_b64_tr_b16 v[186:187], v133 offset:0x400
	ds_read_b64_tr_b16 v[188:189], v135 offset:0x400
	ds_read_b64_tr_b16 v[190:191], v133 offset:0x600
	ds_read_b64_tr_b16 v[192:193], v135 offset:0x600
	s_waitcnt lgkmcnt(0)
	v_mfma_f32_32x32x16_bf16 v[48:63], v[146:149], v[194:197], v[48:63]
	v_mfma_f32_32x32x16_bf16 v[96:111], v[128:131], v[150:153], v[96:111]
	ds_read_b64_tr_b16 v[150:151], v133 offset:0x1000
	ds_read_b64_tr_b16 v[152:153], v135 offset:0x1000
	v_mfma_f32_32x32x16_bf16 v[112:127], v[128:131], v[182:185], v[112:127]
	ds_read_b64_tr_b16 v[182:183], v133 offset:0x1200
	ds_read_b64_tr_b16 v[184:185], v135 offset:0x1200
	v_mfma_f32_32x32x16_bf16 v[80:95], v[128:131], v[186:189], v[80:95]
	ds_read_b64_tr_b16 v[186:187], v133 offset:0x1400
	ds_read_b64_tr_b16 v[188:189], v135 offset:0x1400
	ds_read_b64_tr_b16 v[194:195], v133 offset:0x1600
	ds_read_b64_tr_b16 v[196:197], v135 offset:0x1600
	s_waitcnt lgkmcnt(0)
	v_mfma_f32_32x32x16_bf16 v[64:79], v[128:131], v[190:193], v[64:79]
	v_mfma_f32_32x32x16_bf16 v[96:111], v[146:149], v[150:153], v[96:111]
	v_mfma_f32_32x32x16_bf16 v[112:127], v[146:149], v[182:185], v[112:127]
	v_mfma_f32_32x32x16_bf16 v[80:95], v[146:149], v[186:189], v[80:95]
	v_mfma_f32_32x32x16_bf16 v[64:79], v[146:149], v[194:197], v[64:79]
	s_waitcnt vmcnt(4) lgkmcnt(0)
	s_barrier
; #define VM_WAIT() asm volatile("s_waitcnt vmcnt(0)" ::: "memory")
; template <int DK, int DV, bool MLSTM>
; __device__ __forceinline__ void out_unit2(LAS unsigned char* lds, LAS unsigned char* ldstab, const OutArgs a, const int wv) {
;     ...
;     for (int pc = 4; pc < 4 + 2 * NCP; ++pc) {
;         VM_WAIT(); __syncthreads();
;         if (pc + 1 < 4 + 2 * NCP) OUT_DMA(pc + 1);
;         const int cq = pc - 4, dirb = cq >= NCP, cp = dirb ? cq - NCP : cq;
;         const float qs = dirb ? qsb : qsf;
;         const unsigned qa = QP + (cp >> 2) * 32768u + 512u * (cp & 3) + 8192u * rb;
;         const bf16x8 af0 = scale_frag(lds_r128(qa + rb0), qs), af1 = scale_frag(lds_r128(qa + rb1), qs);
;         OUT_MMA(pc & 1);
;     }
	v_add_u32_e32 v133, s13, v173
	v_add_u32_e32 v135, s13, v177
	ds_read_b128 v[128:131], v133 offset:33792
	ds_read_b128 v[146:149], v135 offset:33792
	s_waitcnt lgkmcnt(0)
	v_lshlrev_b32_e32 v135, 16, v128
	v_and_b32_e32 v137, 0xffff0000, v128
	v_mul_f32_e32 v135, v144, v135
	v_mul_f32_e32 v137, v144, v137
	v_cvt_pk_bf16_f32 v128, v135, v137
	v_lshlrev_b32_e32 v135, 16, v129
	v_and_b32_e32 v137, 0xffff0000, v129
	v_mul_f32_e32 v135, v144, v135
	v_mul_f32_e32 v137, v144, v137
	v_cvt_pk_bf16_f32 v129, v135, v137
	v_lshlrev_b32_e32 v135, 16, v130
	v_and_b32_e32 v137, 0xffff0000, v130
	v_mul_f32_e32 v135, v144, v135
	v_mul_f32_e32 v137, v144, v137
	v_cvt_pk_bf16_f32 v130, v135, v137
	v_lshlrev_b32_e32 v135, 16, v131
	v_and_b32_e32 v137, 0xffff0000, v131
	v_mul_f32_e32 v135, v144, v135
	v_mul_f32_e32 v137, v144, v137
	v_cvt_pk_bf16_f32 v131, v135, v137
	v_lshlrev_b32_e32 v135, 16, v146
	v_and_b32_e32 v137, 0xffff0000, v146
	v_mul_f32_e32 v135, v144, v135
	v_mul_f32_e32 v137, v144, v137
	v_cvt_pk_bf16_f32 v146, v135, v137
	v_lshlrev_b32_e32 v135, 16, v147
	v_and_b32_e32 v137, 0xffff0000, v147
	v_mul_f32_e32 v135, v144, v135
	v_mul_f32_e32 v137, v144, v137
	v_cvt_pk_bf16_f32 v147, v135, v137
	v_lshlrev_b32_e32 v135, 16, v148
	v_and_b32_e32 v137, 0xffff0000, v148
	v_mul_f32_e32 v135, v144, v135
	v_mul_f32_e32 v137, v144, v137
	v_cvt_pk_bf16_f32 v148, v135, v137
	v_lshlrev_b32_e32 v135, 16, v149
	v_and_b32_e32 v137, 0xffff0000, v149
	v_mul_f32_e32 v135, v144, v135
	v_mul_f32_e32 v137, v144, v137
	v_cvt_pk_bf16_f32 v149, v135, v137
	v_mov_b32_e32 v133, v175
	ds_read_b64_tr_b16 v[150:151], v133 offset:0
	v_mov_b32_e32 v135, v181
	ds_read_b64_tr_b16 v[152:153], v135 offset:0
	ds_read_b64_tr_b16 v[182:183], v133 offset:0x200
	ds_read_b64_tr_b16 v[184:185], v135 offset:0x200
	ds_read_b64_tr_b16 v[186:187], v133 offset:0x400
	ds_read_b64_tr_b16 v[188:189], v135 offset:0x400
	ds_read_b64_tr_b16 v[190:191], v133 offset:0x600
	ds_read_b64_tr_b16 v[192:193], v135 offset:0x600
	s_waitcnt lgkmcnt(0)
	s_nop 0
	v_mfma_f32_32x32x16_bf16 v[16:31], v[128:131], v[150:153], v[16:31]
	ds_read_b64_tr_b16 v[150:151], v133 offset:0x1000
	ds_read_b64_tr_b16 v[152:153], v135 offset:0x1000
	v_mfma_f32_32x32x16_bf16 v[0:15], v[128:131], v[182:185], v[0:15]
	ds_read_b64_tr_b16 v[182:183], v133 offset:0x1200
	ds_read_b64_tr_b16 v[184:185], v135 offset:0x1200
	v_mfma_f32_32x32x16_bf16 v[32:47], v[128:131], v[186:189], v[32:47]
	ds_read_b64_tr_b16 v[186:187], v133 offset:0x1400
	ds_read_b64_tr_b16 v[188:189], v135 offset:0x1400
	ds_read_b64_tr_b16 v[194:195], v133 offset:0x1600
	ds_read_b64_tr_b16 v[196:197], v135 offset:0x1600
	s_waitcnt lgkmcnt(0)
	v_mfma_f32_32x32x16_bf16 v[48:63], v[128:131], v[190:193], v[48:63]
	v_mfma_f32_32x32x16_bf16 v[16:31], v[146:149], v[150:153], v[16:31]
	v_add_u32_e32 v133, 0x2000, v133
	ds_read_b64_tr_b16 v[150:151], v133 offset:0
	v_add_u32_e32 v135, 0x2000, v135
	ds_read_b64_tr_b16 v[152:153], v135 offset:0
	v_mfma_f32_32x32x16_bf16 v[0:15], v[146:149], v[182:185], v[0:15]
	ds_read_b64_tr_b16 v[182:183], v133 offset:0x200
	ds_read_b64_tr_b16 v[184:185], v135 offset:0x200
	v_mfma_f32_32x32x16_bf16 v[32:47], v[146:149], v[186:189], v[32:47]
	ds_read_b64_tr_b16 v[186:187], v133 offset:0x400
	ds_read_b64_tr_b16 v[188:189], v135 offset:0x400
	ds_read_b64_tr_b16 v[190:191], v133 offset:0x600
	ds_read_b64_tr_b16 v[192:193], v135 offset:0x600
	s_waitcnt lgkmcnt(0)
	v_mfma_f32_32x32x16_bf16 v[48:63], v[146:149], v[194:197], v[48:63]
	v_mfma_f32_32x32x16_bf16 v[96:111], v[128:131], v[150:153], v[96:111]
	ds_read_b64_tr_b16 v[150:151], v133 offset:0x1000
	ds_read_b64_tr_b16 v[152:153], v135 offset:0x1000
	v_mfma_f32_32x32x16_bf16 v[112:127], v[128:131], v[182:185], v[112:127]
	ds_read_b64_tr_b16 v[182:183], v133 offset:0x1200
	ds_read_b64_tr_b16 v[184:185], v135 offset:0x1200
	v_mfma_f32_32x32x16_bf16 v[80:95], v[128:131], v[186:189], v[80:95]
	ds_read_b64_tr_b16 v[186:187], v133 offset:0x1400
	ds_read_b64_tr_b16 v[188:189], v135 offset:0x1400
	ds_read_b64_tr_b16 v[194:195], v133 offset:0x1600
	ds_read_b64_tr_b16 v[196:197], v135 offset:0x1600
	s_waitcnt lgkmcnt(0)
	v_mfma_f32_32x32x16_bf16 v[64:79], v[128:131], v[190:193], v[64:79]
	v_mfma_f32_32x32x16_bf16 v[96:111], v[146:149], v[150:153], v[96:111]
	v_mfma_f32_32x32x16_bf16 v[112:127], v[146:149], v[182:185], v[112:127]
	v_mfma_f32_32x32x16_bf16 v[80:95], v[146:149], v[186:189], v[80:95]
	v_mfma_f32_32x32x16_bf16 v[64:79], v[146:149], v[194:197], v[64:79]
	s_waitcnt vmcnt(0) lgkmcnt(0)
	s_barrier
; #define VM_WAIT() asm volatile("s_waitcnt vmcnt(0)" ::: "memory")
; template <int DK, int DV, bool MLSTM>
; __device__ __forceinline__ void out_unit2(LAS unsigned char* lds, LAS unsigned char* ldstab, const OutArgs a, const int wv) {
;     ...
;     for (int pc = 4; pc < 4 + 2 * NCP; ++pc) {
;         VM_WAIT(); __syncthreads();
;         if (pc + 1 < 4 + 2 * NCP) OUT_DMA(pc + 1);
;         const int cq = pc - 4, dirb = cq >= NCP, cp = dirb ? cq - NCP : cq;
;         const float qs = dirb ? qsb : qsf;
;         const unsigned qa = QP + (cp >> 2) * 32768u + 512u * (cp & 3) + 8192u * rb;
;         const bf16x8 af0 = scale_frag(lds_r128(qa + rb0), qs), af1 = scale_frag(lds_r128(qa + rb1), qs);
;         OUT_MMA(pc & 1);
;     }
	v_add_u32_e32 v133, s13, v173
	v_add_u32_e32 v135, s13, v177
	ds_read_b128 v[128:131], v133 offset:34304
	ds_read_b128 v[146:149], v135 offset:34304
	s_waitcnt lgkmcnt(0)
	v_lshlrev_b32_e32 v135, 16, v128
	v_and_b32_e32 v137, 0xffff0000, v128
	v_mul_f32_e32 v135, v144, v135
	v_mul_f32_e32 v137, v144, v137
	v_cvt_pk_bf16_f32 v128, v135, v137
	v_lshlrev_b32_e32 v135, 16, v129
	v_and_b32_e32 v137, 0xffff0000, v129
	v_mul_f32_e32 v135, v144, v135
	v_mul_f32_e32 v137, v144, v137
	v_cvt_pk_bf16_f32 v129, v135, v137
	v_lshlrev_b32_e32 v135, 16, v130
	v_and_b32_e32 v137, 0xffff0000, v130
	v_mul_f32_e32 v135, v144, v135
	v_mul_f32_e32 v137, v144, v137
	v_cvt_pk_bf16_f32 v130, v135, v137
	v_lshlrev_b32_e32 v135, 16, v131
	v_and_b32_e32 v137, 0xffff0000, v131
	v_mul_f32_e32 v135, v144, v135
	v_mul_f32_e32 v137, v144, v137
	v_cvt_pk_bf16_f32 v131, v135, v137
	v_lshlrev_b32_e32 v135, 16, v146
	v_and_b32_e32 v137, 0xffff0000, v146
	v_mul_f32_e32 v135, v144, v135
	v_mul_f32_e32 v137, v144, v137
	v_cvt_pk_bf16_f32 v146, v135, v137
	v_lshlrev_b32_e32 v135, 16, v147
	v_and_b32_e32 v137, 0xffff0000, v147
	v_mul_f32_e32 v135, v144, v135
	v_mul_f32_e32 v137, v144, v137
	v_cvt_pk_bf16_f32 v147, v135, v137
	v_lshlrev_b32_e32 v135, 16, v148
	v_and_b32_e32 v137, 0xffff0000, v148
	v_mul_f32_e32 v135, v144, v135
	v_mul_f32_e32 v137, v144, v137
	v_cvt_pk_bf16_f32 v148, v135, v137
	v_lshlrev_b32_e32 v135, 16, v149
	v_and_b32_e32 v137, 0xffff0000, v149
	v_mul_f32_e32 v135, v144, v135
	v_mul_f32_e32 v137, v144, v137
	v_cvt_pk_bf16_f32 v149, v135, v137
	v_add_u32_e32 v133, 0x10000, v175
	ds_read_b64_tr_b16 v[150:151], v133 offset:0
	v_add_u32_e32 v135, 0x10000, v181
	ds_read_b64_tr_b16 v[152:153], v135 offset:0
	ds_read_b64_tr_b16 v[182:183], v133 offset:0x200
	ds_read_b64_tr_b16 v[184:185], v135 offset:0x200
	ds_read_b64_tr_b16 v[186:187], v133 offset:0x400
	ds_read_b64_tr_b16 v[188:189], v135 offset:0x400
	ds_read_b64_tr_b16 v[190:191], v133 offset:0x600
	ds_read_b64_tr_b16 v[192:193], v135 offset:0x600
	s_waitcnt lgkmcnt(0)
	s_nop 0
	v_mfma_f32_32x32x16_bf16 v[16:31], v[128:131], v[150:153], v[16:31]
	ds_read_b64_tr_b16 v[150:151], v133 offset:0x1000
	ds_read_b64_tr_b16 v[152:153], v135 offset:0x1000
	v_mfma_f32_32x32x16_bf16 v[0:15], v[128:131], v[182:185], v[0:15]
	ds_read_b64_tr_b16 v[182:183], v133 offset:0x1200
	ds_read_b64_tr_b16 v[184:185], v135 offset:0x1200
	v_mfma_f32_32x32x16_bf16 v[32:47], v[128:131], v[186:189], v[32:47]
	ds_read_b64_tr_b16 v[186:187], v133 offset:0x1400
	ds_read_b64_tr_b16 v[188:189], v135 offset:0x1400
	ds_read_b64_tr_b16 v[194:195], v133 offset:0x1600
	ds_read_b64_tr_b16 v[196:197], v135 offset:0x1600
	s_waitcnt lgkmcnt(0)
	v_mfma_f32_32x32x16_bf16 v[48:63], v[128:131], v[190:193], v[48:63]
	v_mfma_f32_32x32x16_bf16 v[16:31], v[146:149], v[150:153], v[16:31]
	v_add_u32_e32 v133, 0x2000, v133
	ds_read_b64_tr_b16 v[150:151], v133 offset:0
	v_add_u32_e32 v135, 0x2000, v135
	ds_read_b64_tr_b16 v[152:153], v135 offset:0
	v_mfma_f32_32x32x16_bf16 v[0:15], v[146:149], v[182:185], v[0:15]
	ds_read_b64_tr_b16 v[182:183], v133 offset:0x200
	ds_read_b64_tr_b16 v[184:185], v135 offset:0x200
	v_mfma_f32_32x32x16_bf16 v[32:47], v[146:149], v[186:189], v[32:47]
	ds_read_b64_tr_b16 v[186:187], v133 offset:0x400
	ds_read_b64_tr_b16 v[188:189], v135 offset:0x400
	ds_read_b64_tr_b16 v[190:191], v133 offset:0x600
	ds_read_b64_tr_b16 v[192:193], v135 offset:0x600
	s_waitcnt lgkmcnt(0)
	v_mfma_f32_32x32x16_bf16 v[48:63], v[146:149], v[194:197], v[48:63]
	v_mfma_f32_32x32x16_bf16 v[96:111], v[128:131], v[150:153], v[96:111]
	ds_read_b64_tr_b16 v[150:151], v133 offset:0x1000
	ds_read_b64_tr_b16 v[152:153], v135 offset:0x1000
	v_mfma_f32_32x32x16_bf16 v[112:127], v[128:131], v[182:185], v[112:127]
	ds_read_b64_tr_b16 v[182:183], v133 offset:0x1200
	ds_read_b64_tr_b16 v[184:185], v135 offset:0x1200
	v_mfma_f32_32x32x16_bf16 v[80:95], v[128:131], v[186:189], v[80:95]
	ds_read_b64_tr_b16 v[186:187], v133 offset:0x1400
	ds_read_b64_tr_b16 v[188:189], v135 offset:0x1400
	ds_read_b64_tr_b16 v[194:195], v133 offset:0x1600
	ds_read_b64_tr_b16 v[196:197], v135 offset:0x1600
	s_waitcnt lgkmcnt(0)
	v_mfma_f32_32x32x16_bf16 v[64:79], v[128:131], v[190:193], v[64:79]
	v_mfma_f32_32x32x16_bf16 v[96:111], v[146:149], v[150:153], v[96:111]
	v_mfma_f32_32x32x16_bf16 v[112:127], v[146:149], v[182:185], v[112:127]
	v_mfma_f32_32x32x16_bf16 v[80:95], v[146:149], v[186:189], v[80:95]
	v_mfma_f32_32x32x16_bf16 v[64:79], v[146:149], v[194:197], v[64:79]
